# three quarters of the layer-1 w_down transposition in the layer-1 in-projection idle slot, region loads issued three steps ahead
# speedup vs baseline: 1.0058x; 1.0023x over previous
; #define LDS_WAIT() asm volatile("s_waitcnt lgkmcnt(0)" ::: "memory")
;     const int pr = item >> 1, kb = 2 * (pr / nblk) + (item & 1), nb = pr % nblk, k0 = 64 * kb, n0 = 32 * nb;
;     const int nr = n0 + (lane & 31); const int sc = MAP == 1 ? src_col_in(nr) : nr;
;     float v[32];
; #pragma unroll
;     for (int i = 0; i < 32; ++i) v[i] = sc >= 0 ? W[(size_t)(k0 + 2 * i + (lane >> 5)) * Nsrc + sc] : 0.f;
; #pragma unroll
;     for (int i = 0; i < 32; ++i) { const int k = k0 + 2 * i + (lane >> 5); float x = v[i] * wscale; if (KS) x *= (k < ksplit ? ksA[k] : ksB[k - ksplit]); scr[(2 * i + (lane >> 5)) * 33 + (lane & 31)] = x; }
;     LDS_WAIT(); asm volatile("" ::: "memory");
; __global__ void __launch_bounds__(NWAVES * 64, 2) hybrid_fwd(Args args) {
;     ...
;             p0_transpose_item_f8<false>(args.in[16] + (size_t)l * FF * DM, FF, DM, DM / 32, (unsigned char*)(ws + WS_WDN + l * SZ_WDN), 128.f, args.in[16], args.in[16], 0, scr, r, lane);
.LBB0_575:
	s_waitcnt vmcnt(0)
	s_barrier
	s_cmpk_lt_u32 s77, 0xa0
	s_cbranch_scc1 .Llite_skip
	s_sub_i32 s16, s77, 160
	v_and_b32_e32 v17, 63, v0
	v_lshrrev_b32_e32 v18, 6, v0
	v_lshrrev_b32_e32 v14, 5, v17
	v_lshl_add_u32 v15, v18, 4, v14
	v_and_b32_e32 v16, 31, v17
	v_xor_b32_e32 v16, v16, v18
	v_lshlrev_b32_e32 v16, 4, v16
	v_lshl_add_u32 v4, v15, 9, v16
	v_add_u32_e32 v5, 0x10000, v4
	v_and_b32_e32 v16, 31, v17
	v_lshlrev_b32_e32 v16, 4, v16
	s_mov_b32 s21, 0x4000
	v_mad_u32_u24 v10, v15, s21, v16
	v_and_b32_e32 v14, 7, v17
	v_lshrrev_b32_e32 v15, 5, v17
	v_lshl_add_u32 v15, v18, 2, v15
	v_xor_b32_e32 v15, v15, v14
	v_lshlrev_b32_e32 v15, 4, v15
	v_lshl_add_u32 v15, v14, 13, v15
	v_bfe_u32 v16, v17, 3, 2
	v_lshl_add_u32 v6, v16, 2, v15
	v_add_u32_e32 v7, 0x10000, v6
	v_and_b32_e32 v14, 7, v17
	v_lshrrev_b32_e32 v15, 5, v17
	v_lshl_add_u32 v15, v18, 2, v15
	v_add_u32_e32 v15, 2, v15
	v_xor_b32_e32 v15, v15, v14
	v_lshlrev_b32_e32 v15, 4, v15
	v_lshl_add_u32 v15, v14, 13, v15
	v_bfe_u32 v16, v17, 3, 2
	v_lshl_add_u32 v8, v16, 2, v15
	v_add_u32_e32 v9, 0x10000, v8
	v_lshrrev_b32_e32 v14, 3, v17
	v_lshl_add_u32 v14, v18, 4, v14
	v_and_b32_e32 v15, 7, v17
	v_lshlrev_b32_e32 v15, 4, v15
	v_lshl_add_u32 v11, v14, 14, v15
	v_lshrrev_b32_e32 v14, 3, v17
	v_lshl_add_u32 v14, v18, 4, v14
	v_add_u32_e32 v14, 8, v14
	v_and_b32_e32 v15, 7, v17
	v_lshlrev_b32_e32 v15, 4, v15
	v_lshl_add_u32 v12, v14, 14, v15
	v_mov_b32_e32 v13, 0x43e00000
	s_mov_b32 s20, 0xc3e00000
	v_readlane_b32 s2, v253, 35
	v_readlane_b32 s3, v253, 36
	v_readlane_b32 s4, v253, 41
	v_readlane_b32 s5, v253, 42
	s_add_u32 s2, s2, 0x10000000
	s_addc_u32 s3, s3, 0
	s_add_u32 s4, s4, 0x27600000
	s_addc_u32 s5, s5, 0
	s_add_i32 s17, s16, 0
	s_min_u32 s17, s17, 0xbff
	s_lshr_b32 s18, s17, 5
	s_add_i32 s18, s18, 32
	s_and_b32 s19, s17, 31
	s_lshl_b32 s18, s18, 21
	s_lshl_b32 s19, s19, 9
	s_add_u32 s18, s18, s19
	s_add_u32 s12, s2, s18
	s_addc_u32 s13, s3, 0
	global_load_dwordx4 v[36:39], v10, s[12:13]
	s_add_u32 s12, s12, 0x8000
	s_addc_u32 s13, s13, 0
	global_load_dwordx4 v[40:43], v10, s[12:13]
	s_add_u32 s12, s12, 0x8000
	s_addc_u32 s13, s13, 0
	global_load_dwordx4 v[44:47], v10, s[12:13]
	s_add_u32 s12, s12, 0x8000
	s_addc_u32 s13, s13, 0
	global_load_dwordx4 v[48:51], v10, s[12:13]
	s_add_u32 s12, s12, 0x8000
	s_addc_u32 s13, s13, 0
	global_load_dwordx4 v[52:55], v10, s[12:13]
	s_add_u32 s12, s12, 0x8000
	s_addc_u32 s13, s13, 0
	global_load_dwordx4 v[56:59], v10, s[12:13]
	s_add_u32 s12, s12, 0x8000
	s_addc_u32 s13, s13, 0
	global_load_dwordx4 v[60:63], v10, s[12:13]
	s_add_u32 s12, s12, 0x8000
	s_addc_u32 s13, s13, 0
	global_load_dwordx4 v[64:67], v10, s[12:13]
	s_add_i32 s17, s16, 96
	s_min_u32 s17, s17, 0xbff
	s_lshr_b32 s18, s17, 5
	s_add_i32 s18, s18, 32
	s_and_b32 s19, s17, 31
	s_lshl_b32 s18, s18, 21
	s_lshl_b32 s19, s19, 9
	s_add_u32 s18, s18, s19
	s_add_u32 s12, s2, s18
	s_addc_u32 s13, s3, 0
	global_load_dwordx4 v[68:71], v10, s[12:13]
	s_add_u32 s12, s12, 0x8000
	s_addc_u32 s13, s13, 0
	global_load_dwordx4 v[72:75], v10, s[12:13]
	s_add_u32 s12, s12, 0x8000
	s_addc_u32 s13, s13, 0
	global_load_dwordx4 v[76:79], v10, s[12:13]
	s_add_u32 s12, s12, 0x8000
	s_addc_u32 s13, s13, 0
	global_load_dwordx4 v[80:83], v10, s[12:13]
	s_add_u32 s12, s12, 0x8000
	s_addc_u32 s13, s13, 0
	global_load_dwordx4 v[84:87], v10, s[12:13]
	s_add_u32 s12, s12, 0x8000
	s_addc_u32 s13, s13, 0
	global_load_dwordx4 v[88:91], v10, s[12:13]
	s_add_u32 s12, s12, 0x8000
	s_addc_u32 s13, s13, 0
	global_load_dwordx4 v[92:95], v10, s[12:13]
	s_add_u32 s12, s12, 0x8000
	s_addc_u32 s13, s13, 0
	global_load_dwordx4 v[96:99], v10, s[12:13]
	s_add_i32 s17, s16, 192
	s_min_u32 s17, s17, 0xbff
	s_lshr_b32 s18, s17, 5
	s_add_i32 s18, s18, 32
	s_and_b32 s19, s17, 31
	s_lshl_b32 s18, s18, 21
	s_lshl_b32 s19, s19, 9
	s_add_u32 s18, s18, s19
	s_add_u32 s12, s2, s18
	s_addc_u32 s13, s3, 0
	global_load_dwordx4 v[100:103], v10, s[12:13]
	s_add_u32 s12, s12, 0x8000
	s_addc_u32 s13, s13, 0
	global_load_dwordx4 v[104:107], v10, s[12:13]
	s_add_u32 s12, s12, 0x8000
	s_addc_u32 s13, s13, 0
	global_load_dwordx4 v[108:111], v10, s[12:13]
	s_add_u32 s12, s12, 0x8000
	s_addc_u32 s13, s13, 0
	global_load_dwordx4 v[112:115], v10, s[12:13]
	s_add_u32 s12, s12, 0x8000
	s_addc_u32 s13, s13, 0
	global_load_dwordx4 v[116:119], v10, s[12:13]
	s_add_u32 s12, s12, 0x8000
	s_addc_u32 s13, s13, 0
	global_load_dwordx4 v[120:123], v10, s[12:13]
	s_add_u32 s12, s12, 0x8000
	s_addc_u32 s13, s13, 0
	global_load_dwordx4 v[124:127], v10, s[12:13]
	s_add_u32 s12, s12, 0x8000
	s_addc_u32 s13, s13, 0
	global_load_dwordx4 v[128:131], v10, s[12:13]
	s_waitcnt vmcnt(16)
	v_mul_f32_e32 v36, 0x43000000, v36
	v_mul_f32_e32 v37, 0x43000000, v37
	v_mul_f32_e32 v38, 0x43000000, v38
	v_mul_f32_e32 v39, 0x43000000, v39
	ds_write_b128 v4, v[36:39]
	v_mul_f32_e32 v40, 0x43000000, v40
	v_mul_f32_e32 v41, 0x43000000, v41
	v_mul_f32_e32 v42, 0x43000000, v42
	v_mul_f32_e32 v43, 0x43000000, v43
	ds_write_b128 v4, v[40:43] offset:1024
	v_mul_f32_e32 v44, 0x43000000, v44
	v_mul_f32_e32 v45, 0x43000000, v45
	v_mul_f32_e32 v46, 0x43000000, v46
	v_mul_f32_e32 v47, 0x43000000, v47
	ds_write_b128 v4, v[44:47] offset:2048
	v_mul_f32_e32 v48, 0x43000000, v48
	v_mul_f32_e32 v49, 0x43000000, v49
	v_mul_f32_e32 v50, 0x43000000, v50
	v_mul_f32_e32 v51, 0x43000000, v51
	ds_write_b128 v4, v[48:51] offset:3072
	v_mul_f32_e32 v52, 0x43000000, v52
	v_mul_f32_e32 v53, 0x43000000, v53
	v_mul_f32_e32 v54, 0x43000000, v54
	v_mul_f32_e32 v55, 0x43000000, v55
	ds_write_b128 v4, v[52:55] offset:4096
	v_mul_f32_e32 v56, 0x43000000, v56
	v_mul_f32_e32 v57, 0x43000000, v57
	v_mul_f32_e32 v58, 0x43000000, v58
	v_mul_f32_e32 v59, 0x43000000, v59
	ds_write_b128 v4, v[56:59] offset:5120
	v_mul_f32_e32 v60, 0x43000000, v60
	v_mul_f32_e32 v61, 0x43000000, v61
	v_mul_f32_e32 v62, 0x43000000, v62
	v_mul_f32_e32 v63, 0x43000000, v63
	ds_write_b128 v4, v[60:63] offset:6144
	v_mul_f32_e32 v64, 0x43000000, v64
	v_mul_f32_e32 v65, 0x43000000, v65
	v_mul_f32_e32 v66, 0x43000000, v66
	v_mul_f32_e32 v67, 0x43000000, v67
	ds_write_b128 v4, v[64:67] offset:7168
	s_waitcnt lgkmcnt(0)
	s_barrier
; #define GAS __attribute__((address_space(1)))
; #define LAS __attribute__((address_space(3)))
; #define LDS_WAIT() asm volatile("s_waitcnt lgkmcnt(0)" ::: "memory")
; __device__ __forceinline__ unsigned pk4_fp8(float a, float b, float c, float d) {
;     a = fminf(fmaxf(a, -448.f), 448.f); b = fminf(fmaxf(b, -448.f), 448.f); c = fminf(fmaxf(c, -448.f), 448.f); d = fminf(fmaxf(d, -448.f), 448.f);
;     int w = __builtin_amdgcn_cvt_pk_fp8_f32(a, b, 0, false); w = __builtin_amdgcn_cvt_pk_fp8_f32(c, d, w, true); return (unsigned)w; }
;     ...
;     for (int i = 0; i < 32; ++i) v[i] = sc >= 0 ? W[(size_t)(k0 + 2 * i + (lane >> 5)) * Nsrc + sc] : 0.f;
; #pragma unroll
;     for (int i = 0; i < 32; ++i) { const int k = k0 + 2 * i + (lane >> 5); float x = v[i] * wscale; if (KS) x *= (k < ksplit ? ksA[k] : ksB[k - ksplit]); scr[(2 * i + (lane >> 5)) * 33 + (lane & 31)] = x; }
;     LDS_WAIT(); asm volatile("" ::: "memory");
;     const int c = lane & 7;
; #pragma unroll
;     for (int j = 0; j < 4; ++j) { const int n = (lane >> 3) + 8 * j; const LAS float* s = scr + (8 * c) * 33 + n;
;         const unsigned long long o = (unsigned long long)pg8::pk4_fp8(s[0 * 33], s[1 * 33], s[2 * 33], s[3 * 33]) | ((unsigned long long)pg8::pk4_fp8(s[4 * 33], s[5 * 33], s[6 * 33], s[7 * 33]) << 32);
;         *(GAS unsigned long long*)(WT + (size_t)(n0 + n) * K + k0 + 8 * c) = o; }
	s_add_i32 s17, s16, 288
	s_min_u32 s17, s17, 0xbff
	s_lshr_b32 s18, s17, 5
	s_add_i32 s18, s18, 32
	s_and_b32 s19, s17, 31
	s_lshl_b32 s18, s18, 21
	s_lshl_b32 s19, s19, 9
	s_add_u32 s18, s18, s19
	s_add_u32 s12, s2, s18
	s_addc_u32 s13, s3, 0
	global_load_dwordx4 v[36:39], v10, s[12:13]
	s_add_u32 s12, s12, 0x8000
	s_addc_u32 s13, s13, 0
	global_load_dwordx4 v[40:43], v10, s[12:13]
	s_add_u32 s12, s12, 0x8000
	s_addc_u32 s13, s13, 0
	global_load_dwordx4 v[44:47], v10, s[12:13]
	s_add_u32 s12, s12, 0x8000
	s_addc_u32 s13, s13, 0
	global_load_dwordx4 v[48:51], v10, s[12:13]
	s_add_u32 s12, s12, 0x8000
	s_addc_u32 s13, s13, 0
	global_load_dwordx4 v[52:55], v10, s[12:13]
	s_add_u32 s12, s12, 0x8000
	s_addc_u32 s13, s13, 0
	global_load_dwordx4 v[56:59], v10, s[12:13]
	s_add_u32 s12, s12, 0x8000
	s_addc_u32 s13, s13, 0
	global_load_dwordx4 v[60:63], v10, s[12:13]
	s_add_u32 s12, s12, 0x8000
	s_addc_u32 s13, s13, 0
	global_load_dwordx4 v[64:67], v10, s[12:13]
	s_add_i32 s17, s16, 0
	s_min_u32 s17, s17, 0xbff
	s_lshr_b32 s18, s17, 5
	s_add_i32 s18, s18, 32
	s_and_b32 s19, s17, 31
	s_lshl_b32 s19, s19, 21
	s_lshl_b32 s18, s18, 7
	s_add_u32 s18, s18, s19
	s_add_u32 s14, s4, s18
	s_addc_u32 s15, s5, 0
	ds_read_b32 v132, v6
	ds_read_b32 v133, v6 offset:512
	ds_read_b32 v134, v6 offset:1024
	ds_read_b32 v135, v6 offset:1536
	ds_read_b32 v136, v6 offset:2048
	ds_read_b32 v137, v6 offset:2560
	ds_read_b32 v138, v6 offset:3072
	ds_read_b32 v139, v6 offset:3584
	ds_read_b32 v140, v6 offset:4096
	ds_read_b32 v141, v6 offset:4608
	ds_read_b32 v142, v6 offset:5120
	ds_read_b32 v143, v6 offset:5632
	ds_read_b32 v144, v6 offset:6144
	ds_read_b32 v145, v6 offset:6656
	ds_read_b32 v146, v6 offset:7168
	ds_read_b32 v147, v6 offset:7680
	s_waitcnt lgkmcnt(0)
	v_max_f32_e32 v132, v132, v132
	v_max_f32_e32 v133, v133, v133
	v_max_f32_e32 v134, v134, v134
	v_max_f32_e32 v135, v135, v135
	v_max_f32_e32 v136, v136, v136
	v_max_f32_e32 v137, v137, v137
	v_max_f32_e32 v138, v138, v138
	v_max_f32_e32 v139, v139, v139
	v_max_f32_e32 v140, v140, v140
	v_max_f32_e32 v141, v141, v141
	v_max_f32_e32 v142, v142, v142
	v_max_f32_e32 v143, v143, v143
	v_max_f32_e32 v144, v144, v144
	v_max_f32_e32 v145, v145, v145
	v_max_f32_e32 v146, v146, v146
	v_max_f32_e32 v147, v147, v147
	v_med3_f32 v132, v132, s20, v13
	v_med3_f32 v133, v133, s20, v13
	v_med3_f32 v134, v134, s20, v13
	v_med3_f32 v135, v135, s20, v13
	v_med3_f32 v136, v136, s20, v13
	v_med3_f32 v137, v137, s20, v13
	v_med3_f32 v138, v138, s20, v13
	v_med3_f32 v139, v139, s20, v13
	v_med3_f32 v140, v140, s20, v13
	v_med3_f32 v141, v141, s20, v13
	v_med3_f32 v142, v142, s20, v13
	v_med3_f32 v143, v143, s20, v13
	v_med3_f32 v144, v144, s20, v13
	v_med3_f32 v145, v145, s20, v13
	v_med3_f32 v146, v146, s20, v13
	v_med3_f32 v147, v147, s20, v13
	v_mov_b32_e32 v148, 0
	v_mov_b32_e32 v149, 0
	v_mov_b32_e32 v150, 0
	v_mov_b32_e32 v151, 0
	v_cvt_pk_fp8_f32 v148, v132, v133
	v_cvt_pk_fp8_f32 v149, v136, v137
	v_cvt_pk_fp8_f32 v150, v140, v141
	v_cvt_pk_fp8_f32 v151, v144, v145
	v_cvt_pk_fp8_f32 v148, v134, v135 op_sel:[0,0,1]
	v_cvt_pk_fp8_f32 v149, v138, v139 op_sel:[0,0,1]
	v_cvt_pk_fp8_f32 v150, v142, v143 op_sel:[0,0,1]
	v_cvt_pk_fp8_f32 v151, v146, v147 op_sel:[0,0,1]
	s_nop 0
	global_store_dwordx4 v11, v[148:151], s[14:15]
	ds_read_b32 v132, v8
	ds_read_b32 v133, v8 offset:512
	ds_read_b32 v134, v8 offset:1024
	ds_read_b32 v135, v8 offset:1536
	ds_read_b32 v136, v8 offset:2048
	ds_read_b32 v137, v8 offset:2560
	ds_read_b32 v138, v8 offset:3072
	ds_read_b32 v139, v8 offset:3584
	ds_read_b32 v140, v8 offset:4096
	ds_read_b32 v141, v8 offset:4608
	ds_read_b32 v142, v8 offset:5120
	ds_read_b32 v143, v8 offset:5632
	ds_read_b32 v144, v8 offset:6144
	ds_read_b32 v145, v8 offset:6656
	ds_read_b32 v146, v8 offset:7168
	ds_read_b32 v147, v8 offset:7680
	s_waitcnt lgkmcnt(0)
	v_max_f32_e32 v132, v132, v132
	v_max_f32_e32 v133, v133, v133
	v_max_f32_e32 v134, v134, v134
	v_max_f32_e32 v135, v135, v135
	v_max_f32_e32 v136, v136, v136
	v_max_f32_e32 v137, v137, v137
	v_max_f32_e32 v138, v138, v138
	v_max_f32_e32 v139, v139, v139
	v_max_f32_e32 v140, v140, v140
	v_max_f32_e32 v141, v141, v141
	v_max_f32_e32 v142, v142, v142
	v_max_f32_e32 v143, v143, v143
	v_max_f32_e32 v144, v144, v144
	v_max_f32_e32 v145, v145, v145
	v_max_f32_e32 v146, v146, v146
	v_max_f32_e32 v147, v147, v147
	v_med3_f32 v132, v132, s20, v13
	v_med3_f32 v133, v133, s20, v13
	v_med3_f32 v134, v134, s20, v13
	v_med3_f32 v135, v135, s20, v13
	v_med3_f32 v136, v136, s20, v13
	v_med3_f32 v137, v137, s20, v13
	v_med3_f32 v138, v138, s20, v13
	v_med3_f32 v139, v139, s20, v13
	v_med3_f32 v140, v140, s20, v13
	v_med3_f32 v141, v141, s20, v13
	v_med3_f32 v142, v142, s20, v13
	v_med3_f32 v143, v143, s20, v13
	v_med3_f32 v144, v144, s20, v13
	v_med3_f32 v145, v145, s20, v13
	v_med3_f32 v146, v146, s20, v13
	v_med3_f32 v147, v147, s20, v13
	v_mov_b32_e32 v148, 0
	v_mov_b32_e32 v149, 0
	v_mov_b32_e32 v150, 0
	v_mov_b32_e32 v151, 0
	v_cvt_pk_fp8_f32 v148, v132, v133
	v_cvt_pk_fp8_f32 v149, v136, v137
	v_cvt_pk_fp8_f32 v150, v140, v141
	v_cvt_pk_fp8_f32 v151, v144, v145
	v_cvt_pk_fp8_f32 v148, v134, v135 op_sel:[0,0,1]
	v_cvt_pk_fp8_f32 v149, v138, v139 op_sel:[0,0,1]
	v_cvt_pk_fp8_f32 v150, v142, v143 op_sel:[0,0,1]
	v_cvt_pk_fp8_f32 v151, v146, v147 op_sel:[0,0,1]
	s_nop 0
	global_store_dwordx4 v12, v[148:151], s[14:15]
	s_waitcnt vmcnt(18)
	v_mul_f32_e32 v68, 0x43000000, v68
	v_mul_f32_e32 v69, 0x43000000, v69
	v_mul_f32_e32 v70, 0x43000000, v70
	v_mul_f32_e32 v71, 0x43000000, v71
	ds_write_b128 v5, v[68:71]
	v_mul_f32_e32 v72, 0x43000000, v72
	v_mul_f32_e32 v73, 0x43000000, v73
	v_mul_f32_e32 v74, 0x43000000, v74
	v_mul_f32_e32 v75, 0x43000000, v75
	ds_write_b128 v5, v[72:75] offset:1024
	v_mul_f32_e32 v76, 0x43000000, v76
	v_mul_f32_e32 v77, 0x43000000, v77
	v_mul_f32_e32 v78, 0x43000000, v78
	v_mul_f32_e32 v79, 0x43000000, v79
	ds_write_b128 v5, v[76:79] offset:2048
	v_mul_f32_e32 v80, 0x43000000, v80
	v_mul_f32_e32 v81, 0x43000000, v81
	v_mul_f32_e32 v82, 0x43000000, v82
	v_mul_f32_e32 v83, 0x43000000, v83
	ds_write_b128 v5, v[80:83] offset:3072
	v_mul_f32_e32 v84, 0x43000000, v84
	v_mul_f32_e32 v85, 0x43000000, v85
	v_mul_f32_e32 v86, 0x43000000, v86
	v_mul_f32_e32 v87, 0x43000000, v87
	ds_write_b128 v5, v[84:87] offset:4096
	v_mul_f32_e32 v88, 0x43000000, v88
	v_mul_f32_e32 v89, 0x43000000, v89
	v_mul_f32_e32 v90, 0x43000000, v90
	v_mul_f32_e32 v91, 0x43000000, v91
	ds_write_b128 v5, v[88:91] offset:5120
	v_mul_f32_e32 v92, 0x43000000, v92
	v_mul_f32_e32 v93, 0x43000000, v93
	v_mul_f32_e32 v94, 0x43000000, v94
	v_mul_f32_e32 v95, 0x43000000, v95
	ds_write_b128 v5, v[92:95] offset:6144
	v_mul_f32_e32 v96, 0x43000000, v96
	v_mul_f32_e32 v97, 0x43000000, v97
	v_mul_f32_e32 v98, 0x43000000, v98
	v_mul_f32_e32 v99, 0x43000000, v99
	ds_write_b128 v5, v[96:99] offset:7168
	s_waitcnt lgkmcnt(0)
	s_barrier
; #define GAS __attribute__((address_space(1)))
; #define LAS __attribute__((address_space(3)))
; #define LDS_WAIT() asm volatile("s_waitcnt lgkmcnt(0)" ::: "memory")
; __device__ __forceinline__ unsigned pk4_fp8(float a, float b, float c, float d) {
;     a = fminf(fmaxf(a, -448.f), 448.f); b = fminf(fmaxf(b, -448.f), 448.f); c = fminf(fmaxf(c, -448.f), 448.f); d = fminf(fmaxf(d, -448.f), 448.f);
;     int w = __builtin_amdgcn_cvt_pk_fp8_f32(a, b, 0, false); w = __builtin_amdgcn_cvt_pk_fp8_f32(c, d, w, true); return (unsigned)w; }
;     ...
;     for (int i = 0; i < 32; ++i) v[i] = sc >= 0 ? W[(size_t)(k0 + 2 * i + (lane >> 5)) * Nsrc + sc] : 0.f;
; #pragma unroll
;     for (int i = 0; i < 32; ++i) { const int k = k0 + 2 * i + (lane >> 5); float x = v[i] * wscale; if (KS) x *= (k < ksplit ? ksA[k] : ksB[k - ksplit]); scr[(2 * i + (lane >> 5)) * 33 + (lane & 31)] = x; }
;     LDS_WAIT(); asm volatile("" ::: "memory");
;     const int c = lane & 7;
; #pragma unroll
;     for (int j = 0; j < 4; ++j) { const int n = (lane >> 3) + 8 * j; const LAS float* s = scr + (8 * c) * 33 + n;
;         const unsigned long long o = (unsigned long long)pg8::pk4_fp8(s[0 * 33], s[1 * 33], s[2 * 33], s[3 * 33]) | ((unsigned long long)pg8::pk4_fp8(s[4 * 33], s[5 * 33], s[6 * 33], s[7 * 33]) << 32);
;         *(GAS unsigned long long*)(WT + (size_t)(n0 + n) * K + k0 + 8 * c) = o; }
	s_add_i32 s17, s16, 384
	s_min_u32 s17, s17, 0xbff
	s_lshr_b32 s18, s17, 5
	s_add_i32 s18, s18, 32
	s_and_b32 s19, s17, 31
	s_lshl_b32 s18, s18, 21
	s_lshl_b32 s19, s19, 9
	s_add_u32 s18, s18, s19
	s_add_u32 s12, s2, s18
	s_addc_u32 s13, s3, 0
	global_load_dwordx4 v[68:71], v10, s[12:13]
	s_add_u32 s12, s12, 0x8000
	s_addc_u32 s13, s13, 0
	global_load_dwordx4 v[72:75], v10, s[12:13]
	s_add_u32 s12, s12, 0x8000
	s_addc_u32 s13, s13, 0
	global_load_dwordx4 v[76:79], v10, s[12:13]
	s_add_u32 s12, s12, 0x8000
	s_addc_u32 s13, s13, 0
	global_load_dwordx4 v[80:83], v10, s[12:13]
	s_add_u32 s12, s12, 0x8000
	s_addc_u32 s13, s13, 0
	global_load_dwordx4 v[84:87], v10, s[12:13]
	s_add_u32 s12, s12, 0x8000
	s_addc_u32 s13, s13, 0
	global_load_dwordx4 v[88:91], v10, s[12:13]
	s_add_u32 s12, s12, 0x8000
	s_addc_u32 s13, s13, 0
	global_load_dwordx4 v[92:95], v10, s[12:13]
	s_add_u32 s12, s12, 0x8000
	s_addc_u32 s13, s13, 0
	global_load_dwordx4 v[96:99], v10, s[12:13]
	s_add_i32 s17, s16, 96
	s_min_u32 s17, s17, 0xbff
	s_lshr_b32 s18, s17, 5
	s_add_i32 s18, s18, 32
	s_and_b32 s19, s17, 31
	s_lshl_b32 s19, s19, 21
	s_lshl_b32 s18, s18, 7
	s_add_u32 s18, s18, s19
	s_add_u32 s14, s4, s18
	s_addc_u32 s15, s5, 0
	ds_read_b32 v132, v7
	ds_read_b32 v133, v7 offset:512
	ds_read_b32 v134, v7 offset:1024
	ds_read_b32 v135, v7 offset:1536
	ds_read_b32 v136, v7 offset:2048
	ds_read_b32 v137, v7 offset:2560
	ds_read_b32 v138, v7 offset:3072
	ds_read_b32 v139, v7 offset:3584
	ds_read_b32 v140, v7 offset:4096
	ds_read_b32 v141, v7 offset:4608
	ds_read_b32 v142, v7 offset:5120
	ds_read_b32 v143, v7 offset:5632
	ds_read_b32 v144, v7 offset:6144
	ds_read_b32 v145, v7 offset:6656
	ds_read_b32 v146, v7 offset:7168
	ds_read_b32 v147, v7 offset:7680
	s_waitcnt lgkmcnt(0)
	v_max_f32_e32 v132, v132, v132
	v_max_f32_e32 v133, v133, v133
	v_max_f32_e32 v134, v134, v134
	v_max_f32_e32 v135, v135, v135
	v_max_f32_e32 v136, v136, v136
	v_max_f32_e32 v137, v137, v137
	v_max_f32_e32 v138, v138, v138
	v_max_f32_e32 v139, v139, v139
	v_max_f32_e32 v140, v140, v140
	v_max_f32_e32 v141, v141, v141
	v_max_f32_e32 v142, v142, v142
	v_max_f32_e32 v143, v143, v143
	v_max_f32_e32 v144, v144, v144
	v_max_f32_e32 v145, v145, v145
	v_max_f32_e32 v146, v146, v146
	v_max_f32_e32 v147, v147, v147
	v_med3_f32 v132, v132, s20, v13
	v_med3_f32 v133, v133, s20, v13
	v_med3_f32 v134, v134, s20, v13
	v_med3_f32 v135, v135, s20, v13
	v_med3_f32 v136, v136, s20, v13
	v_med3_f32 v137, v137, s20, v13
	v_med3_f32 v138, v138, s20, v13
	v_med3_f32 v139, v139, s20, v13
	v_med3_f32 v140, v140, s20, v13
	v_med3_f32 v141, v141, s20, v13
	v_med3_f32 v142, v142, s20, v13
	v_med3_f32 v143, v143, s20, v13
	v_med3_f32 v144, v144, s20, v13
	v_med3_f32 v145, v145, s20, v13
	v_med3_f32 v146, v146, s20, v13
	v_med3_f32 v147, v147, s20, v13
	v_mov_b32_e32 v148, 0
	v_mov_b32_e32 v149, 0
	v_mov_b32_e32 v150, 0
	v_mov_b32_e32 v151, 0
	v_cvt_pk_fp8_f32 v148, v132, v133
	v_cvt_pk_fp8_f32 v149, v136, v137
	v_cvt_pk_fp8_f32 v150, v140, v141
	v_cvt_pk_fp8_f32 v151, v144, v145
	v_cvt_pk_fp8_f32 v148, v134, v135 op_sel:[0,0,1]
	v_cvt_pk_fp8_f32 v149, v138, v139 op_sel:[0,0,1]
	v_cvt_pk_fp8_f32 v150, v142, v143 op_sel:[0,0,1]
	v_cvt_pk_fp8_f32 v151, v146, v147 op_sel:[0,0,1]
	s_nop 0
	global_store_dwordx4 v11, v[148:151], s[14:15]
	ds_read_b32 v132, v9
	ds_read_b32 v133, v9 offset:512
	ds_read_b32 v134, v9 offset:1024
	ds_read_b32 v135, v9 offset:1536
	ds_read_b32 v136, v9 offset:2048
	ds_read_b32 v137, v9 offset:2560
	ds_read_b32 v138, v9 offset:3072
	ds_read_b32 v139, v9 offset:3584
	ds_read_b32 v140, v9 offset:4096
	ds_read_b32 v141, v9 offset:4608
	ds_read_b32 v142, v9 offset:5120
	ds_read_b32 v143, v9 offset:5632
	ds_read_b32 v144, v9 offset:6144
	ds_read_b32 v145, v9 offset:6656
	ds_read_b32 v146, v9 offset:7168
	ds_read_b32 v147, v9 offset:7680
	s_waitcnt lgkmcnt(0)
	v_max_f32_e32 v132, v132, v132
	v_max_f32_e32 v133, v133, v133
	v_max_f32_e32 v134, v134, v134
	v_max_f32_e32 v135, v135, v135
	v_max_f32_e32 v136, v136, v136
	v_max_f32_e32 v137, v137, v137
	v_max_f32_e32 v138, v138, v138
	v_max_f32_e32 v139, v139, v139
	v_max_f32_e32 v140, v140, v140
	v_max_f32_e32 v141, v141, v141
	v_max_f32_e32 v142, v142, v142
	v_max_f32_e32 v143, v143, v143
	v_max_f32_e32 v144, v144, v144
	v_max_f32_e32 v145, v145, v145
	v_max_f32_e32 v146, v146, v146
	v_max_f32_e32 v147, v147, v147
	v_med3_f32 v132, v132, s20, v13
	v_med3_f32 v133, v133, s20, v13
	v_med3_f32 v134, v134, s20, v13
	v_med3_f32 v135, v135, s20, v13
	v_med3_f32 v136, v136, s20, v13
	v_med3_f32 v137, v137, s20, v13
	v_med3_f32 v138, v138, s20, v13
	v_med3_f32 v139, v139, s20, v13
	v_med3_f32 v140, v140, s20, v13
	v_med3_f32 v141, v141, s20, v13
	v_med3_f32 v142, v142, s20, v13
	v_med3_f32 v143, v143, s20, v13
	v_med3_f32 v144, v144, s20, v13
	v_med3_f32 v145, v145, s20, v13
	v_med3_f32 v146, v146, s20, v13
	v_med3_f32 v147, v147, s20, v13
	v_mov_b32_e32 v148, 0
	v_mov_b32_e32 v149, 0
	v_mov_b32_e32 v150, 0
	v_mov_b32_e32 v151, 0
	v_cvt_pk_fp8_f32 v148, v132, v133
	v_cvt_pk_fp8_f32 v149, v136, v137
	v_cvt_pk_fp8_f32 v150, v140, v141
	v_cvt_pk_fp8_f32 v151, v144, v145
	v_cvt_pk_fp8_f32 v148, v134, v135 op_sel:[0,0,1]
	v_cvt_pk_fp8_f32 v149, v138, v139 op_sel:[0,0,1]
	v_cvt_pk_fp8_f32 v150, v142, v143 op_sel:[0,0,1]
	v_cvt_pk_fp8_f32 v151, v146, v147 op_sel:[0,0,1]
	s_nop 0
	global_store_dwordx4 v12, v[148:151], s[14:15]
	s_waitcnt vmcnt(20)
	v_mul_f32_e32 v100, 0x43000000, v100
	v_mul_f32_e32 v101, 0x43000000, v101
	v_mul_f32_e32 v102, 0x43000000, v102
	v_mul_f32_e32 v103, 0x43000000, v103
	ds_write_b128 v4, v[100:103]
	v_mul_f32_e32 v104, 0x43000000, v104
	v_mul_f32_e32 v105, 0x43000000, v105
	v_mul_f32_e32 v106, 0x43000000, v106
	v_mul_f32_e32 v107, 0x43000000, v107
	ds_write_b128 v4, v[104:107] offset:1024
	v_mul_f32_e32 v108, 0x43000000, v108
	v_mul_f32_e32 v109, 0x43000000, v109
	v_mul_f32_e32 v110, 0x43000000, v110
	v_mul_f32_e32 v111, 0x43000000, v111
	ds_write_b128 v4, v[108:111] offset:2048
	v_mul_f32_e32 v112, 0x43000000, v112
	v_mul_f32_e32 v113, 0x43000000, v113
	v_mul_f32_e32 v114, 0x43000000, v114
	v_mul_f32_e32 v115, 0x43000000, v115
	ds_write_b128 v4, v[112:115] offset:3072
	v_mul_f32_e32 v116, 0x43000000, v116
	v_mul_f32_e32 v117, 0x43000000, v117
	v_mul_f32_e32 v118, 0x43000000, v118
	v_mul_f32_e32 v119, 0x43000000, v119
	ds_write_b128 v4, v[116:119] offset:4096
	v_mul_f32_e32 v120, 0x43000000, v120
	v_mul_f32_e32 v121, 0x43000000, v121
	v_mul_f32_e32 v122, 0x43000000, v122
	v_mul_f32_e32 v123, 0x43000000, v123
	ds_write_b128 v4, v[120:123] offset:5120
	v_mul_f32_e32 v124, 0x43000000, v124
	v_mul_f32_e32 v125, 0x43000000, v125
	v_mul_f32_e32 v126, 0x43000000, v126
	v_mul_f32_e32 v127, 0x43000000, v127
	ds_write_b128 v4, v[124:127] offset:6144
	v_mul_f32_e32 v128, 0x43000000, v128
	v_mul_f32_e32 v129, 0x43000000, v129
	v_mul_f32_e32 v130, 0x43000000, v130
	v_mul_f32_e32 v131, 0x43000000, v131
	ds_write_b128 v4, v[128:131] offset:7168
	s_waitcnt lgkmcnt(0)
	s_barrier
; #define GAS __attribute__((address_space(1)))
; #define LAS __attribute__((address_space(3)))
; #define LDS_WAIT() asm volatile("s_waitcnt lgkmcnt(0)" ::: "memory")
; __device__ __forceinline__ unsigned pk4_fp8(float a, float b, float c, float d) {
;     a = fminf(fmaxf(a, -448.f), 448.f); b = fminf(fmaxf(b, -448.f), 448.f); c = fminf(fmaxf(c, -448.f), 448.f); d = fminf(fmaxf(d, -448.f), 448.f);
;     int w = __builtin_amdgcn_cvt_pk_fp8_f32(a, b, 0, false); w = __builtin_amdgcn_cvt_pk_fp8_f32(c, d, w, true); return (unsigned)w; }
;     ...
;     for (int i = 0; i < 32; ++i) v[i] = sc >= 0 ? W[(size_t)(k0 + 2 * i + (lane >> 5)) * Nsrc + sc] : 0.f;
; #pragma unroll
;     for (int i = 0; i < 32; ++i) { const int k = k0 + 2 * i + (lane >> 5); float x = v[i] * wscale; if (KS) x *= (k < ksplit ? ksA[k] : ksB[k - ksplit]); scr[(2 * i + (lane >> 5)) * 33 + (lane & 31)] = x; }
;     LDS_WAIT(); asm volatile("" ::: "memory");
;     const int c = lane & 7;
; #pragma unroll
;     for (int j = 0; j < 4; ++j) { const int n = (lane >> 3) + 8 * j; const LAS float* s = scr + (8 * c) * 33 + n;
;         const unsigned long long o = (unsigned long long)pg8::pk4_fp8(s[0 * 33], s[1 * 33], s[2 * 33], s[3 * 33]) | ((unsigned long long)pg8::pk4_fp8(s[4 * 33], s[5 * 33], s[6 * 33], s[7 * 33]) << 32);
;         *(GAS unsigned long long*)(WT + (size_t)(n0 + n) * K + k0 + 8 * c) = o; }
	s_add_i32 s17, s16, 480
	s_min_u32 s17, s17, 0xbff
	s_lshr_b32 s18, s17, 5
	s_add_i32 s18, s18, 32
	s_and_b32 s19, s17, 31
	s_lshl_b32 s18, s18, 21
	s_lshl_b32 s19, s19, 9
	s_add_u32 s18, s18, s19
	s_add_u32 s12, s2, s18
	s_addc_u32 s13, s3, 0
	global_load_dwordx4 v[100:103], v10, s[12:13]
	s_add_u32 s12, s12, 0x8000
	s_addc_u32 s13, s13, 0
	global_load_dwordx4 v[104:107], v10, s[12:13]
	s_add_u32 s12, s12, 0x8000
	s_addc_u32 s13, s13, 0
	global_load_dwordx4 v[108:111], v10, s[12:13]
	s_add_u32 s12, s12, 0x8000
	s_addc_u32 s13, s13, 0
	global_load_dwordx4 v[112:115], v10, s[12:13]
	s_add_u32 s12, s12, 0x8000
	s_addc_u32 s13, s13, 0
	global_load_dwordx4 v[116:119], v10, s[12:13]
	s_add_u32 s12, s12, 0x8000
	s_addc_u32 s13, s13, 0
	global_load_dwordx4 v[120:123], v10, s[12:13]
	s_add_u32 s12, s12, 0x8000
	s_addc_u32 s13, s13, 0
	global_load_dwordx4 v[124:127], v10, s[12:13]
	s_add_u32 s12, s12, 0x8000
	s_addc_u32 s13, s13, 0
	global_load_dwordx4 v[128:131], v10, s[12:13]
	s_add_i32 s17, s16, 192
	s_min_u32 s17, s17, 0xbff
	s_lshr_b32 s18, s17, 5
	s_add_i32 s18, s18, 32
	s_and_b32 s19, s17, 31
	s_lshl_b32 s19, s19, 21
	s_lshl_b32 s18, s18, 7
	s_add_u32 s18, s18, s19
	s_add_u32 s14, s4, s18
	s_addc_u32 s15, s5, 0
	ds_read_b32 v132, v6
	ds_read_b32 v133, v6 offset:512
	ds_read_b32 v134, v6 offset:1024
	ds_read_b32 v135, v6 offset:1536
	ds_read_b32 v136, v6 offset:2048
	ds_read_b32 v137, v6 offset:2560
	ds_read_b32 v138, v6 offset:3072
	ds_read_b32 v139, v6 offset:3584
	ds_read_b32 v140, v6 offset:4096
	ds_read_b32 v141, v6 offset:4608
	ds_read_b32 v142, v6 offset:5120
	ds_read_b32 v143, v6 offset:5632
	ds_read_b32 v144, v6 offset:6144
	ds_read_b32 v145, v6 offset:6656
	ds_read_b32 v146, v6 offset:7168
	ds_read_b32 v147, v6 offset:7680
	s_waitcnt lgkmcnt(0)
	v_max_f32_e32 v132, v132, v132
	v_max_f32_e32 v133, v133, v133
	v_max_f32_e32 v134, v134, v134
	v_max_f32_e32 v135, v135, v135
	v_max_f32_e32 v136, v136, v136
	v_max_f32_e32 v137, v137, v137
	v_max_f32_e32 v138, v138, v138
	v_max_f32_e32 v139, v139, v139
	v_max_f32_e32 v140, v140, v140
	v_max_f32_e32 v141, v141, v141
	v_max_f32_e32 v142, v142, v142
	v_max_f32_e32 v143, v143, v143
	v_max_f32_e32 v144, v144, v144
	v_max_f32_e32 v145, v145, v145
	v_max_f32_e32 v146, v146, v146
	v_max_f32_e32 v147, v147, v147
	v_med3_f32 v132, v132, s20, v13
	v_med3_f32 v133, v133, s20, v13
	v_med3_f32 v134, v134, s20, v13
	v_med3_f32 v135, v135, s20, v13
	v_med3_f32 v136, v136, s20, v13
	v_med3_f32 v137, v137, s20, v13
	v_med3_f32 v138, v138, s20, v13
	v_med3_f32 v139, v139, s20, v13
	v_med3_f32 v140, v140, s20, v13
	v_med3_f32 v141, v141, s20, v13
	v_med3_f32 v142, v142, s20, v13
	v_med3_f32 v143, v143, s20, v13
	v_med3_f32 v144, v144, s20, v13
	v_med3_f32 v145, v145, s20, v13
	v_med3_f32 v146, v146, s20, v13
	v_med3_f32 v147, v147, s20, v13
	v_mov_b32_e32 v148, 0
	v_mov_b32_e32 v149, 0
	v_mov_b32_e32 v150, 0
	v_mov_b32_e32 v151, 0
	v_cvt_pk_fp8_f32 v148, v132, v133
	v_cvt_pk_fp8_f32 v149, v136, v137
	v_cvt_pk_fp8_f32 v150, v140, v141
	v_cvt_pk_fp8_f32 v151, v144, v145
	v_cvt_pk_fp8_f32 v148, v134, v135 op_sel:[0,0,1]
	v_cvt_pk_fp8_f32 v149, v138, v139 op_sel:[0,0,1]
	v_cvt_pk_fp8_f32 v150, v142, v143 op_sel:[0,0,1]
	v_cvt_pk_fp8_f32 v151, v146, v147 op_sel:[0,0,1]
	s_nop 0
	global_store_dwordx4 v11, v[148:151], s[14:15]
	ds_read_b32 v132, v8
	ds_read_b32 v133, v8 offset:512
	ds_read_b32 v134, v8 offset:1024
	ds_read_b32 v135, v8 offset:1536
	ds_read_b32 v136, v8 offset:2048
	ds_read_b32 v137, v8 offset:2560
	ds_read_b32 v138, v8 offset:3072
	ds_read_b32 v139, v8 offset:3584
	ds_read_b32 v140, v8 offset:4096
	ds_read_b32 v141, v8 offset:4608
	ds_read_b32 v142, v8 offset:5120
	ds_read_b32 v143, v8 offset:5632
	ds_read_b32 v144, v8 offset:6144
	ds_read_b32 v145, v8 offset:6656
	ds_read_b32 v146, v8 offset:7168
	ds_read_b32 v147, v8 offset:7680
	s_waitcnt lgkmcnt(0)
	v_max_f32_e32 v132, v132, v132
	v_max_f32_e32 v133, v133, v133
	v_max_f32_e32 v134, v134, v134
	v_max_f32_e32 v135, v135, v135
	v_max_f32_e32 v136, v136, v136
	v_max_f32_e32 v137, v137, v137
	v_max_f32_e32 v138, v138, v138
	v_max_f32_e32 v139, v139, v139
	v_max_f32_e32 v140, v140, v140
	v_max_f32_e32 v141, v141, v141
	v_max_f32_e32 v142, v142, v142
	v_max_f32_e32 v143, v143, v143
	v_max_f32_e32 v144, v144, v144
	v_max_f32_e32 v145, v145, v145
	v_max_f32_e32 v146, v146, v146
	v_max_f32_e32 v147, v147, v147
	v_med3_f32 v132, v132, s20, v13
	v_med3_f32 v133, v133, s20, v13
	v_med3_f32 v134, v134, s20, v13
	v_med3_f32 v135, v135, s20, v13
	v_med3_f32 v136, v136, s20, v13
	v_med3_f32 v137, v137, s20, v13
	v_med3_f32 v138, v138, s20, v13
	v_med3_f32 v139, v139, s20, v13
	v_med3_f32 v140, v140, s20, v13
	v_med3_f32 v141, v141, s20, v13
	v_med3_f32 v142, v142, s20, v13
	v_med3_f32 v143, v143, s20, v13
	v_med3_f32 v144, v144, s20, v13
	v_med3_f32 v145, v145, s20, v13
	v_med3_f32 v146, v146, s20, v13
	v_med3_f32 v147, v147, s20, v13
	v_mov_b32_e32 v148, 0
	v_mov_b32_e32 v149, 0
	v_mov_b32_e32 v150, 0
	v_mov_b32_e32 v151, 0
	v_cvt_pk_fp8_f32 v148, v132, v133
	v_cvt_pk_fp8_f32 v149, v136, v137
	v_cvt_pk_fp8_f32 v150, v140, v141
	v_cvt_pk_fp8_f32 v151, v144, v145
	v_cvt_pk_fp8_f32 v148, v134, v135 op_sel:[0,0,1]
	v_cvt_pk_fp8_f32 v149, v138, v139 op_sel:[0,0,1]
	v_cvt_pk_fp8_f32 v150, v142, v143 op_sel:[0,0,1]
	v_cvt_pk_fp8_f32 v151, v146, v147 op_sel:[0,0,1]
	s_nop 0
	global_store_dwordx4 v12, v[148:151], s[14:15]
	s_waitcnt vmcnt(22)
	v_mul_f32_e32 v36, 0x43000000, v36
	v_mul_f32_e32 v37, 0x43000000, v37
	v_mul_f32_e32 v38, 0x43000000, v38
	v_mul_f32_e32 v39, 0x43000000, v39
	ds_write_b128 v5, v[36:39]
	v_mul_f32_e32 v40, 0x43000000, v40
	v_mul_f32_e32 v41, 0x43000000, v41
	v_mul_f32_e32 v42, 0x43000000, v42
	v_mul_f32_e32 v43, 0x43000000, v43
	ds_write_b128 v5, v[40:43] offset:1024
	v_mul_f32_e32 v44, 0x43000000, v44
	v_mul_f32_e32 v45, 0x43000000, v45
	v_mul_f32_e32 v46, 0x43000000, v46
	v_mul_f32_e32 v47, 0x43000000, v47
	ds_write_b128 v5, v[44:47] offset:2048
	v_mul_f32_e32 v48, 0x43000000, v48
	v_mul_f32_e32 v49, 0x43000000, v49
	v_mul_f32_e32 v50, 0x43000000, v50
	v_mul_f32_e32 v51, 0x43000000, v51
	ds_write_b128 v5, v[48:51] offset:3072
	v_mul_f32_e32 v52, 0x43000000, v52
	v_mul_f32_e32 v53, 0x43000000, v53
	v_mul_f32_e32 v54, 0x43000000, v54
	v_mul_f32_e32 v55, 0x43000000, v55
	ds_write_b128 v5, v[52:55] offset:4096
	v_mul_f32_e32 v56, 0x43000000, v56
	v_mul_f32_e32 v57, 0x43000000, v57
	v_mul_f32_e32 v58, 0x43000000, v58
	v_mul_f32_e32 v59, 0x43000000, v59
	ds_write_b128 v5, v[56:59] offset:5120
	v_mul_f32_e32 v60, 0x43000000, v60
	v_mul_f32_e32 v61, 0x43000000, v61
	v_mul_f32_e32 v62, 0x43000000, v62
	v_mul_f32_e32 v63, 0x43000000, v63
	ds_write_b128 v5, v[60:63] offset:6144
	v_mul_f32_e32 v64, 0x43000000, v64
	v_mul_f32_e32 v65, 0x43000000, v65
	v_mul_f32_e32 v66, 0x43000000, v66
	v_mul_f32_e32 v67, 0x43000000, v67
	ds_write_b128 v5, v[64:67] offset:7168
	s_waitcnt lgkmcnt(0)
	s_barrier
; #define GAS __attribute__((address_space(1)))
; #define LAS __attribute__((address_space(3)))
; #define LDS_WAIT() asm volatile("s_waitcnt lgkmcnt(0)" ::: "memory")
; __device__ __forceinline__ unsigned pk4_fp8(float a, float b, float c, float d) {
;     a = fminf(fmaxf(a, -448.f), 448.f); b = fminf(fmaxf(b, -448.f), 448.f); c = fminf(fmaxf(c, -448.f), 448.f); d = fminf(fmaxf(d, -448.f), 448.f);
;     int w = __builtin_amdgcn_cvt_pk_fp8_f32(a, b, 0, false); w = __builtin_amdgcn_cvt_pk_fp8_f32(c, d, w, true); return (unsigned)w; }
;     const int pr = item >> 1, kb = 2 * (pr / nblk) + (item & 1), nb = pr % nblk, k0 = 64 * kb, n0 = 32 * nb;
;     const int nr = n0 + (lane & 31); const int sc = MAP == 1 ? src_col_in(nr) : nr;
;     float v[32];
; #pragma unroll
;     for (int i = 0; i < 32; ++i) v[i] = sc >= 0 ? W[(size_t)(k0 + 2 * i + (lane >> 5)) * Nsrc + sc] : 0.f;
; #pragma unroll
;     for (int i = 0; i < 32; ++i) { const int k = k0 + 2 * i + (lane >> 5); float x = v[i] * wscale; if (KS) x *= (k < ksplit ? ksA[k] : ksB[k - ksplit]); scr[(2 * i + (lane >> 5)) * 33 + (lane & 31)] = x; }
;     LDS_WAIT(); asm volatile("" ::: "memory");
;     const int c = lane & 7;
; #pragma unroll
;     for (int j = 0; j < 4; ++j) { const int n = (lane >> 3) + 8 * j; const LAS float* s = scr + (8 * c) * 33 + n;
;         const unsigned long long o = (unsigned long long)pg8::pk4_fp8(s[0 * 33], s[1 * 33], s[2 * 33], s[3 * 33]) | ((unsigned long long)pg8::pk4_fp8(s[4 * 33], s[5 * 33], s[6 * 33], s[7 * 33]) << 32);
;         *(GAS unsigned long long*)(WT + (size_t)(n0 + n) * K + k0 + 8 * c) = o; }
;     LDS_WAIT(); asm volatile("" ::: "memory");
; }
	s_add_i32 s17, s16, 576
	s_min_u32 s17, s17, 0xbff
	s_lshr_b32 s18, s17, 5
	s_add_i32 s18, s18, 32
	s_and_b32 s19, s17, 31
	s_lshl_b32 s18, s18, 21
	s_lshl_b32 s19, s19, 9
	s_add_u32 s18, s18, s19
	s_add_u32 s12, s2, s18
	s_addc_u32 s13, s3, 0
	global_load_dwordx4 v[36:39], v10, s[12:13]
	s_add_u32 s12, s12, 0x8000
	s_addc_u32 s13, s13, 0
	global_load_dwordx4 v[40:43], v10, s[12:13]
	s_add_u32 s12, s12, 0x8000
	s_addc_u32 s13, s13, 0
	global_load_dwordx4 v[44:47], v10, s[12:13]
	s_add_u32 s12, s12, 0x8000
	s_addc_u32 s13, s13, 0
	global_load_dwordx4 v[48:51], v10, s[12:13]
	s_add_u32 s12, s12, 0x8000
	s_addc_u32 s13, s13, 0
	global_load_dwordx4 v[52:55], v10, s[12:13]
	s_add_u32 s12, s12, 0x8000
	s_addc_u32 s13, s13, 0
	global_load_dwordx4 v[56:59], v10, s[12:13]
	s_add_u32 s12, s12, 0x8000
	s_addc_u32 s13, s13, 0
	global_load_dwordx4 v[60:63], v10, s[12:13]
	s_add_u32 s12, s12, 0x8000
	s_addc_u32 s13, s13, 0
	global_load_dwordx4 v[64:67], v10, s[12:13]
	s_add_i32 s17, s16, 288
	s_min_u32 s17, s17, 0xbff
	s_lshr_b32 s18, s17, 5
	s_add_i32 s18, s18, 32
	s_and_b32 s19, s17, 31
	s_lshl_b32 s19, s19, 21
	s_lshl_b32 s18, s18, 7
	s_add_u32 s18, s18, s19
	s_add_u32 s14, s4, s18
	s_addc_u32 s15, s5, 0
	ds_read_b32 v132, v7
	ds_read_b32 v133, v7 offset:512
	ds_read_b32 v134, v7 offset:1024
	ds_read_b32 v135, v7 offset:1536
	ds_read_b32 v136, v7 offset:2048
	ds_read_b32 v137, v7 offset:2560
	ds_read_b32 v138, v7 offset:3072
	ds_read_b32 v139, v7 offset:3584
	ds_read_b32 v140, v7 offset:4096
	ds_read_b32 v141, v7 offset:4608
	ds_read_b32 v142, v7 offset:5120
	ds_read_b32 v143, v7 offset:5632
	ds_read_b32 v144, v7 offset:6144
	ds_read_b32 v145, v7 offset:6656
	ds_read_b32 v146, v7 offset:7168
	ds_read_b32 v147, v7 offset:7680
	s_waitcnt lgkmcnt(0)
	v_max_f32_e32 v132, v132, v132
	v_max_f32_e32 v133, v133, v133
	v_max_f32_e32 v134, v134, v134
	v_max_f32_e32 v135, v135, v135
	v_max_f32_e32 v136, v136, v136
	v_max_f32_e32 v137, v137, v137
	v_max_f32_e32 v138, v138, v138
	v_max_f32_e32 v139, v139, v139
	v_max_f32_e32 v140, v140, v140
	v_max_f32_e32 v141, v141, v141
	v_max_f32_e32 v142, v142, v142
	v_max_f32_e32 v143, v143, v143
	v_max_f32_e32 v144, v144, v144
	v_max_f32_e32 v145, v145, v145
	v_max_f32_e32 v146, v146, v146
	v_max_f32_e32 v147, v147, v147
	v_med3_f32 v132, v132, s20, v13
	v_med3_f32 v133, v133, s20, v13
	v_med3_f32 v134, v134, s20, v13
	v_med3_f32 v135, v135, s20, v13
	v_med3_f32 v136, v136, s20, v13
	v_med3_f32 v137, v137, s20, v13
	v_med3_f32 v138, v138, s20, v13
	v_med3_f32 v139, v139, s20, v13
	v_med3_f32 v140, v140, s20, v13
	v_med3_f32 v141, v141, s20, v13
	v_med3_f32 v142, v142, s20, v13
	v_med3_f32 v143, v143, s20, v13
	v_med3_f32 v144, v144, s20, v13
	v_med3_f32 v145, v145, s20, v13
	v_med3_f32 v146, v146, s20, v13
	v_med3_f32 v147, v147, s20, v13
	v_mov_b32_e32 v148, 0
	v_mov_b32_e32 v149, 0
	v_mov_b32_e32 v150, 0
	v_mov_b32_e32 v151, 0
	v_cvt_pk_fp8_f32 v148, v132, v133
	v_cvt_pk_fp8_f32 v149, v136, v137
	v_cvt_pk_fp8_f32 v150, v140, v141
	v_cvt_pk_fp8_f32 v151, v144, v145
	v_cvt_pk_fp8_f32 v148, v134, v135 op_sel:[0,0,1]
	v_cvt_pk_fp8_f32 v149, v138, v139 op_sel:[0,0,1]
	v_cvt_pk_fp8_f32 v150, v142, v143 op_sel:[0,0,1]
	v_cvt_pk_fp8_f32 v151, v146, v147 op_sel:[0,0,1]
	s_nop 0
	global_store_dwordx4 v11, v[148:151], s[14:15]
	ds_read_b32 v132, v9
	ds_read_b32 v133, v9 offset:512
	ds_read_b32 v134, v9 offset:1024
	ds_read_b32 v135, v9 offset:1536
	ds_read_b32 v136, v9 offset:2048
	ds_read_b32 v137, v9 offset:2560
	ds_read_b32 v138, v9 offset:3072
	ds_read_b32 v139, v9 offset:3584
	ds_read_b32 v140, v9 offset:4096
	ds_read_b32 v141, v9 offset:4608
	ds_read_b32 v142, v9 offset:5120
	ds_read_b32 v143, v9 offset:5632
	ds_read_b32 v144, v9 offset:6144
	ds_read_b32 v145, v9 offset:6656
	ds_read_b32 v146, v9 offset:7168
	ds_read_b32 v147, v9 offset:7680
	s_waitcnt lgkmcnt(0)
	v_max_f32_e32 v132, v132, v132
	v_max_f32_e32 v133, v133, v133
	v_max_f32_e32 v134, v134, v134
	v_max_f32_e32 v135, v135, v135
	v_max_f32_e32 v136, v136, v136
	v_max_f32_e32 v137, v137, v137
	v_max_f32_e32 v138, v138, v138
	v_max_f32_e32 v139, v139, v139
	v_max_f32_e32 v140, v140, v140
	v_max_f32_e32 v141, v141, v141
	v_max_f32_e32 v142, v142, v142
	v_max_f32_e32 v143, v143, v143
	v_max_f32_e32 v144, v144, v144
	v_max_f32_e32 v145, v145, v145
	v_max_f32_e32 v146, v146, v146
	v_max_f32_e32 v147, v147, v147
	v_med3_f32 v132, v132, s20, v13
	v_med3_f32 v133, v133, s20, v13
	v_med3_f32 v134, v134, s20, v13
	v_med3_f32 v135, v135, s20, v13
	v_med3_f32 v136, v136, s20, v13
	v_med3_f32 v137, v137, s20, v13
	v_med3_f32 v138, v138, s20, v13
	v_med3_f32 v139, v139, s20, v13
	v_med3_f32 v140, v140, s20, v13
	v_med3_f32 v141, v141, s20, v13
	v_med3_f32 v142, v142, s20, v13
	v_med3_f32 v143, v143, s20, v13
	v_med3_f32 v144, v144, s20, v13
	v_med3_f32 v145, v145, s20, v13
	v_med3_f32 v146, v146, s20, v13
	v_med3_f32 v147, v147, s20, v13
	v_mov_b32_e32 v148, 0
	v_mov_b32_e32 v149, 0
	v_mov_b32_e32 v150, 0
	v_mov_b32_e32 v151, 0
	v_cvt_pk_fp8_f32 v148, v132, v133
	v_cvt_pk_fp8_f32 v149, v136, v137
	v_cvt_pk_fp8_f32 v150, v140, v141
	v_cvt_pk_fp8_f32 v151, v144, v145
	v_cvt_pk_fp8_f32 v148, v134, v135 op_sel:[0,0,1]
	v_cvt_pk_fp8_f32 v149, v138, v139 op_sel:[0,0,1]
	v_cvt_pk_fp8_f32 v150, v142, v143 op_sel:[0,0,1]
	v_cvt_pk_fp8_f32 v151, v146, v147 op_sel:[0,0,1]
	s_nop 0
	global_store_dwordx4 v12, v[148:151], s[14:15]
	s_waitcnt vmcnt(22)
	v_mul_f32_e32 v68, 0x43000000, v68
	v_mul_f32_e32 v69, 0x43000000, v69
	v_mul_f32_e32 v70, 0x43000000, v70
	v_mul_f32_e32 v71, 0x43000000, v71
	ds_write_b128 v4, v[68:71]
	v_mul_f32_e32 v72, 0x43000000, v72
	v_mul_f32_e32 v73, 0x43000000, v73
	v_mul_f32_e32 v74, 0x43000000, v74
	v_mul_f32_e32 v75, 0x43000000, v75
	ds_write_b128 v4, v[72:75] offset:1024
	v_mul_f32_e32 v76, 0x43000000, v76
	v_mul_f32_e32 v77, 0x43000000, v77
	v_mul_f32_e32 v78, 0x43000000, v78
	v_mul_f32_e32 v79, 0x43000000, v79
	ds_write_b128 v4, v[76:79] offset:2048
	v_mul_f32_e32 v80, 0x43000000, v80
	v_mul_f32_e32 v81, 0x43000000, v81
	v_mul_f32_e32 v82, 0x43000000, v82
	v_mul_f32_e32 v83, 0x43000000, v83
	ds_write_b128 v4, v[80:83] offset:3072
	v_mul_f32_e32 v84, 0x43000000, v84
	v_mul_f32_e32 v85, 0x43000000, v85
	v_mul_f32_e32 v86, 0x43000000, v86
	v_mul_f32_e32 v87, 0x43000000, v87
	ds_write_b128 v4, v[84:87] offset:4096
	v_mul_f32_e32 v88, 0x43000000, v88
	v_mul_f32_e32 v89, 0x43000000, v89
	v_mul_f32_e32 v90, 0x43000000, v90
	v_mul_f32_e32 v91, 0x43000000, v91
	ds_write_b128 v4, v[88:91] offset:5120
	v_mul_f32_e32 v92, 0x43000000, v92
	v_mul_f32_e32 v93, 0x43000000, v93
	v_mul_f32_e32 v94, 0x43000000, v94
	v_mul_f32_e32 v95, 0x43000000, v95
	ds_write_b128 v4, v[92:95] offset:6144
	v_mul_f32_e32 v96, 0x43000000, v96
	v_mul_f32_e32 v97, 0x43000000, v97
	v_mul_f32_e32 v98, 0x43000000, v98
	v_mul_f32_e32 v99, 0x43000000, v99
	ds_write_b128 v4, v[96:99] offset:7168
	s_waitcnt lgkmcnt(0)
	s_barrier
; #define GAS __attribute__((address_space(1)))
; #define LAS __attribute__((address_space(3)))
; #define LDS_WAIT() asm volatile("s_waitcnt lgkmcnt(0)" ::: "memory")
; __device__ __forceinline__ unsigned pk4_fp8(float a, float b, float c, float d) {
;     a = fminf(fmaxf(a, -448.f), 448.f); b = fminf(fmaxf(b, -448.f), 448.f); c = fminf(fmaxf(c, -448.f), 448.f); d = fminf(fmaxf(d, -448.f), 448.f);
;     int w = __builtin_amdgcn_cvt_pk_fp8_f32(a, b, 0, false); w = __builtin_amdgcn_cvt_pk_fp8_f32(c, d, w, true); return (unsigned)w; }
;     const int pr = item >> 1, kb = 2 * (pr / nblk) + (item & 1), nb = pr % nblk, k0 = 64 * kb, n0 = 32 * nb;
;     const int nr = n0 + (lane & 31); const int sc = MAP == 1 ? src_col_in(nr) : nr;
;     float v[32];
; #pragma unroll
;     for (int i = 0; i < 32; ++i) v[i] = sc >= 0 ? W[(size_t)(k0 + 2 * i + (lane >> 5)) * Nsrc + sc] : 0.f;
; #pragma unroll
;     for (int i = 0; i < 32; ++i) { const int k = k0 + 2 * i + (lane >> 5); float x = v[i] * wscale; if (KS) x *= (k < ksplit ? ksA[k] : ksB[k - ksplit]); scr[(2 * i + (lane >> 5)) * 33 + (lane & 31)] = x; }
;     LDS_WAIT(); asm volatile("" ::: "memory");
;     const int c = lane & 7;
; #pragma unroll
;     for (int j = 0; j < 4; ++j) { const int n = (lane >> 3) + 8 * j; const LAS float* s = scr + (8 * c) * 33 + n;
;         const unsigned long long o = (unsigned long long)pg8::pk4_fp8(s[0 * 33], s[1 * 33], s[2 * 33], s[3 * 33]) | ((unsigned long long)pg8::pk4_fp8(s[4 * 33], s[5 * 33], s[6 * 33], s[7 * 33]) << 32);
;         *(GAS unsigned long long*)(WT + (size_t)(n0 + n) * K + k0 + 8 * c) = o; }
;     LDS_WAIT(); asm volatile("" ::: "memory");
; }
	s_add_i32 s17, s16, 672
	s_min_u32 s17, s17, 0xbff
	s_lshr_b32 s18, s17, 5
	s_add_i32 s18, s18, 32
	s_and_b32 s19, s17, 31
	s_lshl_b32 s18, s18, 21
	s_lshl_b32 s19, s19, 9
	s_add_u32 s18, s18, s19
	s_add_u32 s12, s2, s18
	s_addc_u32 s13, s3, 0
	global_load_dwordx4 v[68:71], v10, s[12:13]
	s_add_u32 s12, s12, 0x8000
	s_addc_u32 s13, s13, 0
	global_load_dwordx4 v[72:75], v10, s[12:13]
	s_add_u32 s12, s12, 0x8000
	s_addc_u32 s13, s13, 0
	global_load_dwordx4 v[76:79], v10, s[12:13]
	s_add_u32 s12, s12, 0x8000
	s_addc_u32 s13, s13, 0
	global_load_dwordx4 v[80:83], v10, s[12:13]
	s_add_u32 s12, s12, 0x8000
	s_addc_u32 s13, s13, 0
	global_load_dwordx4 v[84:87], v10, s[12:13]
	s_add_u32 s12, s12, 0x8000
	s_addc_u32 s13, s13, 0
	global_load_dwordx4 v[88:91], v10, s[12:13]
	s_add_u32 s12, s12, 0x8000
	s_addc_u32 s13, s13, 0
	global_load_dwordx4 v[92:95], v10, s[12:13]
	s_add_u32 s12, s12, 0x8000
	s_addc_u32 s13, s13, 0
	global_load_dwordx4 v[96:99], v10, s[12:13]
	s_add_i32 s17, s16, 384
	s_min_u32 s17, s17, 0xbff
	s_lshr_b32 s18, s17, 5
	s_add_i32 s18, s18, 32
	s_and_b32 s19, s17, 31
	s_lshl_b32 s19, s19, 21
	s_lshl_b32 s18, s18, 7
	s_add_u32 s18, s18, s19
	s_add_u32 s14, s4, s18
	s_addc_u32 s15, s5, 0
	ds_read_b32 v132, v6
	ds_read_b32 v133, v6 offset:512
	ds_read_b32 v134, v6 offset:1024
	ds_read_b32 v135, v6 offset:1536
	ds_read_b32 v136, v6 offset:2048
	ds_read_b32 v137, v6 offset:2560
	ds_read_b32 v138, v6 offset:3072
	ds_read_b32 v139, v6 offset:3584
	ds_read_b32 v140, v6 offset:4096
	ds_read_b32 v141, v6 offset:4608
	ds_read_b32 v142, v6 offset:5120
	ds_read_b32 v143, v6 offset:5632
	ds_read_b32 v144, v6 offset:6144
	ds_read_b32 v145, v6 offset:6656
	ds_read_b32 v146, v6 offset:7168
	ds_read_b32 v147, v6 offset:7680
	s_waitcnt lgkmcnt(0)
	v_max_f32_e32 v132, v132, v132
	v_max_f32_e32 v133, v133, v133
	v_max_f32_e32 v134, v134, v134
	v_max_f32_e32 v135, v135, v135
	v_max_f32_e32 v136, v136, v136
	v_max_f32_e32 v137, v137, v137
	v_max_f32_e32 v138, v138, v138
	v_max_f32_e32 v139, v139, v139
	v_max_f32_e32 v140, v140, v140
	v_max_f32_e32 v141, v141, v141
	v_max_f32_e32 v142, v142, v142
	v_max_f32_e32 v143, v143, v143
	v_max_f32_e32 v144, v144, v144
	v_max_f32_e32 v145, v145, v145
	v_max_f32_e32 v146, v146, v146
	v_max_f32_e32 v147, v147, v147
	v_med3_f32 v132, v132, s20, v13
	v_med3_f32 v133, v133, s20, v13
	v_med3_f32 v134, v134, s20, v13
	v_med3_f32 v135, v135, s20, v13
	v_med3_f32 v136, v136, s20, v13
	v_med3_f32 v137, v137, s20, v13
	v_med3_f32 v138, v138, s20, v13
	v_med3_f32 v139, v139, s20, v13
	v_med3_f32 v140, v140, s20, v13
	v_med3_f32 v141, v141, s20, v13
	v_med3_f32 v142, v142, s20, v13
	v_med3_f32 v143, v143, s20, v13
	v_med3_f32 v144, v144, s20, v13
	v_med3_f32 v145, v145, s20, v13
	v_med3_f32 v146, v146, s20, v13
	v_med3_f32 v147, v147, s20, v13
	v_mov_b32_e32 v148, 0
	v_mov_b32_e32 v149, 0
	v_mov_b32_e32 v150, 0
	v_mov_b32_e32 v151, 0
	v_cvt_pk_fp8_f32 v148, v132, v133
	v_cvt_pk_fp8_f32 v149, v136, v137
	v_cvt_pk_fp8_f32 v150, v140, v141
	v_cvt_pk_fp8_f32 v151, v144, v145
	v_cvt_pk_fp8_f32 v148, v134, v135 op_sel:[0,0,1]
	v_cvt_pk_fp8_f32 v149, v138, v139 op_sel:[0,0,1]
	v_cvt_pk_fp8_f32 v150, v142, v143 op_sel:[0,0,1]
	v_cvt_pk_fp8_f32 v151, v146, v147 op_sel:[0,0,1]
	s_nop 0
	global_store_dwordx4 v11, v[148:151], s[14:15]
	ds_read_b32 v132, v8
	ds_read_b32 v133, v8 offset:512
	ds_read_b32 v134, v8 offset:1024
	ds_read_b32 v135, v8 offset:1536
	ds_read_b32 v136, v8 offset:2048
	ds_read_b32 v137, v8 offset:2560
	ds_read_b32 v138, v8 offset:3072
	ds_read_b32 v139, v8 offset:3584
	ds_read_b32 v140, v8 offset:4096
	ds_read_b32 v141, v8 offset:4608
	ds_read_b32 v142, v8 offset:5120
	ds_read_b32 v143, v8 offset:5632
	ds_read_b32 v144, v8 offset:6144
	ds_read_b32 v145, v8 offset:6656
	ds_read_b32 v146, v8 offset:7168
	ds_read_b32 v147, v8 offset:7680
	s_waitcnt lgkmcnt(0)
	v_max_f32_e32 v132, v132, v132
	v_max_f32_e32 v133, v133, v133
	v_max_f32_e32 v134, v134, v134
	v_max_f32_e32 v135, v135, v135
	v_max_f32_e32 v136, v136, v136
	v_max_f32_e32 v137, v137, v137
	v_max_f32_e32 v138, v138, v138
	v_max_f32_e32 v139, v139, v139
	v_max_f32_e32 v140, v140, v140
	v_max_f32_e32 v141, v141, v141
	v_max_f32_e32 v142, v142, v142
	v_max_f32_e32 v143, v143, v143
	v_max_f32_e32 v144, v144, v144
	v_max_f32_e32 v145, v145, v145
	v_max_f32_e32 v146, v146, v146
	v_max_f32_e32 v147, v147, v147
	v_med3_f32 v132, v132, s20, v13
	v_med3_f32 v133, v133, s20, v13
	v_med3_f32 v134, v134, s20, v13
	v_med3_f32 v135, v135, s20, v13
	v_med3_f32 v136, v136, s20, v13
	v_med3_f32 v137, v137, s20, v13
	v_med3_f32 v138, v138, s20, v13
	v_med3_f32 v139, v139, s20, v13
	v_med3_f32 v140, v140, s20, v13
	v_med3_f32 v141, v141, s20, v13
	v_med3_f32 v142, v142, s20, v13
	v_med3_f32 v143, v143, s20, v13
	v_med3_f32 v144, v144, s20, v13
	v_med3_f32 v145, v145, s20, v13
	v_med3_f32 v146, v146, s20, v13
	v_med3_f32 v147, v147, s20, v13
	v_mov_b32_e32 v148, 0
	v_mov_b32_e32 v149, 0
	v_mov_b32_e32 v150, 0
	v_mov_b32_e32 v151, 0
	v_cvt_pk_fp8_f32 v148, v132, v133
	v_cvt_pk_fp8_f32 v149, v136, v137
	v_cvt_pk_fp8_f32 v150, v140, v141
	v_cvt_pk_fp8_f32 v151, v144, v145
	v_cvt_pk_fp8_f32 v148, v134, v135 op_sel:[0,0,1]
	v_cvt_pk_fp8_f32 v149, v138, v139 op_sel:[0,0,1]
	v_cvt_pk_fp8_f32 v150, v142, v143 op_sel:[0,0,1]
	v_cvt_pk_fp8_f32 v151, v146, v147 op_sel:[0,0,1]
	s_nop 0
	global_store_dwordx4 v12, v[148:151], s[14:15]
	s_waitcnt vmcnt(22)
	v_mul_f32_e32 v100, 0x43000000, v100
	v_mul_f32_e32 v101, 0x43000000, v101
	v_mul_f32_e32 v102, 0x43000000, v102
	v_mul_f32_e32 v103, 0x43000000, v103
	ds_write_b128 v5, v[100:103]
	v_mul_f32_e32 v104, 0x43000000, v104
	v_mul_f32_e32 v105, 0x43000000, v105
	v_mul_f32_e32 v106, 0x43000000, v106
	v_mul_f32_e32 v107, 0x43000000, v107
	ds_write_b128 v5, v[104:107] offset:1024
	v_mul_f32_e32 v108, 0x43000000, v108
	v_mul_f32_e32 v109, 0x43000000, v109
	v_mul_f32_e32 v110, 0x43000000, v110
	v_mul_f32_e32 v111, 0x43000000, v111
	ds_write_b128 v5, v[108:111] offset:2048
	v_mul_f32_e32 v112, 0x43000000, v112
	v_mul_f32_e32 v113, 0x43000000, v113
	v_mul_f32_e32 v114, 0x43000000, v114
	v_mul_f32_e32 v115, 0x43000000, v115
	ds_write_b128 v5, v[112:115] offset:3072
	v_mul_f32_e32 v116, 0x43000000, v116
	v_mul_f32_e32 v117, 0x43000000, v117
	v_mul_f32_e32 v118, 0x43000000, v118
	v_mul_f32_e32 v119, 0x43000000, v119
	ds_write_b128 v5, v[116:119] offset:4096
	v_mul_f32_e32 v120, 0x43000000, v120
	v_mul_f32_e32 v121, 0x43000000, v121
	v_mul_f32_e32 v122, 0x43000000, v122
	v_mul_f32_e32 v123, 0x43000000, v123
	ds_write_b128 v5, v[120:123] offset:5120
	v_mul_f32_e32 v124, 0x43000000, v124
	v_mul_f32_e32 v125, 0x43000000, v125
	v_mul_f32_e32 v126, 0x43000000, v126
	v_mul_f32_e32 v127, 0x43000000, v127
	ds_write_b128 v5, v[124:127] offset:6144
	v_mul_f32_e32 v128, 0x43000000, v128
	v_mul_f32_e32 v129, 0x43000000, v129
	v_mul_f32_e32 v130, 0x43000000, v130
	v_mul_f32_e32 v131, 0x43000000, v131
	ds_write_b128 v5, v[128:131] offset:7168
	s_waitcnt lgkmcnt(0)
	s_barrier
; #define GAS __attribute__((address_space(1)))
; #define LAS __attribute__((address_space(3)))
; #define LDS_WAIT() asm volatile("s_waitcnt lgkmcnt(0)" ::: "memory")
; __device__ __forceinline__ unsigned pk4_fp8(float a, float b, float c, float d) {
;     a = fminf(fmaxf(a, -448.f), 448.f); b = fminf(fmaxf(b, -448.f), 448.f); c = fminf(fmaxf(c, -448.f), 448.f); d = fminf(fmaxf(d, -448.f), 448.f);
;     int w = __builtin_amdgcn_cvt_pk_fp8_f32(a, b, 0, false); w = __builtin_amdgcn_cvt_pk_fp8_f32(c, d, w, true); return (unsigned)w; }
;     const int pr = item >> 1, kb = 2 * (pr / nblk) + (item & 1), nb = pr % nblk, k0 = 64 * kb, n0 = 32 * nb;
;     const int nr = n0 + (lane & 31); const int sc = MAP == 1 ? src_col_in(nr) : nr;
;     float v[32];
; #pragma unroll
;     for (int i = 0; i < 32; ++i) v[i] = sc >= 0 ? W[(size_t)(k0 + 2 * i + (lane >> 5)) * Nsrc + sc] : 0.f;
; #pragma unroll
;     for (int i = 0; i < 32; ++i) { const int k = k0 + 2 * i + (lane >> 5); float x = v[i] * wscale; if (KS) x *= (k < ksplit ? ksA[k] : ksB[k - ksplit]); scr[(2 * i + (lane >> 5)) * 33 + (lane & 31)] = x; }
;     LDS_WAIT(); asm volatile("" ::: "memory");
;     const int c = lane & 7;
; #pragma unroll
;     for (int j = 0; j < 4; ++j) { const int n = (lane >> 3) + 8 * j; const LAS float* s = scr + (8 * c) * 33 + n;
;         const unsigned long long o = (unsigned long long)pg8::pk4_fp8(s[0 * 33], s[1 * 33], s[2 * 33], s[3 * 33]) | ((unsigned long long)pg8::pk4_fp8(s[4 * 33], s[5 * 33], s[6 * 33], s[7 * 33]) << 32);
;         *(GAS unsigned long long*)(WT + (size_t)(n0 + n) * K + k0 + 8 * c) = o; }
;     LDS_WAIT(); asm volatile("" ::: "memory");
; }
	s_add_i32 s17, s16, 768
	s_min_u32 s17, s17, 0xbff
	s_lshr_b32 s18, s17, 5
	s_add_i32 s18, s18, 32
	s_and_b32 s19, s17, 31
	s_lshl_b32 s18, s18, 21
	s_lshl_b32 s19, s19, 9
	s_add_u32 s18, s18, s19
	s_add_u32 s12, s2, s18
	s_addc_u32 s13, s3, 0
	global_load_dwordx4 v[100:103], v10, s[12:13]
	s_add_u32 s12, s12, 0x8000
	s_addc_u32 s13, s13, 0
	global_load_dwordx4 v[104:107], v10, s[12:13]
	s_add_u32 s12, s12, 0x8000
	s_addc_u32 s13, s13, 0
	global_load_dwordx4 v[108:111], v10, s[12:13]
	s_add_u32 s12, s12, 0x8000
	s_addc_u32 s13, s13, 0
	global_load_dwordx4 v[112:115], v10, s[12:13]
	s_add_u32 s12, s12, 0x8000
	s_addc_u32 s13, s13, 0
	global_load_dwordx4 v[116:119], v10, s[12:13]
	s_add_u32 s12, s12, 0x8000
	s_addc_u32 s13, s13, 0
	global_load_dwordx4 v[120:123], v10, s[12:13]
	s_add_u32 s12, s12, 0x8000
	s_addc_u32 s13, s13, 0
	global_load_dwordx4 v[124:127], v10, s[12:13]
	s_add_u32 s12, s12, 0x8000
	s_addc_u32 s13, s13, 0
	global_load_dwordx4 v[128:131], v10, s[12:13]
	s_add_i32 s17, s16, 480
	s_min_u32 s17, s17, 0xbff
	s_lshr_b32 s18, s17, 5
	s_add_i32 s18, s18, 32
	s_and_b32 s19, s17, 31
	s_lshl_b32 s19, s19, 21
	s_lshl_b32 s18, s18, 7
	s_add_u32 s18, s18, s19
	s_add_u32 s14, s4, s18
	s_addc_u32 s15, s5, 0
	ds_read_b32 v132, v7
	ds_read_b32 v133, v7 offset:512
	ds_read_b32 v134, v7 offset:1024
	ds_read_b32 v135, v7 offset:1536
	ds_read_b32 v136, v7 offset:2048
	ds_read_b32 v137, v7 offset:2560
	ds_read_b32 v138, v7 offset:3072
	ds_read_b32 v139, v7 offset:3584
	ds_read_b32 v140, v7 offset:4096
	ds_read_b32 v141, v7 offset:4608
	ds_read_b32 v142, v7 offset:5120
	ds_read_b32 v143, v7 offset:5632
	ds_read_b32 v144, v7 offset:6144
	ds_read_b32 v145, v7 offset:6656
	ds_read_b32 v146, v7 offset:7168
	ds_read_b32 v147, v7 offset:7680
	s_waitcnt lgkmcnt(0)
	v_max_f32_e32 v132, v132, v132
	v_max_f32_e32 v133, v133, v133
	v_max_f32_e32 v134, v134, v134
	v_max_f32_e32 v135, v135, v135
	v_max_f32_e32 v136, v136, v136
	v_max_f32_e32 v137, v137, v137
	v_max_f32_e32 v138, v138, v138
	v_max_f32_e32 v139, v139, v139
	v_max_f32_e32 v140, v140, v140
	v_max_f32_e32 v141, v141, v141
	v_max_f32_e32 v142, v142, v142
	v_max_f32_e32 v143, v143, v143
	v_max_f32_e32 v144, v144, v144
	v_max_f32_e32 v145, v145, v145
	v_max_f32_e32 v146, v146, v146
	v_max_f32_e32 v147, v147, v147
	v_med3_f32 v132, v132, s20, v13
	v_med3_f32 v133, v133, s20, v13
	v_med3_f32 v134, v134, s20, v13
	v_med3_f32 v135, v135, s20, v13
	v_med3_f32 v136, v136, s20, v13
	v_med3_f32 v137, v137, s20, v13
	v_med3_f32 v138, v138, s20, v13
	v_med3_f32 v139, v139, s20, v13
	v_med3_f32 v140, v140, s20, v13
	v_med3_f32 v141, v141, s20, v13
	v_med3_f32 v142, v142, s20, v13
	v_med3_f32 v143, v143, s20, v13
	v_med3_f32 v144, v144, s20, v13
	v_med3_f32 v145, v145, s20, v13
	v_med3_f32 v146, v146, s20, v13
	v_med3_f32 v147, v147, s20, v13
	v_mov_b32_e32 v148, 0
	v_mov_b32_e32 v149, 0
	v_mov_b32_e32 v150, 0
	v_mov_b32_e32 v151, 0
	v_cvt_pk_fp8_f32 v148, v132, v133
	v_cvt_pk_fp8_f32 v149, v136, v137
	v_cvt_pk_fp8_f32 v150, v140, v141
	v_cvt_pk_fp8_f32 v151, v144, v145
	v_cvt_pk_fp8_f32 v148, v134, v135 op_sel:[0,0,1]
	v_cvt_pk_fp8_f32 v149, v138, v139 op_sel:[0,0,1]
	v_cvt_pk_fp8_f32 v150, v142, v143 op_sel:[0,0,1]
	v_cvt_pk_fp8_f32 v151, v146, v147 op_sel:[0,0,1]
	s_nop 0
	global_store_dwordx4 v11, v[148:151], s[14:15]
	ds_read_b32 v132, v9
	ds_read_b32 v133, v9 offset:512
	ds_read_b32 v134, v9 offset:1024
	ds_read_b32 v135, v9 offset:1536
	ds_read_b32 v136, v9 offset:2048
	ds_read_b32 v137, v9 offset:2560
	ds_read_b32 v138, v9 offset:3072
	ds_read_b32 v139, v9 offset:3584
	ds_read_b32 v140, v9 offset:4096
	ds_read_b32 v141, v9 offset:4608
	ds_read_b32 v142, v9 offset:5120
	ds_read_b32 v143, v9 offset:5632
	ds_read_b32 v144, v9 offset:6144
	ds_read_b32 v145, v9 offset:6656
	ds_read_b32 v146, v9 offset:7168
	ds_read_b32 v147, v9 offset:7680
	s_waitcnt lgkmcnt(0)
	v_max_f32_e32 v132, v132, v132
	v_max_f32_e32 v133, v133, v133
	v_max_f32_e32 v134, v134, v134
	v_max_f32_e32 v135, v135, v135
	v_max_f32_e32 v136, v136, v136
	v_max_f32_e32 v137, v137, v137
	v_max_f32_e32 v138, v138, v138
	v_max_f32_e32 v139, v139, v139
	v_max_f32_e32 v140, v140, v140
	v_max_f32_e32 v141, v141, v141
	v_max_f32_e32 v142, v142, v142
	v_max_f32_e32 v143, v143, v143
	v_max_f32_e32 v144, v144, v144
	v_max_f32_e32 v145, v145, v145
	v_max_f32_e32 v146, v146, v146
	v_max_f32_e32 v147, v147, v147
	v_med3_f32 v132, v132, s20, v13
	v_med3_f32 v133, v133, s20, v13
	v_med3_f32 v134, v134, s20, v13
	v_med3_f32 v135, v135, s20, v13
	v_med3_f32 v136, v136, s20, v13
	v_med3_f32 v137, v137, s20, v13
	v_med3_f32 v138, v138, s20, v13
	v_med3_f32 v139, v139, s20, v13
	v_med3_f32 v140, v140, s20, v13
	v_med3_f32 v141, v141, s20, v13
	v_med3_f32 v142, v142, s20, v13
	v_med3_f32 v143, v143, s20, v13
	v_med3_f32 v144, v144, s20, v13
	v_med3_f32 v145, v145, s20, v13
	v_med3_f32 v146, v146, s20, v13
	v_med3_f32 v147, v147, s20, v13
	v_mov_b32_e32 v148, 0
	v_mov_b32_e32 v149, 0
	v_mov_b32_e32 v150, 0
	v_mov_b32_e32 v151, 0
	v_cvt_pk_fp8_f32 v148, v132, v133
	v_cvt_pk_fp8_f32 v149, v136, v137
	v_cvt_pk_fp8_f32 v150, v140, v141
	v_cvt_pk_fp8_f32 v151, v144, v145
	v_cvt_pk_fp8_f32 v148, v134, v135 op_sel:[0,0,1]
	v_cvt_pk_fp8_f32 v149, v138, v139 op_sel:[0,0,1]
	v_cvt_pk_fp8_f32 v150, v142, v143 op_sel:[0,0,1]
	v_cvt_pk_fp8_f32 v151, v146, v147 op_sel:[0,0,1]
	s_nop 0
	global_store_dwordx4 v12, v[148:151], s[14:15]
	s_waitcnt vmcnt(22)
	v_mul_f32_e32 v36, 0x43000000, v36
	v_mul_f32_e32 v37, 0x43000000, v37
	v_mul_f32_e32 v38, 0x43000000, v38
	v_mul_f32_e32 v39, 0x43000000, v39
	ds_write_b128 v4, v[36:39]
	v_mul_f32_e32 v40, 0x43000000, v40
	v_mul_f32_e32 v41, 0x43000000, v41
	v_mul_f32_e32 v42, 0x43000000, v42
	v_mul_f32_e32 v43, 0x43000000, v43
	ds_write_b128 v4, v[40:43] offset:1024
	v_mul_f32_e32 v44, 0x43000000, v44
	v_mul_f32_e32 v45, 0x43000000, v45
	v_mul_f32_e32 v46, 0x43000000, v46
	v_mul_f32_e32 v47, 0x43000000, v47
	ds_write_b128 v4, v[44:47] offset:2048
	v_mul_f32_e32 v48, 0x43000000, v48
	v_mul_f32_e32 v49, 0x43000000, v49
	v_mul_f32_e32 v50, 0x43000000, v50
	v_mul_f32_e32 v51, 0x43000000, v51
	ds_write_b128 v4, v[48:51] offset:3072
	v_mul_f32_e32 v52, 0x43000000, v52
	v_mul_f32_e32 v53, 0x43000000, v53
	v_mul_f32_e32 v54, 0x43000000, v54
	v_mul_f32_e32 v55, 0x43000000, v55
	ds_write_b128 v4, v[52:55] offset:4096
	v_mul_f32_e32 v56, 0x43000000, v56
	v_mul_f32_e32 v57, 0x43000000, v57
	v_mul_f32_e32 v58, 0x43000000, v58
	v_mul_f32_e32 v59, 0x43000000, v59
	ds_write_b128 v4, v[56:59] offset:5120
	v_mul_f32_e32 v60, 0x43000000, v60
	v_mul_f32_e32 v61, 0x43000000, v61
	v_mul_f32_e32 v62, 0x43000000, v62
	v_mul_f32_e32 v63, 0x43000000, v63
	ds_write_b128 v4, v[60:63] offset:6144
	v_mul_f32_e32 v64, 0x43000000, v64
	v_mul_f32_e32 v65, 0x43000000, v65
	v_mul_f32_e32 v66, 0x43000000, v66
	v_mul_f32_e32 v67, 0x43000000, v67
	ds_write_b128 v4, v[64:67] offset:7168
	s_waitcnt lgkmcnt(0)
	s_barrier
; #define GAS __attribute__((address_space(1)))
; #define LAS __attribute__((address_space(3)))
; #define LDS_WAIT() asm volatile("s_waitcnt lgkmcnt(0)" ::: "memory")
; __device__ __forceinline__ unsigned pk4_fp8(float a, float b, float c, float d) {
;     a = fminf(fmaxf(a, -448.f), 448.f); b = fminf(fmaxf(b, -448.f), 448.f); c = fminf(fmaxf(c, -448.f), 448.f); d = fminf(fmaxf(d, -448.f), 448.f);
;     int w = __builtin_amdgcn_cvt_pk_fp8_f32(a, b, 0, false); w = __builtin_amdgcn_cvt_pk_fp8_f32(c, d, w, true); return (unsigned)w; }
;     const int pr = item >> 1, kb = 2 * (pr / nblk) + (item & 1), nb = pr % nblk, k0 = 64 * kb, n0 = 32 * nb;
;     const int nr = n0 + (lane & 31); const int sc = MAP == 1 ? src_col_in(nr) : nr;
;     float v[32];
; #pragma unroll
;     for (int i = 0; i < 32; ++i) v[i] = sc >= 0 ? W[(size_t)(k0 + 2 * i + (lane >> 5)) * Nsrc + sc] : 0.f;
; #pragma unroll
;     for (int i = 0; i < 32; ++i) { const int k = k0 + 2 * i + (lane >> 5); float x = v[i] * wscale; if (KS) x *= (k < ksplit ? ksA[k] : ksB[k - ksplit]); scr[(2 * i + (lane >> 5)) * 33 + (lane & 31)] = x; }
;     LDS_WAIT(); asm volatile("" ::: "memory");
;     const int c = lane & 7;
; #pragma unroll
;     for (int j = 0; j < 4; ++j) { const int n = (lane >> 3) + 8 * j; const LAS float* s = scr + (8 * c) * 33 + n;
;         const unsigned long long o = (unsigned long long)pg8::pk4_fp8(s[0 * 33], s[1 * 33], s[2 * 33], s[3 * 33]) | ((unsigned long long)pg8::pk4_fp8(s[4 * 33], s[5 * 33], s[6 * 33], s[7 * 33]) << 32);
;         *(GAS unsigned long long*)(WT + (size_t)(n0 + n) * K + k0 + 8 * c) = o; }
;     LDS_WAIT(); asm volatile("" ::: "memory");
; }
	s_add_i32 s17, s16, 864
	s_min_u32 s17, s17, 0xbff
	s_lshr_b32 s18, s17, 5
	s_add_i32 s18, s18, 32
	s_and_b32 s19, s17, 31
	s_lshl_b32 s18, s18, 21
	s_lshl_b32 s19, s19, 9
	s_add_u32 s18, s18, s19
	s_add_u32 s12, s2, s18
	s_addc_u32 s13, s3, 0
	global_load_dwordx4 v[36:39], v10, s[12:13]
	s_add_u32 s12, s12, 0x8000
	s_addc_u32 s13, s13, 0
	global_load_dwordx4 v[40:43], v10, s[12:13]
	s_add_u32 s12, s12, 0x8000
	s_addc_u32 s13, s13, 0
	global_load_dwordx4 v[44:47], v10, s[12:13]
	s_add_u32 s12, s12, 0x8000
	s_addc_u32 s13, s13, 0
	global_load_dwordx4 v[48:51], v10, s[12:13]
	s_add_u32 s12, s12, 0x8000
	s_addc_u32 s13, s13, 0
	global_load_dwordx4 v[52:55], v10, s[12:13]
	s_add_u32 s12, s12, 0x8000
	s_addc_u32 s13, s13, 0
	global_load_dwordx4 v[56:59], v10, s[12:13]
	s_add_u32 s12, s12, 0x8000
	s_addc_u32 s13, s13, 0
	global_load_dwordx4 v[60:63], v10, s[12:13]
	s_add_u32 s12, s12, 0x8000
	s_addc_u32 s13, s13, 0
	global_load_dwordx4 v[64:67], v10, s[12:13]
	s_add_i32 s17, s16, 576
	s_min_u32 s17, s17, 0xbff
	s_lshr_b32 s18, s17, 5
	s_add_i32 s18, s18, 32
	s_and_b32 s19, s17, 31
	s_lshl_b32 s19, s19, 21
	s_lshl_b32 s18, s18, 7
	s_add_u32 s18, s18, s19
	s_add_u32 s14, s4, s18
	s_addc_u32 s15, s5, 0
	ds_read_b32 v132, v6
	ds_read_b32 v133, v6 offset:512
	ds_read_b32 v134, v6 offset:1024
	ds_read_b32 v135, v6 offset:1536
	ds_read_b32 v136, v6 offset:2048
	ds_read_b32 v137, v6 offset:2560
	ds_read_b32 v138, v6 offset:3072
	ds_read_b32 v139, v6 offset:3584
	ds_read_b32 v140, v6 offset:4096
	ds_read_b32 v141, v6 offset:4608
	ds_read_b32 v142, v6 offset:5120
	ds_read_b32 v143, v6 offset:5632
	ds_read_b32 v144, v6 offset:6144
	ds_read_b32 v145, v6 offset:6656
	ds_read_b32 v146, v6 offset:7168
	ds_read_b32 v147, v6 offset:7680
	s_waitcnt lgkmcnt(0)
	v_max_f32_e32 v132, v132, v132
	v_max_f32_e32 v133, v133, v133
	v_max_f32_e32 v134, v134, v134
	v_max_f32_e32 v135, v135, v135
	v_max_f32_e32 v136, v136, v136
	v_max_f32_e32 v137, v137, v137
	v_max_f32_e32 v138, v138, v138
	v_max_f32_e32 v139, v139, v139
	v_max_f32_e32 v140, v140, v140
	v_max_f32_e32 v141, v141, v141
	v_max_f32_e32 v142, v142, v142
	v_max_f32_e32 v143, v143, v143
	v_max_f32_e32 v144, v144, v144
	v_max_f32_e32 v145, v145, v145
	v_max_f32_e32 v146, v146, v146
	v_max_f32_e32 v147, v147, v147
	v_med3_f32 v132, v132, s20, v13
	v_med3_f32 v133, v133, s20, v13
	v_med3_f32 v134, v134, s20, v13
	v_med3_f32 v135, v135, s20, v13
	v_med3_f32 v136, v136, s20, v13
	v_med3_f32 v137, v137, s20, v13
	v_med3_f32 v138, v138, s20, v13
	v_med3_f32 v139, v139, s20, v13
	v_med3_f32 v140, v140, s20, v13
	v_med3_f32 v141, v141, s20, v13
	v_med3_f32 v142, v142, s20, v13
	v_med3_f32 v143, v143, s20, v13
	v_med3_f32 v144, v144, s20, v13
	v_med3_f32 v145, v145, s20, v13
	v_med3_f32 v146, v146, s20, v13
	v_med3_f32 v147, v147, s20, v13
	v_mov_b32_e32 v148, 0
	v_mov_b32_e32 v149, 0
	v_mov_b32_e32 v150, 0
	v_mov_b32_e32 v151, 0
	v_cvt_pk_fp8_f32 v148, v132, v133
	v_cvt_pk_fp8_f32 v149, v136, v137
	v_cvt_pk_fp8_f32 v150, v140, v141
	v_cvt_pk_fp8_f32 v151, v144, v145
	v_cvt_pk_fp8_f32 v148, v134, v135 op_sel:[0,0,1]
	v_cvt_pk_fp8_f32 v149, v138, v139 op_sel:[0,0,1]
	v_cvt_pk_fp8_f32 v150, v142, v143 op_sel:[0,0,1]
	v_cvt_pk_fp8_f32 v151, v146, v147 op_sel:[0,0,1]
	s_nop 0
	global_store_dwordx4 v11, v[148:151], s[14:15]
	ds_read_b32 v132, v8
	ds_read_b32 v133, v8 offset:512
	ds_read_b32 v134, v8 offset:1024
	ds_read_b32 v135, v8 offset:1536
	ds_read_b32 v136, v8 offset:2048
	ds_read_b32 v137, v8 offset:2560
	ds_read_b32 v138, v8 offset:3072
	ds_read_b32 v139, v8 offset:3584
	ds_read_b32 v140, v8 offset:4096
	ds_read_b32 v141, v8 offset:4608
	ds_read_b32 v142, v8 offset:5120
	ds_read_b32 v143, v8 offset:5632
	ds_read_b32 v144, v8 offset:6144
	ds_read_b32 v145, v8 offset:6656
	ds_read_b32 v146, v8 offset:7168
	ds_read_b32 v147, v8 offset:7680
	s_waitcnt lgkmcnt(0)
	v_max_f32_e32 v132, v132, v132
	v_max_f32_e32 v133, v133, v133
	v_max_f32_e32 v134, v134, v134
	v_max_f32_e32 v135, v135, v135
	v_max_f32_e32 v136, v136, v136
	v_max_f32_e32 v137, v137, v137
	v_max_f32_e32 v138, v138, v138
	v_max_f32_e32 v139, v139, v139
	v_max_f32_e32 v140, v140, v140
	v_max_f32_e32 v141, v141, v141
	v_max_f32_e32 v142, v142, v142
	v_max_f32_e32 v143, v143, v143
	v_max_f32_e32 v144, v144, v144
	v_max_f32_e32 v145, v145, v145
	v_max_f32_e32 v146, v146, v146
	v_max_f32_e32 v147, v147, v147
	v_med3_f32 v132, v132, s20, v13
	v_med3_f32 v133, v133, s20, v13
	v_med3_f32 v134, v134, s20, v13
	v_med3_f32 v135, v135, s20, v13
	v_med3_f32 v136, v136, s20, v13
	v_med3_f32 v137, v137, s20, v13
	v_med3_f32 v138, v138, s20, v13
	v_med3_f32 v139, v139, s20, v13
	v_med3_f32 v140, v140, s20, v13
	v_med3_f32 v141, v141, s20, v13
	v_med3_f32 v142, v142, s20, v13
	v_med3_f32 v143, v143, s20, v13
	v_med3_f32 v144, v144, s20, v13
	v_med3_f32 v145, v145, s20, v13
	v_med3_f32 v146, v146, s20, v13
	v_med3_f32 v147, v147, s20, v13
	v_mov_b32_e32 v148, 0
	v_mov_b32_e32 v149, 0
	v_mov_b32_e32 v150, 0
	v_mov_b32_e32 v151, 0
	v_cvt_pk_fp8_f32 v148, v132, v133
	v_cvt_pk_fp8_f32 v149, v136, v137
	v_cvt_pk_fp8_f32 v150, v140, v141
	v_cvt_pk_fp8_f32 v151, v144, v145
	v_cvt_pk_fp8_f32 v148, v134, v135 op_sel:[0,0,1]
	v_cvt_pk_fp8_f32 v149, v138, v139 op_sel:[0,0,1]
	v_cvt_pk_fp8_f32 v150, v142, v143 op_sel:[0,0,1]
	v_cvt_pk_fp8_f32 v151, v146, v147 op_sel:[0,0,1]
	s_nop 0
	global_store_dwordx4 v12, v[148:151], s[14:15]
	s_waitcnt vmcnt(22)
	v_mul_f32_e32 v68, 0x43000000, v68
	v_mul_f32_e32 v69, 0x43000000, v69
	v_mul_f32_e32 v70, 0x43000000, v70
	v_mul_f32_e32 v71, 0x43000000, v71
	ds_write_b128 v5, v[68:71]
	v_mul_f32_e32 v72, 0x43000000, v72
	v_mul_f32_e32 v73, 0x43000000, v73
	v_mul_f32_e32 v74, 0x43000000, v74
	v_mul_f32_e32 v75, 0x43000000, v75
	ds_write_b128 v5, v[72:75] offset:1024
	v_mul_f32_e32 v76, 0x43000000, v76
	v_mul_f32_e32 v77, 0x43000000, v77
	v_mul_f32_e32 v78, 0x43000000, v78
	v_mul_f32_e32 v79, 0x43000000, v79
	ds_write_b128 v5, v[76:79] offset:2048
	v_mul_f32_e32 v80, 0x43000000, v80
	v_mul_f32_e32 v81, 0x43000000, v81
	v_mul_f32_e32 v82, 0x43000000, v82
	v_mul_f32_e32 v83, 0x43000000, v83
	ds_write_b128 v5, v[80:83] offset:3072
	v_mul_f32_e32 v84, 0x43000000, v84
	v_mul_f32_e32 v85, 0x43000000, v85
	v_mul_f32_e32 v86, 0x43000000, v86
	v_mul_f32_e32 v87, 0x43000000, v87
	ds_write_b128 v5, v[84:87] offset:4096
	v_mul_f32_e32 v88, 0x43000000, v88
	v_mul_f32_e32 v89, 0x43000000, v89
	v_mul_f32_e32 v90, 0x43000000, v90
	v_mul_f32_e32 v91, 0x43000000, v91
	ds_write_b128 v5, v[88:91] offset:5120
	v_mul_f32_e32 v92, 0x43000000, v92
	v_mul_f32_e32 v93, 0x43000000, v93
	v_mul_f32_e32 v94, 0x43000000, v94
	v_mul_f32_e32 v95, 0x43000000, v95
	ds_write_b128 v5, v[92:95] offset:6144
	v_mul_f32_e32 v96, 0x43000000, v96
	v_mul_f32_e32 v97, 0x43000000, v97
	v_mul_f32_e32 v98, 0x43000000, v98
	v_mul_f32_e32 v99, 0x43000000, v99
	ds_write_b128 v5, v[96:99] offset:7168
	s_waitcnt lgkmcnt(0)
	s_barrier
; #define GAS __attribute__((address_space(1)))
; #define LAS __attribute__((address_space(3)))
; #define LDS_WAIT() asm volatile("s_waitcnt lgkmcnt(0)" ::: "memory")
; __device__ __forceinline__ unsigned pk4_fp8(float a, float b, float c, float d) {
;     a = fminf(fmaxf(a, -448.f), 448.f); b = fminf(fmaxf(b, -448.f), 448.f); c = fminf(fmaxf(c, -448.f), 448.f); d = fminf(fmaxf(d, -448.f), 448.f);
;     int w = __builtin_amdgcn_cvt_pk_fp8_f32(a, b, 0, false); w = __builtin_amdgcn_cvt_pk_fp8_f32(c, d, w, true); return (unsigned)w; }
;     const int pr = item >> 1, kb = 2 * (pr / nblk) + (item & 1), nb = pr % nblk, k0 = 64 * kb, n0 = 32 * nb;
;     const int nr = n0 + (lane & 31); const int sc = MAP == 1 ? src_col_in(nr) : nr;
;     float v[32];
; #pragma unroll
;     for (int i = 0; i < 32; ++i) v[i] = sc >= 0 ? W[(size_t)(k0 + 2 * i + (lane >> 5)) * Nsrc + sc] : 0.f;
; #pragma unroll
;     for (int i = 0; i < 32; ++i) { const int k = k0 + 2 * i + (lane >> 5); float x = v[i] * wscale; if (KS) x *= (k < ksplit ? ksA[k] : ksB[k - ksplit]); scr[(2 * i + (lane >> 5)) * 33 + (lane & 31)] = x; }
;     LDS_WAIT(); asm volatile("" ::: "memory");
;     const int c = lane & 7;
; #pragma unroll
;     for (int j = 0; j < 4; ++j) { const int n = (lane >> 3) + 8 * j; const LAS float* s = scr + (8 * c) * 33 + n;
;         const unsigned long long o = (unsigned long long)pg8::pk4_fp8(s[0 * 33], s[1 * 33], s[2 * 33], s[3 * 33]) | ((unsigned long long)pg8::pk4_fp8(s[4 * 33], s[5 * 33], s[6 * 33], s[7 * 33]) << 32);
;         *(GAS unsigned long long*)(WT + (size_t)(n0 + n) * K + k0 + 8 * c) = o; }
;     LDS_WAIT(); asm volatile("" ::: "memory");
; }
	s_add_i32 s17, s16, 960
	s_min_u32 s17, s17, 0xbff
	s_lshr_b32 s18, s17, 5
	s_add_i32 s18, s18, 32
	s_and_b32 s19, s17, 31
	s_lshl_b32 s18, s18, 21
	s_lshl_b32 s19, s19, 9
	s_add_u32 s18, s18, s19
	s_add_u32 s12, s2, s18
	s_addc_u32 s13, s3, 0
	global_load_dwordx4 v[68:71], v10, s[12:13]
	s_add_u32 s12, s12, 0x8000
	s_addc_u32 s13, s13, 0
	global_load_dwordx4 v[72:75], v10, s[12:13]
	s_add_u32 s12, s12, 0x8000
	s_addc_u32 s13, s13, 0
	global_load_dwordx4 v[76:79], v10, s[12:13]
	s_add_u32 s12, s12, 0x8000
	s_addc_u32 s13, s13, 0
	global_load_dwordx4 v[80:83], v10, s[12:13]
	s_add_u32 s12, s12, 0x8000
	s_addc_u32 s13, s13, 0
	global_load_dwordx4 v[84:87], v10, s[12:13]
	s_add_u32 s12, s12, 0x8000
	s_addc_u32 s13, s13, 0
	global_load_dwordx4 v[88:91], v10, s[12:13]
	s_add_u32 s12, s12, 0x8000
	s_addc_u32 s13, s13, 0
	global_load_dwordx4 v[92:95], v10, s[12:13]
	s_add_u32 s12, s12, 0x8000
	s_addc_u32 s13, s13, 0
	global_load_dwordx4 v[96:99], v10, s[12:13]
	s_add_i32 s17, s16, 672
	s_min_u32 s17, s17, 0xbff
	s_lshr_b32 s18, s17, 5
	s_add_i32 s18, s18, 32
	s_and_b32 s19, s17, 31
	s_lshl_b32 s19, s19, 21
	s_lshl_b32 s18, s18, 7
	s_add_u32 s18, s18, s19
	s_add_u32 s14, s4, s18
	s_addc_u32 s15, s5, 0
	ds_read_b32 v132, v7
	ds_read_b32 v133, v7 offset:512
	ds_read_b32 v134, v7 offset:1024
	ds_read_b32 v135, v7 offset:1536
	ds_read_b32 v136, v7 offset:2048
	ds_read_b32 v137, v7 offset:2560
	ds_read_b32 v138, v7 offset:3072
	ds_read_b32 v139, v7 offset:3584
	ds_read_b32 v140, v7 offset:4096
	ds_read_b32 v141, v7 offset:4608
	ds_read_b32 v142, v7 offset:5120
	ds_read_b32 v143, v7 offset:5632
	ds_read_b32 v144, v7 offset:6144
	ds_read_b32 v145, v7 offset:6656
	ds_read_b32 v146, v7 offset:7168
	ds_read_b32 v147, v7 offset:7680
	s_waitcnt lgkmcnt(0)
	v_max_f32_e32 v132, v132, v132
	v_max_f32_e32 v133, v133, v133
	v_max_f32_e32 v134, v134, v134
	v_max_f32_e32 v135, v135, v135
	v_max_f32_e32 v136, v136, v136
	v_max_f32_e32 v137, v137, v137
	v_max_f32_e32 v138, v138, v138
	v_max_f32_e32 v139, v139, v139
	v_max_f32_e32 v140, v140, v140
	v_max_f32_e32 v141, v141, v141
	v_max_f32_e32 v142, v142, v142
	v_max_f32_e32 v143, v143, v143
	v_max_f32_e32 v144, v144, v144
	v_max_f32_e32 v145, v145, v145
	v_max_f32_e32 v146, v146, v146
	v_max_f32_e32 v147, v147, v147
	v_med3_f32 v132, v132, s20, v13
	v_med3_f32 v133, v133, s20, v13
	v_med3_f32 v134, v134, s20, v13
	v_med3_f32 v135, v135, s20, v13
	v_med3_f32 v136, v136, s20, v13
	v_med3_f32 v137, v137, s20, v13
	v_med3_f32 v138, v138, s20, v13
	v_med3_f32 v139, v139, s20, v13
	v_med3_f32 v140, v140, s20, v13
	v_med3_f32 v141, v141, s20, v13
	v_med3_f32 v142, v142, s20, v13
	v_med3_f32 v143, v143, s20, v13
	v_med3_f32 v144, v144, s20, v13
	v_med3_f32 v145, v145, s20, v13
	v_med3_f32 v146, v146, s20, v13
	v_med3_f32 v147, v147, s20, v13
	v_mov_b32_e32 v148, 0
	v_mov_b32_e32 v149, 0
	v_mov_b32_e32 v150, 0
	v_mov_b32_e32 v151, 0
	v_cvt_pk_fp8_f32 v148, v132, v133
	v_cvt_pk_fp8_f32 v149, v136, v137
	v_cvt_pk_fp8_f32 v150, v140, v141
	v_cvt_pk_fp8_f32 v151, v144, v145
	v_cvt_pk_fp8_f32 v148, v134, v135 op_sel:[0,0,1]
	v_cvt_pk_fp8_f32 v149, v138, v139 op_sel:[0,0,1]
	v_cvt_pk_fp8_f32 v150, v142, v143 op_sel:[0,0,1]
	v_cvt_pk_fp8_f32 v151, v146, v147 op_sel:[0,0,1]
	s_nop 0
	global_store_dwordx4 v11, v[148:151], s[14:15]
	ds_read_b32 v132, v9
	ds_read_b32 v133, v9 offset:512
	ds_read_b32 v134, v9 offset:1024
	ds_read_b32 v135, v9 offset:1536
	ds_read_b32 v136, v9 offset:2048
	ds_read_b32 v137, v9 offset:2560
	ds_read_b32 v138, v9 offset:3072
	ds_read_b32 v139, v9 offset:3584
	ds_read_b32 v140, v9 offset:4096
	ds_read_b32 v141, v9 offset:4608
	ds_read_b32 v142, v9 offset:5120
	ds_read_b32 v143, v9 offset:5632
	ds_read_b32 v144, v9 offset:6144
	ds_read_b32 v145, v9 offset:6656
	ds_read_b32 v146, v9 offset:7168
	ds_read_b32 v147, v9 offset:7680
	s_waitcnt lgkmcnt(0)
	v_max_f32_e32 v132, v132, v132
	v_max_f32_e32 v133, v133, v133
	v_max_f32_e32 v134, v134, v134
	v_max_f32_e32 v135, v135, v135
	v_max_f32_e32 v136, v136, v136
	v_max_f32_e32 v137, v137, v137
	v_max_f32_e32 v138, v138, v138
	v_max_f32_e32 v139, v139, v139
	v_max_f32_e32 v140, v140, v140
	v_max_f32_e32 v141, v141, v141
	v_max_f32_e32 v142, v142, v142
	v_max_f32_e32 v143, v143, v143
	v_max_f32_e32 v144, v144, v144
	v_max_f32_e32 v145, v145, v145
	v_max_f32_e32 v146, v146, v146
	v_max_f32_e32 v147, v147, v147
	v_med3_f32 v132, v132, s20, v13
	v_med3_f32 v133, v133, s20, v13
	v_med3_f32 v134, v134, s20, v13
	v_med3_f32 v135, v135, s20, v13
	v_med3_f32 v136, v136, s20, v13
	v_med3_f32 v137, v137, s20, v13
	v_med3_f32 v138, v138, s20, v13
	v_med3_f32 v139, v139, s20, v13
	v_med3_f32 v140, v140, s20, v13
	v_med3_f32 v141, v141, s20, v13
	v_med3_f32 v142, v142, s20, v13
	v_med3_f32 v143, v143, s20, v13
	v_med3_f32 v144, v144, s20, v13
	v_med3_f32 v145, v145, s20, v13
	v_med3_f32 v146, v146, s20, v13
	v_med3_f32 v147, v147, s20, v13
	v_mov_b32_e32 v148, 0
	v_mov_b32_e32 v149, 0
	v_mov_b32_e32 v150, 0
	v_mov_b32_e32 v151, 0
	v_cvt_pk_fp8_f32 v148, v132, v133
	v_cvt_pk_fp8_f32 v149, v136, v137
	v_cvt_pk_fp8_f32 v150, v140, v141
	v_cvt_pk_fp8_f32 v151, v144, v145
	v_cvt_pk_fp8_f32 v148, v134, v135 op_sel:[0,0,1]
	v_cvt_pk_fp8_f32 v149, v138, v139 op_sel:[0,0,1]
	v_cvt_pk_fp8_f32 v150, v142, v143 op_sel:[0,0,1]
	v_cvt_pk_fp8_f32 v151, v146, v147 op_sel:[0,0,1]
	s_nop 0
	global_store_dwordx4 v12, v[148:151], s[14:15]
	s_waitcnt vmcnt(22)
	v_mul_f32_e32 v100, 0x43000000, v100
	v_mul_f32_e32 v101, 0x43000000, v101
	v_mul_f32_e32 v102, 0x43000000, v102
	v_mul_f32_e32 v103, 0x43000000, v103
	ds_write_b128 v4, v[100:103]
	v_mul_f32_e32 v104, 0x43000000, v104
	v_mul_f32_e32 v105, 0x43000000, v105
	v_mul_f32_e32 v106, 0x43000000, v106
	v_mul_f32_e32 v107, 0x43000000, v107
	ds_write_b128 v4, v[104:107] offset:1024
	v_mul_f32_e32 v108, 0x43000000, v108
	v_mul_f32_e32 v109, 0x43000000, v109
	v_mul_f32_e32 v110, 0x43000000, v110
	v_mul_f32_e32 v111, 0x43000000, v111
	ds_write_b128 v4, v[108:111] offset:2048
	v_mul_f32_e32 v112, 0x43000000, v112
	v_mul_f32_e32 v113, 0x43000000, v113
	v_mul_f32_e32 v114, 0x43000000, v114
	v_mul_f32_e32 v115, 0x43000000, v115
	ds_write_b128 v4, v[112:115] offset:3072
	v_mul_f32_e32 v116, 0x43000000, v116
	v_mul_f32_e32 v117, 0x43000000, v117
	v_mul_f32_e32 v118, 0x43000000, v118
	v_mul_f32_e32 v119, 0x43000000, v119
	ds_write_b128 v4, v[116:119] offset:4096
	v_mul_f32_e32 v120, 0x43000000, v120
	v_mul_f32_e32 v121, 0x43000000, v121
	v_mul_f32_e32 v122, 0x43000000, v122
	v_mul_f32_e32 v123, 0x43000000, v123
	ds_write_b128 v4, v[120:123] offset:5120
	v_mul_f32_e32 v124, 0x43000000, v124
	v_mul_f32_e32 v125, 0x43000000, v125
	v_mul_f32_e32 v126, 0x43000000, v126
	v_mul_f32_e32 v127, 0x43000000, v127
	ds_write_b128 v4, v[124:127] offset:6144
	v_mul_f32_e32 v128, 0x43000000, v128
	v_mul_f32_e32 v129, 0x43000000, v129
	v_mul_f32_e32 v130, 0x43000000, v130
	v_mul_f32_e32 v131, 0x43000000, v131
	ds_write_b128 v4, v[128:131] offset:7168
	s_waitcnt lgkmcnt(0)
	s_barrier
; #define GAS __attribute__((address_space(1)))
; #define LAS __attribute__((address_space(3)))
; #define LDS_WAIT() asm volatile("s_waitcnt lgkmcnt(0)" ::: "memory")
; __device__ __forceinline__ unsigned pk4_fp8(float a, float b, float c, float d) {
;     a = fminf(fmaxf(a, -448.f), 448.f); b = fminf(fmaxf(b, -448.f), 448.f); c = fminf(fmaxf(c, -448.f), 448.f); d = fminf(fmaxf(d, -448.f), 448.f);
;     int w = __builtin_amdgcn_cvt_pk_fp8_f32(a, b, 0, false); w = __builtin_amdgcn_cvt_pk_fp8_f32(c, d, w, true); return (unsigned)w; }
;     const int pr = item >> 1, kb = 2 * (pr / nblk) + (item & 1), nb = pr % nblk, k0 = 64 * kb, n0 = 32 * nb;
;     const int nr = n0 + (lane & 31); const int sc = MAP == 1 ? src_col_in(nr) : nr;
;     float v[32];
; #pragma unroll
;     for (int i = 0; i < 32; ++i) v[i] = sc >= 0 ? W[(size_t)(k0 + 2 * i + (lane >> 5)) * Nsrc + sc] : 0.f;
; #pragma unroll
;     for (int i = 0; i < 32; ++i) { const int k = k0 + 2 * i + (lane >> 5); float x = v[i] * wscale; if (KS) x *= (k < ksplit ? ksA[k] : ksB[k - ksplit]); scr[(2 * i + (lane >> 5)) * 33 + (lane & 31)] = x; }
;     LDS_WAIT(); asm volatile("" ::: "memory");
;     const int c = lane & 7;
; #pragma unroll
;     for (int j = 0; j < 4; ++j) { const int n = (lane >> 3) + 8 * j; const LAS float* s = scr + (8 * c) * 33 + n;
;         const unsigned long long o = (unsigned long long)pg8::pk4_fp8(s[0 * 33], s[1 * 33], s[2 * 33], s[3 * 33]) | ((unsigned long long)pg8::pk4_fp8(s[4 * 33], s[5 * 33], s[6 * 33], s[7 * 33]) << 32);
;         *(GAS unsigned long long*)(WT + (size_t)(n0 + n) * K + k0 + 8 * c) = o; }
;     LDS_WAIT(); asm volatile("" ::: "memory");
; }
	s_add_i32 s17, s16, 1056
	s_min_u32 s17, s17, 0xbff
	s_lshr_b32 s18, s17, 5
	s_add_i32 s18, s18, 32
	s_and_b32 s19, s17, 31
	s_lshl_b32 s18, s18, 21
	s_lshl_b32 s19, s19, 9
	s_add_u32 s18, s18, s19
	s_add_u32 s12, s2, s18
	s_addc_u32 s13, s3, 0
	global_load_dwordx4 v[100:103], v10, s[12:13]
	s_add_u32 s12, s12, 0x8000
	s_addc_u32 s13, s13, 0
	global_load_dwordx4 v[104:107], v10, s[12:13]
	s_add_u32 s12, s12, 0x8000
	s_addc_u32 s13, s13, 0
	global_load_dwordx4 v[108:111], v10, s[12:13]
	s_add_u32 s12, s12, 0x8000
	s_addc_u32 s13, s13, 0
	global_load_dwordx4 v[112:115], v10, s[12:13]
	s_add_u32 s12, s12, 0x8000
	s_addc_u32 s13, s13, 0
	global_load_dwordx4 v[116:119], v10, s[12:13]
	s_add_u32 s12, s12, 0x8000
	s_addc_u32 s13, s13, 0
	global_load_dwordx4 v[120:123], v10, s[12:13]
	s_add_u32 s12, s12, 0x8000
	s_addc_u32 s13, s13, 0
	global_load_dwordx4 v[124:127], v10, s[12:13]
	s_add_u32 s12, s12, 0x8000
	s_addc_u32 s13, s13, 0
	global_load_dwordx4 v[128:131], v10, s[12:13]
	s_add_i32 s17, s16, 768
	s_min_u32 s17, s17, 0xbff
	s_lshr_b32 s18, s17, 5
	s_add_i32 s18, s18, 32
	s_and_b32 s19, s17, 31
	s_lshl_b32 s19, s19, 21
	s_lshl_b32 s18, s18, 7
	s_add_u32 s18, s18, s19
	s_add_u32 s14, s4, s18
	s_addc_u32 s15, s5, 0
	ds_read_b32 v132, v6
	ds_read_b32 v133, v6 offset:512
	ds_read_b32 v134, v6 offset:1024
	ds_read_b32 v135, v6 offset:1536
	ds_read_b32 v136, v6 offset:2048
	ds_read_b32 v137, v6 offset:2560
	ds_read_b32 v138, v6 offset:3072
	ds_read_b32 v139, v6 offset:3584
	ds_read_b32 v140, v6 offset:4096
	ds_read_b32 v141, v6 offset:4608
	ds_read_b32 v142, v6 offset:5120
	ds_read_b32 v143, v6 offset:5632
	ds_read_b32 v144, v6 offset:6144
	ds_read_b32 v145, v6 offset:6656
	ds_read_b32 v146, v6 offset:7168
	ds_read_b32 v147, v6 offset:7680
	s_waitcnt lgkmcnt(0)
	v_max_f32_e32 v132, v132, v132
	v_max_f32_e32 v133, v133, v133
	v_max_f32_e32 v134, v134, v134
	v_max_f32_e32 v135, v135, v135
	v_max_f32_e32 v136, v136, v136
	v_max_f32_e32 v137, v137, v137
	v_max_f32_e32 v138, v138, v138
	v_max_f32_e32 v139, v139, v139
	v_max_f32_e32 v140, v140, v140
	v_max_f32_e32 v141, v141, v141
	v_max_f32_e32 v142, v142, v142
	v_max_f32_e32 v143, v143, v143
	v_max_f32_e32 v144, v144, v144
	v_max_f32_e32 v145, v145, v145
	v_max_f32_e32 v146, v146, v146
	v_max_f32_e32 v147, v147, v147
	v_med3_f32 v132, v132, s20, v13
	v_med3_f32 v133, v133, s20, v13
	v_med3_f32 v134, v134, s20, v13
	v_med3_f32 v135, v135, s20, v13
	v_med3_f32 v136, v136, s20, v13
	v_med3_f32 v137, v137, s20, v13
	v_med3_f32 v138, v138, s20, v13
	v_med3_f32 v139, v139, s20, v13
	v_med3_f32 v140, v140, s20, v13
	v_med3_f32 v141, v141, s20, v13
	v_med3_f32 v142, v142, s20, v13
	v_med3_f32 v143, v143, s20, v13
	v_med3_f32 v144, v144, s20, v13
	v_med3_f32 v145, v145, s20, v13
	v_med3_f32 v146, v146, s20, v13
	v_med3_f32 v147, v147, s20, v13
	v_mov_b32_e32 v148, 0
	v_mov_b32_e32 v149, 0
	v_mov_b32_e32 v150, 0
	v_mov_b32_e32 v151, 0
	v_cvt_pk_fp8_f32 v148, v132, v133
	v_cvt_pk_fp8_f32 v149, v136, v137
	v_cvt_pk_fp8_f32 v150, v140, v141
	v_cvt_pk_fp8_f32 v151, v144, v145
	v_cvt_pk_fp8_f32 v148, v134, v135 op_sel:[0,0,1]
	v_cvt_pk_fp8_f32 v149, v138, v139 op_sel:[0,0,1]
	v_cvt_pk_fp8_f32 v150, v142, v143 op_sel:[0,0,1]
	v_cvt_pk_fp8_f32 v151, v146, v147 op_sel:[0,0,1]
	s_nop 0
	global_store_dwordx4 v11, v[148:151], s[14:15]
	ds_read_b32 v132, v8
	ds_read_b32 v133, v8 offset:512
	ds_read_b32 v134, v8 offset:1024
	ds_read_b32 v135, v8 offset:1536
	ds_read_b32 v136, v8 offset:2048
	ds_read_b32 v137, v8 offset:2560
	ds_read_b32 v138, v8 offset:3072
	ds_read_b32 v139, v8 offset:3584
	ds_read_b32 v140, v8 offset:4096
	ds_read_b32 v141, v8 offset:4608
	ds_read_b32 v142, v8 offset:5120
	ds_read_b32 v143, v8 offset:5632
	ds_read_b32 v144, v8 offset:6144
	ds_read_b32 v145, v8 offset:6656
	ds_read_b32 v146, v8 offset:7168
	ds_read_b32 v147, v8 offset:7680
	s_waitcnt lgkmcnt(0)
	v_max_f32_e32 v132, v132, v132
	v_max_f32_e32 v133, v133, v133
	v_max_f32_e32 v134, v134, v134
	v_max_f32_e32 v135, v135, v135
	v_max_f32_e32 v136, v136, v136
	v_max_f32_e32 v137, v137, v137
	v_max_f32_e32 v138, v138, v138
	v_max_f32_e32 v139, v139, v139
	v_max_f32_e32 v140, v140, v140
	v_max_f32_e32 v141, v141, v141
	v_max_f32_e32 v142, v142, v142
	v_max_f32_e32 v143, v143, v143
	v_max_f32_e32 v144, v144, v144
	v_max_f32_e32 v145, v145, v145
	v_max_f32_e32 v146, v146, v146
	v_max_f32_e32 v147, v147, v147
	v_med3_f32 v132, v132, s20, v13
	v_med3_f32 v133, v133, s20, v13
	v_med3_f32 v134, v134, s20, v13
	v_med3_f32 v135, v135, s20, v13
	v_med3_f32 v136, v136, s20, v13
	v_med3_f32 v137, v137, s20, v13
	v_med3_f32 v138, v138, s20, v13
	v_med3_f32 v139, v139, s20, v13
	v_med3_f32 v140, v140, s20, v13
	v_med3_f32 v141, v141, s20, v13
	v_med3_f32 v142, v142, s20, v13
	v_med3_f32 v143, v143, s20, v13
	v_med3_f32 v144, v144, s20, v13
	v_med3_f32 v145, v145, s20, v13
	v_med3_f32 v146, v146, s20, v13
	v_med3_f32 v147, v147, s20, v13
	v_mov_b32_e32 v148, 0
	v_mov_b32_e32 v149, 0
	v_mov_b32_e32 v150, 0
	v_mov_b32_e32 v151, 0
	v_cvt_pk_fp8_f32 v148, v132, v133
	v_cvt_pk_fp8_f32 v149, v136, v137
	v_cvt_pk_fp8_f32 v150, v140, v141
	v_cvt_pk_fp8_f32 v151, v144, v145
	v_cvt_pk_fp8_f32 v148, v134, v135 op_sel:[0,0,1]
	v_cvt_pk_fp8_f32 v149, v138, v139 op_sel:[0,0,1]
	v_cvt_pk_fp8_f32 v150, v142, v143 op_sel:[0,0,1]
	v_cvt_pk_fp8_f32 v151, v146, v147 op_sel:[0,0,1]
	s_nop 0
	global_store_dwordx4 v12, v[148:151], s[14:15]
	s_waitcnt vmcnt(22)
	v_mul_f32_e32 v36, 0x43000000, v36
	v_mul_f32_e32 v37, 0x43000000, v37
	v_mul_f32_e32 v38, 0x43000000, v38
	v_mul_f32_e32 v39, 0x43000000, v39
	ds_write_b128 v5, v[36:39]
	v_mul_f32_e32 v40, 0x43000000, v40
	v_mul_f32_e32 v41, 0x43000000, v41
	v_mul_f32_e32 v42, 0x43000000, v42
	v_mul_f32_e32 v43, 0x43000000, v43
	ds_write_b128 v5, v[40:43] offset:1024
	v_mul_f32_e32 v44, 0x43000000, v44
	v_mul_f32_e32 v45, 0x43000000, v45
	v_mul_f32_e32 v46, 0x43000000, v46
	v_mul_f32_e32 v47, 0x43000000, v47
	ds_write_b128 v5, v[44:47] offset:2048
	v_mul_f32_e32 v48, 0x43000000, v48
	v_mul_f32_e32 v49, 0x43000000, v49
	v_mul_f32_e32 v50, 0x43000000, v50
	v_mul_f32_e32 v51, 0x43000000, v51
	ds_write_b128 v5, v[48:51] offset:3072
	v_mul_f32_e32 v52, 0x43000000, v52
	v_mul_f32_e32 v53, 0x43000000, v53
	v_mul_f32_e32 v54, 0x43000000, v54
	v_mul_f32_e32 v55, 0x43000000, v55
	ds_write_b128 v5, v[52:55] offset:4096
	v_mul_f32_e32 v56, 0x43000000, v56
	v_mul_f32_e32 v57, 0x43000000, v57
	v_mul_f32_e32 v58, 0x43000000, v58
	v_mul_f32_e32 v59, 0x43000000, v59
	ds_write_b128 v5, v[56:59] offset:5120
	v_mul_f32_e32 v60, 0x43000000, v60
	v_mul_f32_e32 v61, 0x43000000, v61
	v_mul_f32_e32 v62, 0x43000000, v62
	v_mul_f32_e32 v63, 0x43000000, v63
	ds_write_b128 v5, v[60:63] offset:6144
	v_mul_f32_e32 v64, 0x43000000, v64
	v_mul_f32_e32 v65, 0x43000000, v65
	v_mul_f32_e32 v66, 0x43000000, v66
	v_mul_f32_e32 v67, 0x43000000, v67
	ds_write_b128 v5, v[64:67] offset:7168
	s_waitcnt lgkmcnt(0)
	s_barrier
; #define GAS __attribute__((address_space(1)))
; #define LAS __attribute__((address_space(3)))
; #define LDS_WAIT() asm volatile("s_waitcnt lgkmcnt(0)" ::: "memory")
; __device__ __forceinline__ unsigned pk4_fp8(float a, float b, float c, float d) {
;     a = fminf(fmaxf(a, -448.f), 448.f); b = fminf(fmaxf(b, -448.f), 448.f); c = fminf(fmaxf(c, -448.f), 448.f); d = fminf(fmaxf(d, -448.f), 448.f);
;     int w = __builtin_amdgcn_cvt_pk_fp8_f32(a, b, 0, false); w = __builtin_amdgcn_cvt_pk_fp8_f32(c, d, w, true); return (unsigned)w; }
;     const int pr = item >> 1, kb = 2 * (pr / nblk) + (item & 1), nb = pr % nblk, k0 = 64 * kb, n0 = 32 * nb;
;     const int nr = n0 + (lane & 31); const int sc = MAP == 1 ? src_col_in(nr) : nr;
;     float v[32];
; #pragma unroll
;     for (int i = 0; i < 32; ++i) v[i] = sc >= 0 ? W[(size_t)(k0 + 2 * i + (lane >> 5)) * Nsrc + sc] : 0.f;
; #pragma unroll
;     for (int i = 0; i < 32; ++i) { const int k = k0 + 2 * i + (lane >> 5); float x = v[i] * wscale; if (KS) x *= (k < ksplit ? ksA[k] : ksB[k - ksplit]); scr[(2 * i + (lane >> 5)) * 33 + (lane & 31)] = x; }
;     LDS_WAIT(); asm volatile("" ::: "memory");
;     const int c = lane & 7;
; #pragma unroll
;     for (int j = 0; j < 4; ++j) { const int n = (lane >> 3) + 8 * j; const LAS float* s = scr + (8 * c) * 33 + n;
;         const unsigned long long o = (unsigned long long)pg8::pk4_fp8(s[0 * 33], s[1 * 33], s[2 * 33], s[3 * 33]) | ((unsigned long long)pg8::pk4_fp8(s[4 * 33], s[5 * 33], s[6 * 33], s[7 * 33]) << 32);
;         *(GAS unsigned long long*)(WT + (size_t)(n0 + n) * K + k0 + 8 * c) = o; }
;     LDS_WAIT(); asm volatile("" ::: "memory");
; }
	s_add_i32 s17, s16, 1152
	s_min_u32 s17, s17, 0xbff
	s_lshr_b32 s18, s17, 5
	s_add_i32 s18, s18, 32
	s_and_b32 s19, s17, 31
	s_lshl_b32 s18, s18, 21
	s_lshl_b32 s19, s19, 9
	s_add_u32 s18, s18, s19
	s_add_u32 s12, s2, s18
	s_addc_u32 s13, s3, 0
	global_load_dwordx4 v[36:39], v10, s[12:13]
	s_add_u32 s12, s12, 0x8000
	s_addc_u32 s13, s13, 0
	global_load_dwordx4 v[40:43], v10, s[12:13]
	s_add_u32 s12, s12, 0x8000
	s_addc_u32 s13, s13, 0
	global_load_dwordx4 v[44:47], v10, s[12:13]
	s_add_u32 s12, s12, 0x8000
	s_addc_u32 s13, s13, 0
	global_load_dwordx4 v[48:51], v10, s[12:13]
	s_add_u32 s12, s12, 0x8000
	s_addc_u32 s13, s13, 0
	global_load_dwordx4 v[52:55], v10, s[12:13]
	s_add_u32 s12, s12, 0x8000
	s_addc_u32 s13, s13, 0
	global_load_dwordx4 v[56:59], v10, s[12:13]
	s_add_u32 s12, s12, 0x8000
	s_addc_u32 s13, s13, 0
	global_load_dwordx4 v[60:63], v10, s[12:13]
	s_add_u32 s12, s12, 0x8000
	s_addc_u32 s13, s13, 0
	global_load_dwordx4 v[64:67], v10, s[12:13]
	s_add_i32 s17, s16, 864
	s_min_u32 s17, s17, 0xbff
	s_lshr_b32 s18, s17, 5
	s_add_i32 s18, s18, 32
	s_and_b32 s19, s17, 31
	s_lshl_b32 s19, s19, 21
	s_lshl_b32 s18, s18, 7
	s_add_u32 s18, s18, s19
	s_add_u32 s14, s4, s18
	s_addc_u32 s15, s5, 0
	ds_read_b32 v132, v7
	ds_read_b32 v133, v7 offset:512
	ds_read_b32 v134, v7 offset:1024
	ds_read_b32 v135, v7 offset:1536
	ds_read_b32 v136, v7 offset:2048
	ds_read_b32 v137, v7 offset:2560
	ds_read_b32 v138, v7 offset:3072
	ds_read_b32 v139, v7 offset:3584
	ds_read_b32 v140, v7 offset:4096
	ds_read_b32 v141, v7 offset:4608
	ds_read_b32 v142, v7 offset:5120
	ds_read_b32 v143, v7 offset:5632
	ds_read_b32 v144, v7 offset:6144
	ds_read_b32 v145, v7 offset:6656
	ds_read_b32 v146, v7 offset:7168
	ds_read_b32 v147, v7 offset:7680
	s_waitcnt lgkmcnt(0)
	v_max_f32_e32 v132, v132, v132
	v_max_f32_e32 v133, v133, v133
	v_max_f32_e32 v134, v134, v134
	v_max_f32_e32 v135, v135, v135
	v_max_f32_e32 v136, v136, v136
	v_max_f32_e32 v137, v137, v137
	v_max_f32_e32 v138, v138, v138
	v_max_f32_e32 v139, v139, v139
	v_max_f32_e32 v140, v140, v140
	v_max_f32_e32 v141, v141, v141
	v_max_f32_e32 v142, v142, v142
	v_max_f32_e32 v143, v143, v143
	v_max_f32_e32 v144, v144, v144
	v_max_f32_e32 v145, v145, v145
	v_max_f32_e32 v146, v146, v146
	v_max_f32_e32 v147, v147, v147
	v_med3_f32 v132, v132, s20, v13
	v_med3_f32 v133, v133, s20, v13
	v_med3_f32 v134, v134, s20, v13
	v_med3_f32 v135, v135, s20, v13
	v_med3_f32 v136, v136, s20, v13
	v_med3_f32 v137, v137, s20, v13
	v_med3_f32 v138, v138, s20, v13
	v_med3_f32 v139, v139, s20, v13
	v_med3_f32 v140, v140, s20, v13
	v_med3_f32 v141, v141, s20, v13
	v_med3_f32 v142, v142, s20, v13
	v_med3_f32 v143, v143, s20, v13
	v_med3_f32 v144, v144, s20, v13
	v_med3_f32 v145, v145, s20, v13
	v_med3_f32 v146, v146, s20, v13
	v_med3_f32 v147, v147, s20, v13
	v_mov_b32_e32 v148, 0
	v_mov_b32_e32 v149, 0
	v_mov_b32_e32 v150, 0
	v_mov_b32_e32 v151, 0
	v_cvt_pk_fp8_f32 v148, v132, v133
	v_cvt_pk_fp8_f32 v149, v136, v137
	v_cvt_pk_fp8_f32 v150, v140, v141
	v_cvt_pk_fp8_f32 v151, v144, v145
	v_cvt_pk_fp8_f32 v148, v134, v135 op_sel:[0,0,1]
	v_cvt_pk_fp8_f32 v149, v138, v139 op_sel:[0,0,1]
	v_cvt_pk_fp8_f32 v150, v142, v143 op_sel:[0,0,1]
	v_cvt_pk_fp8_f32 v151, v146, v147 op_sel:[0,0,1]
	s_nop 0
	global_store_dwordx4 v11, v[148:151], s[14:15]
	ds_read_b32 v132, v9
	ds_read_b32 v133, v9 offset:512
	ds_read_b32 v134, v9 offset:1024
	ds_read_b32 v135, v9 offset:1536
	ds_read_b32 v136, v9 offset:2048
	ds_read_b32 v137, v9 offset:2560
	ds_read_b32 v138, v9 offset:3072
	ds_read_b32 v139, v9 offset:3584
	ds_read_b32 v140, v9 offset:4096
	ds_read_b32 v141, v9 offset:4608
	ds_read_b32 v142, v9 offset:5120
	ds_read_b32 v143, v9 offset:5632
	ds_read_b32 v144, v9 offset:6144
	ds_read_b32 v145, v9 offset:6656
	ds_read_b32 v146, v9 offset:7168
	ds_read_b32 v147, v9 offset:7680
	s_waitcnt lgkmcnt(0)
	v_max_f32_e32 v132, v132, v132
	v_max_f32_e32 v133, v133, v133
	v_max_f32_e32 v134, v134, v134
	v_max_f32_e32 v135, v135, v135
	v_max_f32_e32 v136, v136, v136
	v_max_f32_e32 v137, v137, v137
	v_max_f32_e32 v138, v138, v138
	v_max_f32_e32 v139, v139, v139
	v_max_f32_e32 v140, v140, v140
	v_max_f32_e32 v141, v141, v141
	v_max_f32_e32 v142, v142, v142
	v_max_f32_e32 v143, v143, v143
	v_max_f32_e32 v144, v144, v144
	v_max_f32_e32 v145, v145, v145
	v_max_f32_e32 v146, v146, v146
	v_max_f32_e32 v147, v147, v147
	v_med3_f32 v132, v132, s20, v13
	v_med3_f32 v133, v133, s20, v13
	v_med3_f32 v134, v134, s20, v13
	v_med3_f32 v135, v135, s20, v13
	v_med3_f32 v136, v136, s20, v13
	v_med3_f32 v137, v137, s20, v13
	v_med3_f32 v138, v138, s20, v13
	v_med3_f32 v139, v139, s20, v13
	v_med3_f32 v140, v140, s20, v13
	v_med3_f32 v141, v141, s20, v13
	v_med3_f32 v142, v142, s20, v13
	v_med3_f32 v143, v143, s20, v13
	v_med3_f32 v144, v144, s20, v13
	v_med3_f32 v145, v145, s20, v13
	v_med3_f32 v146, v146, s20, v13
	v_med3_f32 v147, v147, s20, v13
	v_mov_b32_e32 v148, 0
	v_mov_b32_e32 v149, 0
	v_mov_b32_e32 v150, 0
	v_mov_b32_e32 v151, 0
	v_cvt_pk_fp8_f32 v148, v132, v133
	v_cvt_pk_fp8_f32 v149, v136, v137
	v_cvt_pk_fp8_f32 v150, v140, v141
	v_cvt_pk_fp8_f32 v151, v144, v145
	v_cvt_pk_fp8_f32 v148, v134, v135 op_sel:[0,0,1]
	v_cvt_pk_fp8_f32 v149, v138, v139 op_sel:[0,0,1]
	v_cvt_pk_fp8_f32 v150, v142, v143 op_sel:[0,0,1]
	v_cvt_pk_fp8_f32 v151, v146, v147 op_sel:[0,0,1]
	s_nop 0
	global_store_dwordx4 v12, v[148:151], s[14:15]
	s_waitcnt vmcnt(22)
	v_mul_f32_e32 v68, 0x43000000, v68
	v_mul_f32_e32 v69, 0x43000000, v69
	v_mul_f32_e32 v70, 0x43000000, v70
	v_mul_f32_e32 v71, 0x43000000, v71
	ds_write_b128 v4, v[68:71]
	v_mul_f32_e32 v72, 0x43000000, v72
	v_mul_f32_e32 v73, 0x43000000, v73
	v_mul_f32_e32 v74, 0x43000000, v74
	v_mul_f32_e32 v75, 0x43000000, v75
	ds_write_b128 v4, v[72:75] offset:1024
	v_mul_f32_e32 v76, 0x43000000, v76
	v_mul_f32_e32 v77, 0x43000000, v77
	v_mul_f32_e32 v78, 0x43000000, v78
	v_mul_f32_e32 v79, 0x43000000, v79
	ds_write_b128 v4, v[76:79] offset:2048
	v_mul_f32_e32 v80, 0x43000000, v80
	v_mul_f32_e32 v81, 0x43000000, v81
	v_mul_f32_e32 v82, 0x43000000, v82
	v_mul_f32_e32 v83, 0x43000000, v83
	ds_write_b128 v4, v[80:83] offset:3072
	v_mul_f32_e32 v84, 0x43000000, v84
	v_mul_f32_e32 v85, 0x43000000, v85
	v_mul_f32_e32 v86, 0x43000000, v86
	v_mul_f32_e32 v87, 0x43000000, v87
	ds_write_b128 v4, v[84:87] offset:4096
	v_mul_f32_e32 v88, 0x43000000, v88
	v_mul_f32_e32 v89, 0x43000000, v89
	v_mul_f32_e32 v90, 0x43000000, v90
	v_mul_f32_e32 v91, 0x43000000, v91
	ds_write_b128 v4, v[88:91] offset:5120
	v_mul_f32_e32 v92, 0x43000000, v92
	v_mul_f32_e32 v93, 0x43000000, v93
	v_mul_f32_e32 v94, 0x43000000, v94
	v_mul_f32_e32 v95, 0x43000000, v95
	ds_write_b128 v4, v[92:95] offset:6144
	v_mul_f32_e32 v96, 0x43000000, v96
	v_mul_f32_e32 v97, 0x43000000, v97
	v_mul_f32_e32 v98, 0x43000000, v98
	v_mul_f32_e32 v99, 0x43000000, v99
	ds_write_b128 v4, v[96:99] offset:7168
	s_waitcnt lgkmcnt(0)
	s_barrier
; #define GAS __attribute__((address_space(1)))
; #define LAS __attribute__((address_space(3)))
; #define LDS_WAIT() asm volatile("s_waitcnt lgkmcnt(0)" ::: "memory")
; __device__ __forceinline__ unsigned pk4_fp8(float a, float b, float c, float d) {
;     a = fminf(fmaxf(a, -448.f), 448.f); b = fminf(fmaxf(b, -448.f), 448.f); c = fminf(fmaxf(c, -448.f), 448.f); d = fminf(fmaxf(d, -448.f), 448.f);
;     int w = __builtin_amdgcn_cvt_pk_fp8_f32(a, b, 0, false); w = __builtin_amdgcn_cvt_pk_fp8_f32(c, d, w, true); return (unsigned)w; }
;     const int pr = item >> 1, kb = 2 * (pr / nblk) + (item & 1), nb = pr % nblk, k0 = 64 * kb, n0 = 32 * nb;
;     const int nr = n0 + (lane & 31); const int sc = MAP == 1 ? src_col_in(nr) : nr;
;     float v[32];
; #pragma unroll
;     for (int i = 0; i < 32; ++i) v[i] = sc >= 0 ? W[(size_t)(k0 + 2 * i + (lane >> 5)) * Nsrc + sc] : 0.f;
; #pragma unroll
;     for (int i = 0; i < 32; ++i) { const int k = k0 + 2 * i + (lane >> 5); float x = v[i] * wscale; if (KS) x *= (k < ksplit ? ksA[k] : ksB[k - ksplit]); scr[(2 * i + (lane >> 5)) * 33 + (lane & 31)] = x; }
;     LDS_WAIT(); asm volatile("" ::: "memory");
;     const int c = lane & 7;
; #pragma unroll
;     for (int j = 0; j < 4; ++j) { const int n = (lane >> 3) + 8 * j; const LAS float* s = scr + (8 * c) * 33 + n;
;         const unsigned long long o = (unsigned long long)pg8::pk4_fp8(s[0 * 33], s[1 * 33], s[2 * 33], s[3 * 33]) | ((unsigned long long)pg8::pk4_fp8(s[4 * 33], s[5 * 33], s[6 * 33], s[7 * 33]) << 32);
;         *(GAS unsigned long long*)(WT + (size_t)(n0 + n) * K + k0 + 8 * c) = o; }
;     LDS_WAIT(); asm volatile("" ::: "memory");
; }
	s_add_i32 s17, s16, 1248
	s_min_u32 s17, s17, 0xbff
	s_lshr_b32 s18, s17, 5
	s_add_i32 s18, s18, 32
	s_and_b32 s19, s17, 31
	s_lshl_b32 s18, s18, 21
	s_lshl_b32 s19, s19, 9
	s_add_u32 s18, s18, s19
	s_add_u32 s12, s2, s18
	s_addc_u32 s13, s3, 0
	global_load_dwordx4 v[68:71], v10, s[12:13]
	s_add_u32 s12, s12, 0x8000
	s_addc_u32 s13, s13, 0
	global_load_dwordx4 v[72:75], v10, s[12:13]
	s_add_u32 s12, s12, 0x8000
	s_addc_u32 s13, s13, 0
	global_load_dwordx4 v[76:79], v10, s[12:13]
	s_add_u32 s12, s12, 0x8000
	s_addc_u32 s13, s13, 0
	global_load_dwordx4 v[80:83], v10, s[12:13]
	s_add_u32 s12, s12, 0x8000
	s_addc_u32 s13, s13, 0
	global_load_dwordx4 v[84:87], v10, s[12:13]
	s_add_u32 s12, s12, 0x8000
	s_addc_u32 s13, s13, 0
	global_load_dwordx4 v[88:91], v10, s[12:13]
	s_add_u32 s12, s12, 0x8000
	s_addc_u32 s13, s13, 0
	global_load_dwordx4 v[92:95], v10, s[12:13]
	s_add_u32 s12, s12, 0x8000
	s_addc_u32 s13, s13, 0
	global_load_dwordx4 v[96:99], v10, s[12:13]
	s_add_i32 s17, s16, 960
	s_min_u32 s17, s17, 0xbff
	s_lshr_b32 s18, s17, 5
	s_add_i32 s18, s18, 32
	s_and_b32 s19, s17, 31
	s_lshl_b32 s19, s19, 21
	s_lshl_b32 s18, s18, 7
	s_add_u32 s18, s18, s19
	s_add_u32 s14, s4, s18
	s_addc_u32 s15, s5, 0
	ds_read_b32 v132, v6
	ds_read_b32 v133, v6 offset:512
	ds_read_b32 v134, v6 offset:1024
	ds_read_b32 v135, v6 offset:1536
	ds_read_b32 v136, v6 offset:2048
	ds_read_b32 v137, v6 offset:2560
	ds_read_b32 v138, v6 offset:3072
	ds_read_b32 v139, v6 offset:3584
	ds_read_b32 v140, v6 offset:4096
	ds_read_b32 v141, v6 offset:4608
	ds_read_b32 v142, v6 offset:5120
	ds_read_b32 v143, v6 offset:5632
	ds_read_b32 v144, v6 offset:6144
	ds_read_b32 v145, v6 offset:6656
	ds_read_b32 v146, v6 offset:7168
	ds_read_b32 v147, v6 offset:7680
	s_waitcnt lgkmcnt(0)
	v_max_f32_e32 v132, v132, v132
	v_max_f32_e32 v133, v133, v133
	v_max_f32_e32 v134, v134, v134
	v_max_f32_e32 v135, v135, v135
	v_max_f32_e32 v136, v136, v136
	v_max_f32_e32 v137, v137, v137
	v_max_f32_e32 v138, v138, v138
	v_max_f32_e32 v139, v139, v139
	v_max_f32_e32 v140, v140, v140
	v_max_f32_e32 v141, v141, v141
	v_max_f32_e32 v142, v142, v142
	v_max_f32_e32 v143, v143, v143
	v_max_f32_e32 v144, v144, v144
	v_max_f32_e32 v145, v145, v145
	v_max_f32_e32 v146, v146, v146
	v_max_f32_e32 v147, v147, v147
	v_med3_f32 v132, v132, s20, v13
	v_med3_f32 v133, v133, s20, v13
	v_med3_f32 v134, v134, s20, v13
	v_med3_f32 v135, v135, s20, v13
	v_med3_f32 v136, v136, s20, v13
	v_med3_f32 v137, v137, s20, v13
	v_med3_f32 v138, v138, s20, v13
	v_med3_f32 v139, v139, s20, v13
	v_med3_f32 v140, v140, s20, v13
	v_med3_f32 v141, v141, s20, v13
	v_med3_f32 v142, v142, s20, v13
	v_med3_f32 v143, v143, s20, v13
	v_med3_f32 v144, v144, s20, v13
	v_med3_f32 v145, v145, s20, v13
	v_med3_f32 v146, v146, s20, v13
	v_med3_f32 v147, v147, s20, v13
	v_mov_b32_e32 v148, 0
	v_mov_b32_e32 v149, 0
	v_mov_b32_e32 v150, 0
	v_mov_b32_e32 v151, 0
	v_cvt_pk_fp8_f32 v148, v132, v133
	v_cvt_pk_fp8_f32 v149, v136, v137
	v_cvt_pk_fp8_f32 v150, v140, v141
	v_cvt_pk_fp8_f32 v151, v144, v145
	v_cvt_pk_fp8_f32 v148, v134, v135 op_sel:[0,0,1]
	v_cvt_pk_fp8_f32 v149, v138, v139 op_sel:[0,0,1]
	v_cvt_pk_fp8_f32 v150, v142, v143 op_sel:[0,0,1]
	v_cvt_pk_fp8_f32 v151, v146, v147 op_sel:[0,0,1]
	s_nop 0
	global_store_dwordx4 v11, v[148:151], s[14:15]
	ds_read_b32 v132, v8
	ds_read_b32 v133, v8 offset:512
	ds_read_b32 v134, v8 offset:1024
	ds_read_b32 v135, v8 offset:1536
	ds_read_b32 v136, v8 offset:2048
	ds_read_b32 v137, v8 offset:2560
	ds_read_b32 v138, v8 offset:3072
	ds_read_b32 v139, v8 offset:3584
	ds_read_b32 v140, v8 offset:4096
	ds_read_b32 v141, v8 offset:4608
	ds_read_b32 v142, v8 offset:5120
	ds_read_b32 v143, v8 offset:5632
	ds_read_b32 v144, v8 offset:6144
	ds_read_b32 v145, v8 offset:6656
	ds_read_b32 v146, v8 offset:7168
	ds_read_b32 v147, v8 offset:7680
	s_waitcnt lgkmcnt(0)
	v_max_f32_e32 v132, v132, v132
	v_max_f32_e32 v133, v133, v133
	v_max_f32_e32 v134, v134, v134
	v_max_f32_e32 v135, v135, v135
	v_max_f32_e32 v136, v136, v136
	v_max_f32_e32 v137, v137, v137
	v_max_f32_e32 v138, v138, v138
	v_max_f32_e32 v139, v139, v139
	v_max_f32_e32 v140, v140, v140
	v_max_f32_e32 v141, v141, v141
	v_max_f32_e32 v142, v142, v142
	v_max_f32_e32 v143, v143, v143
	v_max_f32_e32 v144, v144, v144
	v_max_f32_e32 v145, v145, v145
	v_max_f32_e32 v146, v146, v146
	v_max_f32_e32 v147, v147, v147
	v_med3_f32 v132, v132, s20, v13
	v_med3_f32 v133, v133, s20, v13
	v_med3_f32 v134, v134, s20, v13
	v_med3_f32 v135, v135, s20, v13
	v_med3_f32 v136, v136, s20, v13
	v_med3_f32 v137, v137, s20, v13
	v_med3_f32 v138, v138, s20, v13
	v_med3_f32 v139, v139, s20, v13
	v_med3_f32 v140, v140, s20, v13
	v_med3_f32 v141, v141, s20, v13
	v_med3_f32 v142, v142, s20, v13
	v_med3_f32 v143, v143, s20, v13
	v_med3_f32 v144, v144, s20, v13
	v_med3_f32 v145, v145, s20, v13
	v_med3_f32 v146, v146, s20, v13
	v_med3_f32 v147, v147, s20, v13
	v_mov_b32_e32 v148, 0
	v_mov_b32_e32 v149, 0
	v_mov_b32_e32 v150, 0
	v_mov_b32_e32 v151, 0
	v_cvt_pk_fp8_f32 v148, v132, v133
	v_cvt_pk_fp8_f32 v149, v136, v137
	v_cvt_pk_fp8_f32 v150, v140, v141
	v_cvt_pk_fp8_f32 v151, v144, v145
	v_cvt_pk_fp8_f32 v148, v134, v135 op_sel:[0,0,1]
	v_cvt_pk_fp8_f32 v149, v138, v139 op_sel:[0,0,1]
	v_cvt_pk_fp8_f32 v150, v142, v143 op_sel:[0,0,1]
	v_cvt_pk_fp8_f32 v151, v146, v147 op_sel:[0,0,1]
	s_nop 0
	global_store_dwordx4 v12, v[148:151], s[14:15]
	s_waitcnt vmcnt(22)
	v_mul_f32_e32 v100, 0x43000000, v100
	v_mul_f32_e32 v101, 0x43000000, v101
	v_mul_f32_e32 v102, 0x43000000, v102
	v_mul_f32_e32 v103, 0x43000000, v103
	ds_write_b128 v5, v[100:103]
	v_mul_f32_e32 v104, 0x43000000, v104
	v_mul_f32_e32 v105, 0x43000000, v105
	v_mul_f32_e32 v106, 0x43000000, v106
	v_mul_f32_e32 v107, 0x43000000, v107
	ds_write_b128 v5, v[104:107] offset:1024
	v_mul_f32_e32 v108, 0x43000000, v108
	v_mul_f32_e32 v109, 0x43000000, v109
	v_mul_f32_e32 v110, 0x43000000, v110
	v_mul_f32_e32 v111, 0x43000000, v111
	ds_write_b128 v5, v[108:111] offset:2048
	v_mul_f32_e32 v112, 0x43000000, v112
	v_mul_f32_e32 v113, 0x43000000, v113
	v_mul_f32_e32 v114, 0x43000000, v114
	v_mul_f32_e32 v115, 0x43000000, v115
	ds_write_b128 v5, v[112:115] offset:3072
	v_mul_f32_e32 v116, 0x43000000, v116
	v_mul_f32_e32 v117, 0x43000000, v117
	v_mul_f32_e32 v118, 0x43000000, v118
	v_mul_f32_e32 v119, 0x43000000, v119
	ds_write_b128 v5, v[116:119] offset:4096
	v_mul_f32_e32 v120, 0x43000000, v120
	v_mul_f32_e32 v121, 0x43000000, v121
	v_mul_f32_e32 v122, 0x43000000, v122
	v_mul_f32_e32 v123, 0x43000000, v123
	ds_write_b128 v5, v[120:123] offset:5120
	v_mul_f32_e32 v124, 0x43000000, v124
	v_mul_f32_e32 v125, 0x43000000, v125
	v_mul_f32_e32 v126, 0x43000000, v126
	v_mul_f32_e32 v127, 0x43000000, v127
	ds_write_b128 v5, v[124:127] offset:6144
	v_mul_f32_e32 v128, 0x43000000, v128
	v_mul_f32_e32 v129, 0x43000000, v129
	v_mul_f32_e32 v130, 0x43000000, v130
	v_mul_f32_e32 v131, 0x43000000, v131
	ds_write_b128 v5, v[128:131] offset:7168
	s_waitcnt lgkmcnt(0)
	s_barrier
; #define GAS __attribute__((address_space(1)))
; #define LAS __attribute__((address_space(3)))
; #define LDS_WAIT() asm volatile("s_waitcnt lgkmcnt(0)" ::: "memory")
; __device__ __forceinline__ unsigned pk4_fp8(float a, float b, float c, float d) {
;     a = fminf(fmaxf(a, -448.f), 448.f); b = fminf(fmaxf(b, -448.f), 448.f); c = fminf(fmaxf(c, -448.f), 448.f); d = fminf(fmaxf(d, -448.f), 448.f);
;     int w = __builtin_amdgcn_cvt_pk_fp8_f32(a, b, 0, false); w = __builtin_amdgcn_cvt_pk_fp8_f32(c, d, w, true); return (unsigned)w; }
;     const int pr = item >> 1, kb = 2 * (pr / nblk) + (item & 1), nb = pr % nblk, k0 = 64 * kb, n0 = 32 * nb;
;     const int nr = n0 + (lane & 31); const int sc = MAP == 1 ? src_col_in(nr) : nr;
;     float v[32];
; #pragma unroll
;     for (int i = 0; i < 32; ++i) v[i] = sc >= 0 ? W[(size_t)(k0 + 2 * i + (lane >> 5)) * Nsrc + sc] : 0.f;
; #pragma unroll
;     for (int i = 0; i < 32; ++i) { const int k = k0 + 2 * i + (lane >> 5); float x = v[i] * wscale; if (KS) x *= (k < ksplit ? ksA[k] : ksB[k - ksplit]); scr[(2 * i + (lane >> 5)) * 33 + (lane & 31)] = x; }
;     LDS_WAIT(); asm volatile("" ::: "memory");
;     const int c = lane & 7;
; #pragma unroll
;     for (int j = 0; j < 4; ++j) { const int n = (lane >> 3) + 8 * j; const LAS float* s = scr + (8 * c) * 33 + n;
;         const unsigned long long o = (unsigned long long)pg8::pk4_fp8(s[0 * 33], s[1 * 33], s[2 * 33], s[3 * 33]) | ((unsigned long long)pg8::pk4_fp8(s[4 * 33], s[5 * 33], s[6 * 33], s[7 * 33]) << 32);
;         *(GAS unsigned long long*)(WT + (size_t)(n0 + n) * K + k0 + 8 * c) = o; }
;     LDS_WAIT(); asm volatile("" ::: "memory");
; }
	s_add_i32 s17, s16, 1344
	s_min_u32 s17, s17, 0xbff
	s_lshr_b32 s18, s17, 5
	s_add_i32 s18, s18, 32
	s_and_b32 s19, s17, 31
	s_lshl_b32 s18, s18, 21
	s_lshl_b32 s19, s19, 9
	s_add_u32 s18, s18, s19
	s_add_u32 s12, s2, s18
	s_addc_u32 s13, s3, 0
	global_load_dwordx4 v[100:103], v10, s[12:13]
	s_add_u32 s12, s12, 0x8000
	s_addc_u32 s13, s13, 0
	global_load_dwordx4 v[104:107], v10, s[12:13]
	s_add_u32 s12, s12, 0x8000
	s_addc_u32 s13, s13, 0
	global_load_dwordx4 v[108:111], v10, s[12:13]
	s_add_u32 s12, s12, 0x8000
	s_addc_u32 s13, s13, 0
	global_load_dwordx4 v[112:115], v10, s[12:13]
	s_add_u32 s12, s12, 0x8000
	s_addc_u32 s13, s13, 0
	global_load_dwordx4 v[116:119], v10, s[12:13]
	s_add_u32 s12, s12, 0x8000
	s_addc_u32 s13, s13, 0
	global_load_dwordx4 v[120:123], v10, s[12:13]
	s_add_u32 s12, s12, 0x8000
	s_addc_u32 s13, s13, 0
	global_load_dwordx4 v[124:127], v10, s[12:13]
	s_add_u32 s12, s12, 0x8000
	s_addc_u32 s13, s13, 0
	global_load_dwordx4 v[128:131], v10, s[12:13]
	s_add_i32 s17, s16, 1056
	s_min_u32 s17, s17, 0xbff
	s_lshr_b32 s18, s17, 5
	s_add_i32 s18, s18, 32
	s_and_b32 s19, s17, 31
	s_lshl_b32 s19, s19, 21
	s_lshl_b32 s18, s18, 7
	s_add_u32 s18, s18, s19
	s_add_u32 s14, s4, s18
	s_addc_u32 s15, s5, 0
	ds_read_b32 v132, v7
	ds_read_b32 v133, v7 offset:512
	ds_read_b32 v134, v7 offset:1024
	ds_read_b32 v135, v7 offset:1536
	ds_read_b32 v136, v7 offset:2048
	ds_read_b32 v137, v7 offset:2560
	ds_read_b32 v138, v7 offset:3072
	ds_read_b32 v139, v7 offset:3584
	ds_read_b32 v140, v7 offset:4096
	ds_read_b32 v141, v7 offset:4608
	ds_read_b32 v142, v7 offset:5120
	ds_read_b32 v143, v7 offset:5632
	ds_read_b32 v144, v7 offset:6144
	ds_read_b32 v145, v7 offset:6656
	ds_read_b32 v146, v7 offset:7168
	ds_read_b32 v147, v7 offset:7680
	s_waitcnt lgkmcnt(0)
	v_max_f32_e32 v132, v132, v132
	v_max_f32_e32 v133, v133, v133
	v_max_f32_e32 v134, v134, v134
	v_max_f32_e32 v135, v135, v135
	v_max_f32_e32 v136, v136, v136
	v_max_f32_e32 v137, v137, v137
	v_max_f32_e32 v138, v138, v138
	v_max_f32_e32 v139, v139, v139
	v_max_f32_e32 v140, v140, v140
	v_max_f32_e32 v141, v141, v141
	v_max_f32_e32 v142, v142, v142
	v_max_f32_e32 v143, v143, v143
	v_max_f32_e32 v144, v144, v144
	v_max_f32_e32 v145, v145, v145
	v_max_f32_e32 v146, v146, v146
	v_max_f32_e32 v147, v147, v147
	v_med3_f32 v132, v132, s20, v13
	v_med3_f32 v133, v133, s20, v13
	v_med3_f32 v134, v134, s20, v13
	v_med3_f32 v135, v135, s20, v13
	v_med3_f32 v136, v136, s20, v13
	v_med3_f32 v137, v137, s20, v13
	v_med3_f32 v138, v138, s20, v13
	v_med3_f32 v139, v139, s20, v13
	v_med3_f32 v140, v140, s20, v13
	v_med3_f32 v141, v141, s20, v13
	v_med3_f32 v142, v142, s20, v13
	v_med3_f32 v143, v143, s20, v13
	v_med3_f32 v144, v144, s20, v13
	v_med3_f32 v145, v145, s20, v13
	v_med3_f32 v146, v146, s20, v13
	v_med3_f32 v147, v147, s20, v13
	v_mov_b32_e32 v148, 0
	v_mov_b32_e32 v149, 0
	v_mov_b32_e32 v150, 0
	v_mov_b32_e32 v151, 0
	v_cvt_pk_fp8_f32 v148, v132, v133
	v_cvt_pk_fp8_f32 v149, v136, v137
	v_cvt_pk_fp8_f32 v150, v140, v141
	v_cvt_pk_fp8_f32 v151, v144, v145
	v_cvt_pk_fp8_f32 v148, v134, v135 op_sel:[0,0,1]
	v_cvt_pk_fp8_f32 v149, v138, v139 op_sel:[0,0,1]
	v_cvt_pk_fp8_f32 v150, v142, v143 op_sel:[0,0,1]
	v_cvt_pk_fp8_f32 v151, v146, v147 op_sel:[0,0,1]
	s_nop 0
	global_store_dwordx4 v11, v[148:151], s[14:15]
	ds_read_b32 v132, v9
	ds_read_b32 v133, v9 offset:512
	ds_read_b32 v134, v9 offset:1024
	ds_read_b32 v135, v9 offset:1536
	ds_read_b32 v136, v9 offset:2048
	ds_read_b32 v137, v9 offset:2560
	ds_read_b32 v138, v9 offset:3072
	ds_read_b32 v139, v9 offset:3584
	ds_read_b32 v140, v9 offset:4096
	ds_read_b32 v141, v9 offset:4608
	ds_read_b32 v142, v9 offset:5120
	ds_read_b32 v143, v9 offset:5632
	ds_read_b32 v144, v9 offset:6144
	ds_read_b32 v145, v9 offset:6656
	ds_read_b32 v146, v9 offset:7168
	ds_read_b32 v147, v9 offset:7680
	s_waitcnt lgkmcnt(0)
	v_max_f32_e32 v132, v132, v132
	v_max_f32_e32 v133, v133, v133
	v_max_f32_e32 v134, v134, v134
	v_max_f32_e32 v135, v135, v135
	v_max_f32_e32 v136, v136, v136
	v_max_f32_e32 v137, v137, v137
	v_max_f32_e32 v138, v138, v138
	v_max_f32_e32 v139, v139, v139
	v_max_f32_e32 v140, v140, v140
	v_max_f32_e32 v141, v141, v141
	v_max_f32_e32 v142, v142, v142
	v_max_f32_e32 v143, v143, v143
	v_max_f32_e32 v144, v144, v144
	v_max_f32_e32 v145, v145, v145
	v_max_f32_e32 v146, v146, v146
	v_max_f32_e32 v147, v147, v147
	v_med3_f32 v132, v132, s20, v13
	v_med3_f32 v133, v133, s20, v13
	v_med3_f32 v134, v134, s20, v13
	v_med3_f32 v135, v135, s20, v13
	v_med3_f32 v136, v136, s20, v13
	v_med3_f32 v137, v137, s20, v13
	v_med3_f32 v138, v138, s20, v13
	v_med3_f32 v139, v139, s20, v13
	v_med3_f32 v140, v140, s20, v13
	v_med3_f32 v141, v141, s20, v13
	v_med3_f32 v142, v142, s20, v13
	v_med3_f32 v143, v143, s20, v13
	v_med3_f32 v144, v144, s20, v13
	v_med3_f32 v145, v145, s20, v13
	v_med3_f32 v146, v146, s20, v13
	v_med3_f32 v147, v147, s20, v13
	v_mov_b32_e32 v148, 0
	v_mov_b32_e32 v149, 0
	v_mov_b32_e32 v150, 0
	v_mov_b32_e32 v151, 0
	v_cvt_pk_fp8_f32 v148, v132, v133
	v_cvt_pk_fp8_f32 v149, v136, v137
	v_cvt_pk_fp8_f32 v150, v140, v141
	v_cvt_pk_fp8_f32 v151, v144, v145
	v_cvt_pk_fp8_f32 v148, v134, v135 op_sel:[0,0,1]
	v_cvt_pk_fp8_f32 v149, v138, v139 op_sel:[0,0,1]
	v_cvt_pk_fp8_f32 v150, v142, v143 op_sel:[0,0,1]
	v_cvt_pk_fp8_f32 v151, v146, v147 op_sel:[0,0,1]
	s_nop 0
	global_store_dwordx4 v12, v[148:151], s[14:15]
	s_waitcnt vmcnt(22)
	v_mul_f32_e32 v36, 0x43000000, v36
	v_mul_f32_e32 v37, 0x43000000, v37
	v_mul_f32_e32 v38, 0x43000000, v38
	v_mul_f32_e32 v39, 0x43000000, v39
	ds_write_b128 v4, v[36:39]
	v_mul_f32_e32 v40, 0x43000000, v40
	v_mul_f32_e32 v41, 0x43000000, v41
	v_mul_f32_e32 v42, 0x43000000, v42
	v_mul_f32_e32 v43, 0x43000000, v43
	ds_write_b128 v4, v[40:43] offset:1024
	v_mul_f32_e32 v44, 0x43000000, v44
	v_mul_f32_e32 v45, 0x43000000, v45
	v_mul_f32_e32 v46, 0x43000000, v46
	v_mul_f32_e32 v47, 0x43000000, v47
	ds_write_b128 v4, v[44:47] offset:2048
	v_mul_f32_e32 v48, 0x43000000, v48
	v_mul_f32_e32 v49, 0x43000000, v49
	v_mul_f32_e32 v50, 0x43000000, v50
	v_mul_f32_e32 v51, 0x43000000, v51
	ds_write_b128 v4, v[48:51] offset:3072
	v_mul_f32_e32 v52, 0x43000000, v52
	v_mul_f32_e32 v53, 0x43000000, v53
	v_mul_f32_e32 v54, 0x43000000, v54
	v_mul_f32_e32 v55, 0x43000000, v55
	ds_write_b128 v4, v[52:55] offset:4096
	v_mul_f32_e32 v56, 0x43000000, v56
	v_mul_f32_e32 v57, 0x43000000, v57
	v_mul_f32_e32 v58, 0x43000000, v58
	v_mul_f32_e32 v59, 0x43000000, v59
	ds_write_b128 v4, v[56:59] offset:5120
	v_mul_f32_e32 v60, 0x43000000, v60
	v_mul_f32_e32 v61, 0x43000000, v61
	v_mul_f32_e32 v62, 0x43000000, v62
	v_mul_f32_e32 v63, 0x43000000, v63
	ds_write_b128 v4, v[60:63] offset:6144
	v_mul_f32_e32 v64, 0x43000000, v64
	v_mul_f32_e32 v65, 0x43000000, v65
	v_mul_f32_e32 v66, 0x43000000, v66
	v_mul_f32_e32 v67, 0x43000000, v67
	ds_write_b128 v4, v[64:67] offset:7168
	s_waitcnt lgkmcnt(0)
	s_barrier
; #define GAS __attribute__((address_space(1)))
; #define LAS __attribute__((address_space(3)))
; #define LDS_WAIT() asm volatile("s_waitcnt lgkmcnt(0)" ::: "memory")
; __device__ __forceinline__ unsigned pk4_fp8(float a, float b, float c, float d) {
;     a = fminf(fmaxf(a, -448.f), 448.f); b = fminf(fmaxf(b, -448.f), 448.f); c = fminf(fmaxf(c, -448.f), 448.f); d = fminf(fmaxf(d, -448.f), 448.f);
;     int w = __builtin_amdgcn_cvt_pk_fp8_f32(a, b, 0, false); w = __builtin_amdgcn_cvt_pk_fp8_f32(c, d, w, true); return (unsigned)w; }
;     const int pr = item >> 1, kb = 2 * (pr / nblk) + (item & 1), nb = pr % nblk, k0 = 64 * kb, n0 = 32 * nb;
;     const int nr = n0 + (lane & 31); const int sc = MAP == 1 ? src_col_in(nr) : nr;
;     float v[32];
; #pragma unroll
;     for (int i = 0; i < 32; ++i) v[i] = sc >= 0 ? W[(size_t)(k0 + 2 * i + (lane >> 5)) * Nsrc + sc] : 0.f;
; #pragma unroll
;     for (int i = 0; i < 32; ++i) { const int k = k0 + 2 * i + (lane >> 5); float x = v[i] * wscale; if (KS) x *= (k < ksplit ? ksA[k] : ksB[k - ksplit]); scr[(2 * i + (lane >> 5)) * 33 + (lane & 31)] = x; }
;     LDS_WAIT(); asm volatile("" ::: "memory");
;     const int c = lane & 7;
; #pragma unroll
;     for (int j = 0; j < 4; ++j) { const int n = (lane >> 3) + 8 * j; const LAS float* s = scr + (8 * c) * 33 + n;
;         const unsigned long long o = (unsigned long long)pg8::pk4_fp8(s[0 * 33], s[1 * 33], s[2 * 33], s[3 * 33]) | ((unsigned long long)pg8::pk4_fp8(s[4 * 33], s[5 * 33], s[6 * 33], s[7 * 33]) << 32);
;         *(GAS unsigned long long*)(WT + (size_t)(n0 + n) * K + k0 + 8 * c) = o; }
;     LDS_WAIT(); asm volatile("" ::: "memory");
; }
	s_add_i32 s17, s16, 1440
	s_min_u32 s17, s17, 0xbff
	s_lshr_b32 s18, s17, 5
	s_add_i32 s18, s18, 32
	s_and_b32 s19, s17, 31
	s_lshl_b32 s18, s18, 21
	s_lshl_b32 s19, s19, 9
	s_add_u32 s18, s18, s19
	s_add_u32 s12, s2, s18
	s_addc_u32 s13, s3, 0
	global_load_dwordx4 v[36:39], v10, s[12:13]
	s_add_u32 s12, s12, 0x8000
	s_addc_u32 s13, s13, 0
	global_load_dwordx4 v[40:43], v10, s[12:13]
	s_add_u32 s12, s12, 0x8000
	s_addc_u32 s13, s13, 0
	global_load_dwordx4 v[44:47], v10, s[12:13]
	s_add_u32 s12, s12, 0x8000
	s_addc_u32 s13, s13, 0
	global_load_dwordx4 v[48:51], v10, s[12:13]
	s_add_u32 s12, s12, 0x8000
	s_addc_u32 s13, s13, 0
	global_load_dwordx4 v[52:55], v10, s[12:13]
	s_add_u32 s12, s12, 0x8000
	s_addc_u32 s13, s13, 0
	global_load_dwordx4 v[56:59], v10, s[12:13]
	s_add_u32 s12, s12, 0x8000
	s_addc_u32 s13, s13, 0
	global_load_dwordx4 v[60:63], v10, s[12:13]
	s_add_u32 s12, s12, 0x8000
	s_addc_u32 s13, s13, 0
	global_load_dwordx4 v[64:67], v10, s[12:13]
	s_add_i32 s17, s16, 1152
	s_min_u32 s17, s17, 0xbff
	s_lshr_b32 s18, s17, 5
	s_add_i32 s18, s18, 32
	s_and_b32 s19, s17, 31
	s_lshl_b32 s19, s19, 21
	s_lshl_b32 s18, s18, 7
	s_add_u32 s18, s18, s19
	s_add_u32 s14, s4, s18
	s_addc_u32 s15, s5, 0
	ds_read_b32 v132, v6
	ds_read_b32 v133, v6 offset:512
	ds_read_b32 v134, v6 offset:1024
	ds_read_b32 v135, v6 offset:1536
	ds_read_b32 v136, v6 offset:2048
	ds_read_b32 v137, v6 offset:2560
	ds_read_b32 v138, v6 offset:3072
	ds_read_b32 v139, v6 offset:3584
	ds_read_b32 v140, v6 offset:4096
	ds_read_b32 v141, v6 offset:4608
	ds_read_b32 v142, v6 offset:5120
	ds_read_b32 v143, v6 offset:5632
	ds_read_b32 v144, v6 offset:6144
	ds_read_b32 v145, v6 offset:6656
	ds_read_b32 v146, v6 offset:7168
	ds_read_b32 v147, v6 offset:7680
	s_waitcnt lgkmcnt(0)
	v_max_f32_e32 v132, v132, v132
	v_max_f32_e32 v133, v133, v133
	v_max_f32_e32 v134, v134, v134
	v_max_f32_e32 v135, v135, v135
	v_max_f32_e32 v136, v136, v136
	v_max_f32_e32 v137, v137, v137
	v_max_f32_e32 v138, v138, v138
	v_max_f32_e32 v139, v139, v139
	v_max_f32_e32 v140, v140, v140
	v_max_f32_e32 v141, v141, v141
	v_max_f32_e32 v142, v142, v142
	v_max_f32_e32 v143, v143, v143
	v_max_f32_e32 v144, v144, v144
	v_max_f32_e32 v145, v145, v145
	v_max_f32_e32 v146, v146, v146
	v_max_f32_e32 v147, v147, v147
	v_med3_f32 v132, v132, s20, v13
	v_med3_f32 v133, v133, s20, v13
	v_med3_f32 v134, v134, s20, v13
	v_med3_f32 v135, v135, s20, v13
	v_med3_f32 v136, v136, s20, v13
	v_med3_f32 v137, v137, s20, v13
	v_med3_f32 v138, v138, s20, v13
	v_med3_f32 v139, v139, s20, v13
	v_med3_f32 v140, v140, s20, v13
	v_med3_f32 v141, v141, s20, v13
	v_med3_f32 v142, v142, s20, v13
	v_med3_f32 v143, v143, s20, v13
	v_med3_f32 v144, v144, s20, v13
	v_med3_f32 v145, v145, s20, v13
	v_med3_f32 v146, v146, s20, v13
	v_med3_f32 v147, v147, s20, v13
	v_mov_b32_e32 v148, 0
	v_mov_b32_e32 v149, 0
	v_mov_b32_e32 v150, 0
	v_mov_b32_e32 v151, 0
	v_cvt_pk_fp8_f32 v148, v132, v133
	v_cvt_pk_fp8_f32 v149, v136, v137
	v_cvt_pk_fp8_f32 v150, v140, v141
	v_cvt_pk_fp8_f32 v151, v144, v145
	v_cvt_pk_fp8_f32 v148, v134, v135 op_sel:[0,0,1]
	v_cvt_pk_fp8_f32 v149, v138, v139 op_sel:[0,0,1]
	v_cvt_pk_fp8_f32 v150, v142, v143 op_sel:[0,0,1]
	v_cvt_pk_fp8_f32 v151, v146, v147 op_sel:[0,0,1]
	s_nop 0
	global_store_dwordx4 v11, v[148:151], s[14:15]
	ds_read_b32 v132, v8
	ds_read_b32 v133, v8 offset:512
	ds_read_b32 v134, v8 offset:1024
	ds_read_b32 v135, v8 offset:1536
	ds_read_b32 v136, v8 offset:2048
	ds_read_b32 v137, v8 offset:2560
	ds_read_b32 v138, v8 offset:3072
	ds_read_b32 v139, v8 offset:3584
	ds_read_b32 v140, v8 offset:4096
	ds_read_b32 v141, v8 offset:4608
	ds_read_b32 v142, v8 offset:5120
	ds_read_b32 v143, v8 offset:5632
	ds_read_b32 v144, v8 offset:6144
	ds_read_b32 v145, v8 offset:6656
	ds_read_b32 v146, v8 offset:7168
	ds_read_b32 v147, v8 offset:7680
	s_waitcnt lgkmcnt(0)
	v_max_f32_e32 v132, v132, v132
	v_max_f32_e32 v133, v133, v133
	v_max_f32_e32 v134, v134, v134
	v_max_f32_e32 v135, v135, v135
	v_max_f32_e32 v136, v136, v136
	v_max_f32_e32 v137, v137, v137
	v_max_f32_e32 v138, v138, v138
	v_max_f32_e32 v139, v139, v139
	v_max_f32_e32 v140, v140, v140
	v_max_f32_e32 v141, v141, v141
	v_max_f32_e32 v142, v142, v142
	v_max_f32_e32 v143, v143, v143
	v_max_f32_e32 v144, v144, v144
	v_max_f32_e32 v145, v145, v145
	v_max_f32_e32 v146, v146, v146
	v_max_f32_e32 v147, v147, v147
	v_med3_f32 v132, v132, s20, v13
	v_med3_f32 v133, v133, s20, v13
	v_med3_f32 v134, v134, s20, v13
	v_med3_f32 v135, v135, s20, v13
	v_med3_f32 v136, v136, s20, v13
	v_med3_f32 v137, v137, s20, v13
	v_med3_f32 v138, v138, s20, v13
	v_med3_f32 v139, v139, s20, v13
	v_med3_f32 v140, v140, s20, v13
	v_med3_f32 v141, v141, s20, v13
	v_med3_f32 v142, v142, s20, v13
	v_med3_f32 v143, v143, s20, v13
	v_med3_f32 v144, v144, s20, v13
	v_med3_f32 v145, v145, s20, v13
	v_med3_f32 v146, v146, s20, v13
	v_med3_f32 v147, v147, s20, v13
	v_mov_b32_e32 v148, 0
	v_mov_b32_e32 v149, 0
	v_mov_b32_e32 v150, 0
	v_mov_b32_e32 v151, 0
	v_cvt_pk_fp8_f32 v148, v132, v133
	v_cvt_pk_fp8_f32 v149, v136, v137
	v_cvt_pk_fp8_f32 v150, v140, v141
	v_cvt_pk_fp8_f32 v151, v144, v145
	v_cvt_pk_fp8_f32 v148, v134, v135 op_sel:[0,0,1]
	v_cvt_pk_fp8_f32 v149, v138, v139 op_sel:[0,0,1]
	v_cvt_pk_fp8_f32 v150, v142, v143 op_sel:[0,0,1]
	v_cvt_pk_fp8_f32 v151, v146, v147 op_sel:[0,0,1]
	s_nop 0
	global_store_dwordx4 v12, v[148:151], s[14:15]
	s_waitcnt vmcnt(22)
	v_mul_f32_e32 v68, 0x43000000, v68
	v_mul_f32_e32 v69, 0x43000000, v69
	v_mul_f32_e32 v70, 0x43000000, v70
	v_mul_f32_e32 v71, 0x43000000, v71
	ds_write_b128 v5, v[68:71]
	v_mul_f32_e32 v72, 0x43000000, v72
	v_mul_f32_e32 v73, 0x43000000, v73
	v_mul_f32_e32 v74, 0x43000000, v74
	v_mul_f32_e32 v75, 0x43000000, v75
	ds_write_b128 v5, v[72:75] offset:1024
	v_mul_f32_e32 v76, 0x43000000, v76
	v_mul_f32_e32 v77, 0x43000000, v77
	v_mul_f32_e32 v78, 0x43000000, v78
	v_mul_f32_e32 v79, 0x43000000, v79
	ds_write_b128 v5, v[76:79] offset:2048
	v_mul_f32_e32 v80, 0x43000000, v80
	v_mul_f32_e32 v81, 0x43000000, v81
	v_mul_f32_e32 v82, 0x43000000, v82
	v_mul_f32_e32 v83, 0x43000000, v83
	ds_write_b128 v5, v[80:83] offset:3072
	v_mul_f32_e32 v84, 0x43000000, v84
	v_mul_f32_e32 v85, 0x43000000, v85
	v_mul_f32_e32 v86, 0x43000000, v86
	v_mul_f32_e32 v87, 0x43000000, v87
	ds_write_b128 v5, v[84:87] offset:4096
	v_mul_f32_e32 v88, 0x43000000, v88
	v_mul_f32_e32 v89, 0x43000000, v89
	v_mul_f32_e32 v90, 0x43000000, v90
	v_mul_f32_e32 v91, 0x43000000, v91
	ds_write_b128 v5, v[88:91] offset:5120
	v_mul_f32_e32 v92, 0x43000000, v92
	v_mul_f32_e32 v93, 0x43000000, v93
	v_mul_f32_e32 v94, 0x43000000, v94
	v_mul_f32_e32 v95, 0x43000000, v95
	ds_write_b128 v5, v[92:95] offset:6144
	v_mul_f32_e32 v96, 0x43000000, v96
	v_mul_f32_e32 v97, 0x43000000, v97
	v_mul_f32_e32 v98, 0x43000000, v98
	v_mul_f32_e32 v99, 0x43000000, v99
	ds_write_b128 v5, v[96:99] offset:7168
	s_waitcnt lgkmcnt(0)
	s_barrier
; #define GAS __attribute__((address_space(1)))
; #define LAS __attribute__((address_space(3)))
; #define LDS_WAIT() asm volatile("s_waitcnt lgkmcnt(0)" ::: "memory")
;     ...
;     for (int i = 0; i < 32; ++i) v[i] = sc >= 0 ? W[(size_t)(k0 + 2 * i + (lane >> 5)) * Nsrc + sc] : 0.f;
; #pragma unroll
;     for (int i = 0; i < 32; ++i) { const int k = k0 + 2 * i + (lane >> 5); float x = v[i] * wscale; if (KS) x *= (k < ksplit ? ksA[k] : ksB[k - ksplit]); scr[(2 * i + (lane >> 5)) * 33 + (lane & 31)] = x; }
;     LDS_WAIT(); asm volatile("" ::: "memory");
;     const int c = lane & 7;
; #pragma unroll
;     for (int j = 0; j < 4; ++j) { const int n = (lane >> 3) + 8 * j; const LAS float* s = scr + (8 * c) * 33 + n;
;         const unsigned long long o = (unsigned long long)pg8::pk4_fp8(s[0 * 33], s[1 * 33], s[2 * 33], s[3 * 33]) | ((unsigned long long)pg8::pk4_fp8(s[4 * 33], s[5 * 33], s[6 * 33], s[7 * 33]) << 32);
;         *(GAS unsigned long long*)(WT + (size_t)(n0 + n) * K + k0 + 8 * c) = o; }
	s_add_i32 s17, s16, 1536
	s_min_u32 s17, s17, 0xbff
	s_lshr_b32 s18, s17, 5
	s_add_i32 s18, s18, 32
	s_and_b32 s19, s17, 31
	s_lshl_b32 s18, s18, 21
	s_lshl_b32 s19, s19, 9
	s_add_u32 s18, s18, s19
	s_add_u32 s12, s2, s18
	s_addc_u32 s13, s3, 0
	global_load_dwordx4 v[68:71], v10, s[12:13]
	s_add_u32 s12, s12, 0x8000
	s_addc_u32 s13, s13, 0
	global_load_dwordx4 v[72:75], v10, s[12:13]
	s_add_u32 s12, s12, 0x8000
	s_addc_u32 s13, s13, 0
	global_load_dwordx4 v[76:79], v10, s[12:13]
	s_add_u32 s12, s12, 0x8000
	s_addc_u32 s13, s13, 0
	global_load_dwordx4 v[80:83], v10, s[12:13]
	s_add_u32 s12, s12, 0x8000
	s_addc_u32 s13, s13, 0
	global_load_dwordx4 v[84:87], v10, s[12:13]
	s_add_u32 s12, s12, 0x8000
	s_addc_u32 s13, s13, 0
	global_load_dwordx4 v[88:91], v10, s[12:13]
	s_add_u32 s12, s12, 0x8000
	s_addc_u32 s13, s13, 0
	global_load_dwordx4 v[92:95], v10, s[12:13]
	s_add_u32 s12, s12, 0x8000
	s_addc_u32 s13, s13, 0
	global_load_dwordx4 v[96:99], v10, s[12:13]
	s_add_i32 s17, s16, 1248
	s_min_u32 s17, s17, 0xbff
	s_lshr_b32 s18, s17, 5
	s_add_i32 s18, s18, 32
	s_and_b32 s19, s17, 31
	s_lshl_b32 s19, s19, 21
	s_lshl_b32 s18, s18, 7
	s_add_u32 s18, s18, s19
	s_add_u32 s14, s4, s18
	s_addc_u32 s15, s5, 0
	ds_read_b32 v132, v7
	ds_read_b32 v133, v7 offset:512
	ds_read_b32 v134, v7 offset:1024
	ds_read_b32 v135, v7 offset:1536
	ds_read_b32 v136, v7 offset:2048
	ds_read_b32 v137, v7 offset:2560
	ds_read_b32 v138, v7 offset:3072
	ds_read_b32 v139, v7 offset:3584
	ds_read_b32 v140, v7 offset:4096
	ds_read_b32 v141, v7 offset:4608
	ds_read_b32 v142, v7 offset:5120
	ds_read_b32 v143, v7 offset:5632
	ds_read_b32 v144, v7 offset:6144
	ds_read_b32 v145, v7 offset:6656
	ds_read_b32 v146, v7 offset:7168
	ds_read_b32 v147, v7 offset:7680
	s_waitcnt lgkmcnt(0)
	v_max_f32_e32 v132, v132, v132
	v_max_f32_e32 v133, v133, v133
	v_max_f32_e32 v134, v134, v134
	v_max_f32_e32 v135, v135, v135
	v_max_f32_e32 v136, v136, v136
	v_max_f32_e32 v137, v137, v137
	v_max_f32_e32 v138, v138, v138
	v_max_f32_e32 v139, v139, v139
	v_max_f32_e32 v140, v140, v140
	v_max_f32_e32 v141, v141, v141
	v_max_f32_e32 v142, v142, v142
	v_max_f32_e32 v143, v143, v143
	v_max_f32_e32 v144, v144, v144
	v_max_f32_e32 v145, v145, v145
	v_max_f32_e32 v146, v146, v146
	v_max_f32_e32 v147, v147, v147
	v_med3_f32 v132, v132, s20, v13
	v_med3_f32 v133, v133, s20, v13
	v_med3_f32 v134, v134, s20, v13
	v_med3_f32 v135, v135, s20, v13
	v_med3_f32 v136, v136, s20, v13
	v_med3_f32 v137, v137, s20, v13
	v_med3_f32 v138, v138, s20, v13
	v_med3_f32 v139, v139, s20, v13
	v_med3_f32 v140, v140, s20, v13
	v_med3_f32 v141, v141, s20, v13
	v_med3_f32 v142, v142, s20, v13
	v_med3_f32 v143, v143, s20, v13
	v_med3_f32 v144, v144, s20, v13
	v_med3_f32 v145, v145, s20, v13
	v_med3_f32 v146, v146, s20, v13
	v_med3_f32 v147, v147, s20, v13
	v_mov_b32_e32 v148, 0
	v_mov_b32_e32 v149, 0
	v_mov_b32_e32 v150, 0
	v_mov_b32_e32 v151, 0
	v_cvt_pk_fp8_f32 v148, v132, v133
	v_cvt_pk_fp8_f32 v149, v136, v137
	v_cvt_pk_fp8_f32 v150, v140, v141
	v_cvt_pk_fp8_f32 v151, v144, v145
	v_cvt_pk_fp8_f32 v148, v134, v135 op_sel:[0,0,1]
	v_cvt_pk_fp8_f32 v149, v138, v139 op_sel:[0,0,1]
	v_cvt_pk_fp8_f32 v150, v142, v143 op_sel:[0,0,1]
	v_cvt_pk_fp8_f32 v151, v146, v147 op_sel:[0,0,1]
	s_nop 0
	global_store_dwordx4 v11, v[148:151], s[14:15]
	ds_read_b32 v132, v9
	ds_read_b32 v133, v9 offset:512
	ds_read_b32 v134, v9 offset:1024
	ds_read_b32 v135, v9 offset:1536
	ds_read_b32 v136, v9 offset:2048
	ds_read_b32 v137, v9 offset:2560
	ds_read_b32 v138, v9 offset:3072
	ds_read_b32 v139, v9 offset:3584
	ds_read_b32 v140, v9 offset:4096
	ds_read_b32 v141, v9 offset:4608
	ds_read_b32 v142, v9 offset:5120
	ds_read_b32 v143, v9 offset:5632
	ds_read_b32 v144, v9 offset:6144
	ds_read_b32 v145, v9 offset:6656
	ds_read_b32 v146, v9 offset:7168
	ds_read_b32 v147, v9 offset:7680
	s_waitcnt lgkmcnt(0)
	v_max_f32_e32 v132, v132, v132
	v_max_f32_e32 v133, v133, v133
	v_max_f32_e32 v134, v134, v134
	v_max_f32_e32 v135, v135, v135
	v_max_f32_e32 v136, v136, v136
	v_max_f32_e32 v137, v137, v137
	v_max_f32_e32 v138, v138, v138
	v_max_f32_e32 v139, v139, v139
	v_max_f32_e32 v140, v140, v140
	v_max_f32_e32 v141, v141, v141
	v_max_f32_e32 v142, v142, v142
	v_max_f32_e32 v143, v143, v143
	v_max_f32_e32 v144, v144, v144
	v_max_f32_e32 v145, v145, v145
	v_max_f32_e32 v146, v146, v146
	v_max_f32_e32 v147, v147, v147
	v_med3_f32 v132, v132, s20, v13
	v_med3_f32 v133, v133, s20, v13
	v_med3_f32 v134, v134, s20, v13
	v_med3_f32 v135, v135, s20, v13
	v_med3_f32 v136, v136, s20, v13
	v_med3_f32 v137, v137, s20, v13
	v_med3_f32 v138, v138, s20, v13
	v_med3_f32 v139, v139, s20, v13
	v_med3_f32 v140, v140, s20, v13
	v_med3_f32 v141, v141, s20, v13
	v_med3_f32 v142, v142, s20, v13
	v_med3_f32 v143, v143, s20, v13
	v_med3_f32 v144, v144, s20, v13
	v_med3_f32 v145, v145, s20, v13
	v_med3_f32 v146, v146, s20, v13
	v_med3_f32 v147, v147, s20, v13
	v_mov_b32_e32 v148, 0
	v_mov_b32_e32 v149, 0
	v_mov_b32_e32 v150, 0
	v_mov_b32_e32 v151, 0
	v_cvt_pk_fp8_f32 v148, v132, v133
	v_cvt_pk_fp8_f32 v149, v136, v137
	v_cvt_pk_fp8_f32 v150, v140, v141
	v_cvt_pk_fp8_f32 v151, v144, v145
	v_cvt_pk_fp8_f32 v148, v134, v135 op_sel:[0,0,1]
	v_cvt_pk_fp8_f32 v149, v138, v139 op_sel:[0,0,1]
	v_cvt_pk_fp8_f32 v150, v142, v143 op_sel:[0,0,1]
	v_cvt_pk_fp8_f32 v151, v146, v147 op_sel:[0,0,1]
	s_nop 0
	global_store_dwordx4 v12, v[148:151], s[14:15]
	s_waitcnt vmcnt(22)
	v_mul_f32_e32 v100, 0x43000000, v100
	v_mul_f32_e32 v101, 0x43000000, v101
	v_mul_f32_e32 v102, 0x43000000, v102
	v_mul_f32_e32 v103, 0x43000000, v103
	ds_write_b128 v4, v[100:103]
	v_mul_f32_e32 v104, 0x43000000, v104
	v_mul_f32_e32 v105, 0x43000000, v105
	v_mul_f32_e32 v106, 0x43000000, v106
	v_mul_f32_e32 v107, 0x43000000, v107
	ds_write_b128 v4, v[104:107] offset:1024
	v_mul_f32_e32 v108, 0x43000000, v108
	v_mul_f32_e32 v109, 0x43000000, v109
	v_mul_f32_e32 v110, 0x43000000, v110
	v_mul_f32_e32 v111, 0x43000000, v111
	ds_write_b128 v4, v[108:111] offset:2048
	v_mul_f32_e32 v112, 0x43000000, v112
	v_mul_f32_e32 v113, 0x43000000, v113
	v_mul_f32_e32 v114, 0x43000000, v114
	v_mul_f32_e32 v115, 0x43000000, v115
	ds_write_b128 v4, v[112:115] offset:3072
	v_mul_f32_e32 v116, 0x43000000, v116
	v_mul_f32_e32 v117, 0x43000000, v117
	v_mul_f32_e32 v118, 0x43000000, v118
	v_mul_f32_e32 v119, 0x43000000, v119
	ds_write_b128 v4, v[116:119] offset:4096
	v_mul_f32_e32 v120, 0x43000000, v120
	v_mul_f32_e32 v121, 0x43000000, v121
	v_mul_f32_e32 v122, 0x43000000, v122
	v_mul_f32_e32 v123, 0x43000000, v123
	ds_write_b128 v4, v[120:123] offset:5120
	v_mul_f32_e32 v124, 0x43000000, v124
	v_mul_f32_e32 v125, 0x43000000, v125
	v_mul_f32_e32 v126, 0x43000000, v126
	v_mul_f32_e32 v127, 0x43000000, v127
	ds_write_b128 v4, v[124:127] offset:6144
	v_mul_f32_e32 v128, 0x43000000, v128
	v_mul_f32_e32 v129, 0x43000000, v129
	v_mul_f32_e32 v130, 0x43000000, v130
	v_mul_f32_e32 v131, 0x43000000, v131
	ds_write_b128 v4, v[128:131] offset:7168
	s_waitcnt lgkmcnt(0)
	s_barrier
; #define GAS __attribute__((address_space(1)))
; #define LAS __attribute__((address_space(3)))
; #define LDS_WAIT() asm volatile("s_waitcnt lgkmcnt(0)" ::: "memory")
;     ...
;     for (int i = 0; i < 32; ++i) v[i] = sc >= 0 ? W[(size_t)(k0 + 2 * i + (lane >> 5)) * Nsrc + sc] : 0.f;
; #pragma unroll
;     for (int i = 0; i < 32; ++i) { const int k = k0 + 2 * i + (lane >> 5); float x = v[i] * wscale; if (KS) x *= (k < ksplit ? ksA[k] : ksB[k - ksplit]); scr[(2 * i + (lane >> 5)) * 33 + (lane & 31)] = x; }
;     LDS_WAIT(); asm volatile("" ::: "memory");
;     const int c = lane & 7;
; #pragma unroll
;     for (int j = 0; j < 4; ++j) { const int n = (lane >> 3) + 8 * j; const LAS float* s = scr + (8 * c) * 33 + n;
;         const unsigned long long o = (unsigned long long)pg8::pk4_fp8(s[0 * 33], s[1 * 33], s[2 * 33], s[3 * 33]) | ((unsigned long long)pg8::pk4_fp8(s[4 * 33], s[5 * 33], s[6 * 33], s[7 * 33]) << 32);
;         *(GAS unsigned long long*)(WT + (size_t)(n0 + n) * K + k0 + 8 * c) = o; }
	s_add_i32 s17, s16, 1632
	s_min_u32 s17, s17, 0xbff
	s_lshr_b32 s18, s17, 5
	s_add_i32 s18, s18, 32
	s_and_b32 s19, s17, 31
	s_lshl_b32 s18, s18, 21
	s_lshl_b32 s19, s19, 9
	s_add_u32 s18, s18, s19
	s_add_u32 s12, s2, s18
	s_addc_u32 s13, s3, 0
	global_load_dwordx4 v[100:103], v10, s[12:13]
	s_add_u32 s12, s12, 0x8000
	s_addc_u32 s13, s13, 0
	global_load_dwordx4 v[104:107], v10, s[12:13]
	s_add_u32 s12, s12, 0x8000
	s_addc_u32 s13, s13, 0
	global_load_dwordx4 v[108:111], v10, s[12:13]
	s_add_u32 s12, s12, 0x8000
	s_addc_u32 s13, s13, 0
	global_load_dwordx4 v[112:115], v10, s[12:13]
	s_add_u32 s12, s12, 0x8000
	s_addc_u32 s13, s13, 0
	global_load_dwordx4 v[116:119], v10, s[12:13]
	s_add_u32 s12, s12, 0x8000
	s_addc_u32 s13, s13, 0
	global_load_dwordx4 v[120:123], v10, s[12:13]
	s_add_u32 s12, s12, 0x8000
	s_addc_u32 s13, s13, 0
	global_load_dwordx4 v[124:127], v10, s[12:13]
	s_add_u32 s12, s12, 0x8000
	s_addc_u32 s13, s13, 0
	global_load_dwordx4 v[128:131], v10, s[12:13]
	s_add_i32 s17, s16, 1344
	s_min_u32 s17, s17, 0xbff
	s_lshr_b32 s18, s17, 5
	s_add_i32 s18, s18, 32
	s_and_b32 s19, s17, 31
	s_lshl_b32 s19, s19, 21
	s_lshl_b32 s18, s18, 7
	s_add_u32 s18, s18, s19
	s_add_u32 s14, s4, s18
	s_addc_u32 s15, s5, 0
	ds_read_b32 v132, v6
	ds_read_b32 v133, v6 offset:512
	ds_read_b32 v134, v6 offset:1024
	ds_read_b32 v135, v6 offset:1536
	ds_read_b32 v136, v6 offset:2048
	ds_read_b32 v137, v6 offset:2560
	ds_read_b32 v138, v6 offset:3072
	ds_read_b32 v139, v6 offset:3584
	ds_read_b32 v140, v6 offset:4096
	ds_read_b32 v141, v6 offset:4608
	ds_read_b32 v142, v6 offset:5120
	ds_read_b32 v143, v6 offset:5632
	ds_read_b32 v144, v6 offset:6144
	ds_read_b32 v145, v6 offset:6656
	ds_read_b32 v146, v6 offset:7168
	ds_read_b32 v147, v6 offset:7680
	s_waitcnt lgkmcnt(0)
	v_max_f32_e32 v132, v132, v132
	v_max_f32_e32 v133, v133, v133
	v_max_f32_e32 v134, v134, v134
	v_max_f32_e32 v135, v135, v135
	v_max_f32_e32 v136, v136, v136
	v_max_f32_e32 v137, v137, v137
	v_max_f32_e32 v138, v138, v138
	v_max_f32_e32 v139, v139, v139
	v_max_f32_e32 v140, v140, v140
	v_max_f32_e32 v141, v141, v141
	v_max_f32_e32 v142, v142, v142
	v_max_f32_e32 v143, v143, v143
	v_max_f32_e32 v144, v144, v144
	v_max_f32_e32 v145, v145, v145
	v_max_f32_e32 v146, v146, v146
	v_max_f32_e32 v147, v147, v147
	v_med3_f32 v132, v132, s20, v13
	v_med3_f32 v133, v133, s20, v13
	v_med3_f32 v134, v134, s20, v13
	v_med3_f32 v135, v135, s20, v13
	v_med3_f32 v136, v136, s20, v13
	v_med3_f32 v137, v137, s20, v13
	v_med3_f32 v138, v138, s20, v13
	v_med3_f32 v139, v139, s20, v13
	v_med3_f32 v140, v140, s20, v13
	v_med3_f32 v141, v141, s20, v13
	v_med3_f32 v142, v142, s20, v13
	v_med3_f32 v143, v143, s20, v13
	v_med3_f32 v144, v144, s20, v13
	v_med3_f32 v145, v145, s20, v13
	v_med3_f32 v146, v146, s20, v13
	v_med3_f32 v147, v147, s20, v13
	v_mov_b32_e32 v148, 0
	v_mov_b32_e32 v149, 0
	v_mov_b32_e32 v150, 0
	v_mov_b32_e32 v151, 0
	v_cvt_pk_fp8_f32 v148, v132, v133
	v_cvt_pk_fp8_f32 v149, v136, v137
	v_cvt_pk_fp8_f32 v150, v140, v141
	v_cvt_pk_fp8_f32 v151, v144, v145
	v_cvt_pk_fp8_f32 v148, v134, v135 op_sel:[0,0,1]
	v_cvt_pk_fp8_f32 v149, v138, v139 op_sel:[0,0,1]
	v_cvt_pk_fp8_f32 v150, v142, v143 op_sel:[0,0,1]
	v_cvt_pk_fp8_f32 v151, v146, v147 op_sel:[0,0,1]
	s_nop 0
	global_store_dwordx4 v11, v[148:151], s[14:15]
	ds_read_b32 v132, v8
	ds_read_b32 v133, v8 offset:512
	ds_read_b32 v134, v8 offset:1024
	ds_read_b32 v135, v8 offset:1536
	ds_read_b32 v136, v8 offset:2048
	ds_read_b32 v137, v8 offset:2560
	ds_read_b32 v138, v8 offset:3072
	ds_read_b32 v139, v8 offset:3584
	ds_read_b32 v140, v8 offset:4096
	ds_read_b32 v141, v8 offset:4608
	ds_read_b32 v142, v8 offset:5120
	ds_read_b32 v143, v8 offset:5632
	ds_read_b32 v144, v8 offset:6144
	ds_read_b32 v145, v8 offset:6656
	ds_read_b32 v146, v8 offset:7168
	ds_read_b32 v147, v8 offset:7680
	s_waitcnt lgkmcnt(0)
	v_max_f32_e32 v132, v132, v132
	v_max_f32_e32 v133, v133, v133
	v_max_f32_e32 v134, v134, v134
	v_max_f32_e32 v135, v135, v135
	v_max_f32_e32 v136, v136, v136
	v_max_f32_e32 v137, v137, v137
	v_max_f32_e32 v138, v138, v138
	v_max_f32_e32 v139, v139, v139
	v_max_f32_e32 v140, v140, v140
	v_max_f32_e32 v141, v141, v141
	v_max_f32_e32 v142, v142, v142
	v_max_f32_e32 v143, v143, v143
	v_max_f32_e32 v144, v144, v144
	v_max_f32_e32 v145, v145, v145
	v_max_f32_e32 v146, v146, v146
	v_max_f32_e32 v147, v147, v147
	v_med3_f32 v132, v132, s20, v13
	v_med3_f32 v133, v133, s20, v13
	v_med3_f32 v134, v134, s20, v13
	v_med3_f32 v135, v135, s20, v13
	v_med3_f32 v136, v136, s20, v13
	v_med3_f32 v137, v137, s20, v13
	v_med3_f32 v138, v138, s20, v13
	v_med3_f32 v139, v139, s20, v13
	v_med3_f32 v140, v140, s20, v13
	v_med3_f32 v141, v141, s20, v13
	v_med3_f32 v142, v142, s20, v13
	v_med3_f32 v143, v143, s20, v13
	v_med3_f32 v144, v144, s20, v13
	v_med3_f32 v145, v145, s20, v13
	v_med3_f32 v146, v146, s20, v13
	v_med3_f32 v147, v147, s20, v13
	v_mov_b32_e32 v148, 0
	v_mov_b32_e32 v149, 0
	v_mov_b32_e32 v150, 0
	v_mov_b32_e32 v151, 0
	v_cvt_pk_fp8_f32 v148, v132, v133
	v_cvt_pk_fp8_f32 v149, v136, v137
	v_cvt_pk_fp8_f32 v150, v140, v141
	v_cvt_pk_fp8_f32 v151, v144, v145
	v_cvt_pk_fp8_f32 v148, v134, v135 op_sel:[0,0,1]
	v_cvt_pk_fp8_f32 v149, v138, v139 op_sel:[0,0,1]
	v_cvt_pk_fp8_f32 v150, v142, v143 op_sel:[0,0,1]
	v_cvt_pk_fp8_f32 v151, v146, v147 op_sel:[0,0,1]
	s_nop 0
	global_store_dwordx4 v12, v[148:151], s[14:15]
	s_waitcnt vmcnt(22)
	v_mul_f32_e32 v36, 0x43000000, v36
	v_mul_f32_e32 v37, 0x43000000, v37
	v_mul_f32_e32 v38, 0x43000000, v38
	v_mul_f32_e32 v39, 0x43000000, v39
	ds_write_b128 v5, v[36:39]
	v_mul_f32_e32 v40, 0x43000000, v40
	v_mul_f32_e32 v41, 0x43000000, v41
	v_mul_f32_e32 v42, 0x43000000, v42
	v_mul_f32_e32 v43, 0x43000000, v43
	ds_write_b128 v5, v[40:43] offset:1024
	v_mul_f32_e32 v44, 0x43000000, v44
	v_mul_f32_e32 v45, 0x43000000, v45
	v_mul_f32_e32 v46, 0x43000000, v46
	v_mul_f32_e32 v47, 0x43000000, v47
	ds_write_b128 v5, v[44:47] offset:2048
	v_mul_f32_e32 v48, 0x43000000, v48
	v_mul_f32_e32 v49, 0x43000000, v49
	v_mul_f32_e32 v50, 0x43000000, v50
	v_mul_f32_e32 v51, 0x43000000, v51
	ds_write_b128 v5, v[48:51] offset:3072
	v_mul_f32_e32 v52, 0x43000000, v52
	v_mul_f32_e32 v53, 0x43000000, v53
	v_mul_f32_e32 v54, 0x43000000, v54
	v_mul_f32_e32 v55, 0x43000000, v55
	ds_write_b128 v5, v[52:55] offset:4096
	v_mul_f32_e32 v56, 0x43000000, v56
	v_mul_f32_e32 v57, 0x43000000, v57
	v_mul_f32_e32 v58, 0x43000000, v58
	v_mul_f32_e32 v59, 0x43000000, v59
	ds_write_b128 v5, v[56:59] offset:5120
	v_mul_f32_e32 v60, 0x43000000, v60
	v_mul_f32_e32 v61, 0x43000000, v61
	v_mul_f32_e32 v62, 0x43000000, v62
	v_mul_f32_e32 v63, 0x43000000, v63
	ds_write_b128 v5, v[60:63] offset:6144
	v_mul_f32_e32 v64, 0x43000000, v64
	v_mul_f32_e32 v65, 0x43000000, v65
	v_mul_f32_e32 v66, 0x43000000, v66
	v_mul_f32_e32 v67, 0x43000000, v67
	ds_write_b128 v5, v[64:67] offset:7168
	s_waitcnt lgkmcnt(0)
	s_barrier
; #define GAS __attribute__((address_space(1)))
; #define LAS __attribute__((address_space(3)))
; #define LDS_WAIT() asm volatile("s_waitcnt lgkmcnt(0)" ::: "memory")
;     ...
;     for (int i = 0; i < 32; ++i) v[i] = sc >= 0 ? W[(size_t)(k0 + 2 * i + (lane >> 5)) * Nsrc + sc] : 0.f;
; #pragma unroll
;     for (int i = 0; i < 32; ++i) { const int k = k0 + 2 * i + (lane >> 5); float x = v[i] * wscale; if (KS) x *= (k < ksplit ? ksA[k] : ksB[k - ksplit]); scr[(2 * i + (lane >> 5)) * 33 + (lane & 31)] = x; }
;     LDS_WAIT(); asm volatile("" ::: "memory");
;     const int c = lane & 7;
; #pragma unroll
;     for (int j = 0; j < 4; ++j) { const int n = (lane >> 3) + 8 * j; const LAS float* s = scr + (8 * c) * 33 + n;
;         const unsigned long long o = (unsigned long long)pg8::pk4_fp8(s[0 * 33], s[1 * 33], s[2 * 33], s[3 * 33]) | ((unsigned long long)pg8::pk4_fp8(s[4 * 33], s[5 * 33], s[6 * 33], s[7 * 33]) << 32);
;         *(GAS unsigned long long*)(WT + (size_t)(n0 + n) * K + k0 + 8 * c) = o; }
	s_add_i32 s17, s16, 1728
	s_min_u32 s17, s17, 0xbff
	s_lshr_b32 s18, s17, 5
	s_add_i32 s18, s18, 32
	s_and_b32 s19, s17, 31
	s_lshl_b32 s18, s18, 21
	s_lshl_b32 s19, s19, 9
	s_add_u32 s18, s18, s19
	s_add_u32 s12, s2, s18
	s_addc_u32 s13, s3, 0
	global_load_dwordx4 v[36:39], v10, s[12:13]
	s_add_u32 s12, s12, 0x8000
	s_addc_u32 s13, s13, 0
	global_load_dwordx4 v[40:43], v10, s[12:13]
	s_add_u32 s12, s12, 0x8000
	s_addc_u32 s13, s13, 0
	global_load_dwordx4 v[44:47], v10, s[12:13]
	s_add_u32 s12, s12, 0x8000
	s_addc_u32 s13, s13, 0
	global_load_dwordx4 v[48:51], v10, s[12:13]
	s_add_u32 s12, s12, 0x8000
	s_addc_u32 s13, s13, 0
	global_load_dwordx4 v[52:55], v10, s[12:13]
	s_add_u32 s12, s12, 0x8000
	s_addc_u32 s13, s13, 0
	global_load_dwordx4 v[56:59], v10, s[12:13]
	s_add_u32 s12, s12, 0x8000
	s_addc_u32 s13, s13, 0
	global_load_dwordx4 v[60:63], v10, s[12:13]
	s_add_u32 s12, s12, 0x8000
	s_addc_u32 s13, s13, 0
	global_load_dwordx4 v[64:67], v10, s[12:13]
	s_add_i32 s17, s16, 1440
	s_min_u32 s17, s17, 0xbff
	s_lshr_b32 s18, s17, 5
	s_add_i32 s18, s18, 32
	s_and_b32 s19, s17, 31
	s_lshl_b32 s19, s19, 21
	s_lshl_b32 s18, s18, 7
	s_add_u32 s18, s18, s19
	s_add_u32 s14, s4, s18
	s_addc_u32 s15, s5, 0
	ds_read_b32 v132, v7
	ds_read_b32 v133, v7 offset:512
	ds_read_b32 v134, v7 offset:1024
	ds_read_b32 v135, v7 offset:1536
	ds_read_b32 v136, v7 offset:2048
	ds_read_b32 v137, v7 offset:2560
	ds_read_b32 v138, v7 offset:3072
	ds_read_b32 v139, v7 offset:3584
	ds_read_b32 v140, v7 offset:4096
	ds_read_b32 v141, v7 offset:4608
	ds_read_b32 v142, v7 offset:5120
	ds_read_b32 v143, v7 offset:5632
	ds_read_b32 v144, v7 offset:6144
	ds_read_b32 v145, v7 offset:6656
	ds_read_b32 v146, v7 offset:7168
	ds_read_b32 v147, v7 offset:7680
	s_waitcnt lgkmcnt(0)
	v_max_f32_e32 v132, v132, v132
	v_max_f32_e32 v133, v133, v133
	v_max_f32_e32 v134, v134, v134
	v_max_f32_e32 v135, v135, v135
	v_max_f32_e32 v136, v136, v136
	v_max_f32_e32 v137, v137, v137
	v_max_f32_e32 v138, v138, v138
	v_max_f32_e32 v139, v139, v139
	v_max_f32_e32 v140, v140, v140
	v_max_f32_e32 v141, v141, v141
	v_max_f32_e32 v142, v142, v142
	v_max_f32_e32 v143, v143, v143
	v_max_f32_e32 v144, v144, v144
	v_max_f32_e32 v145, v145, v145
	v_max_f32_e32 v146, v146, v146
	v_max_f32_e32 v147, v147, v147
	v_med3_f32 v132, v132, s20, v13
	v_med3_f32 v133, v133, s20, v13
	v_med3_f32 v134, v134, s20, v13
	v_med3_f32 v135, v135, s20, v13
	v_med3_f32 v136, v136, s20, v13
	v_med3_f32 v137, v137, s20, v13
	v_med3_f32 v138, v138, s20, v13
	v_med3_f32 v139, v139, s20, v13
	v_med3_f32 v140, v140, s20, v13
	v_med3_f32 v141, v141, s20, v13
	v_med3_f32 v142, v142, s20, v13
	v_med3_f32 v143, v143, s20, v13
	v_med3_f32 v144, v144, s20, v13
	v_med3_f32 v145, v145, s20, v13
	v_med3_f32 v146, v146, s20, v13
	v_med3_f32 v147, v147, s20, v13
	v_mov_b32_e32 v148, 0
	v_mov_b32_e32 v149, 0
	v_mov_b32_e32 v150, 0
	v_mov_b32_e32 v151, 0
	v_cvt_pk_fp8_f32 v148, v132, v133
	v_cvt_pk_fp8_f32 v149, v136, v137
	v_cvt_pk_fp8_f32 v150, v140, v141
	v_cvt_pk_fp8_f32 v151, v144, v145
	v_cvt_pk_fp8_f32 v148, v134, v135 op_sel:[0,0,1]
	v_cvt_pk_fp8_f32 v149, v138, v139 op_sel:[0,0,1]
	v_cvt_pk_fp8_f32 v150, v142, v143 op_sel:[0,0,1]
	v_cvt_pk_fp8_f32 v151, v146, v147 op_sel:[0,0,1]
	s_nop 0
	global_store_dwordx4 v11, v[148:151], s[14:15]
	ds_read_b32 v132, v9
	ds_read_b32 v133, v9 offset:512
	ds_read_b32 v134, v9 offset:1024
	ds_read_b32 v135, v9 offset:1536
	ds_read_b32 v136, v9 offset:2048
	ds_read_b32 v137, v9 offset:2560
	ds_read_b32 v138, v9 offset:3072
	ds_read_b32 v139, v9 offset:3584
	ds_read_b32 v140, v9 offset:4096
	ds_read_b32 v141, v9 offset:4608
	ds_read_b32 v142, v9 offset:5120
	ds_read_b32 v143, v9 offset:5632
	ds_read_b32 v144, v9 offset:6144
	ds_read_b32 v145, v9 offset:6656
	ds_read_b32 v146, v9 offset:7168
	ds_read_b32 v147, v9 offset:7680
	s_waitcnt lgkmcnt(0)
	v_max_f32_e32 v132, v132, v132
	v_max_f32_e32 v133, v133, v133
	v_max_f32_e32 v134, v134, v134
	v_max_f32_e32 v135, v135, v135
	v_max_f32_e32 v136, v136, v136
	v_max_f32_e32 v137, v137, v137
	v_max_f32_e32 v138, v138, v138
	v_max_f32_e32 v139, v139, v139
	v_max_f32_e32 v140, v140, v140
	v_max_f32_e32 v141, v141, v141
	v_max_f32_e32 v142, v142, v142
	v_max_f32_e32 v143, v143, v143
	v_max_f32_e32 v144, v144, v144
	v_max_f32_e32 v145, v145, v145
	v_max_f32_e32 v146, v146, v146
	v_max_f32_e32 v147, v147, v147
	v_med3_f32 v132, v132, s20, v13
	v_med3_f32 v133, v133, s20, v13
	v_med3_f32 v134, v134, s20, v13
	v_med3_f32 v135, v135, s20, v13
	v_med3_f32 v136, v136, s20, v13
	v_med3_f32 v137, v137, s20, v13
	v_med3_f32 v138, v138, s20, v13
	v_med3_f32 v139, v139, s20, v13
	v_med3_f32 v140, v140, s20, v13
	v_med3_f32 v141, v141, s20, v13
	v_med3_f32 v142, v142, s20, v13
	v_med3_f32 v143, v143, s20, v13
	v_med3_f32 v144, v144, s20, v13
	v_med3_f32 v145, v145, s20, v13
	v_med3_f32 v146, v146, s20, v13
	v_med3_f32 v147, v147, s20, v13
	v_mov_b32_e32 v148, 0
	v_mov_b32_e32 v149, 0
	v_mov_b32_e32 v150, 0
	v_mov_b32_e32 v151, 0
	v_cvt_pk_fp8_f32 v148, v132, v133
	v_cvt_pk_fp8_f32 v149, v136, v137
	v_cvt_pk_fp8_f32 v150, v140, v141
	v_cvt_pk_fp8_f32 v151, v144, v145
	v_cvt_pk_fp8_f32 v148, v134, v135 op_sel:[0,0,1]
	v_cvt_pk_fp8_f32 v149, v138, v139 op_sel:[0,0,1]
	v_cvt_pk_fp8_f32 v150, v142, v143 op_sel:[0,0,1]
	v_cvt_pk_fp8_f32 v151, v146, v147 op_sel:[0,0,1]
	s_nop 0
	global_store_dwordx4 v12, v[148:151], s[14:15]
	s_waitcnt vmcnt(22)
	v_mul_f32_e32 v68, 0x43000000, v68
	v_mul_f32_e32 v69, 0x43000000, v69
	v_mul_f32_e32 v70, 0x43000000, v70
	v_mul_f32_e32 v71, 0x43000000, v71
	ds_write_b128 v4, v[68:71]
	v_mul_f32_e32 v72, 0x43000000, v72
	v_mul_f32_e32 v73, 0x43000000, v73
	v_mul_f32_e32 v74, 0x43000000, v74
	v_mul_f32_e32 v75, 0x43000000, v75
	ds_write_b128 v4, v[72:75] offset:1024
	v_mul_f32_e32 v76, 0x43000000, v76
	v_mul_f32_e32 v77, 0x43000000, v77
	v_mul_f32_e32 v78, 0x43000000, v78
	v_mul_f32_e32 v79, 0x43000000, v79
	ds_write_b128 v4, v[76:79] offset:2048
	v_mul_f32_e32 v80, 0x43000000, v80
	v_mul_f32_e32 v81, 0x43000000, v81
	v_mul_f32_e32 v82, 0x43000000, v82
	v_mul_f32_e32 v83, 0x43000000, v83
	ds_write_b128 v4, v[80:83] offset:3072
	v_mul_f32_e32 v84, 0x43000000, v84
	v_mul_f32_e32 v85, 0x43000000, v85
	v_mul_f32_e32 v86, 0x43000000, v86
	v_mul_f32_e32 v87, 0x43000000, v87
	ds_write_b128 v4, v[84:87] offset:4096
	v_mul_f32_e32 v88, 0x43000000, v88
	v_mul_f32_e32 v89, 0x43000000, v89
	v_mul_f32_e32 v90, 0x43000000, v90
	v_mul_f32_e32 v91, 0x43000000, v91
	ds_write_b128 v4, v[88:91] offset:5120
	v_mul_f32_e32 v92, 0x43000000, v92
	v_mul_f32_e32 v93, 0x43000000, v93
	v_mul_f32_e32 v94, 0x43000000, v94
	v_mul_f32_e32 v95, 0x43000000, v95
	ds_write_b128 v4, v[92:95] offset:6144
	v_mul_f32_e32 v96, 0x43000000, v96
	v_mul_f32_e32 v97, 0x43000000, v97
	v_mul_f32_e32 v98, 0x43000000, v98
	v_mul_f32_e32 v99, 0x43000000, v99
	ds_write_b128 v4, v[96:99] offset:7168
	s_waitcnt lgkmcnt(0)
	s_barrier
; #define GAS __attribute__((address_space(1)))
; #define LAS __attribute__((address_space(3)))
; #define LDS_WAIT() asm volatile("s_waitcnt lgkmcnt(0)" ::: "memory")
;     ...
;     for (int i = 0; i < 32; ++i) v[i] = sc >= 0 ? W[(size_t)(k0 + 2 * i + (lane >> 5)) * Nsrc + sc] : 0.f;
; #pragma unroll
;     for (int i = 0; i < 32; ++i) { const int k = k0 + 2 * i + (lane >> 5); float x = v[i] * wscale; if (KS) x *= (k < ksplit ? ksA[k] : ksB[k - ksplit]); scr[(2 * i + (lane >> 5)) * 33 + (lane & 31)] = x; }
;     LDS_WAIT(); asm volatile("" ::: "memory");
;     const int c = lane & 7;
; #pragma unroll
;     for (int j = 0; j < 4; ++j) { const int n = (lane >> 3) + 8 * j; const LAS float* s = scr + (8 * c) * 33 + n;
;         const unsigned long long o = (unsigned long long)pg8::pk4_fp8(s[0 * 33], s[1 * 33], s[2 * 33], s[3 * 33]) | ((unsigned long long)pg8::pk4_fp8(s[4 * 33], s[5 * 33], s[6 * 33], s[7 * 33]) << 32);
;         *(GAS unsigned long long*)(WT + (size_t)(n0 + n) * K + k0 + 8 * c) = o; }
	s_add_i32 s17, s16, 1824
	s_min_u32 s17, s17, 0xbff
	s_lshr_b32 s18, s17, 5
	s_add_i32 s18, s18, 32
	s_and_b32 s19, s17, 31
	s_lshl_b32 s18, s18, 21
	s_lshl_b32 s19, s19, 9
	s_add_u32 s18, s18, s19
	s_add_u32 s12, s2, s18
	s_addc_u32 s13, s3, 0
	global_load_dwordx4 v[68:71], v10, s[12:13]
	s_add_u32 s12, s12, 0x8000
	s_addc_u32 s13, s13, 0
	global_load_dwordx4 v[72:75], v10, s[12:13]
	s_add_u32 s12, s12, 0x8000
	s_addc_u32 s13, s13, 0
	global_load_dwordx4 v[76:79], v10, s[12:13]
	s_add_u32 s12, s12, 0x8000
	s_addc_u32 s13, s13, 0
	global_load_dwordx4 v[80:83], v10, s[12:13]
	s_add_u32 s12, s12, 0x8000
	s_addc_u32 s13, s13, 0
	global_load_dwordx4 v[84:87], v10, s[12:13]
	s_add_u32 s12, s12, 0x8000
	s_addc_u32 s13, s13, 0
	global_load_dwordx4 v[88:91], v10, s[12:13]
	s_add_u32 s12, s12, 0x8000
	s_addc_u32 s13, s13, 0
	global_load_dwordx4 v[92:95], v10, s[12:13]
	s_add_u32 s12, s12, 0x8000
	s_addc_u32 s13, s13, 0
	global_load_dwordx4 v[96:99], v10, s[12:13]
	s_add_i32 s17, s16, 1536
	s_min_u32 s17, s17, 0xbff
	s_lshr_b32 s18, s17, 5
	s_add_i32 s18, s18, 32
	s_and_b32 s19, s17, 31
	s_lshl_b32 s19, s19, 21
	s_lshl_b32 s18, s18, 7
	s_add_u32 s18, s18, s19
	s_add_u32 s14, s4, s18
	s_addc_u32 s15, s5, 0
	ds_read_b32 v132, v6
	ds_read_b32 v133, v6 offset:512
	ds_read_b32 v134, v6 offset:1024
	ds_read_b32 v135, v6 offset:1536
	ds_read_b32 v136, v6 offset:2048
	ds_read_b32 v137, v6 offset:2560
	ds_read_b32 v138, v6 offset:3072
	ds_read_b32 v139, v6 offset:3584
	ds_read_b32 v140, v6 offset:4096
	ds_read_b32 v141, v6 offset:4608
	ds_read_b32 v142, v6 offset:5120
	ds_read_b32 v143, v6 offset:5632
	ds_read_b32 v144, v6 offset:6144
	ds_read_b32 v145, v6 offset:6656
	ds_read_b32 v146, v6 offset:7168
	ds_read_b32 v147, v6 offset:7680
	s_waitcnt lgkmcnt(0)
	v_max_f32_e32 v132, v132, v132
	v_max_f32_e32 v133, v133, v133
	v_max_f32_e32 v134, v134, v134
	v_max_f32_e32 v135, v135, v135
	v_max_f32_e32 v136, v136, v136
	v_max_f32_e32 v137, v137, v137
	v_max_f32_e32 v138, v138, v138
	v_max_f32_e32 v139, v139, v139
	v_max_f32_e32 v140, v140, v140
	v_max_f32_e32 v141, v141, v141
	v_max_f32_e32 v142, v142, v142
	v_max_f32_e32 v143, v143, v143
	v_max_f32_e32 v144, v144, v144
	v_max_f32_e32 v145, v145, v145
	v_max_f32_e32 v146, v146, v146
	v_max_f32_e32 v147, v147, v147
	v_med3_f32 v132, v132, s20, v13
	v_med3_f32 v133, v133, s20, v13
	v_med3_f32 v134, v134, s20, v13
	v_med3_f32 v135, v135, s20, v13
	v_med3_f32 v136, v136, s20, v13
	v_med3_f32 v137, v137, s20, v13
	v_med3_f32 v138, v138, s20, v13
	v_med3_f32 v139, v139, s20, v13
	v_med3_f32 v140, v140, s20, v13
	v_med3_f32 v141, v141, s20, v13
	v_med3_f32 v142, v142, s20, v13
	v_med3_f32 v143, v143, s20, v13
	v_med3_f32 v144, v144, s20, v13
	v_med3_f32 v145, v145, s20, v13
	v_med3_f32 v146, v146, s20, v13
	v_med3_f32 v147, v147, s20, v13
	v_mov_b32_e32 v148, 0
	v_mov_b32_e32 v149, 0
	v_mov_b32_e32 v150, 0
	v_mov_b32_e32 v151, 0
	v_cvt_pk_fp8_f32 v148, v132, v133
	v_cvt_pk_fp8_f32 v149, v136, v137
	v_cvt_pk_fp8_f32 v150, v140, v141
	v_cvt_pk_fp8_f32 v151, v144, v145
	v_cvt_pk_fp8_f32 v148, v134, v135 op_sel:[0,0,1]
	v_cvt_pk_fp8_f32 v149, v138, v139 op_sel:[0,0,1]
	v_cvt_pk_fp8_f32 v150, v142, v143 op_sel:[0,0,1]
	v_cvt_pk_fp8_f32 v151, v146, v147 op_sel:[0,0,1]
	s_nop 0
	global_store_dwordx4 v11, v[148:151], s[14:15]
	ds_read_b32 v132, v8
	ds_read_b32 v133, v8 offset:512
	ds_read_b32 v134, v8 offset:1024
	ds_read_b32 v135, v8 offset:1536
	ds_read_b32 v136, v8 offset:2048
	ds_read_b32 v137, v8 offset:2560
	ds_read_b32 v138, v8 offset:3072
	ds_read_b32 v139, v8 offset:3584
	ds_read_b32 v140, v8 offset:4096
	ds_read_b32 v141, v8 offset:4608
	ds_read_b32 v142, v8 offset:5120
	ds_read_b32 v143, v8 offset:5632
	ds_read_b32 v144, v8 offset:6144
	ds_read_b32 v145, v8 offset:6656
	ds_read_b32 v146, v8 offset:7168
	ds_read_b32 v147, v8 offset:7680
	s_waitcnt lgkmcnt(0)
	v_max_f32_e32 v132, v132, v132
	v_max_f32_e32 v133, v133, v133
	v_max_f32_e32 v134, v134, v134
	v_max_f32_e32 v135, v135, v135
	v_max_f32_e32 v136, v136, v136
	v_max_f32_e32 v137, v137, v137
	v_max_f32_e32 v138, v138, v138
	v_max_f32_e32 v139, v139, v139
	v_max_f32_e32 v140, v140, v140
	v_max_f32_e32 v141, v141, v141
	v_max_f32_e32 v142, v142, v142
	v_max_f32_e32 v143, v143, v143
	v_max_f32_e32 v144, v144, v144
	v_max_f32_e32 v145, v145, v145
	v_max_f32_e32 v146, v146, v146
	v_max_f32_e32 v147, v147, v147
	v_med3_f32 v132, v132, s20, v13
	v_med3_f32 v133, v133, s20, v13
	v_med3_f32 v134, v134, s20, v13
	v_med3_f32 v135, v135, s20, v13
	v_med3_f32 v136, v136, s20, v13
	v_med3_f32 v137, v137, s20, v13
	v_med3_f32 v138, v138, s20, v13
	v_med3_f32 v139, v139, s20, v13
	v_med3_f32 v140, v140, s20, v13
	v_med3_f32 v141, v141, s20, v13
	v_med3_f32 v142, v142, s20, v13
	v_med3_f32 v143, v143, s20, v13
	v_med3_f32 v144, v144, s20, v13
	v_med3_f32 v145, v145, s20, v13
	v_med3_f32 v146, v146, s20, v13
	v_med3_f32 v147, v147, s20, v13
	v_mov_b32_e32 v148, 0
	v_mov_b32_e32 v149, 0
	v_mov_b32_e32 v150, 0
	v_mov_b32_e32 v151, 0
	v_cvt_pk_fp8_f32 v148, v132, v133
	v_cvt_pk_fp8_f32 v149, v136, v137
	v_cvt_pk_fp8_f32 v150, v140, v141
	v_cvt_pk_fp8_f32 v151, v144, v145
	v_cvt_pk_fp8_f32 v148, v134, v135 op_sel:[0,0,1]
	v_cvt_pk_fp8_f32 v149, v138, v139 op_sel:[0,0,1]
	v_cvt_pk_fp8_f32 v150, v142, v143 op_sel:[0,0,1]
	v_cvt_pk_fp8_f32 v151, v146, v147 op_sel:[0,0,1]
	s_nop 0
	global_store_dwordx4 v12, v[148:151], s[14:15]
	s_waitcnt vmcnt(22)
	v_mul_f32_e32 v100, 0x43000000, v100
	v_mul_f32_e32 v101, 0x43000000, v101
	v_mul_f32_e32 v102, 0x43000000, v102
	v_mul_f32_e32 v103, 0x43000000, v103
	ds_write_b128 v5, v[100:103]
	v_mul_f32_e32 v104, 0x43000000, v104
	v_mul_f32_e32 v105, 0x43000000, v105
	v_mul_f32_e32 v106, 0x43000000, v106
	v_mul_f32_e32 v107, 0x43000000, v107
	ds_write_b128 v5, v[104:107] offset:1024
	v_mul_f32_e32 v108, 0x43000000, v108
	v_mul_f32_e32 v109, 0x43000000, v109
	v_mul_f32_e32 v110, 0x43000000, v110
	v_mul_f32_e32 v111, 0x43000000, v111
	ds_write_b128 v5, v[108:111] offset:2048
	v_mul_f32_e32 v112, 0x43000000, v112
	v_mul_f32_e32 v113, 0x43000000, v113
	v_mul_f32_e32 v114, 0x43000000, v114
	v_mul_f32_e32 v115, 0x43000000, v115
	ds_write_b128 v5, v[112:115] offset:3072
	v_mul_f32_e32 v116, 0x43000000, v116
	v_mul_f32_e32 v117, 0x43000000, v117
	v_mul_f32_e32 v118, 0x43000000, v118
	v_mul_f32_e32 v119, 0x43000000, v119
	ds_write_b128 v5, v[116:119] offset:4096
	v_mul_f32_e32 v120, 0x43000000, v120
	v_mul_f32_e32 v121, 0x43000000, v121
	v_mul_f32_e32 v122, 0x43000000, v122
	v_mul_f32_e32 v123, 0x43000000, v123
	ds_write_b128 v5, v[120:123] offset:5120
	v_mul_f32_e32 v124, 0x43000000, v124
	v_mul_f32_e32 v125, 0x43000000, v125
	v_mul_f32_e32 v126, 0x43000000, v126
	v_mul_f32_e32 v127, 0x43000000, v127
	ds_write_b128 v5, v[124:127] offset:6144
	v_mul_f32_e32 v128, 0x43000000, v128
	v_mul_f32_e32 v129, 0x43000000, v129
	v_mul_f32_e32 v130, 0x43000000, v130
	v_mul_f32_e32 v131, 0x43000000, v131
	ds_write_b128 v5, v[128:131] offset:7168
	s_waitcnt lgkmcnt(0)
	s_barrier
; #define GAS __attribute__((address_space(1)))
; #define LAS __attribute__((address_space(3)))
; #define LDS_WAIT() asm volatile("s_waitcnt lgkmcnt(0)" ::: "memory")
;     ...
;     for (int i = 0; i < 32; ++i) v[i] = sc >= 0 ? W[(size_t)(k0 + 2 * i + (lane >> 5)) * Nsrc + sc] : 0.f;
; #pragma unroll
;     for (int i = 0; i < 32; ++i) { const int k = k0 + 2 * i + (lane >> 5); float x = v[i] * wscale; if (KS) x *= (k < ksplit ? ksA[k] : ksB[k - ksplit]); scr[(2 * i + (lane >> 5)) * 33 + (lane & 31)] = x; }
;     LDS_WAIT(); asm volatile("" ::: "memory");
;     const int c = lane & 7;
; #pragma unroll
;     for (int j = 0; j < 4; ++j) { const int n = (lane >> 3) + 8 * j; const LAS float* s = scr + (8 * c) * 33 + n;
;         const unsigned long long o = (unsigned long long)pg8::pk4_fp8(s[0 * 33], s[1 * 33], s[2 * 33], s[3 * 33]) | ((unsigned long long)pg8::pk4_fp8(s[4 * 33], s[5 * 33], s[6 * 33], s[7 * 33]) << 32);
;         *(GAS unsigned long long*)(WT + (size_t)(n0 + n) * K + k0 + 8 * c) = o; }
	s_add_i32 s17, s16, 1920
	s_min_u32 s17, s17, 0xbff
	s_lshr_b32 s18, s17, 5
	s_add_i32 s18, s18, 32
	s_and_b32 s19, s17, 31
	s_lshl_b32 s18, s18, 21
	s_lshl_b32 s19, s19, 9
	s_add_u32 s18, s18, s19
	s_add_u32 s12, s2, s18
	s_addc_u32 s13, s3, 0
	global_load_dwordx4 v[100:103], v10, s[12:13]
	s_add_u32 s12, s12, 0x8000
	s_addc_u32 s13, s13, 0
	global_load_dwordx4 v[104:107], v10, s[12:13]
	s_add_u32 s12, s12, 0x8000
	s_addc_u32 s13, s13, 0
	global_load_dwordx4 v[108:111], v10, s[12:13]
	s_add_u32 s12, s12, 0x8000
	s_addc_u32 s13, s13, 0
	global_load_dwordx4 v[112:115], v10, s[12:13]
	s_add_u32 s12, s12, 0x8000
	s_addc_u32 s13, s13, 0
	global_load_dwordx4 v[116:119], v10, s[12:13]
	s_add_u32 s12, s12, 0x8000
	s_addc_u32 s13, s13, 0
	global_load_dwordx4 v[120:123], v10, s[12:13]
	s_add_u32 s12, s12, 0x8000
	s_addc_u32 s13, s13, 0
	global_load_dwordx4 v[124:127], v10, s[12:13]
	s_add_u32 s12, s12, 0x8000
	s_addc_u32 s13, s13, 0
	global_load_dwordx4 v[128:131], v10, s[12:13]
	s_add_i32 s17, s16, 1632
	s_min_u32 s17, s17, 0xbff
	s_lshr_b32 s18, s17, 5
	s_add_i32 s18, s18, 32
	s_and_b32 s19, s17, 31
	s_lshl_b32 s19, s19, 21
	s_lshl_b32 s18, s18, 7
	s_add_u32 s18, s18, s19
	s_add_u32 s14, s4, s18
	s_addc_u32 s15, s5, 0
	ds_read_b32 v132, v7
	ds_read_b32 v133, v7 offset:512
	ds_read_b32 v134, v7 offset:1024
	ds_read_b32 v135, v7 offset:1536
	ds_read_b32 v136, v7 offset:2048
	ds_read_b32 v137, v7 offset:2560
	ds_read_b32 v138, v7 offset:3072
	ds_read_b32 v139, v7 offset:3584
	ds_read_b32 v140, v7 offset:4096
	ds_read_b32 v141, v7 offset:4608
	ds_read_b32 v142, v7 offset:5120
	ds_read_b32 v143, v7 offset:5632
	ds_read_b32 v144, v7 offset:6144
	ds_read_b32 v145, v7 offset:6656
	ds_read_b32 v146, v7 offset:7168
	ds_read_b32 v147, v7 offset:7680
	s_waitcnt lgkmcnt(0)
	v_max_f32_e32 v132, v132, v132
	v_max_f32_e32 v133, v133, v133
	v_max_f32_e32 v134, v134, v134
	v_max_f32_e32 v135, v135, v135
	v_max_f32_e32 v136, v136, v136
	v_max_f32_e32 v137, v137, v137
	v_max_f32_e32 v138, v138, v138
	v_max_f32_e32 v139, v139, v139
	v_max_f32_e32 v140, v140, v140
	v_max_f32_e32 v141, v141, v141
	v_max_f32_e32 v142, v142, v142
	v_max_f32_e32 v143, v143, v143
	v_max_f32_e32 v144, v144, v144
	v_max_f32_e32 v145, v145, v145
	v_max_f32_e32 v146, v146, v146
	v_max_f32_e32 v147, v147, v147
	v_med3_f32 v132, v132, s20, v13
	v_med3_f32 v133, v133, s20, v13
	v_med3_f32 v134, v134, s20, v13
	v_med3_f32 v135, v135, s20, v13
	v_med3_f32 v136, v136, s20, v13
	v_med3_f32 v137, v137, s20, v13
	v_med3_f32 v138, v138, s20, v13
	v_med3_f32 v139, v139, s20, v13
	v_med3_f32 v140, v140, s20, v13
	v_med3_f32 v141, v141, s20, v13
	v_med3_f32 v142, v142, s20, v13
	v_med3_f32 v143, v143, s20, v13
	v_med3_f32 v144, v144, s20, v13
	v_med3_f32 v145, v145, s20, v13
	v_med3_f32 v146, v146, s20, v13
	v_med3_f32 v147, v147, s20, v13
	v_mov_b32_e32 v148, 0
	v_mov_b32_e32 v149, 0
	v_mov_b32_e32 v150, 0
	v_mov_b32_e32 v151, 0
	v_cvt_pk_fp8_f32 v148, v132, v133
	v_cvt_pk_fp8_f32 v149, v136, v137
	v_cvt_pk_fp8_f32 v150, v140, v141
	v_cvt_pk_fp8_f32 v151, v144, v145
	v_cvt_pk_fp8_f32 v148, v134, v135 op_sel:[0,0,1]
	v_cvt_pk_fp8_f32 v149, v138, v139 op_sel:[0,0,1]
	v_cvt_pk_fp8_f32 v150, v142, v143 op_sel:[0,0,1]
	v_cvt_pk_fp8_f32 v151, v146, v147 op_sel:[0,0,1]
	s_nop 0
	global_store_dwordx4 v11, v[148:151], s[14:15]
	ds_read_b32 v132, v9
	ds_read_b32 v133, v9 offset:512
	ds_read_b32 v134, v9 offset:1024
	ds_read_b32 v135, v9 offset:1536
	ds_read_b32 v136, v9 offset:2048
	ds_read_b32 v137, v9 offset:2560
	ds_read_b32 v138, v9 offset:3072
	ds_read_b32 v139, v9 offset:3584
	ds_read_b32 v140, v9 offset:4096
	ds_read_b32 v141, v9 offset:4608
	ds_read_b32 v142, v9 offset:5120
	ds_read_b32 v143, v9 offset:5632
	ds_read_b32 v144, v9 offset:6144
	ds_read_b32 v145, v9 offset:6656
	ds_read_b32 v146, v9 offset:7168
	ds_read_b32 v147, v9 offset:7680
	s_waitcnt lgkmcnt(0)
	v_max_f32_e32 v132, v132, v132
	v_max_f32_e32 v133, v133, v133
	v_max_f32_e32 v134, v134, v134
	v_max_f32_e32 v135, v135, v135
	v_max_f32_e32 v136, v136, v136
	v_max_f32_e32 v137, v137, v137
	v_max_f32_e32 v138, v138, v138
	v_max_f32_e32 v139, v139, v139
	v_max_f32_e32 v140, v140, v140
	v_max_f32_e32 v141, v141, v141
	v_max_f32_e32 v142, v142, v142
	v_max_f32_e32 v143, v143, v143
	v_max_f32_e32 v144, v144, v144
	v_max_f32_e32 v145, v145, v145
	v_max_f32_e32 v146, v146, v146
	v_max_f32_e32 v147, v147, v147
	v_med3_f32 v132, v132, s20, v13
	v_med3_f32 v133, v133, s20, v13
	v_med3_f32 v134, v134, s20, v13
	v_med3_f32 v135, v135, s20, v13
	v_med3_f32 v136, v136, s20, v13
	v_med3_f32 v137, v137, s20, v13
	v_med3_f32 v138, v138, s20, v13
	v_med3_f32 v139, v139, s20, v13
	v_med3_f32 v140, v140, s20, v13
	v_med3_f32 v141, v141, s20, v13
	v_med3_f32 v142, v142, s20, v13
	v_med3_f32 v143, v143, s20, v13
	v_med3_f32 v144, v144, s20, v13
	v_med3_f32 v145, v145, s20, v13
	v_med3_f32 v146, v146, s20, v13
	v_med3_f32 v147, v147, s20, v13
	v_mov_b32_e32 v148, 0
	v_mov_b32_e32 v149, 0
	v_mov_b32_e32 v150, 0
	v_mov_b32_e32 v151, 0
	v_cvt_pk_fp8_f32 v148, v132, v133
	v_cvt_pk_fp8_f32 v149, v136, v137
	v_cvt_pk_fp8_f32 v150, v140, v141
	v_cvt_pk_fp8_f32 v151, v144, v145
	v_cvt_pk_fp8_f32 v148, v134, v135 op_sel:[0,0,1]
	v_cvt_pk_fp8_f32 v149, v138, v139 op_sel:[0,0,1]
	v_cvt_pk_fp8_f32 v150, v142, v143 op_sel:[0,0,1]
	v_cvt_pk_fp8_f32 v151, v146, v147 op_sel:[0,0,1]
	s_nop 0
	global_store_dwordx4 v12, v[148:151], s[14:15]
	s_waitcnt vmcnt(22)
	v_mul_f32_e32 v36, 0x43000000, v36
	v_mul_f32_e32 v37, 0x43000000, v37
	v_mul_f32_e32 v38, 0x43000000, v38
	v_mul_f32_e32 v39, 0x43000000, v39
	ds_write_b128 v4, v[36:39]
	v_mul_f32_e32 v40, 0x43000000, v40
	v_mul_f32_e32 v41, 0x43000000, v41
	v_mul_f32_e32 v42, 0x43000000, v42
	v_mul_f32_e32 v43, 0x43000000, v43
	ds_write_b128 v4, v[40:43] offset:1024
	v_mul_f32_e32 v44, 0x43000000, v44
	v_mul_f32_e32 v45, 0x43000000, v45
	v_mul_f32_e32 v46, 0x43000000, v46
	v_mul_f32_e32 v47, 0x43000000, v47
	ds_write_b128 v4, v[44:47] offset:2048
	v_mul_f32_e32 v48, 0x43000000, v48
	v_mul_f32_e32 v49, 0x43000000, v49
	v_mul_f32_e32 v50, 0x43000000, v50
	v_mul_f32_e32 v51, 0x43000000, v51
	ds_write_b128 v4, v[48:51] offset:3072
	v_mul_f32_e32 v52, 0x43000000, v52
	v_mul_f32_e32 v53, 0x43000000, v53
	v_mul_f32_e32 v54, 0x43000000, v54
	v_mul_f32_e32 v55, 0x43000000, v55
	ds_write_b128 v4, v[52:55] offset:4096
	v_mul_f32_e32 v56, 0x43000000, v56
	v_mul_f32_e32 v57, 0x43000000, v57
	v_mul_f32_e32 v58, 0x43000000, v58
	v_mul_f32_e32 v59, 0x43000000, v59
	ds_write_b128 v4, v[56:59] offset:5120
	v_mul_f32_e32 v60, 0x43000000, v60
	v_mul_f32_e32 v61, 0x43000000, v61
	v_mul_f32_e32 v62, 0x43000000, v62
	v_mul_f32_e32 v63, 0x43000000, v63
	ds_write_b128 v4, v[60:63] offset:6144
	v_mul_f32_e32 v64, 0x43000000, v64
	v_mul_f32_e32 v65, 0x43000000, v65
	v_mul_f32_e32 v66, 0x43000000, v66
	v_mul_f32_e32 v67, 0x43000000, v67
	ds_write_b128 v4, v[64:67] offset:7168
	s_waitcnt lgkmcnt(0)
	s_barrier
; #define GAS __attribute__((address_space(1)))
; #define LAS __attribute__((address_space(3)))
; #define LDS_WAIT() asm volatile("s_waitcnt lgkmcnt(0)" ::: "memory")
;     ...
;     for (int i = 0; i < 32; ++i) v[i] = sc >= 0 ? W[(size_t)(k0 + 2 * i + (lane >> 5)) * Nsrc + sc] : 0.f;
; #pragma unroll
;     for (int i = 0; i < 32; ++i) { const int k = k0 + 2 * i + (lane >> 5); float x = v[i] * wscale; if (KS) x *= (k < ksplit ? ksA[k] : ksB[k - ksplit]); scr[(2 * i + (lane >> 5)) * 33 + (lane & 31)] = x; }
;     LDS_WAIT(); asm volatile("" ::: "memory");
;     const int c = lane & 7;
; #pragma unroll
;     for (int j = 0; j < 4; ++j) { const int n = (lane >> 3) + 8 * j; const LAS float* s = scr + (8 * c) * 33 + n;
;         const unsigned long long o = (unsigned long long)pg8::pk4_fp8(s[0 * 33], s[1 * 33], s[2 * 33], s[3 * 33]) | ((unsigned long long)pg8::pk4_fp8(s[4 * 33], s[5 * 33], s[6 * 33], s[7 * 33]) << 32);
;         *(GAS unsigned long long*)(WT + (size_t)(n0 + n) * K + k0 + 8 * c) = o; }
	s_add_i32 s17, s16, 2016
	s_min_u32 s17, s17, 0xbff
	s_lshr_b32 s18, s17, 5
	s_add_i32 s18, s18, 32
	s_and_b32 s19, s17, 31
	s_lshl_b32 s18, s18, 21
	s_lshl_b32 s19, s19, 9
	s_add_u32 s18, s18, s19
	s_add_u32 s12, s2, s18
	s_addc_u32 s13, s3, 0
	global_load_dwordx4 v[36:39], v10, s[12:13]
	s_add_u32 s12, s12, 0x8000
	s_addc_u32 s13, s13, 0
	global_load_dwordx4 v[40:43], v10, s[12:13]
	s_add_u32 s12, s12, 0x8000
	s_addc_u32 s13, s13, 0
	global_load_dwordx4 v[44:47], v10, s[12:13]
	s_add_u32 s12, s12, 0x8000
	s_addc_u32 s13, s13, 0
	global_load_dwordx4 v[48:51], v10, s[12:13]
	s_add_u32 s12, s12, 0x8000
	s_addc_u32 s13, s13, 0
	global_load_dwordx4 v[52:55], v10, s[12:13]
	s_add_u32 s12, s12, 0x8000
	s_addc_u32 s13, s13, 0
	global_load_dwordx4 v[56:59], v10, s[12:13]
	s_add_u32 s12, s12, 0x8000
	s_addc_u32 s13, s13, 0
	global_load_dwordx4 v[60:63], v10, s[12:13]
	s_add_u32 s12, s12, 0x8000
	s_addc_u32 s13, s13, 0
	global_load_dwordx4 v[64:67], v10, s[12:13]
	s_add_i32 s17, s16, 1728
	s_min_u32 s17, s17, 0xbff
	s_lshr_b32 s18, s17, 5
	s_add_i32 s18, s18, 32
	s_and_b32 s19, s17, 31
	s_lshl_b32 s19, s19, 21
	s_lshl_b32 s18, s18, 7
	s_add_u32 s18, s18, s19
	s_add_u32 s14, s4, s18
	s_addc_u32 s15, s5, 0
	ds_read_b32 v132, v6
	ds_read_b32 v133, v6 offset:512
	ds_read_b32 v134, v6 offset:1024
	ds_read_b32 v135, v6 offset:1536
	ds_read_b32 v136, v6 offset:2048
	ds_read_b32 v137, v6 offset:2560
	ds_read_b32 v138, v6 offset:3072
	ds_read_b32 v139, v6 offset:3584
	ds_read_b32 v140, v6 offset:4096
	ds_read_b32 v141, v6 offset:4608
	ds_read_b32 v142, v6 offset:5120
	ds_read_b32 v143, v6 offset:5632
	ds_read_b32 v144, v6 offset:6144
	ds_read_b32 v145, v6 offset:6656
	ds_read_b32 v146, v6 offset:7168
	ds_read_b32 v147, v6 offset:7680
	s_waitcnt lgkmcnt(0)
	v_max_f32_e32 v132, v132, v132
	v_max_f32_e32 v133, v133, v133
	v_max_f32_e32 v134, v134, v134
	v_max_f32_e32 v135, v135, v135
	v_max_f32_e32 v136, v136, v136
	v_max_f32_e32 v137, v137, v137
	v_max_f32_e32 v138, v138, v138
	v_max_f32_e32 v139, v139, v139
	v_max_f32_e32 v140, v140, v140
	v_max_f32_e32 v141, v141, v141
	v_max_f32_e32 v142, v142, v142
	v_max_f32_e32 v143, v143, v143
	v_max_f32_e32 v144, v144, v144
	v_max_f32_e32 v145, v145, v145
	v_max_f32_e32 v146, v146, v146
	v_max_f32_e32 v147, v147, v147
	v_med3_f32 v132, v132, s20, v13
	v_med3_f32 v133, v133, s20, v13
	v_med3_f32 v134, v134, s20, v13
	v_med3_f32 v135, v135, s20, v13
	v_med3_f32 v136, v136, s20, v13
	v_med3_f32 v137, v137, s20, v13
	v_med3_f32 v138, v138, s20, v13
	v_med3_f32 v139, v139, s20, v13
	v_med3_f32 v140, v140, s20, v13
	v_med3_f32 v141, v141, s20, v13
	v_med3_f32 v142, v142, s20, v13
	v_med3_f32 v143, v143, s20, v13
	v_med3_f32 v144, v144, s20, v13
	v_med3_f32 v145, v145, s20, v13
	v_med3_f32 v146, v146, s20, v13
	v_med3_f32 v147, v147, s20, v13
	v_mov_b32_e32 v148, 0
	v_mov_b32_e32 v149, 0
	v_mov_b32_e32 v150, 0
	v_mov_b32_e32 v151, 0
	v_cvt_pk_fp8_f32 v148, v132, v133
	v_cvt_pk_fp8_f32 v149, v136, v137
	v_cvt_pk_fp8_f32 v150, v140, v141
	v_cvt_pk_fp8_f32 v151, v144, v145
	v_cvt_pk_fp8_f32 v148, v134, v135 op_sel:[0,0,1]
	v_cvt_pk_fp8_f32 v149, v138, v139 op_sel:[0,0,1]
	v_cvt_pk_fp8_f32 v150, v142, v143 op_sel:[0,0,1]
	v_cvt_pk_fp8_f32 v151, v146, v147 op_sel:[0,0,1]
	s_nop 0
	global_store_dwordx4 v11, v[148:151], s[14:15]
	ds_read_b32 v132, v8
	ds_read_b32 v133, v8 offset:512
	ds_read_b32 v134, v8 offset:1024
	ds_read_b32 v135, v8 offset:1536
	ds_read_b32 v136, v8 offset:2048
	ds_read_b32 v137, v8 offset:2560
	ds_read_b32 v138, v8 offset:3072
	ds_read_b32 v139, v8 offset:3584
	ds_read_b32 v140, v8 offset:4096
	ds_read_b32 v141, v8 offset:4608
	ds_read_b32 v142, v8 offset:5120
	ds_read_b32 v143, v8 offset:5632
	ds_read_b32 v144, v8 offset:6144
	ds_read_b32 v145, v8 offset:6656
	ds_read_b32 v146, v8 offset:7168
	ds_read_b32 v147, v8 offset:7680
	s_waitcnt lgkmcnt(0)
	v_max_f32_e32 v132, v132, v132
	v_max_f32_e32 v133, v133, v133
	v_max_f32_e32 v134, v134, v134
	v_max_f32_e32 v135, v135, v135
	v_max_f32_e32 v136, v136, v136
	v_max_f32_e32 v137, v137, v137
	v_max_f32_e32 v138, v138, v138
	v_max_f32_e32 v139, v139, v139
	v_max_f32_e32 v140, v140, v140
	v_max_f32_e32 v141, v141, v141
	v_max_f32_e32 v142, v142, v142
	v_max_f32_e32 v143, v143, v143
	v_max_f32_e32 v144, v144, v144
	v_max_f32_e32 v145, v145, v145
	v_max_f32_e32 v146, v146, v146
	v_max_f32_e32 v147, v147, v147
	v_med3_f32 v132, v132, s20, v13
	v_med3_f32 v133, v133, s20, v13
	v_med3_f32 v134, v134, s20, v13
	v_med3_f32 v135, v135, s20, v13
	v_med3_f32 v136, v136, s20, v13
	v_med3_f32 v137, v137, s20, v13
	v_med3_f32 v138, v138, s20, v13
	v_med3_f32 v139, v139, s20, v13
	v_med3_f32 v140, v140, s20, v13
	v_med3_f32 v141, v141, s20, v13
	v_med3_f32 v142, v142, s20, v13
	v_med3_f32 v143, v143, s20, v13
	v_med3_f32 v144, v144, s20, v13
	v_med3_f32 v145, v145, s20, v13
	v_med3_f32 v146, v146, s20, v13
	v_med3_f32 v147, v147, s20, v13
	v_mov_b32_e32 v148, 0
	v_mov_b32_e32 v149, 0
	v_mov_b32_e32 v150, 0
	v_mov_b32_e32 v151, 0
	v_cvt_pk_fp8_f32 v148, v132, v133
	v_cvt_pk_fp8_f32 v149, v136, v137
	v_cvt_pk_fp8_f32 v150, v140, v141
	v_cvt_pk_fp8_f32 v151, v144, v145
	v_cvt_pk_fp8_f32 v148, v134, v135 op_sel:[0,0,1]
	v_cvt_pk_fp8_f32 v149, v138, v139 op_sel:[0,0,1]
	v_cvt_pk_fp8_f32 v150, v142, v143 op_sel:[0,0,1]
	v_cvt_pk_fp8_f32 v151, v146, v147 op_sel:[0,0,1]
	s_nop 0
	global_store_dwordx4 v12, v[148:151], s[14:15]
	s_waitcnt vmcnt(22)
	v_mul_f32_e32 v68, 0x43000000, v68
	v_mul_f32_e32 v69, 0x43000000, v69
	v_mul_f32_e32 v70, 0x43000000, v70
	v_mul_f32_e32 v71, 0x43000000, v71
	ds_write_b128 v5, v[68:71]
	v_mul_f32_e32 v72, 0x43000000, v72
	v_mul_f32_e32 v73, 0x43000000, v73
	v_mul_f32_e32 v74, 0x43000000, v74
	v_mul_f32_e32 v75, 0x43000000, v75
	ds_write_b128 v5, v[72:75] offset:1024
	v_mul_f32_e32 v76, 0x43000000, v76
	v_mul_f32_e32 v77, 0x43000000, v77
	v_mul_f32_e32 v78, 0x43000000, v78
	v_mul_f32_e32 v79, 0x43000000, v79
	ds_write_b128 v5, v[76:79] offset:2048
	v_mul_f32_e32 v80, 0x43000000, v80
	v_mul_f32_e32 v81, 0x43000000, v81
	v_mul_f32_e32 v82, 0x43000000, v82
	v_mul_f32_e32 v83, 0x43000000, v83
	ds_write_b128 v5, v[80:83] offset:3072
	v_mul_f32_e32 v84, 0x43000000, v84
	v_mul_f32_e32 v85, 0x43000000, v85
	v_mul_f32_e32 v86, 0x43000000, v86
	v_mul_f32_e32 v87, 0x43000000, v87
	ds_write_b128 v5, v[84:87] offset:4096
	v_mul_f32_e32 v88, 0x43000000, v88
	v_mul_f32_e32 v89, 0x43000000, v89
	v_mul_f32_e32 v90, 0x43000000, v90
	v_mul_f32_e32 v91, 0x43000000, v91
	ds_write_b128 v5, v[88:91] offset:5120
	v_mul_f32_e32 v92, 0x43000000, v92
	v_mul_f32_e32 v93, 0x43000000, v93
	v_mul_f32_e32 v94, 0x43000000, v94
	v_mul_f32_e32 v95, 0x43000000, v95
	ds_write_b128 v5, v[92:95] offset:6144
	v_mul_f32_e32 v96, 0x43000000, v96
	v_mul_f32_e32 v97, 0x43000000, v97
	v_mul_f32_e32 v98, 0x43000000, v98
	v_mul_f32_e32 v99, 0x43000000, v99
	ds_write_b128 v5, v[96:99] offset:7168
	s_waitcnt lgkmcnt(0)
	s_barrier
; #define GAS __attribute__((address_space(1)))
; #define LAS __attribute__((address_space(3)))
; #define LDS_WAIT() asm volatile("s_waitcnt lgkmcnt(0)" ::: "memory")
;     ...
;     for (int i = 0; i < 32; ++i) v[i] = sc >= 0 ? W[(size_t)(k0 + 2 * i + (lane >> 5)) * Nsrc + sc] : 0.f;
; #pragma unroll
;     for (int i = 0; i < 32; ++i) { const int k = k0 + 2 * i + (lane >> 5); float x = v[i] * wscale; if (KS) x *= (k < ksplit ? ksA[k] : ksB[k - ksplit]); scr[(2 * i + (lane >> 5)) * 33 + (lane & 31)] = x; }
;     LDS_WAIT(); asm volatile("" ::: "memory");
;     const int c = lane & 7;
; #pragma unroll
;     for (int j = 0; j < 4; ++j) { const int n = (lane >> 3) + 8 * j; const LAS float* s = scr + (8 * c) * 33 + n;
;         const unsigned long long o = (unsigned long long)pg8::pk4_fp8(s[0 * 33], s[1 * 33], s[2 * 33], s[3 * 33]) | ((unsigned long long)pg8::pk4_fp8(s[4 * 33], s[5 * 33], s[6 * 33], s[7 * 33]) << 32);
;         *(GAS unsigned long long*)(WT + (size_t)(n0 + n) * K + k0 + 8 * c) = o; }
	s_add_i32 s17, s16, 2112
	s_min_u32 s17, s17, 0xbff
	s_lshr_b32 s18, s17, 5
	s_add_i32 s18, s18, 32
	s_and_b32 s19, s17, 31
	s_lshl_b32 s18, s18, 21
	s_lshl_b32 s19, s19, 9
	s_add_u32 s18, s18, s19
	s_add_u32 s12, s2, s18
	s_addc_u32 s13, s3, 0
	global_load_dwordx4 v[68:71], v10, s[12:13]
	s_add_u32 s12, s12, 0x8000
	s_addc_u32 s13, s13, 0
	global_load_dwordx4 v[72:75], v10, s[12:13]
	s_add_u32 s12, s12, 0x8000
	s_addc_u32 s13, s13, 0
	global_load_dwordx4 v[76:79], v10, s[12:13]
	s_add_u32 s12, s12, 0x8000
	s_addc_u32 s13, s13, 0
	global_load_dwordx4 v[80:83], v10, s[12:13]
	s_add_u32 s12, s12, 0x8000
	s_addc_u32 s13, s13, 0
	global_load_dwordx4 v[84:87], v10, s[12:13]
	s_add_u32 s12, s12, 0x8000
	s_addc_u32 s13, s13, 0
	global_load_dwordx4 v[88:91], v10, s[12:13]
	s_add_u32 s12, s12, 0x8000
	s_addc_u32 s13, s13, 0
	global_load_dwordx4 v[92:95], v10, s[12:13]
	s_add_u32 s12, s12, 0x8000
	s_addc_u32 s13, s13, 0
	global_load_dwordx4 v[96:99], v10, s[12:13]
	s_add_i32 s17, s16, 1824
	s_min_u32 s17, s17, 0xbff
	s_lshr_b32 s18, s17, 5
	s_add_i32 s18, s18, 32
	s_and_b32 s19, s17, 31
	s_lshl_b32 s19, s19, 21
	s_lshl_b32 s18, s18, 7
	s_add_u32 s18, s18, s19
	s_add_u32 s14, s4, s18
	s_addc_u32 s15, s5, 0
	ds_read_b32 v132, v7
	ds_read_b32 v133, v7 offset:512
	ds_read_b32 v134, v7 offset:1024
	ds_read_b32 v135, v7 offset:1536
	ds_read_b32 v136, v7 offset:2048
	ds_read_b32 v137, v7 offset:2560
	ds_read_b32 v138, v7 offset:3072
	ds_read_b32 v139, v7 offset:3584
	ds_read_b32 v140, v7 offset:4096
	ds_read_b32 v141, v7 offset:4608
	ds_read_b32 v142, v7 offset:5120
	ds_read_b32 v143, v7 offset:5632
	ds_read_b32 v144, v7 offset:6144
	ds_read_b32 v145, v7 offset:6656
	ds_read_b32 v146, v7 offset:7168
	ds_read_b32 v147, v7 offset:7680
	s_waitcnt lgkmcnt(0)
	v_max_f32_e32 v132, v132, v132
	v_max_f32_e32 v133, v133, v133
	v_max_f32_e32 v134, v134, v134
	v_max_f32_e32 v135, v135, v135
	v_max_f32_e32 v136, v136, v136
	v_max_f32_e32 v137, v137, v137
	v_max_f32_e32 v138, v138, v138
	v_max_f32_e32 v139, v139, v139
	v_max_f32_e32 v140, v140, v140
	v_max_f32_e32 v141, v141, v141
	v_max_f32_e32 v142, v142, v142
	v_max_f32_e32 v143, v143, v143
	v_max_f32_e32 v144, v144, v144
	v_max_f32_e32 v145, v145, v145
	v_max_f32_e32 v146, v146, v146
	v_max_f32_e32 v147, v147, v147
	v_med3_f32 v132, v132, s20, v13
	v_med3_f32 v133, v133, s20, v13
	v_med3_f32 v134, v134, s20, v13
	v_med3_f32 v135, v135, s20, v13
	v_med3_f32 v136, v136, s20, v13
	v_med3_f32 v137, v137, s20, v13
	v_med3_f32 v138, v138, s20, v13
	v_med3_f32 v139, v139, s20, v13
	v_med3_f32 v140, v140, s20, v13
	v_med3_f32 v141, v141, s20, v13
	v_med3_f32 v142, v142, s20, v13
	v_med3_f32 v143, v143, s20, v13
	v_med3_f32 v144, v144, s20, v13
	v_med3_f32 v145, v145, s20, v13
	v_med3_f32 v146, v146, s20, v13
	v_med3_f32 v147, v147, s20, v13
	v_mov_b32_e32 v148, 0
	v_mov_b32_e32 v149, 0
	v_mov_b32_e32 v150, 0
	v_mov_b32_e32 v151, 0
	v_cvt_pk_fp8_f32 v148, v132, v133
	v_cvt_pk_fp8_f32 v149, v136, v137
	v_cvt_pk_fp8_f32 v150, v140, v141
	v_cvt_pk_fp8_f32 v151, v144, v145
	v_cvt_pk_fp8_f32 v148, v134, v135 op_sel:[0,0,1]
	v_cvt_pk_fp8_f32 v149, v138, v139 op_sel:[0,0,1]
	v_cvt_pk_fp8_f32 v150, v142, v143 op_sel:[0,0,1]
	v_cvt_pk_fp8_f32 v151, v146, v147 op_sel:[0,0,1]
	s_nop 0
	global_store_dwordx4 v11, v[148:151], s[14:15]
	ds_read_b32 v132, v9
	ds_read_b32 v133, v9 offset:512
	ds_read_b32 v134, v9 offset:1024
	ds_read_b32 v135, v9 offset:1536
	ds_read_b32 v136, v9 offset:2048
	ds_read_b32 v137, v9 offset:2560
	ds_read_b32 v138, v9 offset:3072
	ds_read_b32 v139, v9 offset:3584
	ds_read_b32 v140, v9 offset:4096
	ds_read_b32 v141, v9 offset:4608
	ds_read_b32 v142, v9 offset:5120
	ds_read_b32 v143, v9 offset:5632
	ds_read_b32 v144, v9 offset:6144
	ds_read_b32 v145, v9 offset:6656
	ds_read_b32 v146, v9 offset:7168
	ds_read_b32 v147, v9 offset:7680
	s_waitcnt lgkmcnt(0)
	v_max_f32_e32 v132, v132, v132
	v_max_f32_e32 v133, v133, v133
	v_max_f32_e32 v134, v134, v134
	v_max_f32_e32 v135, v135, v135
	v_max_f32_e32 v136, v136, v136
	v_max_f32_e32 v137, v137, v137
	v_max_f32_e32 v138, v138, v138
	v_max_f32_e32 v139, v139, v139
	v_max_f32_e32 v140, v140, v140
	v_max_f32_e32 v141, v141, v141
	v_max_f32_e32 v142, v142, v142
	v_max_f32_e32 v143, v143, v143
	v_max_f32_e32 v144, v144, v144
	v_max_f32_e32 v145, v145, v145
	v_max_f32_e32 v146, v146, v146
	v_max_f32_e32 v147, v147, v147
	v_med3_f32 v132, v132, s20, v13
	v_med3_f32 v133, v133, s20, v13
	v_med3_f32 v134, v134, s20, v13
	v_med3_f32 v135, v135, s20, v13
	v_med3_f32 v136, v136, s20, v13
	v_med3_f32 v137, v137, s20, v13
	v_med3_f32 v138, v138, s20, v13
	v_med3_f32 v139, v139, s20, v13
	v_med3_f32 v140, v140, s20, v13
	v_med3_f32 v141, v141, s20, v13
	v_med3_f32 v142, v142, s20, v13
	v_med3_f32 v143, v143, s20, v13
	v_med3_f32 v144, v144, s20, v13
	v_med3_f32 v145, v145, s20, v13
	v_med3_f32 v146, v146, s20, v13
	v_med3_f32 v147, v147, s20, v13
	v_mov_b32_e32 v148, 0
	v_mov_b32_e32 v149, 0
	v_mov_b32_e32 v150, 0
	v_mov_b32_e32 v151, 0
	v_cvt_pk_fp8_f32 v148, v132, v133
	v_cvt_pk_fp8_f32 v149, v136, v137
	v_cvt_pk_fp8_f32 v150, v140, v141
	v_cvt_pk_fp8_f32 v151, v144, v145
	v_cvt_pk_fp8_f32 v148, v134, v135 op_sel:[0,0,1]
	v_cvt_pk_fp8_f32 v149, v138, v139 op_sel:[0,0,1]
	v_cvt_pk_fp8_f32 v150, v142, v143 op_sel:[0,0,1]
	v_cvt_pk_fp8_f32 v151, v146, v147 op_sel:[0,0,1]
	s_nop 0
	global_store_dwordx4 v12, v[148:151], s[14:15]
	s_waitcnt vmcnt(22)
	v_mul_f32_e32 v100, 0x43000000, v100
	v_mul_f32_e32 v101, 0x43000000, v101
	v_mul_f32_e32 v102, 0x43000000, v102
	v_mul_f32_e32 v103, 0x43000000, v103
	ds_write_b128 v4, v[100:103]
	v_mul_f32_e32 v104, 0x43000000, v104
	v_mul_f32_e32 v105, 0x43000000, v105
	v_mul_f32_e32 v106, 0x43000000, v106
	v_mul_f32_e32 v107, 0x43000000, v107
	ds_write_b128 v4, v[104:107] offset:1024
	v_mul_f32_e32 v108, 0x43000000, v108
	v_mul_f32_e32 v109, 0x43000000, v109
	v_mul_f32_e32 v110, 0x43000000, v110
	v_mul_f32_e32 v111, 0x43000000, v111
	ds_write_b128 v4, v[108:111] offset:2048
	v_mul_f32_e32 v112, 0x43000000, v112
	v_mul_f32_e32 v113, 0x43000000, v113
	v_mul_f32_e32 v114, 0x43000000, v114
	v_mul_f32_e32 v115, 0x43000000, v115
	ds_write_b128 v4, v[112:115] offset:3072
	v_mul_f32_e32 v116, 0x43000000, v116
	v_mul_f32_e32 v117, 0x43000000, v117
	v_mul_f32_e32 v118, 0x43000000, v118
	v_mul_f32_e32 v119, 0x43000000, v119
	ds_write_b128 v4, v[116:119] offset:4096
	v_mul_f32_e32 v120, 0x43000000, v120
	v_mul_f32_e32 v121, 0x43000000, v121
	v_mul_f32_e32 v122, 0x43000000, v122
	v_mul_f32_e32 v123, 0x43000000, v123
	ds_write_b128 v4, v[120:123] offset:5120
	v_mul_f32_e32 v124, 0x43000000, v124
	v_mul_f32_e32 v125, 0x43000000, v125
	v_mul_f32_e32 v126, 0x43000000, v126
	v_mul_f32_e32 v127, 0x43000000, v127
	ds_write_b128 v4, v[124:127] offset:6144
	v_mul_f32_e32 v128, 0x43000000, v128
	v_mul_f32_e32 v129, 0x43000000, v129
	v_mul_f32_e32 v130, 0x43000000, v130
	v_mul_f32_e32 v131, 0x43000000, v131
	ds_write_b128 v4, v[128:131] offset:7168
	s_waitcnt lgkmcnt(0)
	s_barrier
; #define GAS __attribute__((address_space(1)))
; #define LAS __attribute__((address_space(3)))
; #define LDS_WAIT() asm volatile("s_waitcnt lgkmcnt(0)" ::: "memory")
;     ...
;     for (int i = 0; i < 32; ++i) v[i] = sc >= 0 ? W[(size_t)(k0 + 2 * i + (lane >> 5)) * Nsrc + sc] : 0.f;
; #pragma unroll
;     for (int i = 0; i < 32; ++i) { const int k = k0 + 2 * i + (lane >> 5); float x = v[i] * wscale; if (KS) x *= (k < ksplit ? ksA[k] : ksB[k - ksplit]); scr[(2 * i + (lane >> 5)) * 33 + (lane & 31)] = x; }
;     LDS_WAIT(); asm volatile("" ::: "memory");
;     const int c = lane & 7;
; #pragma unroll
;     for (int j = 0; j < 4; ++j) { const int n = (lane >> 3) + 8 * j; const LAS float* s = scr + (8 * c) * 33 + n;
;         const unsigned long long o = (unsigned long long)pg8::pk4_fp8(s[0 * 33], s[1 * 33], s[2 * 33], s[3 * 33]) | ((unsigned long long)pg8::pk4_fp8(s[4 * 33], s[5 * 33], s[6 * 33], s[7 * 33]) << 32);
;         *(GAS unsigned long long*)(WT + (size_t)(n0 + n) * K + k0 + 8 * c) = o; }
	s_add_i32 s17, s16, 2208
	s_min_u32 s17, s17, 0xbff
	s_lshr_b32 s18, s17, 5
	s_add_i32 s18, s18, 32
	s_and_b32 s19, s17, 31
	s_lshl_b32 s18, s18, 21
	s_lshl_b32 s19, s19, 9
	s_add_u32 s18, s18, s19
	s_add_u32 s12, s2, s18
	s_addc_u32 s13, s3, 0
	global_load_dwordx4 v[100:103], v10, s[12:13]
	s_add_u32 s12, s12, 0x8000
	s_addc_u32 s13, s13, 0
	global_load_dwordx4 v[104:107], v10, s[12:13]
	s_add_u32 s12, s12, 0x8000
	s_addc_u32 s13, s13, 0
	global_load_dwordx4 v[108:111], v10, s[12:13]
	s_add_u32 s12, s12, 0x8000
	s_addc_u32 s13, s13, 0
	global_load_dwordx4 v[112:115], v10, s[12:13]
	s_add_u32 s12, s12, 0x8000
	s_addc_u32 s13, s13, 0
	global_load_dwordx4 v[116:119], v10, s[12:13]
	s_add_u32 s12, s12, 0x8000
	s_addc_u32 s13, s13, 0
	global_load_dwordx4 v[120:123], v10, s[12:13]
	s_add_u32 s12, s12, 0x8000
	s_addc_u32 s13, s13, 0
	global_load_dwordx4 v[124:127], v10, s[12:13]
	s_add_u32 s12, s12, 0x8000
	s_addc_u32 s13, s13, 0
	global_load_dwordx4 v[128:131], v10, s[12:13]
	s_add_i32 s17, s16, 1920
	s_min_u32 s17, s17, 0xbff
	s_lshr_b32 s18, s17, 5
	s_add_i32 s18, s18, 32
	s_and_b32 s19, s17, 31
	s_lshl_b32 s19, s19, 21
	s_lshl_b32 s18, s18, 7
	s_add_u32 s18, s18, s19
	s_add_u32 s14, s4, s18
	s_addc_u32 s15, s5, 0
	ds_read_b32 v132, v6
	ds_read_b32 v133, v6 offset:512
	ds_read_b32 v134, v6 offset:1024
	ds_read_b32 v135, v6 offset:1536
	ds_read_b32 v136, v6 offset:2048
	ds_read_b32 v137, v6 offset:2560
	ds_read_b32 v138, v6 offset:3072
	ds_read_b32 v139, v6 offset:3584
	ds_read_b32 v140, v6 offset:4096
	ds_read_b32 v141, v6 offset:4608
	ds_read_b32 v142, v6 offset:5120
	ds_read_b32 v143, v6 offset:5632
	ds_read_b32 v144, v6 offset:6144
	ds_read_b32 v145, v6 offset:6656
	ds_read_b32 v146, v6 offset:7168
	ds_read_b32 v147, v6 offset:7680
	s_waitcnt lgkmcnt(0)
	v_max_f32_e32 v132, v132, v132
	v_max_f32_e32 v133, v133, v133
	v_max_f32_e32 v134, v134, v134
	v_max_f32_e32 v135, v135, v135
	v_max_f32_e32 v136, v136, v136
	v_max_f32_e32 v137, v137, v137
	v_max_f32_e32 v138, v138, v138
	v_max_f32_e32 v139, v139, v139
	v_max_f32_e32 v140, v140, v140
	v_max_f32_e32 v141, v141, v141
	v_max_f32_e32 v142, v142, v142
	v_max_f32_e32 v143, v143, v143
	v_max_f32_e32 v144, v144, v144
	v_max_f32_e32 v145, v145, v145
	v_max_f32_e32 v146, v146, v146
	v_max_f32_e32 v147, v147, v147
	v_med3_f32 v132, v132, s20, v13
	v_med3_f32 v133, v133, s20, v13
	v_med3_f32 v134, v134, s20, v13
	v_med3_f32 v135, v135, s20, v13
	v_med3_f32 v136, v136, s20, v13
	v_med3_f32 v137, v137, s20, v13
	v_med3_f32 v138, v138, s20, v13
	v_med3_f32 v139, v139, s20, v13
	v_med3_f32 v140, v140, s20, v13
	v_med3_f32 v141, v141, s20, v13
	v_med3_f32 v142, v142, s20, v13
	v_med3_f32 v143, v143, s20, v13
	v_med3_f32 v144, v144, s20, v13
	v_med3_f32 v145, v145, s20, v13
	v_med3_f32 v146, v146, s20, v13
	v_med3_f32 v147, v147, s20, v13
	v_mov_b32_e32 v148, 0
	v_mov_b32_e32 v149, 0
	v_mov_b32_e32 v150, 0
	v_mov_b32_e32 v151, 0
	v_cvt_pk_fp8_f32 v148, v132, v133
	v_cvt_pk_fp8_f32 v149, v136, v137
	v_cvt_pk_fp8_f32 v150, v140, v141
	v_cvt_pk_fp8_f32 v151, v144, v145
	v_cvt_pk_fp8_f32 v148, v134, v135 op_sel:[0,0,1]
	v_cvt_pk_fp8_f32 v149, v138, v139 op_sel:[0,0,1]
	v_cvt_pk_fp8_f32 v150, v142, v143 op_sel:[0,0,1]
	v_cvt_pk_fp8_f32 v151, v146, v147 op_sel:[0,0,1]
	s_nop 0
	global_store_dwordx4 v11, v[148:151], s[14:15]
	ds_read_b32 v132, v8
	ds_read_b32 v133, v8 offset:512
	ds_read_b32 v134, v8 offset:1024
	ds_read_b32 v135, v8 offset:1536
	ds_read_b32 v136, v8 offset:2048
	ds_read_b32 v137, v8 offset:2560
	ds_read_b32 v138, v8 offset:3072
	ds_read_b32 v139, v8 offset:3584
	ds_read_b32 v140, v8 offset:4096
	ds_read_b32 v141, v8 offset:4608
	ds_read_b32 v142, v8 offset:5120
	ds_read_b32 v143, v8 offset:5632
	ds_read_b32 v144, v8 offset:6144
	ds_read_b32 v145, v8 offset:6656
	ds_read_b32 v146, v8 offset:7168
	ds_read_b32 v147, v8 offset:7680
	s_waitcnt lgkmcnt(0)
	v_max_f32_e32 v132, v132, v132
	v_max_f32_e32 v133, v133, v133
	v_max_f32_e32 v134, v134, v134
	v_max_f32_e32 v135, v135, v135
	v_max_f32_e32 v136, v136, v136
	v_max_f32_e32 v137, v137, v137
	v_max_f32_e32 v138, v138, v138
	v_max_f32_e32 v139, v139, v139
	v_max_f32_e32 v140, v140, v140
	v_max_f32_e32 v141, v141, v141
	v_max_f32_e32 v142, v142, v142
	v_max_f32_e32 v143, v143, v143
	v_max_f32_e32 v144, v144, v144
	v_max_f32_e32 v145, v145, v145
	v_max_f32_e32 v146, v146, v146
	v_max_f32_e32 v147, v147, v147
	v_med3_f32 v132, v132, s20, v13
	v_med3_f32 v133, v133, s20, v13
	v_med3_f32 v134, v134, s20, v13
	v_med3_f32 v135, v135, s20, v13
	v_med3_f32 v136, v136, s20, v13
	v_med3_f32 v137, v137, s20, v13
	v_med3_f32 v138, v138, s20, v13
	v_med3_f32 v139, v139, s20, v13
	v_med3_f32 v140, v140, s20, v13
	v_med3_f32 v141, v141, s20, v13
	v_med3_f32 v142, v142, s20, v13
	v_med3_f32 v143, v143, s20, v13
	v_med3_f32 v144, v144, s20, v13
	v_med3_f32 v145, v145, s20, v13
	v_med3_f32 v146, v146, s20, v13
	v_med3_f32 v147, v147, s20, v13
	v_mov_b32_e32 v148, 0
	v_mov_b32_e32 v149, 0
	v_mov_b32_e32 v150, 0
	v_mov_b32_e32 v151, 0
	v_cvt_pk_fp8_f32 v148, v132, v133
	v_cvt_pk_fp8_f32 v149, v136, v137
	v_cvt_pk_fp8_f32 v150, v140, v141
	v_cvt_pk_fp8_f32 v151, v144, v145
	v_cvt_pk_fp8_f32 v148, v134, v135 op_sel:[0,0,1]
	v_cvt_pk_fp8_f32 v149, v138, v139 op_sel:[0,0,1]
	v_cvt_pk_fp8_f32 v150, v142, v143 op_sel:[0,0,1]
	v_cvt_pk_fp8_f32 v151, v146, v147 op_sel:[0,0,1]
	s_nop 0
	global_store_dwordx4 v12, v[148:151], s[14:15]
	s_waitcnt vmcnt(22)
	v_mul_f32_e32 v36, 0x43000000, v36
	v_mul_f32_e32 v37, 0x43000000, v37
	v_mul_f32_e32 v38, 0x43000000, v38
	v_mul_f32_e32 v39, 0x43000000, v39
	ds_write_b128 v5, v[36:39]
	v_mul_f32_e32 v40, 0x43000000, v40
	v_mul_f32_e32 v41, 0x43000000, v41
	v_mul_f32_e32 v42, 0x43000000, v42
	v_mul_f32_e32 v43, 0x43000000, v43
	ds_write_b128 v5, v[40:43] offset:1024
	v_mul_f32_e32 v44, 0x43000000, v44
	v_mul_f32_e32 v45, 0x43000000, v45
	v_mul_f32_e32 v46, 0x43000000, v46
	v_mul_f32_e32 v47, 0x43000000, v47
	ds_write_b128 v5, v[44:47] offset:2048
	v_mul_f32_e32 v48, 0x43000000, v48
	v_mul_f32_e32 v49, 0x43000000, v49
	v_mul_f32_e32 v50, 0x43000000, v50
	v_mul_f32_e32 v51, 0x43000000, v51
	ds_write_b128 v5, v[48:51] offset:3072
	v_mul_f32_e32 v52, 0x43000000, v52
	v_mul_f32_e32 v53, 0x43000000, v53
	v_mul_f32_e32 v54, 0x43000000, v54
	v_mul_f32_e32 v55, 0x43000000, v55
	ds_write_b128 v5, v[52:55] offset:4096
	v_mul_f32_e32 v56, 0x43000000, v56
	v_mul_f32_e32 v57, 0x43000000, v57
	v_mul_f32_e32 v58, 0x43000000, v58
	v_mul_f32_e32 v59, 0x43000000, v59
	ds_write_b128 v5, v[56:59] offset:5120
	v_mul_f32_e32 v60, 0x43000000, v60
	v_mul_f32_e32 v61, 0x43000000, v61
	v_mul_f32_e32 v62, 0x43000000, v62
	v_mul_f32_e32 v63, 0x43000000, v63
	ds_write_b128 v5, v[60:63] offset:6144
	v_mul_f32_e32 v64, 0x43000000, v64
	v_mul_f32_e32 v65, 0x43000000, v65
	v_mul_f32_e32 v66, 0x43000000, v66
	v_mul_f32_e32 v67, 0x43000000, v67
	ds_write_b128 v5, v[64:67] offset:7168
	s_waitcnt lgkmcnt(0)
	s_barrier
; #define GAS __attribute__((address_space(1)))
; #define LAS __attribute__((address_space(3)))
; #define LDS_WAIT() asm volatile("s_waitcnt lgkmcnt(0)" ::: "memory")
;     ...
;     for (int i = 0; i < 32; ++i) v[i] = sc >= 0 ? W[(size_t)(k0 + 2 * i + (lane >> 5)) * Nsrc + sc] : 0.f;
; #pragma unroll
;     for (int i = 0; i < 32; ++i) { const int k = k0 + 2 * i + (lane >> 5); float x = v[i] * wscale; if (KS) x *= (k < ksplit ? ksA[k] : ksB[k - ksplit]); scr[(2 * i + (lane >> 5)) * 33 + (lane & 31)] = x; }
;     LDS_WAIT(); asm volatile("" ::: "memory");
;     const int c = lane & 7;
; #pragma unroll
;     for (int j = 0; j < 4; ++j) { const int n = (lane >> 3) + 8 * j; const LAS float* s = scr + (8 * c) * 33 + n;
;         const unsigned long long o = (unsigned long long)pg8::pk4_fp8(s[0 * 33], s[1 * 33], s[2 * 33], s[3 * 33]) | ((unsigned long long)pg8::pk4_fp8(s[4 * 33], s[5 * 33], s[6 * 33], s[7 * 33]) << 32);
;         *(GAS unsigned long long*)(WT + (size_t)(n0 + n) * K + k0 + 8 * c) = o; }
	s_add_i32 s17, s16, 2304
	s_min_u32 s17, s17, 0xbff
	s_lshr_b32 s18, s17, 5
	s_add_i32 s18, s18, 32
	s_and_b32 s19, s17, 31
	s_lshl_b32 s18, s18, 21
	s_lshl_b32 s19, s19, 9
	s_add_u32 s18, s18, s19
	s_add_u32 s12, s2, s18
	s_addc_u32 s13, s3, 0
	global_load_dwordx4 v[36:39], v10, s[12:13]
	s_add_u32 s12, s12, 0x8000
	s_addc_u32 s13, s13, 0
	global_load_dwordx4 v[40:43], v10, s[12:13]
	s_add_u32 s12, s12, 0x8000
	s_addc_u32 s13, s13, 0
	global_load_dwordx4 v[44:47], v10, s[12:13]
	s_add_u32 s12, s12, 0x8000
	s_addc_u32 s13, s13, 0
	global_load_dwordx4 v[48:51], v10, s[12:13]
	s_add_u32 s12, s12, 0x8000
	s_addc_u32 s13, s13, 0
	global_load_dwordx4 v[52:55], v10, s[12:13]
	s_add_u32 s12, s12, 0x8000
	s_addc_u32 s13, s13, 0
	global_load_dwordx4 v[56:59], v10, s[12:13]
	s_add_u32 s12, s12, 0x8000
	s_addc_u32 s13, s13, 0
	global_load_dwordx4 v[60:63], v10, s[12:13]
	s_add_u32 s12, s12, 0x8000
	s_addc_u32 s13, s13, 0
	global_load_dwordx4 v[64:67], v10, s[12:13]
	s_add_i32 s17, s16, 2016
	s_min_u32 s17, s17, 0xbff
	s_lshr_b32 s18, s17, 5
	s_add_i32 s18, s18, 32
	s_and_b32 s19, s17, 31
	s_lshl_b32 s19, s19, 21
	s_lshl_b32 s18, s18, 7
	s_add_u32 s18, s18, s19
	s_add_u32 s14, s4, s18
	s_addc_u32 s15, s5, 0
	ds_read_b32 v132, v7
	ds_read_b32 v133, v7 offset:512
	ds_read_b32 v134, v7 offset:1024
	ds_read_b32 v135, v7 offset:1536
	ds_read_b32 v136, v7 offset:2048
	ds_read_b32 v137, v7 offset:2560
	ds_read_b32 v138, v7 offset:3072
	ds_read_b32 v139, v7 offset:3584
	ds_read_b32 v140, v7 offset:4096
	ds_read_b32 v141, v7 offset:4608
	ds_read_b32 v142, v7 offset:5120
	ds_read_b32 v143, v7 offset:5632
	ds_read_b32 v144, v7 offset:6144
	ds_read_b32 v145, v7 offset:6656
	ds_read_b32 v146, v7 offset:7168
	ds_read_b32 v147, v7 offset:7680
	s_waitcnt lgkmcnt(0)
	v_max_f32_e32 v132, v132, v132
	v_max_f32_e32 v133, v133, v133
	v_max_f32_e32 v134, v134, v134
	v_max_f32_e32 v135, v135, v135
	v_max_f32_e32 v136, v136, v136
	v_max_f32_e32 v137, v137, v137
	v_max_f32_e32 v138, v138, v138
	v_max_f32_e32 v139, v139, v139
	v_max_f32_e32 v140, v140, v140
	v_max_f32_e32 v141, v141, v141
	v_max_f32_e32 v142, v142, v142
	v_max_f32_e32 v143, v143, v143
	v_max_f32_e32 v144, v144, v144
	v_max_f32_e32 v145, v145, v145
	v_max_f32_e32 v146, v146, v146
	v_max_f32_e32 v147, v147, v147
	v_med3_f32 v132, v132, s20, v13
	v_med3_f32 v133, v133, s20, v13
	v_med3_f32 v134, v134, s20, v13
	v_med3_f32 v135, v135, s20, v13
	v_med3_f32 v136, v136, s20, v13
	v_med3_f32 v137, v137, s20, v13
	v_med3_f32 v138, v138, s20, v13
	v_med3_f32 v139, v139, s20, v13
	v_med3_f32 v140, v140, s20, v13
	v_med3_f32 v141, v141, s20, v13
	v_med3_f32 v142, v142, s20, v13
	v_med3_f32 v143, v143, s20, v13
	v_med3_f32 v144, v144, s20, v13
	v_med3_f32 v145, v145, s20, v13
	v_med3_f32 v146, v146, s20, v13
	v_med3_f32 v147, v147, s20, v13
	v_mov_b32_e32 v148, 0
	v_mov_b32_e32 v149, 0
	v_mov_b32_e32 v150, 0
	v_mov_b32_e32 v151, 0
	v_cvt_pk_fp8_f32 v148, v132, v133
	v_cvt_pk_fp8_f32 v149, v136, v137
	v_cvt_pk_fp8_f32 v150, v140, v141
	v_cvt_pk_fp8_f32 v151, v144, v145
	v_cvt_pk_fp8_f32 v148, v134, v135 op_sel:[0,0,1]
	v_cvt_pk_fp8_f32 v149, v138, v139 op_sel:[0,0,1]
	v_cvt_pk_fp8_f32 v150, v142, v143 op_sel:[0,0,1]
	v_cvt_pk_fp8_f32 v151, v146, v147 op_sel:[0,0,1]
	s_nop 0
	global_store_dwordx4 v11, v[148:151], s[14:15]
	ds_read_b32 v132, v9
	ds_read_b32 v133, v9 offset:512
	ds_read_b32 v134, v9 offset:1024
	ds_read_b32 v135, v9 offset:1536
	ds_read_b32 v136, v9 offset:2048
	ds_read_b32 v137, v9 offset:2560
	ds_read_b32 v138, v9 offset:3072
	ds_read_b32 v139, v9 offset:3584
	ds_read_b32 v140, v9 offset:4096
	ds_read_b32 v141, v9 offset:4608
	ds_read_b32 v142, v9 offset:5120
	ds_read_b32 v143, v9 offset:5632
	ds_read_b32 v144, v9 offset:6144
	ds_read_b32 v145, v9 offset:6656
	ds_read_b32 v146, v9 offset:7168
	ds_read_b32 v147, v9 offset:7680
	s_waitcnt lgkmcnt(0)
	v_max_f32_e32 v132, v132, v132
	v_max_f32_e32 v133, v133, v133
	v_max_f32_e32 v134, v134, v134
	v_max_f32_e32 v135, v135, v135
	v_max_f32_e32 v136, v136, v136
	v_max_f32_e32 v137, v137, v137
	v_max_f32_e32 v138, v138, v138
	v_max_f32_e32 v139, v139, v139
	v_max_f32_e32 v140, v140, v140
	v_max_f32_e32 v141, v141, v141
	v_max_f32_e32 v142, v142, v142
	v_max_f32_e32 v143, v143, v143
	v_max_f32_e32 v144, v144, v144
	v_max_f32_e32 v145, v145, v145
	v_max_f32_e32 v146, v146, v146
	v_max_f32_e32 v147, v147, v147
	v_med3_f32 v132, v132, s20, v13
	v_med3_f32 v133, v133, s20, v13
	v_med3_f32 v134, v134, s20, v13
	v_med3_f32 v135, v135, s20, v13
	v_med3_f32 v136, v136, s20, v13
	v_med3_f32 v137, v137, s20, v13
	v_med3_f32 v138, v138, s20, v13
	v_med3_f32 v139, v139, s20, v13
	v_med3_f32 v140, v140, s20, v13
	v_med3_f32 v141, v141, s20, v13
	v_med3_f32 v142, v142, s20, v13
	v_med3_f32 v143, v143, s20, v13
	v_med3_f32 v144, v144, s20, v13
	v_med3_f32 v145, v145, s20, v13
	v_med3_f32 v146, v146, s20, v13
	v_med3_f32 v147, v147, s20, v13
	v_mov_b32_e32 v148, 0
	v_mov_b32_e32 v149, 0
	v_mov_b32_e32 v150, 0
	v_mov_b32_e32 v151, 0
	v_cvt_pk_fp8_f32 v148, v132, v133
	v_cvt_pk_fp8_f32 v149, v136, v137
	v_cvt_pk_fp8_f32 v150, v140, v141
	v_cvt_pk_fp8_f32 v151, v144, v145
	v_cvt_pk_fp8_f32 v148, v134, v135 op_sel:[0,0,1]
	v_cvt_pk_fp8_f32 v149, v138, v139 op_sel:[0,0,1]
	v_cvt_pk_fp8_f32 v150, v142, v143 op_sel:[0,0,1]
	v_cvt_pk_fp8_f32 v151, v146, v147 op_sel:[0,0,1]
	s_nop 0
	global_store_dwordx4 v12, v[148:151], s[14:15]
	s_waitcnt vmcnt(22)
	v_mul_f32_e32 v68, 0x43000000, v68
	v_mul_f32_e32 v69, 0x43000000, v69
	v_mul_f32_e32 v70, 0x43000000, v70
	v_mul_f32_e32 v71, 0x43000000, v71
	ds_write_b128 v4, v[68:71]
	v_mul_f32_e32 v72, 0x43000000, v72
	v_mul_f32_e32 v73, 0x43000000, v73
	v_mul_f32_e32 v74, 0x43000000, v74
	v_mul_f32_e32 v75, 0x43000000, v75
	ds_write_b128 v4, v[72:75] offset:1024
	v_mul_f32_e32 v76, 0x43000000, v76
	v_mul_f32_e32 v77, 0x43000000, v77
	v_mul_f32_e32 v78, 0x43000000, v78
	v_mul_f32_e32 v79, 0x43000000, v79
	ds_write_b128 v4, v[76:79] offset:2048
	v_mul_f32_e32 v80, 0x43000000, v80
	v_mul_f32_e32 v81, 0x43000000, v81
	v_mul_f32_e32 v82, 0x43000000, v82
	v_mul_f32_e32 v83, 0x43000000, v83
	ds_write_b128 v4, v[80:83] offset:3072
	v_mul_f32_e32 v84, 0x43000000, v84
	v_mul_f32_e32 v85, 0x43000000, v85
	v_mul_f32_e32 v86, 0x43000000, v86
	v_mul_f32_e32 v87, 0x43000000, v87
	ds_write_b128 v4, v[84:87] offset:4096
	v_mul_f32_e32 v88, 0x43000000, v88
	v_mul_f32_e32 v89, 0x43000000, v89
	v_mul_f32_e32 v90, 0x43000000, v90
	v_mul_f32_e32 v91, 0x43000000, v91
	ds_write_b128 v4, v[88:91] offset:5120
	v_mul_f32_e32 v92, 0x43000000, v92
	v_mul_f32_e32 v93, 0x43000000, v93
	v_mul_f32_e32 v94, 0x43000000, v94
	v_mul_f32_e32 v95, 0x43000000, v95
	ds_write_b128 v4, v[92:95] offset:6144
	v_mul_f32_e32 v96, 0x43000000, v96
	v_mul_f32_e32 v97, 0x43000000, v97
	v_mul_f32_e32 v98, 0x43000000, v98
	v_mul_f32_e32 v99, 0x43000000, v99
	ds_write_b128 v4, v[96:99] offset:7168
	s_waitcnt lgkmcnt(0)
	s_barrier
; #define GAS __attribute__((address_space(1)))
; #define LAS __attribute__((address_space(3)))
; #define LDS_WAIT() asm volatile("s_waitcnt lgkmcnt(0)" ::: "memory")
;     ...
;     for (int i = 0; i < 32; ++i) v[i] = sc >= 0 ? W[(size_t)(k0 + 2 * i + (lane >> 5)) * Nsrc + sc] : 0.f;
; #pragma unroll
;     for (int i = 0; i < 32; ++i) { const int k = k0 + 2 * i + (lane >> 5); float x = v[i] * wscale; if (KS) x *= (k < ksplit ? ksA[k] : ksB[k - ksplit]); scr[(2 * i + (lane >> 5)) * 33 + (lane & 31)] = x; }
;     LDS_WAIT(); asm volatile("" ::: "memory");
;     const int c = lane & 7;
; #pragma unroll
;     for (int j = 0; j < 4; ++j) { const int n = (lane >> 3) + 8 * j; const LAS float* s = scr + (8 * c) * 33 + n;
;         const unsigned long long o = (unsigned long long)pg8::pk4_fp8(s[0 * 33], s[1 * 33], s[2 * 33], s[3 * 33]) | ((unsigned long long)pg8::pk4_fp8(s[4 * 33], s[5 * 33], s[6 * 33], s[7 * 33]) << 32);
;         *(GAS unsigned long long*)(WT + (size_t)(n0 + n) * K + k0 + 8 * c) = o; }
	s_add_i32 s17, s16, 2400
	s_min_u32 s17, s17, 0xbff
	s_lshr_b32 s18, s17, 5
	s_add_i32 s18, s18, 32
	s_and_b32 s19, s17, 31
	s_lshl_b32 s18, s18, 21
	s_lshl_b32 s19, s19, 9
	s_add_u32 s18, s18, s19
	s_add_u32 s12, s2, s18
	s_addc_u32 s13, s3, 0
	global_load_dwordx4 v[68:71], v10, s[12:13]
	s_add_u32 s12, s12, 0x8000
	s_addc_u32 s13, s13, 0
	global_load_dwordx4 v[72:75], v10, s[12:13]
	s_add_u32 s12, s12, 0x8000
	s_addc_u32 s13, s13, 0
	global_load_dwordx4 v[76:79], v10, s[12:13]
	s_add_u32 s12, s12, 0x8000
	s_addc_u32 s13, s13, 0
	global_load_dwordx4 v[80:83], v10, s[12:13]
	s_add_u32 s12, s12, 0x8000
	s_addc_u32 s13, s13, 0
	global_load_dwordx4 v[84:87], v10, s[12:13]
	s_add_u32 s12, s12, 0x8000
	s_addc_u32 s13, s13, 0
	global_load_dwordx4 v[88:91], v10, s[12:13]
	s_add_u32 s12, s12, 0x8000
	s_addc_u32 s13, s13, 0
	global_load_dwordx4 v[92:95], v10, s[12:13]
	s_add_u32 s12, s12, 0x8000
	s_addc_u32 s13, s13, 0
	global_load_dwordx4 v[96:99], v10, s[12:13]
	s_add_i32 s17, s16, 2112
	s_min_u32 s17, s17, 0xbff
	s_lshr_b32 s18, s17, 5
	s_add_i32 s18, s18, 32
	s_and_b32 s19, s17, 31
	s_lshl_b32 s19, s19, 21
	s_lshl_b32 s18, s18, 7
	s_add_u32 s18, s18, s19
	s_add_u32 s14, s4, s18
	s_addc_u32 s15, s5, 0
	ds_read_b32 v132, v6
	ds_read_b32 v133, v6 offset:512
	ds_read_b32 v134, v6 offset:1024
	ds_read_b32 v135, v6 offset:1536
	ds_read_b32 v136, v6 offset:2048
	ds_read_b32 v137, v6 offset:2560
	ds_read_b32 v138, v6 offset:3072
	ds_read_b32 v139, v6 offset:3584
	ds_read_b32 v140, v6 offset:4096
	ds_read_b32 v141, v6 offset:4608
	ds_read_b32 v142, v6 offset:5120
	ds_read_b32 v143, v6 offset:5632
	ds_read_b32 v144, v6 offset:6144
	ds_read_b32 v145, v6 offset:6656
	ds_read_b32 v146, v6 offset:7168
	ds_read_b32 v147, v6 offset:7680
	s_waitcnt lgkmcnt(0)
	v_max_f32_e32 v132, v132, v132
	v_max_f32_e32 v133, v133, v133
	v_max_f32_e32 v134, v134, v134
	v_max_f32_e32 v135, v135, v135
	v_max_f32_e32 v136, v136, v136
	v_max_f32_e32 v137, v137, v137
	v_max_f32_e32 v138, v138, v138
	v_max_f32_e32 v139, v139, v139
	v_max_f32_e32 v140, v140, v140
	v_max_f32_e32 v141, v141, v141
	v_max_f32_e32 v142, v142, v142
	v_max_f32_e32 v143, v143, v143
	v_max_f32_e32 v144, v144, v144
	v_max_f32_e32 v145, v145, v145
	v_max_f32_e32 v146, v146, v146
	v_max_f32_e32 v147, v147, v147
	v_med3_f32 v132, v132, s20, v13
	v_med3_f32 v133, v133, s20, v13
	v_med3_f32 v134, v134, s20, v13
	v_med3_f32 v135, v135, s20, v13
	v_med3_f32 v136, v136, s20, v13
	v_med3_f32 v137, v137, s20, v13
	v_med3_f32 v138, v138, s20, v13
	v_med3_f32 v139, v139, s20, v13
	v_med3_f32 v140, v140, s20, v13
	v_med3_f32 v141, v141, s20, v13
	v_med3_f32 v142, v142, s20, v13
	v_med3_f32 v143, v143, s20, v13
	v_med3_f32 v144, v144, s20, v13
	v_med3_f32 v145, v145, s20, v13
	v_med3_f32 v146, v146, s20, v13
	v_med3_f32 v147, v147, s20, v13
	v_mov_b32_e32 v148, 0
	v_mov_b32_e32 v149, 0
	v_mov_b32_e32 v150, 0
	v_mov_b32_e32 v151, 0
	v_cvt_pk_fp8_f32 v148, v132, v133
	v_cvt_pk_fp8_f32 v149, v136, v137
	v_cvt_pk_fp8_f32 v150, v140, v141
	v_cvt_pk_fp8_f32 v151, v144, v145
	v_cvt_pk_fp8_f32 v148, v134, v135 op_sel:[0,0,1]
	v_cvt_pk_fp8_f32 v149, v138, v139 op_sel:[0,0,1]
	v_cvt_pk_fp8_f32 v150, v142, v143 op_sel:[0,0,1]
	v_cvt_pk_fp8_f32 v151, v146, v147 op_sel:[0,0,1]
	s_nop 0
	global_store_dwordx4 v11, v[148:151], s[14:15]
	ds_read_b32 v132, v8
	ds_read_b32 v133, v8 offset:512
	ds_read_b32 v134, v8 offset:1024
	ds_read_b32 v135, v8 offset:1536
	ds_read_b32 v136, v8 offset:2048
	ds_read_b32 v137, v8 offset:2560
	ds_read_b32 v138, v8 offset:3072
	ds_read_b32 v139, v8 offset:3584
	ds_read_b32 v140, v8 offset:4096
	ds_read_b32 v141, v8 offset:4608
	ds_read_b32 v142, v8 offset:5120
	ds_read_b32 v143, v8 offset:5632
	ds_read_b32 v144, v8 offset:6144
	ds_read_b32 v145, v8 offset:6656
	ds_read_b32 v146, v8 offset:7168
	ds_read_b32 v147, v8 offset:7680
	s_waitcnt lgkmcnt(0)
	v_max_f32_e32 v132, v132, v132
	v_max_f32_e32 v133, v133, v133
	v_max_f32_e32 v134, v134, v134
	v_max_f32_e32 v135, v135, v135
	v_max_f32_e32 v136, v136, v136
	v_max_f32_e32 v137, v137, v137
	v_max_f32_e32 v138, v138, v138
	v_max_f32_e32 v139, v139, v139
	v_max_f32_e32 v140, v140, v140
	v_max_f32_e32 v141, v141, v141
	v_max_f32_e32 v142, v142, v142
	v_max_f32_e32 v143, v143, v143
	v_max_f32_e32 v144, v144, v144
	v_max_f32_e32 v145, v145, v145
	v_max_f32_e32 v146, v146, v146
	v_max_f32_e32 v147, v147, v147
	v_med3_f32 v132, v132, s20, v13
	v_med3_f32 v133, v133, s20, v13
	v_med3_f32 v134, v134, s20, v13
	v_med3_f32 v135, v135, s20, v13
	v_med3_f32 v136, v136, s20, v13
	v_med3_f32 v137, v137, s20, v13
	v_med3_f32 v138, v138, s20, v13
	v_med3_f32 v139, v139, s20, v13
	v_med3_f32 v140, v140, s20, v13
	v_med3_f32 v141, v141, s20, v13
	v_med3_f32 v142, v142, s20, v13
	v_med3_f32 v143, v143, s20, v13
	v_med3_f32 v144, v144, s20, v13
	v_med3_f32 v145, v145, s20, v13
	v_med3_f32 v146, v146, s20, v13
	v_med3_f32 v147, v147, s20, v13
	v_mov_b32_e32 v148, 0
	v_mov_b32_e32 v149, 0
	v_mov_b32_e32 v150, 0
	v_mov_b32_e32 v151, 0
	v_cvt_pk_fp8_f32 v148, v132, v133
	v_cvt_pk_fp8_f32 v149, v136, v137
	v_cvt_pk_fp8_f32 v150, v140, v141
	v_cvt_pk_fp8_f32 v151, v144, v145
	v_cvt_pk_fp8_f32 v148, v134, v135 op_sel:[0,0,1]
	v_cvt_pk_fp8_f32 v149, v138, v139 op_sel:[0,0,1]
	v_cvt_pk_fp8_f32 v150, v142, v143 op_sel:[0,0,1]
	v_cvt_pk_fp8_f32 v151, v146, v147 op_sel:[0,0,1]
	s_nop 0
	global_store_dwordx4 v12, v[148:151], s[14:15]
	s_waitcnt vmcnt(22)
	v_mul_f32_e32 v100, 0x43000000, v100
	v_mul_f32_e32 v101, 0x43000000, v101
	v_mul_f32_e32 v102, 0x43000000, v102
	v_mul_f32_e32 v103, 0x43000000, v103
	ds_write_b128 v5, v[100:103]
	v_mul_f32_e32 v104, 0x43000000, v104
	v_mul_f32_e32 v105, 0x43000000, v105
	v_mul_f32_e32 v106, 0x43000000, v106
	v_mul_f32_e32 v107, 0x43000000, v107
	ds_write_b128 v5, v[104:107] offset:1024
	v_mul_f32_e32 v108, 0x43000000, v108
	v_mul_f32_e32 v109, 0x43000000, v109
	v_mul_f32_e32 v110, 0x43000000, v110
	v_mul_f32_e32 v111, 0x43000000, v111
	ds_write_b128 v5, v[108:111] offset:2048
	v_mul_f32_e32 v112, 0x43000000, v112
	v_mul_f32_e32 v113, 0x43000000, v113
	v_mul_f32_e32 v114, 0x43000000, v114
	v_mul_f32_e32 v115, 0x43000000, v115
	ds_write_b128 v5, v[112:115] offset:3072
	v_mul_f32_e32 v116, 0x43000000, v116
	v_mul_f32_e32 v117, 0x43000000, v117
	v_mul_f32_e32 v118, 0x43000000, v118
	v_mul_f32_e32 v119, 0x43000000, v119
	ds_write_b128 v5, v[116:119] offset:4096
	v_mul_f32_e32 v120, 0x43000000, v120
	v_mul_f32_e32 v121, 0x43000000, v121
	v_mul_f32_e32 v122, 0x43000000, v122
	v_mul_f32_e32 v123, 0x43000000, v123
	ds_write_b128 v5, v[120:123] offset:5120
	v_mul_f32_e32 v124, 0x43000000, v124
	v_mul_f32_e32 v125, 0x43000000, v125
	v_mul_f32_e32 v126, 0x43000000, v126
	v_mul_f32_e32 v127, 0x43000000, v127
	ds_write_b128 v5, v[124:127] offset:6144
	v_mul_f32_e32 v128, 0x43000000, v128
	v_mul_f32_e32 v129, 0x43000000, v129
	v_mul_f32_e32 v130, 0x43000000, v130
	v_mul_f32_e32 v131, 0x43000000, v131
	ds_write_b128 v5, v[128:131] offset:7168
	s_waitcnt lgkmcnt(0)
	s_barrier
; #define GAS __attribute__((address_space(1)))
; #define LAS __attribute__((address_space(3)))
; #define LDS_WAIT() asm volatile("s_waitcnt lgkmcnt(0)" ::: "memory")
;     ...
;     for (int i = 0; i < 32; ++i) v[i] = sc >= 0 ? W[(size_t)(k0 + 2 * i + (lane >> 5)) * Nsrc + sc] : 0.f;
; #pragma unroll
;     for (int i = 0; i < 32; ++i) { const int k = k0 + 2 * i + (lane >> 5); float x = v[i] * wscale; if (KS) x *= (k < ksplit ? ksA[k] : ksB[k - ksplit]); scr[(2 * i + (lane >> 5)) * 33 + (lane & 31)] = x; }
;     LDS_WAIT(); asm volatile("" ::: "memory");
;     const int c = lane & 7;
; #pragma unroll
;     for (int j = 0; j < 4; ++j) { const int n = (lane >> 3) + 8 * j; const LAS float* s = scr + (8 * c) * 33 + n;
;         const unsigned long long o = (unsigned long long)pg8::pk4_fp8(s[0 * 33], s[1 * 33], s[2 * 33], s[3 * 33]) | ((unsigned long long)pg8::pk4_fp8(s[4 * 33], s[5 * 33], s[6 * 33], s[7 * 33]) << 32);
;         *(GAS unsigned long long*)(WT + (size_t)(n0 + n) * K + k0 + 8 * c) = o; }
	s_add_i32 s17, s16, 2496
	s_min_u32 s17, s17, 0xbff
	s_lshr_b32 s18, s17, 5
	s_add_i32 s18, s18, 32
	s_and_b32 s19, s17, 31
	s_lshl_b32 s18, s18, 21
	s_lshl_b32 s19, s19, 9
	s_add_u32 s18, s18, s19
	s_add_u32 s12, s2, s18
	s_addc_u32 s13, s3, 0
	global_load_dwordx4 v[100:103], v10, s[12:13]
	s_add_u32 s12, s12, 0x8000
	s_addc_u32 s13, s13, 0
	global_load_dwordx4 v[104:107], v10, s[12:13]
	s_add_u32 s12, s12, 0x8000
	s_addc_u32 s13, s13, 0
	global_load_dwordx4 v[108:111], v10, s[12:13]
	s_add_u32 s12, s12, 0x8000
	s_addc_u32 s13, s13, 0
	global_load_dwordx4 v[112:115], v10, s[12:13]
	s_add_u32 s12, s12, 0x8000
	s_addc_u32 s13, s13, 0
	global_load_dwordx4 v[116:119], v10, s[12:13]
	s_add_u32 s12, s12, 0x8000
	s_addc_u32 s13, s13, 0
	global_load_dwordx4 v[120:123], v10, s[12:13]
	s_add_u32 s12, s12, 0x8000
	s_addc_u32 s13, s13, 0
	global_load_dwordx4 v[124:127], v10, s[12:13]
	s_add_u32 s12, s12, 0x8000
	s_addc_u32 s13, s13, 0
	global_load_dwordx4 v[128:131], v10, s[12:13]
	s_add_i32 s17, s16, 2208
	s_min_u32 s17, s17, 0xbff
	s_lshr_b32 s18, s17, 5
	s_add_i32 s18, s18, 32
	s_and_b32 s19, s17, 31
	s_lshl_b32 s19, s19, 21
	s_lshl_b32 s18, s18, 7
	s_add_u32 s18, s18, s19
	s_add_u32 s14, s4, s18
	s_addc_u32 s15, s5, 0
	ds_read_b32 v132, v7
	ds_read_b32 v133, v7 offset:512
	ds_read_b32 v134, v7 offset:1024
	ds_read_b32 v135, v7 offset:1536
	ds_read_b32 v136, v7 offset:2048
	ds_read_b32 v137, v7 offset:2560
	ds_read_b32 v138, v7 offset:3072
	ds_read_b32 v139, v7 offset:3584
	ds_read_b32 v140, v7 offset:4096
	ds_read_b32 v141, v7 offset:4608
	ds_read_b32 v142, v7 offset:5120
	ds_read_b32 v143, v7 offset:5632
	ds_read_b32 v144, v7 offset:6144
	ds_read_b32 v145, v7 offset:6656
	ds_read_b32 v146, v7 offset:7168
	ds_read_b32 v147, v7 offset:7680
	s_waitcnt lgkmcnt(0)
	v_max_f32_e32 v132, v132, v132
	v_max_f32_e32 v133, v133, v133
	v_max_f32_e32 v134, v134, v134
	v_max_f32_e32 v135, v135, v135
	v_max_f32_e32 v136, v136, v136
	v_max_f32_e32 v137, v137, v137
	v_max_f32_e32 v138, v138, v138
	v_max_f32_e32 v139, v139, v139
	v_max_f32_e32 v140, v140, v140
	v_max_f32_e32 v141, v141, v141
	v_max_f32_e32 v142, v142, v142
	v_max_f32_e32 v143, v143, v143
	v_max_f32_e32 v144, v144, v144
	v_max_f32_e32 v145, v145, v145
	v_max_f32_e32 v146, v146, v146
	v_max_f32_e32 v147, v147, v147
	v_med3_f32 v132, v132, s20, v13
	v_med3_f32 v133, v133, s20, v13
	v_med3_f32 v134, v134, s20, v13
	v_med3_f32 v135, v135, s20, v13
	v_med3_f32 v136, v136, s20, v13
	v_med3_f32 v137, v137, s20, v13
	v_med3_f32 v138, v138, s20, v13
	v_med3_f32 v139, v139, s20, v13
	v_med3_f32 v140, v140, s20, v13
	v_med3_f32 v141, v141, s20, v13
	v_med3_f32 v142, v142, s20, v13
	v_med3_f32 v143, v143, s20, v13
	v_med3_f32 v144, v144, s20, v13
	v_med3_f32 v145, v145, s20, v13
	v_med3_f32 v146, v146, s20, v13
	v_med3_f32 v147, v147, s20, v13
	v_mov_b32_e32 v148, 0
	v_mov_b32_e32 v149, 0
	v_mov_b32_e32 v150, 0
	v_mov_b32_e32 v151, 0
	v_cvt_pk_fp8_f32 v148, v132, v133
	v_cvt_pk_fp8_f32 v149, v136, v137
	v_cvt_pk_fp8_f32 v150, v140, v141
	v_cvt_pk_fp8_f32 v151, v144, v145
	v_cvt_pk_fp8_f32 v148, v134, v135 op_sel:[0,0,1]
	v_cvt_pk_fp8_f32 v149, v138, v139 op_sel:[0,0,1]
	v_cvt_pk_fp8_f32 v150, v142, v143 op_sel:[0,0,1]
	v_cvt_pk_fp8_f32 v151, v146, v147 op_sel:[0,0,1]
	s_nop 0
	global_store_dwordx4 v11, v[148:151], s[14:15]
	ds_read_b32 v132, v9
	ds_read_b32 v133, v9 offset:512
	ds_read_b32 v134, v9 offset:1024
	ds_read_b32 v135, v9 offset:1536
	ds_read_b32 v136, v9 offset:2048
	ds_read_b32 v137, v9 offset:2560
	ds_read_b32 v138, v9 offset:3072
	ds_read_b32 v139, v9 offset:3584
	ds_read_b32 v140, v9 offset:4096
	ds_read_b32 v141, v9 offset:4608
	ds_read_b32 v142, v9 offset:5120
	ds_read_b32 v143, v9 offset:5632
	ds_read_b32 v144, v9 offset:6144
	ds_read_b32 v145, v9 offset:6656
	ds_read_b32 v146, v9 offset:7168
	ds_read_b32 v147, v9 offset:7680
	s_waitcnt lgkmcnt(0)
	v_max_f32_e32 v132, v132, v132
	v_max_f32_e32 v133, v133, v133
	v_max_f32_e32 v134, v134, v134
	v_max_f32_e32 v135, v135, v135
	v_max_f32_e32 v136, v136, v136
	v_max_f32_e32 v137, v137, v137
	v_max_f32_e32 v138, v138, v138
	v_max_f32_e32 v139, v139, v139
	v_max_f32_e32 v140, v140, v140
	v_max_f32_e32 v141, v141, v141
	v_max_f32_e32 v142, v142, v142
	v_max_f32_e32 v143, v143, v143
	v_max_f32_e32 v144, v144, v144
	v_max_f32_e32 v145, v145, v145
	v_max_f32_e32 v146, v146, v146
	v_max_f32_e32 v147, v147, v147
	v_med3_f32 v132, v132, s20, v13
	v_med3_f32 v133, v133, s20, v13
	v_med3_f32 v134, v134, s20, v13
	v_med3_f32 v135, v135, s20, v13
	v_med3_f32 v136, v136, s20, v13
	v_med3_f32 v137, v137, s20, v13
	v_med3_f32 v138, v138, s20, v13
	v_med3_f32 v139, v139, s20, v13
	v_med3_f32 v140, v140, s20, v13
	v_med3_f32 v141, v141, s20, v13
	v_med3_f32 v142, v142, s20, v13
	v_med3_f32 v143, v143, s20, v13
	v_med3_f32 v144, v144, s20, v13
	v_med3_f32 v145, v145, s20, v13
	v_med3_f32 v146, v146, s20, v13
	v_med3_f32 v147, v147, s20, v13
	v_mov_b32_e32 v148, 0
	v_mov_b32_e32 v149, 0
	v_mov_b32_e32 v150, 0
	v_mov_b32_e32 v151, 0
	v_cvt_pk_fp8_f32 v148, v132, v133
	v_cvt_pk_fp8_f32 v149, v136, v137
	v_cvt_pk_fp8_f32 v150, v140, v141
	v_cvt_pk_fp8_f32 v151, v144, v145
	v_cvt_pk_fp8_f32 v148, v134, v135 op_sel:[0,0,1]
	v_cvt_pk_fp8_f32 v149, v138, v139 op_sel:[0,0,1]
	v_cvt_pk_fp8_f32 v150, v142, v143 op_sel:[0,0,1]
	v_cvt_pk_fp8_f32 v151, v146, v147 op_sel:[0,0,1]
	s_nop 0
	global_store_dwordx4 v12, v[148:151], s[14:15]
	s_waitcnt vmcnt(22)
	v_mul_f32_e32 v36, 0x43000000, v36
	v_mul_f32_e32 v37, 0x43000000, v37
	v_mul_f32_e32 v38, 0x43000000, v38
	v_mul_f32_e32 v39, 0x43000000, v39
	ds_write_b128 v4, v[36:39]
	v_mul_f32_e32 v40, 0x43000000, v40
	v_mul_f32_e32 v41, 0x43000000, v41
	v_mul_f32_e32 v42, 0x43000000, v42
	v_mul_f32_e32 v43, 0x43000000, v43
	ds_write_b128 v4, v[40:43] offset:1024
	v_mul_f32_e32 v44, 0x43000000, v44
	v_mul_f32_e32 v45, 0x43000000, v45
	v_mul_f32_e32 v46, 0x43000000, v46
	v_mul_f32_e32 v47, 0x43000000, v47
	ds_write_b128 v4, v[44:47] offset:2048
	v_mul_f32_e32 v48, 0x43000000, v48
	v_mul_f32_e32 v49, 0x43000000, v49
	v_mul_f32_e32 v50, 0x43000000, v50
	v_mul_f32_e32 v51, 0x43000000, v51
	ds_write_b128 v4, v[48:51] offset:3072
	v_mul_f32_e32 v52, 0x43000000, v52
	v_mul_f32_e32 v53, 0x43000000, v53
	v_mul_f32_e32 v54, 0x43000000, v54
	v_mul_f32_e32 v55, 0x43000000, v55
	ds_write_b128 v4, v[52:55] offset:4096
	v_mul_f32_e32 v56, 0x43000000, v56
	v_mul_f32_e32 v57, 0x43000000, v57
	v_mul_f32_e32 v58, 0x43000000, v58
	v_mul_f32_e32 v59, 0x43000000, v59
	ds_write_b128 v4, v[56:59] offset:5120
	v_mul_f32_e32 v60, 0x43000000, v60
	v_mul_f32_e32 v61, 0x43000000, v61
	v_mul_f32_e32 v62, 0x43000000, v62
	v_mul_f32_e32 v63, 0x43000000, v63
	ds_write_b128 v4, v[60:63] offset:6144
	v_mul_f32_e32 v64, 0x43000000, v64
	v_mul_f32_e32 v65, 0x43000000, v65
	v_mul_f32_e32 v66, 0x43000000, v66
	v_mul_f32_e32 v67, 0x43000000, v67
	ds_write_b128 v4, v[64:67] offset:7168
	s_waitcnt lgkmcnt(0)
	s_barrier
; #define GAS __attribute__((address_space(1)))
; #define LAS __attribute__((address_space(3)))
; #define LDS_WAIT() asm volatile("s_waitcnt lgkmcnt(0)" ::: "memory")
;     ...
;     for (int i = 0; i < 32; ++i) v[i] = sc >= 0 ? W[(size_t)(k0 + 2 * i + (lane >> 5)) * Nsrc + sc] : 0.f;
; #pragma unroll
;     for (int i = 0; i < 32; ++i) { const int k = k0 + 2 * i + (lane >> 5); float x = v[i] * wscale; if (KS) x *= (k < ksplit ? ksA[k] : ksB[k - ksplit]); scr[(2 * i + (lane >> 5)) * 33 + (lane & 31)] = x; }
;     LDS_WAIT(); asm volatile("" ::: "memory");
;     const int c = lane & 7;
; #pragma unroll
;     for (int j = 0; j < 4; ++j) { const int n = (lane >> 3) + 8 * j; const LAS float* s = scr + (8 * c) * 33 + n;
;         const unsigned long long o = (unsigned long long)pg8::pk4_fp8(s[0 * 33], s[1 * 33], s[2 * 33], s[3 * 33]) | ((unsigned long long)pg8::pk4_fp8(s[4 * 33], s[5 * 33], s[6 * 33], s[7 * 33]) << 32);
;         *(GAS unsigned long long*)(WT + (size_t)(n0 + n) * K + k0 + 8 * c) = o; }
	s_add_i32 s17, s16, 2592
	s_min_u32 s17, s17, 0xbff
	s_lshr_b32 s18, s17, 5
	s_add_i32 s18, s18, 32
	s_and_b32 s19, s17, 31
	s_lshl_b32 s18, s18, 21
	s_lshl_b32 s19, s19, 9
	s_add_u32 s18, s18, s19
	s_add_u32 s12, s2, s18
	s_addc_u32 s13, s3, 0
	global_load_dwordx4 v[36:39], v10, s[12:13]
	s_add_u32 s12, s12, 0x8000
	s_addc_u32 s13, s13, 0
	global_load_dwordx4 v[40:43], v10, s[12:13]
	s_add_u32 s12, s12, 0x8000
	s_addc_u32 s13, s13, 0
	global_load_dwordx4 v[44:47], v10, s[12:13]
	s_add_u32 s12, s12, 0x8000
	s_addc_u32 s13, s13, 0
	global_load_dwordx4 v[48:51], v10, s[12:13]
	s_add_u32 s12, s12, 0x8000
	s_addc_u32 s13, s13, 0
	global_load_dwordx4 v[52:55], v10, s[12:13]
	s_add_u32 s12, s12, 0x8000
	s_addc_u32 s13, s13, 0
	global_load_dwordx4 v[56:59], v10, s[12:13]
	s_add_u32 s12, s12, 0x8000
	s_addc_u32 s13, s13, 0
	global_load_dwordx4 v[60:63], v10, s[12:13]
	s_add_u32 s12, s12, 0x8000
	s_addc_u32 s13, s13, 0
	global_load_dwordx4 v[64:67], v10, s[12:13]
	s_add_i32 s17, s16, 2304
	s_min_u32 s17, s17, 0xbff
	s_lshr_b32 s18, s17, 5
	s_add_i32 s18, s18, 32
	s_and_b32 s19, s17, 31
	s_lshl_b32 s19, s19, 21
	s_lshl_b32 s18, s18, 7
	s_add_u32 s18, s18, s19
	s_add_u32 s14, s4, s18
	s_addc_u32 s15, s5, 0
	ds_read_b32 v132, v6
	ds_read_b32 v133, v6 offset:512
	ds_read_b32 v134, v6 offset:1024
	ds_read_b32 v135, v6 offset:1536
	ds_read_b32 v136, v6 offset:2048
	ds_read_b32 v137, v6 offset:2560
	ds_read_b32 v138, v6 offset:3072
	ds_read_b32 v139, v6 offset:3584
	ds_read_b32 v140, v6 offset:4096
	ds_read_b32 v141, v6 offset:4608
	ds_read_b32 v142, v6 offset:5120
	ds_read_b32 v143, v6 offset:5632
	ds_read_b32 v144, v6 offset:6144
	ds_read_b32 v145, v6 offset:6656
	ds_read_b32 v146, v6 offset:7168
	ds_read_b32 v147, v6 offset:7680
	s_waitcnt lgkmcnt(0)
	v_max_f32_e32 v132, v132, v132
	v_max_f32_e32 v133, v133, v133
	v_max_f32_e32 v134, v134, v134
	v_max_f32_e32 v135, v135, v135
	v_max_f32_e32 v136, v136, v136
	v_max_f32_e32 v137, v137, v137
	v_max_f32_e32 v138, v138, v138
	v_max_f32_e32 v139, v139, v139
	v_max_f32_e32 v140, v140, v140
	v_max_f32_e32 v141, v141, v141
	v_max_f32_e32 v142, v142, v142
	v_max_f32_e32 v143, v143, v143
	v_max_f32_e32 v144, v144, v144
	v_max_f32_e32 v145, v145, v145
	v_max_f32_e32 v146, v146, v146
	v_max_f32_e32 v147, v147, v147
	v_med3_f32 v132, v132, s20, v13
	v_med3_f32 v133, v133, s20, v13
	v_med3_f32 v134, v134, s20, v13
	v_med3_f32 v135, v135, s20, v13
	v_med3_f32 v136, v136, s20, v13
	v_med3_f32 v137, v137, s20, v13
	v_med3_f32 v138, v138, s20, v13
	v_med3_f32 v139, v139, s20, v13
	v_med3_f32 v140, v140, s20, v13
	v_med3_f32 v141, v141, s20, v13
	v_med3_f32 v142, v142, s20, v13
	v_med3_f32 v143, v143, s20, v13
	v_med3_f32 v144, v144, s20, v13
	v_med3_f32 v145, v145, s20, v13
	v_med3_f32 v146, v146, s20, v13
	v_med3_f32 v147, v147, s20, v13
	v_mov_b32_e32 v148, 0
	v_mov_b32_e32 v149, 0
	v_mov_b32_e32 v150, 0
	v_mov_b32_e32 v151, 0
	v_cvt_pk_fp8_f32 v148, v132, v133
	v_cvt_pk_fp8_f32 v149, v136, v137
	v_cvt_pk_fp8_f32 v150, v140, v141
	v_cvt_pk_fp8_f32 v151, v144, v145
	v_cvt_pk_fp8_f32 v148, v134, v135 op_sel:[0,0,1]
	v_cvt_pk_fp8_f32 v149, v138, v139 op_sel:[0,0,1]
	v_cvt_pk_fp8_f32 v150, v142, v143 op_sel:[0,0,1]
	v_cvt_pk_fp8_f32 v151, v146, v147 op_sel:[0,0,1]
	s_nop 0
	global_store_dwordx4 v11, v[148:151], s[14:15]
	ds_read_b32 v132, v8
	ds_read_b32 v133, v8 offset:512
	ds_read_b32 v134, v8 offset:1024
	ds_read_b32 v135, v8 offset:1536
	ds_read_b32 v136, v8 offset:2048
	ds_read_b32 v137, v8 offset:2560
	ds_read_b32 v138, v8 offset:3072
	ds_read_b32 v139, v8 offset:3584
	ds_read_b32 v140, v8 offset:4096
	ds_read_b32 v141, v8 offset:4608
	ds_read_b32 v142, v8 offset:5120
	ds_read_b32 v143, v8 offset:5632
	ds_read_b32 v144, v8 offset:6144
	ds_read_b32 v145, v8 offset:6656
	ds_read_b32 v146, v8 offset:7168
	ds_read_b32 v147, v8 offset:7680
	s_waitcnt lgkmcnt(0)
	v_max_f32_e32 v132, v132, v132
	v_max_f32_e32 v133, v133, v133
	v_max_f32_e32 v134, v134, v134
	v_max_f32_e32 v135, v135, v135
	v_max_f32_e32 v136, v136, v136
	v_max_f32_e32 v137, v137, v137
	v_max_f32_e32 v138, v138, v138
	v_max_f32_e32 v139, v139, v139
	v_max_f32_e32 v140, v140, v140
	v_max_f32_e32 v141, v141, v141
	v_max_f32_e32 v142, v142, v142
	v_max_f32_e32 v143, v143, v143
	v_max_f32_e32 v144, v144, v144
	v_max_f32_e32 v145, v145, v145
	v_max_f32_e32 v146, v146, v146
	v_max_f32_e32 v147, v147, v147
	v_med3_f32 v132, v132, s20, v13
	v_med3_f32 v133, v133, s20, v13
	v_med3_f32 v134, v134, s20, v13
	v_med3_f32 v135, v135, s20, v13
	v_med3_f32 v136, v136, s20, v13
	v_med3_f32 v137, v137, s20, v13
	v_med3_f32 v138, v138, s20, v13
	v_med3_f32 v139, v139, s20, v13
	v_med3_f32 v140, v140, s20, v13
	v_med3_f32 v141, v141, s20, v13
	v_med3_f32 v142, v142, s20, v13
	v_med3_f32 v143, v143, s20, v13
	v_med3_f32 v144, v144, s20, v13
	v_med3_f32 v145, v145, s20, v13
	v_med3_f32 v146, v146, s20, v13
	v_med3_f32 v147, v147, s20, v13
	v_mov_b32_e32 v148, 0
	v_mov_b32_e32 v149, 0
	v_mov_b32_e32 v150, 0
	v_mov_b32_e32 v151, 0
	v_cvt_pk_fp8_f32 v148, v132, v133
	v_cvt_pk_fp8_f32 v149, v136, v137
	v_cvt_pk_fp8_f32 v150, v140, v141
	v_cvt_pk_fp8_f32 v151, v144, v145
	v_cvt_pk_fp8_f32 v148, v134, v135 op_sel:[0,0,1]
	v_cvt_pk_fp8_f32 v149, v138, v139 op_sel:[0,0,1]
	v_cvt_pk_fp8_f32 v150, v142, v143 op_sel:[0,0,1]
	v_cvt_pk_fp8_f32 v151, v146, v147 op_sel:[0,0,1]
	s_nop 0
	global_store_dwordx4 v12, v[148:151], s[14:15]
	s_waitcnt vmcnt(22)
	v_mul_f32_e32 v68, 0x43000000, v68
	v_mul_f32_e32 v69, 0x43000000, v69
	v_mul_f32_e32 v70, 0x43000000, v70
	v_mul_f32_e32 v71, 0x43000000, v71
	ds_write_b128 v5, v[68:71]
	v_mul_f32_e32 v72, 0x43000000, v72
	v_mul_f32_e32 v73, 0x43000000, v73
	v_mul_f32_e32 v74, 0x43000000, v74
	v_mul_f32_e32 v75, 0x43000000, v75
	ds_write_b128 v5, v[72:75] offset:1024
	v_mul_f32_e32 v76, 0x43000000, v76
	v_mul_f32_e32 v77, 0x43000000, v77
	v_mul_f32_e32 v78, 0x43000000, v78
	v_mul_f32_e32 v79, 0x43000000, v79
	ds_write_b128 v5, v[76:79] offset:2048
	v_mul_f32_e32 v80, 0x43000000, v80
	v_mul_f32_e32 v81, 0x43000000, v81
	v_mul_f32_e32 v82, 0x43000000, v82
	v_mul_f32_e32 v83, 0x43000000, v83
	ds_write_b128 v5, v[80:83] offset:3072
	v_mul_f32_e32 v84, 0x43000000, v84
	v_mul_f32_e32 v85, 0x43000000, v85
	v_mul_f32_e32 v86, 0x43000000, v86
	v_mul_f32_e32 v87, 0x43000000, v87
	ds_write_b128 v5, v[84:87] offset:4096
	v_mul_f32_e32 v88, 0x43000000, v88
	v_mul_f32_e32 v89, 0x43000000, v89
	v_mul_f32_e32 v90, 0x43000000, v90
	v_mul_f32_e32 v91, 0x43000000, v91
	ds_write_b128 v5, v[88:91] offset:5120
	v_mul_f32_e32 v92, 0x43000000, v92
	v_mul_f32_e32 v93, 0x43000000, v93
	v_mul_f32_e32 v94, 0x43000000, v94
	v_mul_f32_e32 v95, 0x43000000, v95
	ds_write_b128 v5, v[92:95] offset:6144
	v_mul_f32_e32 v96, 0x43000000, v96
	v_mul_f32_e32 v97, 0x43000000, v97
	v_mul_f32_e32 v98, 0x43000000, v98
	v_mul_f32_e32 v99, 0x43000000, v99
	ds_write_b128 v5, v[96:99] offset:7168
	s_waitcnt lgkmcnt(0)
	s_barrier
; #define GAS __attribute__((address_space(1)))
; #define LAS __attribute__((address_space(3)))
; #define LDS_WAIT() asm volatile("s_waitcnt lgkmcnt(0)" ::: "memory")
; __device__ __forceinline__ unsigned pk4_fp8(float a, float b, float c, float d) {
;     a = fminf(fmaxf(a, -448.f), 448.f); b = fminf(fmaxf(b, -448.f), 448.f); c = fminf(fmaxf(c, -448.f), 448.f); d = fminf(fmaxf(d, -448.f), 448.f);
;     int w = __builtin_amdgcn_cvt_pk_fp8_f32(a, b, 0, false); w = __builtin_amdgcn_cvt_pk_fp8_f32(c, d, w, true); return (unsigned)w; }
;     const int pr = item >> 1, kb = 2 * (pr / nblk) + (item & 1), nb = pr % nblk, k0 = 64 * kb, n0 = 32 * nb;
;     const int nr = n0 + (lane & 31); const int sc = MAP == 1 ? src_col_in(nr) : nr;
;     float v[32];
; #pragma unroll
;     for (int i = 0; i < 32; ++i) v[i] = sc >= 0 ? W[(size_t)(k0 + 2 * i + (lane >> 5)) * Nsrc + sc] : 0.f;
; #pragma unroll
;     for (int i = 0; i < 32; ++i) { const int k = k0 + 2 * i + (lane >> 5); float x = v[i] * wscale; if (KS) x *= (k < ksplit ? ksA[k] : ksB[k - ksplit]); scr[(2 * i + (lane >> 5)) * 33 + (lane & 31)] = x; }
;     LDS_WAIT(); asm volatile("" ::: "memory");
;     const int c = lane & 7;
; #pragma unroll
;     for (int j = 0; j < 4; ++j) { const int n = (lane >> 3) + 8 * j; const LAS float* s = scr + (8 * c) * 33 + n;
;         const unsigned long long o = (unsigned long long)pg8::pk4_fp8(s[0 * 33], s[1 * 33], s[2 * 33], s[3 * 33]) | ((unsigned long long)pg8::pk4_fp8(s[4 * 33], s[5 * 33], s[6 * 33], s[7 * 33]) << 32);
;         *(GAS unsigned long long*)(WT + (size_t)(n0 + n) * K + k0 + 8 * c) = o; }
;     LDS_WAIT(); asm volatile("" ::: "memory");
	s_add_i32 s17, s16, 2688
	s_min_u32 s17, s17, 0xbff
	s_lshr_b32 s18, s17, 5
	s_add_i32 s18, s18, 32
	s_and_b32 s19, s17, 31
	s_lshl_b32 s18, s18, 21
	s_lshl_b32 s19, s19, 9
	s_add_u32 s18, s18, s19
	s_add_u32 s12, s2, s18
	s_addc_u32 s13, s3, 0
	global_load_dwordx4 v[68:71], v10, s[12:13]
	s_add_u32 s12, s12, 0x8000
	s_addc_u32 s13, s13, 0
	global_load_dwordx4 v[72:75], v10, s[12:13]
	s_add_u32 s12, s12, 0x8000
	s_addc_u32 s13, s13, 0
	global_load_dwordx4 v[76:79], v10, s[12:13]
	s_add_u32 s12, s12, 0x8000
	s_addc_u32 s13, s13, 0
	global_load_dwordx4 v[80:83], v10, s[12:13]
	s_add_u32 s12, s12, 0x8000
	s_addc_u32 s13, s13, 0
	global_load_dwordx4 v[84:87], v10, s[12:13]
	s_add_u32 s12, s12, 0x8000
	s_addc_u32 s13, s13, 0
	global_load_dwordx4 v[88:91], v10, s[12:13]
	s_add_u32 s12, s12, 0x8000
	s_addc_u32 s13, s13, 0
	global_load_dwordx4 v[92:95], v10, s[12:13]
	s_add_u32 s12, s12, 0x8000
	s_addc_u32 s13, s13, 0
	global_load_dwordx4 v[96:99], v10, s[12:13]
	s_add_i32 s17, s16, 2400
	s_min_u32 s17, s17, 0xbff
	s_lshr_b32 s18, s17, 5
	s_add_i32 s18, s18, 32
	s_and_b32 s19, s17, 31
	s_lshl_b32 s19, s19, 21
	s_lshl_b32 s18, s18, 7
	s_add_u32 s18, s18, s19
	s_add_u32 s14, s4, s18
	s_addc_u32 s15, s5, 0
	ds_read_b32 v132, v7
	ds_read_b32 v133, v7 offset:512
	ds_read_b32 v134, v7 offset:1024
	ds_read_b32 v135, v7 offset:1536
	ds_read_b32 v136, v7 offset:2048
	ds_read_b32 v137, v7 offset:2560
	ds_read_b32 v138, v7 offset:3072
	ds_read_b32 v139, v7 offset:3584
	ds_read_b32 v140, v7 offset:4096
	ds_read_b32 v141, v7 offset:4608
	ds_read_b32 v142, v7 offset:5120
	ds_read_b32 v143, v7 offset:5632
	ds_read_b32 v144, v7 offset:6144
	ds_read_b32 v145, v7 offset:6656
	ds_read_b32 v146, v7 offset:7168
	ds_read_b32 v147, v7 offset:7680
	s_waitcnt lgkmcnt(0)
	v_max_f32_e32 v132, v132, v132
	v_max_f32_e32 v133, v133, v133
	v_max_f32_e32 v134, v134, v134
	v_max_f32_e32 v135, v135, v135
	v_max_f32_e32 v136, v136, v136
	v_max_f32_e32 v137, v137, v137
	v_max_f32_e32 v138, v138, v138
	v_max_f32_e32 v139, v139, v139
	v_max_f32_e32 v140, v140, v140
	v_max_f32_e32 v141, v141, v141
	v_max_f32_e32 v142, v142, v142
	v_max_f32_e32 v143, v143, v143
	v_max_f32_e32 v144, v144, v144
	v_max_f32_e32 v145, v145, v145
	v_max_f32_e32 v146, v146, v146
	v_max_f32_e32 v147, v147, v147
	v_med3_f32 v132, v132, s20, v13
	v_med3_f32 v133, v133, s20, v13
	v_med3_f32 v134, v134, s20, v13
	v_med3_f32 v135, v135, s20, v13
	v_med3_f32 v136, v136, s20, v13
	v_med3_f32 v137, v137, s20, v13
	v_med3_f32 v138, v138, s20, v13
	v_med3_f32 v139, v139, s20, v13
	v_med3_f32 v140, v140, s20, v13
	v_med3_f32 v141, v141, s20, v13
	v_med3_f32 v142, v142, s20, v13
	v_med3_f32 v143, v143, s20, v13
	v_med3_f32 v144, v144, s20, v13
	v_med3_f32 v145, v145, s20, v13
	v_med3_f32 v146, v146, s20, v13
	v_med3_f32 v147, v147, s20, v13
	v_mov_b32_e32 v148, 0
	v_mov_b32_e32 v149, 0
	v_mov_b32_e32 v150, 0
	v_mov_b32_e32 v151, 0
	v_cvt_pk_fp8_f32 v148, v132, v133
	v_cvt_pk_fp8_f32 v149, v136, v137
	v_cvt_pk_fp8_f32 v150, v140, v141
	v_cvt_pk_fp8_f32 v151, v144, v145
	v_cvt_pk_fp8_f32 v148, v134, v135 op_sel:[0,0,1]
	v_cvt_pk_fp8_f32 v149, v138, v139 op_sel:[0,0,1]
	v_cvt_pk_fp8_f32 v150, v142, v143 op_sel:[0,0,1]
	v_cvt_pk_fp8_f32 v151, v146, v147 op_sel:[0,0,1]
	s_nop 0
	global_store_dwordx4 v11, v[148:151], s[14:15]
	ds_read_b32 v132, v9
	ds_read_b32 v133, v9 offset:512
	ds_read_b32 v134, v9 offset:1024
	ds_read_b32 v135, v9 offset:1536
	ds_read_b32 v136, v9 offset:2048
	ds_read_b32 v137, v9 offset:2560
	ds_read_b32 v138, v9 offset:3072
	ds_read_b32 v139, v9 offset:3584
	ds_read_b32 v140, v9 offset:4096
	ds_read_b32 v141, v9 offset:4608
	ds_read_b32 v142, v9 offset:5120
	ds_read_b32 v143, v9 offset:5632
	ds_read_b32 v144, v9 offset:6144
	ds_read_b32 v145, v9 offset:6656
	ds_read_b32 v146, v9 offset:7168
	ds_read_b32 v147, v9 offset:7680
	s_waitcnt lgkmcnt(0)
	v_max_f32_e32 v132, v132, v132
	v_max_f32_e32 v133, v133, v133
	v_max_f32_e32 v134, v134, v134
	v_max_f32_e32 v135, v135, v135
	v_max_f32_e32 v136, v136, v136
	v_max_f32_e32 v137, v137, v137
	v_max_f32_e32 v138, v138, v138
	v_max_f32_e32 v139, v139, v139
	v_max_f32_e32 v140, v140, v140
	v_max_f32_e32 v141, v141, v141
	v_max_f32_e32 v142, v142, v142
	v_max_f32_e32 v143, v143, v143
	v_max_f32_e32 v144, v144, v144
	v_max_f32_e32 v145, v145, v145
	v_max_f32_e32 v146, v146, v146
	v_max_f32_e32 v147, v147, v147
	v_med3_f32 v132, v132, s20, v13
	v_med3_f32 v133, v133, s20, v13
	v_med3_f32 v134, v134, s20, v13
	v_med3_f32 v135, v135, s20, v13
	v_med3_f32 v136, v136, s20, v13
	v_med3_f32 v137, v137, s20, v13
	v_med3_f32 v138, v138, s20, v13
	v_med3_f32 v139, v139, s20, v13
	v_med3_f32 v140, v140, s20, v13
	v_med3_f32 v141, v141, s20, v13
	v_med3_f32 v142, v142, s20, v13
	v_med3_f32 v143, v143, s20, v13
	v_med3_f32 v144, v144, s20, v13
	v_med3_f32 v145, v145, s20, v13
	v_med3_f32 v146, v146, s20, v13
	v_med3_f32 v147, v147, s20, v13
	v_mov_b32_e32 v148, 0
	v_mov_b32_e32 v149, 0
	v_mov_b32_e32 v150, 0
	v_mov_b32_e32 v151, 0
	v_cvt_pk_fp8_f32 v148, v132, v133
	v_cvt_pk_fp8_f32 v149, v136, v137
	v_cvt_pk_fp8_f32 v150, v140, v141
	v_cvt_pk_fp8_f32 v151, v144, v145
	v_cvt_pk_fp8_f32 v148, v134, v135 op_sel:[0,0,1]
	v_cvt_pk_fp8_f32 v149, v138, v139 op_sel:[0,0,1]
	v_cvt_pk_fp8_f32 v150, v142, v143 op_sel:[0,0,1]
	v_cvt_pk_fp8_f32 v151, v146, v147 op_sel:[0,0,1]
	s_nop 0
	global_store_dwordx4 v12, v[148:151], s[14:15]
	s_waitcnt vmcnt(22)
	v_mul_f32_e32 v100, 0x43000000, v100
	v_mul_f32_e32 v101, 0x43000000, v101
	v_mul_f32_e32 v102, 0x43000000, v102
	v_mul_f32_e32 v103, 0x43000000, v103
	ds_write_b128 v4, v[100:103]
	v_mul_f32_e32 v104, 0x43000000, v104
	v_mul_f32_e32 v105, 0x43000000, v105
	v_mul_f32_e32 v106, 0x43000000, v106
	v_mul_f32_e32 v107, 0x43000000, v107
	ds_write_b128 v4, v[104:107] offset:1024
	v_mul_f32_e32 v108, 0x43000000, v108
	v_mul_f32_e32 v109, 0x43000000, v109
	v_mul_f32_e32 v110, 0x43000000, v110
	v_mul_f32_e32 v111, 0x43000000, v111
	ds_write_b128 v4, v[108:111] offset:2048
	v_mul_f32_e32 v112, 0x43000000, v112
	v_mul_f32_e32 v113, 0x43000000, v113
	v_mul_f32_e32 v114, 0x43000000, v114
	v_mul_f32_e32 v115, 0x43000000, v115
	ds_write_b128 v4, v[112:115] offset:3072
	v_mul_f32_e32 v116, 0x43000000, v116
	v_mul_f32_e32 v117, 0x43000000, v117
	v_mul_f32_e32 v118, 0x43000000, v118
	v_mul_f32_e32 v119, 0x43000000, v119
	ds_write_b128 v4, v[116:119] offset:4096
	v_mul_f32_e32 v120, 0x43000000, v120
	v_mul_f32_e32 v121, 0x43000000, v121
	v_mul_f32_e32 v122, 0x43000000, v122
	v_mul_f32_e32 v123, 0x43000000, v123
	ds_write_b128 v4, v[120:123] offset:5120
	v_mul_f32_e32 v124, 0x43000000, v124
	v_mul_f32_e32 v125, 0x43000000, v125
	v_mul_f32_e32 v126, 0x43000000, v126
	v_mul_f32_e32 v127, 0x43000000, v127
	ds_write_b128 v4, v[124:127] offset:6144
	v_mul_f32_e32 v128, 0x43000000, v128
	v_mul_f32_e32 v129, 0x43000000, v129
	v_mul_f32_e32 v130, 0x43000000, v130
	v_mul_f32_e32 v131, 0x43000000, v131
	ds_write_b128 v4, v[128:131] offset:7168
	s_waitcnt lgkmcnt(0)
	s_barrier
; #define GAS __attribute__((address_space(1)))
; #define LAS __attribute__((address_space(3)))
; #define LDS_WAIT() asm volatile("s_waitcnt lgkmcnt(0)" ::: "memory")
; __device__ __forceinline__ unsigned pk4_fp8(float a, float b, float c, float d) {
;     a = fminf(fmaxf(a, -448.f), 448.f); b = fminf(fmaxf(b, -448.f), 448.f); c = fminf(fmaxf(c, -448.f), 448.f); d = fminf(fmaxf(d, -448.f), 448.f);
;     int w = __builtin_amdgcn_cvt_pk_fp8_f32(a, b, 0, false); w = __builtin_amdgcn_cvt_pk_fp8_f32(c, d, w, true); return (unsigned)w; }
;     const int pr = item >> 1, kb = 2 * (pr / nblk) + (item & 1), nb = pr % nblk, k0 = 64 * kb, n0 = 32 * nb;
;     const int nr = n0 + (lane & 31); const int sc = MAP == 1 ? src_col_in(nr) : nr;
;     float v[32];
; #pragma unroll
;     for (int i = 0; i < 32; ++i) v[i] = sc >= 0 ? W[(size_t)(k0 + 2 * i + (lane >> 5)) * Nsrc + sc] : 0.f;
; #pragma unroll
;     for (int i = 0; i < 32; ++i) { const int k = k0 + 2 * i + (lane >> 5); float x = v[i] * wscale; if (KS) x *= (k < ksplit ? ksA[k] : ksB[k - ksplit]); scr[(2 * i + (lane >> 5)) * 33 + (lane & 31)] = x; }
;     LDS_WAIT(); asm volatile("" ::: "memory");
;     const int c = lane & 7;
; #pragma unroll
;     for (int j = 0; j < 4; ++j) { const int n = (lane >> 3) + 8 * j; const LAS float* s = scr + (8 * c) * 33 + n;
;         const unsigned long long o = (unsigned long long)pg8::pk4_fp8(s[0 * 33], s[1 * 33], s[2 * 33], s[3 * 33]) | ((unsigned long long)pg8::pk4_fp8(s[4 * 33], s[5 * 33], s[6 * 33], s[7 * 33]) << 32);
;         *(GAS unsigned long long*)(WT + (size_t)(n0 + n) * K + k0 + 8 * c) = o; }
;     LDS_WAIT(); asm volatile("" ::: "memory");
	s_add_i32 s17, s16, 2784
	s_min_u32 s17, s17, 0xbff
	s_lshr_b32 s18, s17, 5
	s_add_i32 s18, s18, 32
	s_and_b32 s19, s17, 31
	s_lshl_b32 s18, s18, 21
	s_lshl_b32 s19, s19, 9
	s_add_u32 s18, s18, s19
	s_add_u32 s12, s2, s18
	s_addc_u32 s13, s3, 0
	global_load_dwordx4 v[100:103], v10, s[12:13]
	s_add_u32 s12, s12, 0x8000
	s_addc_u32 s13, s13, 0
	global_load_dwordx4 v[104:107], v10, s[12:13]
	s_add_u32 s12, s12, 0x8000
	s_addc_u32 s13, s13, 0
	global_load_dwordx4 v[108:111], v10, s[12:13]
	s_add_u32 s12, s12, 0x8000
	s_addc_u32 s13, s13, 0
	global_load_dwordx4 v[112:115], v10, s[12:13]
	s_add_u32 s12, s12, 0x8000
	s_addc_u32 s13, s13, 0
	global_load_dwordx4 v[116:119], v10, s[12:13]
	s_add_u32 s12, s12, 0x8000
	s_addc_u32 s13, s13, 0
	global_load_dwordx4 v[120:123], v10, s[12:13]
	s_add_u32 s12, s12, 0x8000
	s_addc_u32 s13, s13, 0
	global_load_dwordx4 v[124:127], v10, s[12:13]
	s_add_u32 s12, s12, 0x8000
	s_addc_u32 s13, s13, 0
	global_load_dwordx4 v[128:131], v10, s[12:13]
	s_add_i32 s17, s16, 2496
	s_min_u32 s17, s17, 0xbff
	s_lshr_b32 s18, s17, 5
	s_add_i32 s18, s18, 32
	s_and_b32 s19, s17, 31
	s_lshl_b32 s19, s19, 21
	s_lshl_b32 s18, s18, 7
	s_add_u32 s18, s18, s19
	s_add_u32 s14, s4, s18
	s_addc_u32 s15, s5, 0
	ds_read_b32 v132, v6
	ds_read_b32 v133, v6 offset:512
	ds_read_b32 v134, v6 offset:1024
	ds_read_b32 v135, v6 offset:1536
	ds_read_b32 v136, v6 offset:2048
	ds_read_b32 v137, v6 offset:2560
	ds_read_b32 v138, v6 offset:3072
	ds_read_b32 v139, v6 offset:3584
	ds_read_b32 v140, v6 offset:4096
	ds_read_b32 v141, v6 offset:4608
	ds_read_b32 v142, v6 offset:5120
	ds_read_b32 v143, v6 offset:5632
	ds_read_b32 v144, v6 offset:6144
	ds_read_b32 v145, v6 offset:6656
	ds_read_b32 v146, v6 offset:7168
	ds_read_b32 v147, v6 offset:7680
	s_waitcnt lgkmcnt(0)
	v_max_f32_e32 v132, v132, v132
	v_max_f32_e32 v133, v133, v133
	v_max_f32_e32 v134, v134, v134
	v_max_f32_e32 v135, v135, v135
	v_max_f32_e32 v136, v136, v136
	v_max_f32_e32 v137, v137, v137
	v_max_f32_e32 v138, v138, v138
	v_max_f32_e32 v139, v139, v139
	v_max_f32_e32 v140, v140, v140
	v_max_f32_e32 v141, v141, v141
	v_max_f32_e32 v142, v142, v142
	v_max_f32_e32 v143, v143, v143
	v_max_f32_e32 v144, v144, v144
	v_max_f32_e32 v145, v145, v145
	v_max_f32_e32 v146, v146, v146
	v_max_f32_e32 v147, v147, v147
	v_med3_f32 v132, v132, s20, v13
	v_med3_f32 v133, v133, s20, v13
	v_med3_f32 v134, v134, s20, v13
	v_med3_f32 v135, v135, s20, v13
	v_med3_f32 v136, v136, s20, v13
	v_med3_f32 v137, v137, s20, v13
	v_med3_f32 v138, v138, s20, v13
	v_med3_f32 v139, v139, s20, v13
	v_med3_f32 v140, v140, s20, v13
	v_med3_f32 v141, v141, s20, v13
	v_med3_f32 v142, v142, s20, v13
	v_med3_f32 v143, v143, s20, v13
	v_med3_f32 v144, v144, s20, v13
	v_med3_f32 v145, v145, s20, v13
	v_med3_f32 v146, v146, s20, v13
	v_med3_f32 v147, v147, s20, v13
	v_mov_b32_e32 v148, 0
	v_mov_b32_e32 v149, 0
	v_mov_b32_e32 v150, 0
	v_mov_b32_e32 v151, 0
	v_cvt_pk_fp8_f32 v148, v132, v133
	v_cvt_pk_fp8_f32 v149, v136, v137
	v_cvt_pk_fp8_f32 v150, v140, v141
	v_cvt_pk_fp8_f32 v151, v144, v145
	v_cvt_pk_fp8_f32 v148, v134, v135 op_sel:[0,0,1]
	v_cvt_pk_fp8_f32 v149, v138, v139 op_sel:[0,0,1]
	v_cvt_pk_fp8_f32 v150, v142, v143 op_sel:[0,0,1]
	v_cvt_pk_fp8_f32 v151, v146, v147 op_sel:[0,0,1]
	s_nop 0
	global_store_dwordx4 v11, v[148:151], s[14:15]
	ds_read_b32 v132, v8
	ds_read_b32 v133, v8 offset:512
	ds_read_b32 v134, v8 offset:1024
	ds_read_b32 v135, v8 offset:1536
	ds_read_b32 v136, v8 offset:2048
	ds_read_b32 v137, v8 offset:2560
	ds_read_b32 v138, v8 offset:3072
	ds_read_b32 v139, v8 offset:3584
	ds_read_b32 v140, v8 offset:4096
	ds_read_b32 v141, v8 offset:4608
	ds_read_b32 v142, v8 offset:5120
	ds_read_b32 v143, v8 offset:5632
	ds_read_b32 v144, v8 offset:6144
	ds_read_b32 v145, v8 offset:6656
	ds_read_b32 v146, v8 offset:7168
	ds_read_b32 v147, v8 offset:7680
	s_waitcnt lgkmcnt(0)
	v_max_f32_e32 v132, v132, v132
	v_max_f32_e32 v133, v133, v133
	v_max_f32_e32 v134, v134, v134
	v_max_f32_e32 v135, v135, v135
	v_max_f32_e32 v136, v136, v136
	v_max_f32_e32 v137, v137, v137
	v_max_f32_e32 v138, v138, v138
	v_max_f32_e32 v139, v139, v139
	v_max_f32_e32 v140, v140, v140
	v_max_f32_e32 v141, v141, v141
	v_max_f32_e32 v142, v142, v142
	v_max_f32_e32 v143, v143, v143
	v_max_f32_e32 v144, v144, v144
	v_max_f32_e32 v145, v145, v145
	v_max_f32_e32 v146, v146, v146
	v_max_f32_e32 v147, v147, v147
	v_med3_f32 v132, v132, s20, v13
	v_med3_f32 v133, v133, s20, v13
	v_med3_f32 v134, v134, s20, v13
	v_med3_f32 v135, v135, s20, v13
	v_med3_f32 v136, v136, s20, v13
	v_med3_f32 v137, v137, s20, v13
	v_med3_f32 v138, v138, s20, v13
	v_med3_f32 v139, v139, s20, v13
	v_med3_f32 v140, v140, s20, v13
	v_med3_f32 v141, v141, s20, v13
	v_med3_f32 v142, v142, s20, v13
	v_med3_f32 v143, v143, s20, v13
	v_med3_f32 v144, v144, s20, v13
	v_med3_f32 v145, v145, s20, v13
	v_med3_f32 v146, v146, s20, v13
	v_med3_f32 v147, v147, s20, v13
	v_mov_b32_e32 v148, 0
	v_mov_b32_e32 v149, 0
	v_mov_b32_e32 v150, 0
	v_mov_b32_e32 v151, 0
	v_cvt_pk_fp8_f32 v148, v132, v133
	v_cvt_pk_fp8_f32 v149, v136, v137
	v_cvt_pk_fp8_f32 v150, v140, v141
	v_cvt_pk_fp8_f32 v151, v144, v145
	v_cvt_pk_fp8_f32 v148, v134, v135 op_sel:[0,0,1]
	v_cvt_pk_fp8_f32 v149, v138, v139 op_sel:[0,0,1]
	v_cvt_pk_fp8_f32 v150, v142, v143 op_sel:[0,0,1]
	v_cvt_pk_fp8_f32 v151, v146, v147 op_sel:[0,0,1]
	s_nop 0
	global_store_dwordx4 v12, v[148:151], s[14:15]
	s_waitcnt vmcnt(22)
	v_mul_f32_e32 v36, 0x43000000, v36
	v_mul_f32_e32 v37, 0x43000000, v37
	v_mul_f32_e32 v38, 0x43000000, v38
	v_mul_f32_e32 v39, 0x43000000, v39
	ds_write_b128 v5, v[36:39]
	v_mul_f32_e32 v40, 0x43000000, v40
	v_mul_f32_e32 v41, 0x43000000, v41
	v_mul_f32_e32 v42, 0x43000000, v42
	v_mul_f32_e32 v43, 0x43000000, v43
	ds_write_b128 v5, v[40:43] offset:1024
	v_mul_f32_e32 v44, 0x43000000, v44
	v_mul_f32_e32 v45, 0x43000000, v45
	v_mul_f32_e32 v46, 0x43000000, v46
	v_mul_f32_e32 v47, 0x43000000, v47
	ds_write_b128 v5, v[44:47] offset:2048
	v_mul_f32_e32 v48, 0x43000000, v48
	v_mul_f32_e32 v49, 0x43000000, v49
	v_mul_f32_e32 v50, 0x43000000, v50
	v_mul_f32_e32 v51, 0x43000000, v51
	ds_write_b128 v5, v[48:51] offset:3072
	v_mul_f32_e32 v52, 0x43000000, v52
	v_mul_f32_e32 v53, 0x43000000, v53
	v_mul_f32_e32 v54, 0x43000000, v54
	v_mul_f32_e32 v55, 0x43000000, v55
	ds_write_b128 v5, v[52:55] offset:4096
	v_mul_f32_e32 v56, 0x43000000, v56
	v_mul_f32_e32 v57, 0x43000000, v57
	v_mul_f32_e32 v58, 0x43000000, v58
	v_mul_f32_e32 v59, 0x43000000, v59
	ds_write_b128 v5, v[56:59] offset:5120
	v_mul_f32_e32 v60, 0x43000000, v60
	v_mul_f32_e32 v61, 0x43000000, v61
	v_mul_f32_e32 v62, 0x43000000, v62
	v_mul_f32_e32 v63, 0x43000000, v63
	ds_write_b128 v5, v[60:63] offset:6144
	v_mul_f32_e32 v64, 0x43000000, v64
	v_mul_f32_e32 v65, 0x43000000, v65
	v_mul_f32_e32 v66, 0x43000000, v66
	v_mul_f32_e32 v67, 0x43000000, v67
	ds_write_b128 v5, v[64:67] offset:7168
	s_waitcnt lgkmcnt(0)
	s_barrier
; #define GAS __attribute__((address_space(1)))
; #define LAS __attribute__((address_space(3)))
; #define LDS_WAIT() asm volatile("s_waitcnt lgkmcnt(0)" ::: "memory")
; __device__ __forceinline__ unsigned pk4_fp8(float a, float b, float c, float d) {
;     a = fminf(fmaxf(a, -448.f), 448.f); b = fminf(fmaxf(b, -448.f), 448.f); c = fminf(fmaxf(c, -448.f), 448.f); d = fminf(fmaxf(d, -448.f), 448.f);
;     int w = __builtin_amdgcn_cvt_pk_fp8_f32(a, b, 0, false); w = __builtin_amdgcn_cvt_pk_fp8_f32(c, d, w, true); return (unsigned)w; }
;     const int pr = item >> 1, kb = 2 * (pr / nblk) + (item & 1), nb = pr % nblk, k0 = 64 * kb, n0 = 32 * nb;
;     const int nr = n0 + (lane & 31); const int sc = MAP == 1 ? src_col_in(nr) : nr;
;     float v[32];
; #pragma unroll
;     for (int i = 0; i < 32; ++i) v[i] = sc >= 0 ? W[(size_t)(k0 + 2 * i + (lane >> 5)) * Nsrc + sc] : 0.f;
; #pragma unroll
;     for (int i = 0; i < 32; ++i) { const int k = k0 + 2 * i + (lane >> 5); float x = v[i] * wscale; if (KS) x *= (k < ksplit ? ksA[k] : ksB[k - ksplit]); scr[(2 * i + (lane >> 5)) * 33 + (lane & 31)] = x; }
;     LDS_WAIT(); asm volatile("" ::: "memory");
;     const int c = lane & 7;
; #pragma unroll
;     for (int j = 0; j < 4; ++j) { const int n = (lane >> 3) + 8 * j; const LAS float* s = scr + (8 * c) * 33 + n;
;         const unsigned long long o = (unsigned long long)pg8::pk4_fp8(s[0 * 33], s[1 * 33], s[2 * 33], s[3 * 33]) | ((unsigned long long)pg8::pk4_fp8(s[4 * 33], s[5 * 33], s[6 * 33], s[7 * 33]) << 32);
;         *(GAS unsigned long long*)(WT + (size_t)(n0 + n) * K + k0 + 8 * c) = o; }
;     LDS_WAIT(); asm volatile("" ::: "memory");
	s_add_i32 s17, s16, 2880
	s_min_u32 s17, s17, 0xbff
	s_lshr_b32 s18, s17, 5
	s_add_i32 s18, s18, 32
	s_and_b32 s19, s17, 31
	s_lshl_b32 s18, s18, 21
	s_lshl_b32 s19, s19, 9
	s_add_u32 s18, s18, s19
	s_add_u32 s12, s2, s18
	s_addc_u32 s13, s3, 0
	global_load_dwordx4 v[36:39], v10, s[12:13]
	s_add_u32 s12, s12, 0x8000
	s_addc_u32 s13, s13, 0
	global_load_dwordx4 v[40:43], v10, s[12:13]
	s_add_u32 s12, s12, 0x8000
	s_addc_u32 s13, s13, 0
	global_load_dwordx4 v[44:47], v10, s[12:13]
	s_add_u32 s12, s12, 0x8000
	s_addc_u32 s13, s13, 0
	global_load_dwordx4 v[48:51], v10, s[12:13]
	s_add_u32 s12, s12, 0x8000
	s_addc_u32 s13, s13, 0
	global_load_dwordx4 v[52:55], v10, s[12:13]
	s_add_u32 s12, s12, 0x8000
	s_addc_u32 s13, s13, 0
	global_load_dwordx4 v[56:59], v10, s[12:13]
	s_add_u32 s12, s12, 0x8000
	s_addc_u32 s13, s13, 0
	global_load_dwordx4 v[60:63], v10, s[12:13]
	s_add_u32 s12, s12, 0x8000
	s_addc_u32 s13, s13, 0
	global_load_dwordx4 v[64:67], v10, s[12:13]
	s_add_i32 s17, s16, 2592
	s_min_u32 s17, s17, 0xbff
	s_lshr_b32 s18, s17, 5
	s_add_i32 s18, s18, 32
	s_and_b32 s19, s17, 31
	s_lshl_b32 s19, s19, 21
	s_lshl_b32 s18, s18, 7
	s_add_u32 s18, s18, s19
	s_add_u32 s14, s4, s18
	s_addc_u32 s15, s5, 0
	ds_read_b32 v132, v7
	ds_read_b32 v133, v7 offset:512
	ds_read_b32 v134, v7 offset:1024
	ds_read_b32 v135, v7 offset:1536
	ds_read_b32 v136, v7 offset:2048
	ds_read_b32 v137, v7 offset:2560
	ds_read_b32 v138, v7 offset:3072
	ds_read_b32 v139, v7 offset:3584
	ds_read_b32 v140, v7 offset:4096
	ds_read_b32 v141, v7 offset:4608
	ds_read_b32 v142, v7 offset:5120
	ds_read_b32 v143, v7 offset:5632
	ds_read_b32 v144, v7 offset:6144
	ds_read_b32 v145, v7 offset:6656
	ds_read_b32 v146, v7 offset:7168
	ds_read_b32 v147, v7 offset:7680
	s_waitcnt lgkmcnt(0)
	v_max_f32_e32 v132, v132, v132
	v_max_f32_e32 v133, v133, v133
	v_max_f32_e32 v134, v134, v134
	v_max_f32_e32 v135, v135, v135
	v_max_f32_e32 v136, v136, v136
	v_max_f32_e32 v137, v137, v137
	v_max_f32_e32 v138, v138, v138
	v_max_f32_e32 v139, v139, v139
	v_max_f32_e32 v140, v140, v140
	v_max_f32_e32 v141, v141, v141
	v_max_f32_e32 v142, v142, v142
	v_max_f32_e32 v143, v143, v143
	v_max_f32_e32 v144, v144, v144
	v_max_f32_e32 v145, v145, v145
	v_max_f32_e32 v146, v146, v146
	v_max_f32_e32 v147, v147, v147
	v_med3_f32 v132, v132, s20, v13
	v_med3_f32 v133, v133, s20, v13
	v_med3_f32 v134, v134, s20, v13
	v_med3_f32 v135, v135, s20, v13
	v_med3_f32 v136, v136, s20, v13
	v_med3_f32 v137, v137, s20, v13
	v_med3_f32 v138, v138, s20, v13
	v_med3_f32 v139, v139, s20, v13
	v_med3_f32 v140, v140, s20, v13
	v_med3_f32 v141, v141, s20, v13
	v_med3_f32 v142, v142, s20, v13
	v_med3_f32 v143, v143, s20, v13
	v_med3_f32 v144, v144, s20, v13
	v_med3_f32 v145, v145, s20, v13
	v_med3_f32 v146, v146, s20, v13
	v_med3_f32 v147, v147, s20, v13
	v_mov_b32_e32 v148, 0
	v_mov_b32_e32 v149, 0
	v_mov_b32_e32 v150, 0
	v_mov_b32_e32 v151, 0
	v_cvt_pk_fp8_f32 v148, v132, v133
	v_cvt_pk_fp8_f32 v149, v136, v137
	v_cvt_pk_fp8_f32 v150, v140, v141
	v_cvt_pk_fp8_f32 v151, v144, v145
	v_cvt_pk_fp8_f32 v148, v134, v135 op_sel:[0,0,1]
	v_cvt_pk_fp8_f32 v149, v138, v139 op_sel:[0,0,1]
	v_cvt_pk_fp8_f32 v150, v142, v143 op_sel:[0,0,1]
	v_cvt_pk_fp8_f32 v151, v146, v147 op_sel:[0,0,1]
	s_nop 0
	global_store_dwordx4 v11, v[148:151], s[14:15]
	ds_read_b32 v132, v9
	ds_read_b32 v133, v9 offset:512
	ds_read_b32 v134, v9 offset:1024
	ds_read_b32 v135, v9 offset:1536
	ds_read_b32 v136, v9 offset:2048
	ds_read_b32 v137, v9 offset:2560
	ds_read_b32 v138, v9 offset:3072
	ds_read_b32 v139, v9 offset:3584
	ds_read_b32 v140, v9 offset:4096
	ds_read_b32 v141, v9 offset:4608
	ds_read_b32 v142, v9 offset:5120
	ds_read_b32 v143, v9 offset:5632
	ds_read_b32 v144, v9 offset:6144
	ds_read_b32 v145, v9 offset:6656
	ds_read_b32 v146, v9 offset:7168
	ds_read_b32 v147, v9 offset:7680
	s_waitcnt lgkmcnt(0)
	v_max_f32_e32 v132, v132, v132
	v_max_f32_e32 v133, v133, v133
	v_max_f32_e32 v134, v134, v134
	v_max_f32_e32 v135, v135, v135
	v_max_f32_e32 v136, v136, v136
	v_max_f32_e32 v137, v137, v137
	v_max_f32_e32 v138, v138, v138
	v_max_f32_e32 v139, v139, v139
	v_max_f32_e32 v140, v140, v140
	v_max_f32_e32 v141, v141, v141
	v_max_f32_e32 v142, v142, v142
	v_max_f32_e32 v143, v143, v143
	v_max_f32_e32 v144, v144, v144
	v_max_f32_e32 v145, v145, v145
	v_max_f32_e32 v146, v146, v146
	v_max_f32_e32 v147, v147, v147
	v_med3_f32 v132, v132, s20, v13
	v_med3_f32 v133, v133, s20, v13
	v_med3_f32 v134, v134, s20, v13
	v_med3_f32 v135, v135, s20, v13
	v_med3_f32 v136, v136, s20, v13
	v_med3_f32 v137, v137, s20, v13
	v_med3_f32 v138, v138, s20, v13
	v_med3_f32 v139, v139, s20, v13
	v_med3_f32 v140, v140, s20, v13
	v_med3_f32 v141, v141, s20, v13
	v_med3_f32 v142, v142, s20, v13
	v_med3_f32 v143, v143, s20, v13
	v_med3_f32 v144, v144, s20, v13
	v_med3_f32 v145, v145, s20, v13
	v_med3_f32 v146, v146, s20, v13
	v_med3_f32 v147, v147, s20, v13
	v_mov_b32_e32 v148, 0
	v_mov_b32_e32 v149, 0
	v_mov_b32_e32 v150, 0
	v_mov_b32_e32 v151, 0
	v_cvt_pk_fp8_f32 v148, v132, v133
	v_cvt_pk_fp8_f32 v149, v136, v137
	v_cvt_pk_fp8_f32 v150, v140, v141
	v_cvt_pk_fp8_f32 v151, v144, v145
	v_cvt_pk_fp8_f32 v148, v134, v135 op_sel:[0,0,1]
	v_cvt_pk_fp8_f32 v149, v138, v139 op_sel:[0,0,1]
	v_cvt_pk_fp8_f32 v150, v142, v143 op_sel:[0,0,1]
	v_cvt_pk_fp8_f32 v151, v146, v147 op_sel:[0,0,1]
	s_nop 0
	global_store_dwordx4 v12, v[148:151], s[14:15]
	s_waitcnt vmcnt(22)
	v_mul_f32_e32 v68, 0x43000000, v68
	v_mul_f32_e32 v69, 0x43000000, v69
	v_mul_f32_e32 v70, 0x43000000, v70
	v_mul_f32_e32 v71, 0x43000000, v71
	ds_write_b128 v4, v[68:71]
	v_mul_f32_e32 v72, 0x43000000, v72
	v_mul_f32_e32 v73, 0x43000000, v73
	v_mul_f32_e32 v74, 0x43000000, v74
	v_mul_f32_e32 v75, 0x43000000, v75
	ds_write_b128 v4, v[72:75] offset:1024
	v_mul_f32_e32 v76, 0x43000000, v76
	v_mul_f32_e32 v77, 0x43000000, v77
	v_mul_f32_e32 v78, 0x43000000, v78
	v_mul_f32_e32 v79, 0x43000000, v79
	ds_write_b128 v4, v[76:79] offset:2048
	v_mul_f32_e32 v80, 0x43000000, v80
	v_mul_f32_e32 v81, 0x43000000, v81
	v_mul_f32_e32 v82, 0x43000000, v82
	v_mul_f32_e32 v83, 0x43000000, v83
	ds_write_b128 v4, v[80:83] offset:3072
	v_mul_f32_e32 v84, 0x43000000, v84
	v_mul_f32_e32 v85, 0x43000000, v85
	v_mul_f32_e32 v86, 0x43000000, v86
	v_mul_f32_e32 v87, 0x43000000, v87
	ds_write_b128 v4, v[84:87] offset:4096
	v_mul_f32_e32 v88, 0x43000000, v88
	v_mul_f32_e32 v89, 0x43000000, v89
	v_mul_f32_e32 v90, 0x43000000, v90
	v_mul_f32_e32 v91, 0x43000000, v91
	ds_write_b128 v4, v[88:91] offset:5120
	v_mul_f32_e32 v92, 0x43000000, v92
	v_mul_f32_e32 v93, 0x43000000, v93
	v_mul_f32_e32 v94, 0x43000000, v94
	v_mul_f32_e32 v95, 0x43000000, v95
	ds_write_b128 v4, v[92:95] offset:6144
	v_mul_f32_e32 v96, 0x43000000, v96
	v_mul_f32_e32 v97, 0x43000000, v97
	v_mul_f32_e32 v98, 0x43000000, v98
	v_mul_f32_e32 v99, 0x43000000, v99
	ds_write_b128 v4, v[96:99] offset:7168
	s_waitcnt lgkmcnt(0)
	s_barrier
; #define GAS __attribute__((address_space(1)))
; #define LAS __attribute__((address_space(3)))
; #define LDS_WAIT() asm volatile("s_waitcnt lgkmcnt(0)" ::: "memory")
; __device__ __forceinline__ unsigned pk4_fp8(float a, float b, float c, float d) {
;     a = fminf(fmaxf(a, -448.f), 448.f); b = fminf(fmaxf(b, -448.f), 448.f); c = fminf(fmaxf(c, -448.f), 448.f); d = fminf(fmaxf(d, -448.f), 448.f);
;     int w = __builtin_amdgcn_cvt_pk_fp8_f32(a, b, 0, false); w = __builtin_amdgcn_cvt_pk_fp8_f32(c, d, w, true); return (unsigned)w; }
;     const int pr = item >> 1, kb = 2 * (pr / nblk) + (item & 1), nb = pr % nblk, k0 = 64 * kb, n0 = 32 * nb;
;     const int nr = n0 + (lane & 31); const int sc = MAP == 1 ? src_col_in(nr) : nr;
;     float v[32];
; #pragma unroll
;     for (int i = 0; i < 32; ++i) v[i] = sc >= 0 ? W[(size_t)(k0 + 2 * i + (lane >> 5)) * Nsrc + sc] : 0.f;
; #pragma unroll
;     for (int i = 0; i < 32; ++i) { const int k = k0 + 2 * i + (lane >> 5); float x = v[i] * wscale; if (KS) x *= (k < ksplit ? ksA[k] : ksB[k - ksplit]); scr[(2 * i + (lane >> 5)) * 33 + (lane & 31)] = x; }
;     LDS_WAIT(); asm volatile("" ::: "memory");
;     const int c = lane & 7;
; #pragma unroll
;     for (int j = 0; j < 4; ++j) { const int n = (lane >> 3) + 8 * j; const LAS float* s = scr + (8 * c) * 33 + n;
;         const unsigned long long o = (unsigned long long)pg8::pk4_fp8(s[0 * 33], s[1 * 33], s[2 * 33], s[3 * 33]) | ((unsigned long long)pg8::pk4_fp8(s[4 * 33], s[5 * 33], s[6 * 33], s[7 * 33]) << 32);
;         *(GAS unsigned long long*)(WT + (size_t)(n0 + n) * K + k0 + 8 * c) = o; }
;     LDS_WAIT(); asm volatile("" ::: "memory");
	s_add_i32 s17, s16, 2976
	s_min_u32 s17, s17, 0xbff
	s_lshr_b32 s18, s17, 5
	s_add_i32 s18, s18, 32
	s_and_b32 s19, s17, 31
	s_lshl_b32 s18, s18, 21
	s_lshl_b32 s19, s19, 9
	s_add_u32 s18, s18, s19
	s_add_u32 s12, s2, s18
	s_addc_u32 s13, s3, 0
	global_load_dwordx4 v[68:71], v10, s[12:13]
	s_add_u32 s12, s12, 0x8000
	s_addc_u32 s13, s13, 0
	global_load_dwordx4 v[72:75], v10, s[12:13]
	s_add_u32 s12, s12, 0x8000
	s_addc_u32 s13, s13, 0
	global_load_dwordx4 v[76:79], v10, s[12:13]
	s_add_u32 s12, s12, 0x8000
	s_addc_u32 s13, s13, 0
	global_load_dwordx4 v[80:83], v10, s[12:13]
	s_add_u32 s12, s12, 0x8000
	s_addc_u32 s13, s13, 0
	global_load_dwordx4 v[84:87], v10, s[12:13]
	s_add_u32 s12, s12, 0x8000
	s_addc_u32 s13, s13, 0
	global_load_dwordx4 v[88:91], v10, s[12:13]
	s_add_u32 s12, s12, 0x8000
	s_addc_u32 s13, s13, 0
	global_load_dwordx4 v[92:95], v10, s[12:13]
	s_add_u32 s12, s12, 0x8000
	s_addc_u32 s13, s13, 0
	global_load_dwordx4 v[96:99], v10, s[12:13]
	s_add_i32 s17, s16, 2688
	s_min_u32 s17, s17, 0xbff
	s_lshr_b32 s18, s17, 5
	s_add_i32 s18, s18, 32
	s_and_b32 s19, s17, 31
	s_lshl_b32 s19, s19, 21
	s_lshl_b32 s18, s18, 7
	s_add_u32 s18, s18, s19
	s_add_u32 s14, s4, s18
	s_addc_u32 s15, s5, 0
	ds_read_b32 v132, v6
	ds_read_b32 v133, v6 offset:512
	ds_read_b32 v134, v6 offset:1024
	ds_read_b32 v135, v6 offset:1536
	ds_read_b32 v136, v6 offset:2048
	ds_read_b32 v137, v6 offset:2560
	ds_read_b32 v138, v6 offset:3072
	ds_read_b32 v139, v6 offset:3584
	ds_read_b32 v140, v6 offset:4096
	ds_read_b32 v141, v6 offset:4608
	ds_read_b32 v142, v6 offset:5120
	ds_read_b32 v143, v6 offset:5632
	ds_read_b32 v144, v6 offset:6144
	ds_read_b32 v145, v6 offset:6656
	ds_read_b32 v146, v6 offset:7168
	ds_read_b32 v147, v6 offset:7680
	s_waitcnt lgkmcnt(0)
	v_max_f32_e32 v132, v132, v132
	v_max_f32_e32 v133, v133, v133
	v_max_f32_e32 v134, v134, v134
	v_max_f32_e32 v135, v135, v135
	v_max_f32_e32 v136, v136, v136
	v_max_f32_e32 v137, v137, v137
	v_max_f32_e32 v138, v138, v138
	v_max_f32_e32 v139, v139, v139
	v_max_f32_e32 v140, v140, v140
	v_max_f32_e32 v141, v141, v141
	v_max_f32_e32 v142, v142, v142
	v_max_f32_e32 v143, v143, v143
	v_max_f32_e32 v144, v144, v144
	v_max_f32_e32 v145, v145, v145
	v_max_f32_e32 v146, v146, v146
	v_max_f32_e32 v147, v147, v147
	v_med3_f32 v132, v132, s20, v13
	v_med3_f32 v133, v133, s20, v13
	v_med3_f32 v134, v134, s20, v13
	v_med3_f32 v135, v135, s20, v13
	v_med3_f32 v136, v136, s20, v13
	v_med3_f32 v137, v137, s20, v13
	v_med3_f32 v138, v138, s20, v13
	v_med3_f32 v139, v139, s20, v13
	v_med3_f32 v140, v140, s20, v13
	v_med3_f32 v141, v141, s20, v13
	v_med3_f32 v142, v142, s20, v13
	v_med3_f32 v143, v143, s20, v13
	v_med3_f32 v144, v144, s20, v13
	v_med3_f32 v145, v145, s20, v13
	v_med3_f32 v146, v146, s20, v13
	v_med3_f32 v147, v147, s20, v13
	v_mov_b32_e32 v148, 0
	v_mov_b32_e32 v149, 0
	v_mov_b32_e32 v150, 0
	v_mov_b32_e32 v151, 0
	v_cvt_pk_fp8_f32 v148, v132, v133
	v_cvt_pk_fp8_f32 v149, v136, v137
	v_cvt_pk_fp8_f32 v150, v140, v141
	v_cvt_pk_fp8_f32 v151, v144, v145
	v_cvt_pk_fp8_f32 v148, v134, v135 op_sel:[0,0,1]
	v_cvt_pk_fp8_f32 v149, v138, v139 op_sel:[0,0,1]
	v_cvt_pk_fp8_f32 v150, v142, v143 op_sel:[0,0,1]
	v_cvt_pk_fp8_f32 v151, v146, v147 op_sel:[0,0,1]
	s_nop 0
	global_store_dwordx4 v11, v[148:151], s[14:15]
	ds_read_b32 v132, v8
	ds_read_b32 v133, v8 offset:512
	ds_read_b32 v134, v8 offset:1024
	ds_read_b32 v135, v8 offset:1536
	ds_read_b32 v136, v8 offset:2048
	ds_read_b32 v137, v8 offset:2560
	ds_read_b32 v138, v8 offset:3072
	ds_read_b32 v139, v8 offset:3584
	ds_read_b32 v140, v8 offset:4096
	ds_read_b32 v141, v8 offset:4608
	ds_read_b32 v142, v8 offset:5120
	ds_read_b32 v143, v8 offset:5632
	ds_read_b32 v144, v8 offset:6144
	ds_read_b32 v145, v8 offset:6656
	ds_read_b32 v146, v8 offset:7168
	ds_read_b32 v147, v8 offset:7680
	s_waitcnt lgkmcnt(0)
	v_max_f32_e32 v132, v132, v132
	v_max_f32_e32 v133, v133, v133
	v_max_f32_e32 v134, v134, v134
	v_max_f32_e32 v135, v135, v135
	v_max_f32_e32 v136, v136, v136
	v_max_f32_e32 v137, v137, v137
	v_max_f32_e32 v138, v138, v138
	v_max_f32_e32 v139, v139, v139
	v_max_f32_e32 v140, v140, v140
	v_max_f32_e32 v141, v141, v141
	v_max_f32_e32 v142, v142, v142
	v_max_f32_e32 v143, v143, v143
	v_max_f32_e32 v144, v144, v144
	v_max_f32_e32 v145, v145, v145
	v_max_f32_e32 v146, v146, v146
	v_max_f32_e32 v147, v147, v147
	v_med3_f32 v132, v132, s20, v13
	v_med3_f32 v133, v133, s20, v13
	v_med3_f32 v134, v134, s20, v13
	v_med3_f32 v135, v135, s20, v13
	v_med3_f32 v136, v136, s20, v13
	v_med3_f32 v137, v137, s20, v13
	v_med3_f32 v138, v138, s20, v13
	v_med3_f32 v139, v139, s20, v13
	v_med3_f32 v140, v140, s20, v13
	v_med3_f32 v141, v141, s20, v13
	v_med3_f32 v142, v142, s20, v13
	v_med3_f32 v143, v143, s20, v13
	v_med3_f32 v144, v144, s20, v13
	v_med3_f32 v145, v145, s20, v13
	v_med3_f32 v146, v146, s20, v13
	v_med3_f32 v147, v147, s20, v13
	v_mov_b32_e32 v148, 0
	v_mov_b32_e32 v149, 0
	v_mov_b32_e32 v150, 0
	v_mov_b32_e32 v151, 0
	v_cvt_pk_fp8_f32 v148, v132, v133
	v_cvt_pk_fp8_f32 v149, v136, v137
	v_cvt_pk_fp8_f32 v150, v140, v141
	v_cvt_pk_fp8_f32 v151, v144, v145
	v_cvt_pk_fp8_f32 v148, v134, v135 op_sel:[0,0,1]
	v_cvt_pk_fp8_f32 v149, v138, v139 op_sel:[0,0,1]
	v_cvt_pk_fp8_f32 v150, v142, v143 op_sel:[0,0,1]
	v_cvt_pk_fp8_f32 v151, v146, v147 op_sel:[0,0,1]
	s_nop 0
	global_store_dwordx4 v12, v[148:151], s[14:15]
	s_waitcnt vmcnt(22)
	v_mul_f32_e32 v100, 0x43000000, v100
	v_mul_f32_e32 v101, 0x43000000, v101
	v_mul_f32_e32 v102, 0x43000000, v102
	v_mul_f32_e32 v103, 0x43000000, v103
	ds_write_b128 v5, v[100:103]
	v_mul_f32_e32 v104, 0x43000000, v104
	v_mul_f32_e32 v105, 0x43000000, v105
	v_mul_f32_e32 v106, 0x43000000, v106
	v_mul_f32_e32 v107, 0x43000000, v107
	ds_write_b128 v5, v[104:107] offset:1024
	v_mul_f32_e32 v108, 0x43000000, v108
	v_mul_f32_e32 v109, 0x43000000, v109
	v_mul_f32_e32 v110, 0x43000000, v110
	v_mul_f32_e32 v111, 0x43000000, v111
	ds_write_b128 v5, v[108:111] offset:2048
	v_mul_f32_e32 v112, 0x43000000, v112
	v_mul_f32_e32 v113, 0x43000000, v113
	v_mul_f32_e32 v114, 0x43000000, v114
	v_mul_f32_e32 v115, 0x43000000, v115
	ds_write_b128 v5, v[112:115] offset:3072
	v_mul_f32_e32 v116, 0x43000000, v116
	v_mul_f32_e32 v117, 0x43000000, v117
	v_mul_f32_e32 v118, 0x43000000, v118
	v_mul_f32_e32 v119, 0x43000000, v119
	ds_write_b128 v5, v[116:119] offset:4096
	v_mul_f32_e32 v120, 0x43000000, v120
	v_mul_f32_e32 v121, 0x43000000, v121
	v_mul_f32_e32 v122, 0x43000000, v122
	v_mul_f32_e32 v123, 0x43000000, v123
	ds_write_b128 v5, v[120:123] offset:5120
	v_mul_f32_e32 v124, 0x43000000, v124
	v_mul_f32_e32 v125, 0x43000000, v125
	v_mul_f32_e32 v126, 0x43000000, v126
	v_mul_f32_e32 v127, 0x43000000, v127
	ds_write_b128 v5, v[124:127] offset:6144
	v_mul_f32_e32 v128, 0x43000000, v128
	v_mul_f32_e32 v129, 0x43000000, v129
	v_mul_f32_e32 v130, 0x43000000, v130
	v_mul_f32_e32 v131, 0x43000000, v131
	ds_write_b128 v5, v[128:131] offset:7168
	s_waitcnt lgkmcnt(0)
	s_barrier
; #define GAS __attribute__((address_space(1)))
; #define LAS __attribute__((address_space(3)))
; #define LDS_WAIT() asm volatile("s_waitcnt lgkmcnt(0)" ::: "memory")
; __device__ __forceinline__ unsigned pk4_fp8(float a, float b, float c, float d) {
;     a = fminf(fmaxf(a, -448.f), 448.f); b = fminf(fmaxf(b, -448.f), 448.f); c = fminf(fmaxf(c, -448.f), 448.f); d = fminf(fmaxf(d, -448.f), 448.f);
;     int w = __builtin_amdgcn_cvt_pk_fp8_f32(a, b, 0, false); w = __builtin_amdgcn_cvt_pk_fp8_f32(c, d, w, true); return (unsigned)w; }
;     const int pr = item >> 1, kb = 2 * (pr / nblk) + (item & 1), nb = pr % nblk, k0 = 64 * kb, n0 = 32 * nb;
;     const int nr = n0 + (lane & 31); const int sc = MAP == 1 ? src_col_in(nr) : nr;
;     float v[32];
; #pragma unroll
;     for (int i = 0; i < 32; ++i) v[i] = sc >= 0 ? W[(size_t)(k0 + 2 * i + (lane >> 5)) * Nsrc + sc] : 0.f;
; #pragma unroll
;     for (int i = 0; i < 32; ++i) { const int k = k0 + 2 * i + (lane >> 5); float x = v[i] * wscale; if (KS) x *= (k < ksplit ? ksA[k] : ksB[k - ksplit]); scr[(2 * i + (lane >> 5)) * 33 + (lane & 31)] = x; }
;     LDS_WAIT(); asm volatile("" ::: "memory");
;     const int c = lane & 7;
; #pragma unroll
;     for (int j = 0; j < 4; ++j) { const int n = (lane >> 3) + 8 * j; const LAS float* s = scr + (8 * c) * 33 + n;
;         const unsigned long long o = (unsigned long long)pg8::pk4_fp8(s[0 * 33], s[1 * 33], s[2 * 33], s[3 * 33]) | ((unsigned long long)pg8::pk4_fp8(s[4 * 33], s[5 * 33], s[6 * 33], s[7 * 33]) << 32);
;         *(GAS unsigned long long*)(WT + (size_t)(n0 + n) * K + k0 + 8 * c) = o; }
;     LDS_WAIT(); asm volatile("" ::: "memory");
	s_add_i32 s17, s16, 2784
	s_min_u32 s17, s17, 0xbff
	s_lshr_b32 s18, s17, 5
	s_add_i32 s18, s18, 32
	s_and_b32 s19, s17, 31
	s_lshl_b32 s19, s19, 21
	s_lshl_b32 s18, s18, 7
	s_add_u32 s18, s18, s19
	s_add_u32 s14, s4, s18
	s_addc_u32 s15, s5, 0
	ds_read_b32 v132, v7
	ds_read_b32 v133, v7 offset:512
	ds_read_b32 v134, v7 offset:1024
	ds_read_b32 v135, v7 offset:1536
	ds_read_b32 v136, v7 offset:2048
	ds_read_b32 v137, v7 offset:2560
	ds_read_b32 v138, v7 offset:3072
	ds_read_b32 v139, v7 offset:3584
	ds_read_b32 v140, v7 offset:4096
	ds_read_b32 v141, v7 offset:4608
	ds_read_b32 v142, v7 offset:5120
	ds_read_b32 v143, v7 offset:5632
	ds_read_b32 v144, v7 offset:6144
	ds_read_b32 v145, v7 offset:6656
	ds_read_b32 v146, v7 offset:7168
	ds_read_b32 v147, v7 offset:7680
	s_waitcnt lgkmcnt(0)
	v_max_f32_e32 v132, v132, v132
	v_max_f32_e32 v133, v133, v133
	v_max_f32_e32 v134, v134, v134
	v_max_f32_e32 v135, v135, v135
	v_max_f32_e32 v136, v136, v136
	v_max_f32_e32 v137, v137, v137
	v_max_f32_e32 v138, v138, v138
	v_max_f32_e32 v139, v139, v139
	v_max_f32_e32 v140, v140, v140
	v_max_f32_e32 v141, v141, v141
	v_max_f32_e32 v142, v142, v142
	v_max_f32_e32 v143, v143, v143
	v_max_f32_e32 v144, v144, v144
	v_max_f32_e32 v145, v145, v145
	v_max_f32_e32 v146, v146, v146
	v_max_f32_e32 v147, v147, v147
	v_med3_f32 v132, v132, s20, v13
	v_med3_f32 v133, v133, s20, v13
	v_med3_f32 v134, v134, s20, v13
	v_med3_f32 v135, v135, s20, v13
	v_med3_f32 v136, v136, s20, v13
	v_med3_f32 v137, v137, s20, v13
	v_med3_f32 v138, v138, s20, v13
	v_med3_f32 v139, v139, s20, v13
	v_med3_f32 v140, v140, s20, v13
	v_med3_f32 v141, v141, s20, v13
	v_med3_f32 v142, v142, s20, v13
	v_med3_f32 v143, v143, s20, v13
	v_med3_f32 v144, v144, s20, v13
	v_med3_f32 v145, v145, s20, v13
	v_med3_f32 v146, v146, s20, v13
	v_med3_f32 v147, v147, s20, v13
	v_mov_b32_e32 v148, 0
	v_mov_b32_e32 v149, 0
	v_mov_b32_e32 v150, 0
	v_mov_b32_e32 v151, 0
	v_cvt_pk_fp8_f32 v148, v132, v133
	v_cvt_pk_fp8_f32 v149, v136, v137
	v_cvt_pk_fp8_f32 v150, v140, v141
	v_cvt_pk_fp8_f32 v151, v144, v145
	v_cvt_pk_fp8_f32 v148, v134, v135 op_sel:[0,0,1]
	v_cvt_pk_fp8_f32 v149, v138, v139 op_sel:[0,0,1]
	v_cvt_pk_fp8_f32 v150, v142, v143 op_sel:[0,0,1]
	v_cvt_pk_fp8_f32 v151, v146, v147 op_sel:[0,0,1]
	s_nop 0
	global_store_dwordx4 v11, v[148:151], s[14:15]
	ds_read_b32 v132, v9
	ds_read_b32 v133, v9 offset:512
	ds_read_b32 v134, v9 offset:1024
	ds_read_b32 v135, v9 offset:1536
	ds_read_b32 v136, v9 offset:2048
	ds_read_b32 v137, v9 offset:2560
	ds_read_b32 v138, v9 offset:3072
	ds_read_b32 v139, v9 offset:3584
	ds_read_b32 v140, v9 offset:4096
	ds_read_b32 v141, v9 offset:4608
	ds_read_b32 v142, v9 offset:5120
	ds_read_b32 v143, v9 offset:5632
	ds_read_b32 v144, v9 offset:6144
	ds_read_b32 v145, v9 offset:6656
	ds_read_b32 v146, v9 offset:7168
	ds_read_b32 v147, v9 offset:7680
	s_waitcnt lgkmcnt(0)
	v_max_f32_e32 v132, v132, v132
	v_max_f32_e32 v133, v133, v133
	v_max_f32_e32 v134, v134, v134
	v_max_f32_e32 v135, v135, v135
	v_max_f32_e32 v136, v136, v136
	v_max_f32_e32 v137, v137, v137
	v_max_f32_e32 v138, v138, v138
	v_max_f32_e32 v139, v139, v139
	v_max_f32_e32 v140, v140, v140
	v_max_f32_e32 v141, v141, v141
	v_max_f32_e32 v142, v142, v142
	v_max_f32_e32 v143, v143, v143
	v_max_f32_e32 v144, v144, v144
	v_max_f32_e32 v145, v145, v145
	v_max_f32_e32 v146, v146, v146
	v_max_f32_e32 v147, v147, v147
	v_med3_f32 v132, v132, s20, v13
	v_med3_f32 v133, v133, s20, v13
	v_med3_f32 v134, v134, s20, v13
	v_med3_f32 v135, v135, s20, v13
	v_med3_f32 v136, v136, s20, v13
	v_med3_f32 v137, v137, s20, v13
	v_med3_f32 v138, v138, s20, v13
	v_med3_f32 v139, v139, s20, v13
	v_med3_f32 v140, v140, s20, v13
	v_med3_f32 v141, v141, s20, v13
	v_med3_f32 v142, v142, s20, v13
	v_med3_f32 v143, v143, s20, v13
	v_med3_f32 v144, v144, s20, v13
	v_med3_f32 v145, v145, s20, v13
	v_med3_f32 v146, v146, s20, v13
	v_med3_f32 v147, v147, s20, v13
	v_mov_b32_e32 v148, 0
	v_mov_b32_e32 v149, 0
	v_mov_b32_e32 v150, 0
	v_mov_b32_e32 v151, 0
	v_cvt_pk_fp8_f32 v148, v132, v133
	v_cvt_pk_fp8_f32 v149, v136, v137
	v_cvt_pk_fp8_f32 v150, v140, v141
	v_cvt_pk_fp8_f32 v151, v144, v145
	v_cvt_pk_fp8_f32 v148, v134, v135 op_sel:[0,0,1]
	v_cvt_pk_fp8_f32 v149, v138, v139 op_sel:[0,0,1]
	v_cvt_pk_fp8_f32 v150, v142, v143 op_sel:[0,0,1]
	v_cvt_pk_fp8_f32 v151, v146, v147 op_sel:[0,0,1]
	s_nop 0
	global_store_dwordx4 v12, v[148:151], s[14:15]
	s_waitcnt vmcnt(14)
	v_mul_f32_e32 v36, 0x43000000, v36
	v_mul_f32_e32 v37, 0x43000000, v37
	v_mul_f32_e32 v38, 0x43000000, v38
	v_mul_f32_e32 v39, 0x43000000, v39
	ds_write_b128 v4, v[36:39]
	v_mul_f32_e32 v40, 0x43000000, v40
	v_mul_f32_e32 v41, 0x43000000, v41
	v_mul_f32_e32 v42, 0x43000000, v42
	v_mul_f32_e32 v43, 0x43000000, v43
	ds_write_b128 v4, v[40:43] offset:1024
	v_mul_f32_e32 v44, 0x43000000, v44
	v_mul_f32_e32 v45, 0x43000000, v45
	v_mul_f32_e32 v46, 0x43000000, v46
	v_mul_f32_e32 v47, 0x43000000, v47
	ds_write_b128 v4, v[44:47] offset:2048
	v_mul_f32_e32 v48, 0x43000000, v48
	v_mul_f32_e32 v49, 0x43000000, v49
	v_mul_f32_e32 v50, 0x43000000, v50
	v_mul_f32_e32 v51, 0x43000000, v51
	ds_write_b128 v4, v[48:51] offset:3072
	v_mul_f32_e32 v52, 0x43000000, v52
	v_mul_f32_e32 v53, 0x43000000, v53
	v_mul_f32_e32 v54, 0x43000000, v54
	v_mul_f32_e32 v55, 0x43000000, v55
	ds_write_b128 v4, v[52:55] offset:4096
	v_mul_f32_e32 v56, 0x43000000, v56
	v_mul_f32_e32 v57, 0x43000000, v57
	v_mul_f32_e32 v58, 0x43000000, v58
	v_mul_f32_e32 v59, 0x43000000, v59
	ds_write_b128 v4, v[56:59] offset:5120
	v_mul_f32_e32 v60, 0x43000000, v60
	v_mul_f32_e32 v61, 0x43000000, v61
	v_mul_f32_e32 v62, 0x43000000, v62
	v_mul_f32_e32 v63, 0x43000000, v63
	ds_write_b128 v4, v[60:63] offset:6144
	v_mul_f32_e32 v64, 0x43000000, v64
	v_mul_f32_e32 v65, 0x43000000, v65
	v_mul_f32_e32 v66, 0x43000000, v66
	v_mul_f32_e32 v67, 0x43000000, v67
	ds_write_b128 v4, v[64:67] offset:7168
	s_waitcnt lgkmcnt(0)
	s_barrier
; #define GAS __attribute__((address_space(1)))
; #define LAS __attribute__((address_space(3)))
; #define LDS_WAIT() asm volatile("s_waitcnt lgkmcnt(0)" ::: "memory")
; __device__ __forceinline__ unsigned pk4_fp8(float a, float b, float c, float d) {
;     a = fminf(fmaxf(a, -448.f), 448.f); b = fminf(fmaxf(b, -448.f), 448.f); c = fminf(fmaxf(c, -448.f), 448.f); d = fminf(fmaxf(d, -448.f), 448.f);
;     int w = __builtin_amdgcn_cvt_pk_fp8_f32(a, b, 0, false); w = __builtin_amdgcn_cvt_pk_fp8_f32(c, d, w, true); return (unsigned)w; }
;     const int pr = item >> 1, kb = 2 * (pr / nblk) + (item & 1), nb = pr % nblk, k0 = 64 * kb, n0 = 32 * nb;
;     const int nr = n0 + (lane & 31); const int sc = MAP == 1 ? src_col_in(nr) : nr;
;     float v[32];
; #pragma unroll
;     for (int i = 0; i < 32; ++i) v[i] = sc >= 0 ? W[(size_t)(k0 + 2 * i + (lane >> 5)) * Nsrc + sc] : 0.f;
; #pragma unroll
;     for (int i = 0; i < 32; ++i) { const int k = k0 + 2 * i + (lane >> 5); float x = v[i] * wscale; if (KS) x *= (k < ksplit ? ksA[k] : ksB[k - ksplit]); scr[(2 * i + (lane >> 5)) * 33 + (lane & 31)] = x; }
;     LDS_WAIT(); asm volatile("" ::: "memory");
;     const int c = lane & 7;
; #pragma unroll
;     for (int j = 0; j < 4; ++j) { const int n = (lane >> 3) + 8 * j; const LAS float* s = scr + (8 * c) * 33 + n;
;         const unsigned long long o = (unsigned long long)pg8::pk4_fp8(s[0 * 33], s[1 * 33], s[2 * 33], s[3 * 33]) | ((unsigned long long)pg8::pk4_fp8(s[4 * 33], s[5 * 33], s[6 * 33], s[7 * 33]) << 32);
;         *(GAS unsigned long long*)(WT + (size_t)(n0 + n) * K + k0 + 8 * c) = o; }
;     LDS_WAIT(); asm volatile("" ::: "memory");
	s_add_i32 s17, s16, 2880
	s_min_u32 s17, s17, 0xbff
	s_lshr_b32 s18, s17, 5
	s_add_i32 s18, s18, 32
	s_and_b32 s19, s17, 31
	s_lshl_b32 s19, s19, 21
	s_lshl_b32 s18, s18, 7
	s_add_u32 s18, s18, s19
	s_add_u32 s14, s4, s18
	s_addc_u32 s15, s5, 0
	ds_read_b32 v132, v6
	ds_read_b32 v133, v6 offset:512
	ds_read_b32 v134, v6 offset:1024
	ds_read_b32 v135, v6 offset:1536
	ds_read_b32 v136, v6 offset:2048
	ds_read_b32 v137, v6 offset:2560
	ds_read_b32 v138, v6 offset:3072
	ds_read_b32 v139, v6 offset:3584
	ds_read_b32 v140, v6 offset:4096
	ds_read_b32 v141, v6 offset:4608
	ds_read_b32 v142, v6 offset:5120
	ds_read_b32 v143, v6 offset:5632
	ds_read_b32 v144, v6 offset:6144
	ds_read_b32 v145, v6 offset:6656
	ds_read_b32 v146, v6 offset:7168
	ds_read_b32 v147, v6 offset:7680
	s_waitcnt lgkmcnt(0)
	v_max_f32_e32 v132, v132, v132
	v_max_f32_e32 v133, v133, v133
	v_max_f32_e32 v134, v134, v134
	v_max_f32_e32 v135, v135, v135
	v_max_f32_e32 v136, v136, v136
	v_max_f32_e32 v137, v137, v137
	v_max_f32_e32 v138, v138, v138
	v_max_f32_e32 v139, v139, v139
	v_max_f32_e32 v140, v140, v140
	v_max_f32_e32 v141, v141, v141
	v_max_f32_e32 v142, v142, v142
	v_max_f32_e32 v143, v143, v143
	v_max_f32_e32 v144, v144, v144
	v_max_f32_e32 v145, v145, v145
	v_max_f32_e32 v146, v146, v146
	v_max_f32_e32 v147, v147, v147
	v_med3_f32 v132, v132, s20, v13
	v_med3_f32 v133, v133, s20, v13
	v_med3_f32 v134, v134, s20, v13
	v_med3_f32 v135, v135, s20, v13
	v_med3_f32 v136, v136, s20, v13
	v_med3_f32 v137, v137, s20, v13
	v_med3_f32 v138, v138, s20, v13
	v_med3_f32 v139, v139, s20, v13
	v_med3_f32 v140, v140, s20, v13
	v_med3_f32 v141, v141, s20, v13
	v_med3_f32 v142, v142, s20, v13
	v_med3_f32 v143, v143, s20, v13
	v_med3_f32 v144, v144, s20, v13
	v_med3_f32 v145, v145, s20, v13
	v_med3_f32 v146, v146, s20, v13
	v_med3_f32 v147, v147, s20, v13
	v_mov_b32_e32 v148, 0
	v_mov_b32_e32 v149, 0
	v_mov_b32_e32 v150, 0
	v_mov_b32_e32 v151, 0
	v_cvt_pk_fp8_f32 v148, v132, v133
	v_cvt_pk_fp8_f32 v149, v136, v137
	v_cvt_pk_fp8_f32 v150, v140, v141
	v_cvt_pk_fp8_f32 v151, v144, v145
	v_cvt_pk_fp8_f32 v148, v134, v135 op_sel:[0,0,1]
	v_cvt_pk_fp8_f32 v149, v138, v139 op_sel:[0,0,1]
	v_cvt_pk_fp8_f32 v150, v142, v143 op_sel:[0,0,1]
	v_cvt_pk_fp8_f32 v151, v146, v147 op_sel:[0,0,1]
	s_nop 0
	global_store_dwordx4 v11, v[148:151], s[14:15]
	ds_read_b32 v132, v8
	ds_read_b32 v133, v8 offset:512
	ds_read_b32 v134, v8 offset:1024
	ds_read_b32 v135, v8 offset:1536
	ds_read_b32 v136, v8 offset:2048
	ds_read_b32 v137, v8 offset:2560
	ds_read_b32 v138, v8 offset:3072
	ds_read_b32 v139, v8 offset:3584
	ds_read_b32 v140, v8 offset:4096
	ds_read_b32 v141, v8 offset:4608
	ds_read_b32 v142, v8 offset:5120
	ds_read_b32 v143, v8 offset:5632
	ds_read_b32 v144, v8 offset:6144
	ds_read_b32 v145, v8 offset:6656
	ds_read_b32 v146, v8 offset:7168
	ds_read_b32 v147, v8 offset:7680
	s_waitcnt lgkmcnt(0)
	v_max_f32_e32 v132, v132, v132
	v_max_f32_e32 v133, v133, v133
	v_max_f32_e32 v134, v134, v134
	v_max_f32_e32 v135, v135, v135
	v_max_f32_e32 v136, v136, v136
	v_max_f32_e32 v137, v137, v137
	v_max_f32_e32 v138, v138, v138
	v_max_f32_e32 v139, v139, v139
	v_max_f32_e32 v140, v140, v140
	v_max_f32_e32 v141, v141, v141
	v_max_f32_e32 v142, v142, v142
	v_max_f32_e32 v143, v143, v143
	v_max_f32_e32 v144, v144, v144
	v_max_f32_e32 v145, v145, v145
	v_max_f32_e32 v146, v146, v146
	v_max_f32_e32 v147, v147, v147
	v_med3_f32 v132, v132, s20, v13
	v_med3_f32 v133, v133, s20, v13
	v_med3_f32 v134, v134, s20, v13
	v_med3_f32 v135, v135, s20, v13
	v_med3_f32 v136, v136, s20, v13
	v_med3_f32 v137, v137, s20, v13
	v_med3_f32 v138, v138, s20, v13
	v_med3_f32 v139, v139, s20, v13
	v_med3_f32 v140, v140, s20, v13
	v_med3_f32 v141, v141, s20, v13
	v_med3_f32 v142, v142, s20, v13
	v_med3_f32 v143, v143, s20, v13
	v_med3_f32 v144, v144, s20, v13
	v_med3_f32 v145, v145, s20, v13
	v_med3_f32 v146, v146, s20, v13
	v_med3_f32 v147, v147, s20, v13
	v_mov_b32_e32 v148, 0
	v_mov_b32_e32 v149, 0
	v_mov_b32_e32 v150, 0
	v_mov_b32_e32 v151, 0
	v_cvt_pk_fp8_f32 v148, v132, v133
	v_cvt_pk_fp8_f32 v149, v136, v137
	v_cvt_pk_fp8_f32 v150, v140, v141
	v_cvt_pk_fp8_f32 v151, v144, v145
	v_cvt_pk_fp8_f32 v148, v134, v135 op_sel:[0,0,1]
	v_cvt_pk_fp8_f32 v149, v138, v139 op_sel:[0,0,1]
	v_cvt_pk_fp8_f32 v150, v142, v143 op_sel:[0,0,1]
	v_cvt_pk_fp8_f32 v151, v146, v147 op_sel:[0,0,1]
	s_nop 0
	global_store_dwordx4 v12, v[148:151], s[14:15]
	s_waitcnt vmcnt(6)
	v_mul_f32_e32 v68, 0x43000000, v68
	v_mul_f32_e32 v69, 0x43000000, v69
	v_mul_f32_e32 v70, 0x43000000, v70
	v_mul_f32_e32 v71, 0x43000000, v71
	ds_write_b128 v5, v[68:71]
	v_mul_f32_e32 v72, 0x43000000, v72
	v_mul_f32_e32 v73, 0x43000000, v73
	v_mul_f32_e32 v74, 0x43000000, v74
	v_mul_f32_e32 v75, 0x43000000, v75
	ds_write_b128 v5, v[72:75] offset:1024
	v_mul_f32_e32 v76, 0x43000000, v76
	v_mul_f32_e32 v77, 0x43000000, v77
	v_mul_f32_e32 v78, 0x43000000, v78
	v_mul_f32_e32 v79, 0x43000000, v79
	ds_write_b128 v5, v[76:79] offset:2048
	v_mul_f32_e32 v80, 0x43000000, v80
	v_mul_f32_e32 v81, 0x43000000, v81
	v_mul_f32_e32 v82, 0x43000000, v82
	v_mul_f32_e32 v83, 0x43000000, v83
	ds_write_b128 v5, v[80:83] offset:3072
	v_mul_f32_e32 v84, 0x43000000, v84
	v_mul_f32_e32 v85, 0x43000000, v85
	v_mul_f32_e32 v86, 0x43000000, v86
	v_mul_f32_e32 v87, 0x43000000, v87
	ds_write_b128 v5, v[84:87] offset:4096
	v_mul_f32_e32 v88, 0x43000000, v88
	v_mul_f32_e32 v89, 0x43000000, v89
	v_mul_f32_e32 v90, 0x43000000, v90
	v_mul_f32_e32 v91, 0x43000000, v91
	ds_write_b128 v5, v[88:91] offset:5120
	v_mul_f32_e32 v92, 0x43000000, v92
	v_mul_f32_e32 v93, 0x43000000, v93
	v_mul_f32_e32 v94, 0x43000000, v94
	v_mul_f32_e32 v95, 0x43000000, v95
	ds_write_b128 v5, v[92:95] offset:6144
	v_mul_f32_e32 v96, 0x43000000, v96
	v_mul_f32_e32 v97, 0x43000000, v97
	v_mul_f32_e32 v98, 0x43000000, v98
	v_mul_f32_e32 v99, 0x43000000, v99
	ds_write_b128 v5, v[96:99] offset:7168
	s_waitcnt lgkmcnt(0)
	s_barrier
; #define GAS __attribute__((address_space(1)))
; #define LAS __attribute__((address_space(3)))
; #define LDS_WAIT() asm volatile("s_waitcnt lgkmcnt(0)" ::: "memory")
; __device__ __forceinline__ unsigned pk4_fp8(float a, float b, float c, float d) {
;     a = fminf(fmaxf(a, -448.f), 448.f); b = fminf(fmaxf(b, -448.f), 448.f); c = fminf(fmaxf(c, -448.f), 448.f); d = fminf(fmaxf(d, -448.f), 448.f);
;     int w = __builtin_amdgcn_cvt_pk_fp8_f32(a, b, 0, false); w = __builtin_amdgcn_cvt_pk_fp8_f32(c, d, w, true); return (unsigned)w; }
;     ...
;     for (int j = 0; j < 4; ++j) { const int n = (lane >> 3) + 8 * j; const LAS float* s = scr + (8 * c) * 33 + n;
;         const unsigned long long o = (unsigned long long)pg8::pk4_fp8(s[0 * 33], s[1 * 33], s[2 * 33], s[3 * 33]) | ((unsigned long long)pg8::pk4_fp8(s[4 * 33], s[5 * 33], s[6 * 33], s[7 * 33]) << 32);
;         *(GAS unsigned long long*)(WT + (size_t)(n0 + n) * K + k0 + 8 * c) = o; }
;     LDS_WAIT(); asm volatile("" ::: "memory");
	s_add_i32 s17, s16, 2976
	s_min_u32 s17, s17, 0xbff
	s_lshr_b32 s18, s17, 5
	s_add_i32 s18, s18, 32
	s_and_b32 s19, s17, 31
	s_lshl_b32 s19, s19, 21
	s_lshl_b32 s18, s18, 7
	s_add_u32 s18, s18, s19
	s_add_u32 s14, s4, s18
	s_addc_u32 s15, s5, 0
	ds_read_b32 v132, v7
	ds_read_b32 v133, v7 offset:512
	ds_read_b32 v134, v7 offset:1024
	ds_read_b32 v135, v7 offset:1536
	ds_read_b32 v136, v7 offset:2048
	ds_read_b32 v137, v7 offset:2560
	ds_read_b32 v138, v7 offset:3072
	ds_read_b32 v139, v7 offset:3584
	ds_read_b32 v140, v7 offset:4096
	ds_read_b32 v141, v7 offset:4608
	ds_read_b32 v142, v7 offset:5120
	ds_read_b32 v143, v7 offset:5632
	ds_read_b32 v144, v7 offset:6144
	ds_read_b32 v145, v7 offset:6656
	ds_read_b32 v146, v7 offset:7168
	ds_read_b32 v147, v7 offset:7680
	s_waitcnt lgkmcnt(0)
	v_max_f32_e32 v132, v132, v132
	v_max_f32_e32 v133, v133, v133
	v_max_f32_e32 v134, v134, v134
	v_max_f32_e32 v135, v135, v135
	v_max_f32_e32 v136, v136, v136
	v_max_f32_e32 v137, v137, v137
	v_max_f32_e32 v138, v138, v138
	v_max_f32_e32 v139, v139, v139
	v_max_f32_e32 v140, v140, v140
	v_max_f32_e32 v141, v141, v141
	v_max_f32_e32 v142, v142, v142
	v_max_f32_e32 v143, v143, v143
	v_max_f32_e32 v144, v144, v144
	v_max_f32_e32 v145, v145, v145
	v_max_f32_e32 v146, v146, v146
	v_max_f32_e32 v147, v147, v147
	v_med3_f32 v132, v132, s20, v13
	v_med3_f32 v133, v133, s20, v13
	v_med3_f32 v134, v134, s20, v13
	v_med3_f32 v135, v135, s20, v13
	v_med3_f32 v136, v136, s20, v13
	v_med3_f32 v137, v137, s20, v13
	v_med3_f32 v138, v138, s20, v13
	v_med3_f32 v139, v139, s20, v13
	v_med3_f32 v140, v140, s20, v13
	v_med3_f32 v141, v141, s20, v13
	v_med3_f32 v142, v142, s20, v13
	v_med3_f32 v143, v143, s20, v13
	v_med3_f32 v144, v144, s20, v13
	v_med3_f32 v145, v145, s20, v13
	v_med3_f32 v146, v146, s20, v13
	v_med3_f32 v147, v147, s20, v13
	v_mov_b32_e32 v148, 0
	v_mov_b32_e32 v149, 0
	v_mov_b32_e32 v150, 0
	v_mov_b32_e32 v151, 0
	v_cvt_pk_fp8_f32 v148, v132, v133
	v_cvt_pk_fp8_f32 v149, v136, v137
	v_cvt_pk_fp8_f32 v150, v140, v141
	v_cvt_pk_fp8_f32 v151, v144, v145
	v_cvt_pk_fp8_f32 v148, v134, v135 op_sel:[0,0,1]
	v_cvt_pk_fp8_f32 v149, v138, v139 op_sel:[0,0,1]
	v_cvt_pk_fp8_f32 v150, v142, v143 op_sel:[0,0,1]
	v_cvt_pk_fp8_f32 v151, v146, v147 op_sel:[0,0,1]
	s_nop 0
	global_store_dwordx4 v11, v[148:151], s[14:15]
	ds_read_b32 v132, v9
	ds_read_b32 v133, v9 offset:512
	ds_read_b32 v134, v9 offset:1024
	ds_read_b32 v135, v9 offset:1536
	ds_read_b32 v136, v9 offset:2048
	ds_read_b32 v137, v9 offset:2560
	ds_read_b32 v138, v9 offset:3072
	ds_read_b32 v139, v9 offset:3584
	ds_read_b32 v140, v9 offset:4096
	ds_read_b32 v141, v9 offset:4608
	ds_read_b32 v142, v9 offset:5120
	ds_read_b32 v143, v9 offset:5632
	ds_read_b32 v144, v9 offset:6144
	ds_read_b32 v145, v9 offset:6656
	ds_read_b32 v146, v9 offset:7168
	ds_read_b32 v147, v9 offset:7680
	s_waitcnt lgkmcnt(0)
	v_max_f32_e32 v132, v132, v132
	v_max_f32_e32 v133, v133, v133
	v_max_f32_e32 v134, v134, v134
	v_max_f32_e32 v135, v135, v135
	v_max_f32_e32 v136, v136, v136
	v_max_f32_e32 v137, v137, v137
	v_max_f32_e32 v138, v138, v138
	v_max_f32_e32 v139, v139, v139
	v_max_f32_e32 v140, v140, v140
	v_max_f32_e32 v141, v141, v141
	v_max_f32_e32 v142, v142, v142
	v_max_f32_e32 v143, v143, v143
	v_max_f32_e32 v144, v144, v144
	v_max_f32_e32 v145, v145, v145
	v_max_f32_e32 v146, v146, v146
	v_max_f32_e32 v147, v147, v147
	v_med3_f32 v132, v132, s20, v13
	v_med3_f32 v133, v133, s20, v13
	v_med3_f32 v134, v134, s20, v13
	v_med3_f32 v135, v135, s20, v13
	v_med3_f32 v136, v136, s20, v13
	v_med3_f32 v137, v137, s20, v13
	v_med3_f32 v138, v138, s20, v13
	v_med3_f32 v139, v139, s20, v13
	v_med3_f32 v140, v140, s20, v13
	v_med3_f32 v141, v141, s20, v13
	v_med3_f32 v142, v142, s20, v13
	v_med3_f32 v143, v143, s20, v13
	v_med3_f32 v144, v144, s20, v13
	v_med3_f32 v145, v145, s20, v13
	v_med3_f32 v146, v146, s20, v13
	v_med3_f32 v147, v147, s20, v13
	v_mov_b32_e32 v148, 0
	v_mov_b32_e32 v149, 0
	v_mov_b32_e32 v150, 0
	v_mov_b32_e32 v151, 0
	v_cvt_pk_fp8_f32 v148, v132, v133
	v_cvt_pk_fp8_f32 v149, v136, v137
	v_cvt_pk_fp8_f32 v150, v140, v141
	v_cvt_pk_fp8_f32 v151, v144, v145
	v_cvt_pk_fp8_f32 v148, v134, v135 op_sel:[0,0,1]
	v_cvt_pk_fp8_f32 v149, v138, v139 op_sel:[0,0,1]
	v_cvt_pk_fp8_f32 v150, v142, v143 op_sel:[0,0,1]
	v_cvt_pk_fp8_f32 v151, v146, v147 op_sel:[0,0,1]
	s_nop 0
	global_store_dwordx4 v12, v[148:151], s[14:15]
	s_waitcnt vmcnt(0) lgkmcnt(0)
	s_barrier
